# lever 4: one static s_setprio 1 for waves 4-7 (set at kernel entry, restored after the recurrence phase), per-cluster priority flips in the GEMM loops deleted
# baseline (speedup 1.0000x reference)
; __device__ __forceinline__ int lane_id() { int l; asm volatile("v_mbcnt_lo_u32_b32 %0, -1, 0\n\tv_mbcnt_hi_u32_b32 %0, -1, %0" : "=v"(l)); return l; }
; #define PG8_LAS __attribute__((address_space(3)))
; __global__ void __launch_bounds__(NT, 2) fwd_kernel(Params p) {
;     extern __shared__ __attribute__((aligned(16))) char lds[];
;     const int WID_ = __builtin_amdgcn_readfirstlane((int)(threadIdx.x >> 6));
;     cg::grid_group grid = cg::this_grid();
;     PG8_LAS unsigned char* ldsl = (PG8_LAS unsigned char*)lds;
;     char* ws = p.ws; char* dout = (char*)p.out; float* out = p.out;
;     ...
;     volatile __attribute__((address_space(3))) unsigned* bst = (volatile __attribute__((address_space(3))) unsigned*)(ldsl + LDS_BYTES - 64);
;     if (WID_ == 0 && lane_id() < 2) bst[lane_id()] = 0u;
;     __syncthreads();
;     const XcdBarrier xbar = xcd_barrier_post(WID_, (unsigned*)(ws + W_CTL * MiB), bst);
_ZN12_GLOBAL__N_110fwd_kernelENS_6ParamsE:
	s_load_dword s3, s[0:1], 0x160
	v_and_b32_e32 v1, 0x3ff, v0
	s_add_u32 s20, s0, 0x158
	v_readfirstlane_b32 s22, v1
	s_addc_u32 s21, s1, 0
	s_load_dwordx8 s[88:95], s[0:1], 0x140
	s_cmp_lt_u32 s22, 64
	s_waitcnt lgkmcnt(0)
	v_writelane_b32 v243, s3, 0
	s_cselect_b64 s[4:5], -1, 0
	v_writelane_b32 v243, s4, 1
	s_cmp_gt_u32 s22, 63
	s_nop 0
	v_writelane_b32 v243, s5, 2
	s_cselect_b64 s[4:5], -1, 0
	s_cmp_gt_u32 s22, 255
	s_cbranch_scc0 .Lprio_k0
	s_setprio 1
.Lprio_k0:
	v_writelane_b32 v243, s4, 3
	s_and_b64 vcc, exec, s[4:5]
	s_nop 0
	v_writelane_b32 v243, s5, 4
	s_cbranch_vccnz .LBB0_4
	v_mbcnt_lo_u32_b32 v2, -1, 0
	v_mbcnt_hi_u32_b32 v2, -1, v2
	s_nop 0
	v_cmp_gt_i32_e32 vcc, 2, v2
	s_and_saveexec_b64 s[6:7], vcc
	s_cbranch_execz .LBB0_3
	v_mbcnt_lo_u32_b32 v2, -1, 0
	v_mbcnt_hi_u32_b32 v2, -1, v2
	v_mov_b32_e32 v3, 0
	v_lshl_add_u32 v2, v2, 2, 0
	v_add_u32_e32 v2, 0x23fc0, v2
	ds_write_b32 v2, v3

; #define PG8_STAGE(bufoff, gbase, voff) do { _Pragma("unroll") for (int _i = 0; _i < 2; ++_i) \
;         __builtin_amdgcn_global_load_lds((const unsigned*)((const char*)(gbase) + (voff)[_i]), (PG8_LAS unsigned*)(lds + (bufoff) + ldsw + _i * 8192), 16, 0, 0); } while (0)
; #define PG8_STAGE_A(bufoff, gbase, h, nx) do { _Pragma("unroll") for (int _i = 0; _i < 2; ++_i) { \
;         const unsigned vo_ = GA ? ((nx) ? vgn[h][_i] : vgc[h][_i]) : voffA[_i]; \
;         __builtin_amdgcn_global_load_lds((const unsigned*)((const char*)(gbase) + vo_), (PG8_LAS unsigned*)(lds + (bufoff) + ldsw + _i * 8192), 16, 0, 0); } } while (0)
; #define PG8_LDA(dst, b, h) do { _Pragma("unroll") for (int m = 0; m < 4; ++m) _Pragma("unroll") for (int k = 0; k < 2; ++k) dst[m][k] = *(const PG8_LAS bf16x8*)(lds + PG8_SA(b, h) + aoff + m * 2048 + k * 1024); } while (0)
; #define PG8_LDB(dst, b, h) do { _Pragma("unroll") for (int n = 0; n < 2; ++n) _Pragma("unroll") for (int k = 0; k < 2; ++k) dst[n][k] = *(const PG8_LAS bf16x8*)(lds + PG8_SB(b, h) + boff + n * 2048 + k * 1024); } while (0)
; #define PG8_WAIT_V(n) asm volatile("s_waitcnt vmcnt(" #n ")" ::: "memory")
; #define PG8_WAIT_L(n) asm volatile("s_waitcnt lgkmcnt(" #n ")" ::: "memory")
; #define PG8_BAR __builtin_amdgcn_s_barrier()
; #define PG8_SCHED __builtin_amdgcn_sched_barrier(0)
; template <class Epi, class Sched>
; __device__ __forceinline__ void gemm_phase(const int WID_, PG8_LAS unsigned char* lds, const Sched& S, const Epi& E) {
;     ...
;         for (int t = 0; t < nt; t += 2) {
;             const bool last = (t == nt - 2);
;             const char* a1 = cA + (size_t)(t + 1) * kstep;
;             const char* a2 = last ? nA : cA + (size_t)(t + 2) * kstep; const char* b2 = last ? nB : cB + (size_t)(t + 2) * kstep;
;             const char* a3 = a2 + kstep; const char* b3 = b2 + kstep;
;             PG8_LDB(B0, 0, 0); PG8_LDB(B1, 0, 1); PG8_SCHED; PG8_LDA(At, 0, 0); PG8_STAGE_A(PG8_SA(1, 1), a1 + hstepA, 1, false);
;             PG8_WAIT_V(8); PG8_WAIT_L(0); PG8_BAR; PG8_MMA(0, 0, At, B0); PG8_MMA(0, 1, At, B1); PG8_BAR; PG8_SCHED;
;             PG8_LDA(At, 0, 1); PG8_STAGE(PG8_SB(0, 0), b2, voffB); PG8_STAGE(PG8_SB(0, 1), b2 + hstepB, voffB); PG8_STAGE_A(PG8_SA(0, 0), a2, 0, last);
;             PG8_WAIT_V(8); PG8_WAIT_L(0); PG8_BAR; PG8_MMA(1, 0, At, B0); PG8_MMA(1, 1, At, B1); PG8_BAR; PG8_SCHED;
.LBB0_114:
	ds_read_b128 v[148:151], v156
	ds_read_b128 v[160:163], v156 offset:1024
	ds_read_b128 v[164:167], v156 offset:2048
	ds_read_b128 v[168:171], v156 offset:3072
	ds_read_b128 v[172:175], v157
	ds_read_b128 v[176:179], v157 offset:1024
	ds_read_b128 v[180:183], v157 offset:2048
	ds_read_b128 v[184:187], v157 offset:3072
	s_add_u32 s22, s20, 0xfffc0080
	s_addc_u32 s23, s21, -1
	s_cmp_eq_u32 s48, 12
	s_cselect_b32 s29, s3, s23
	s_cselect_b32 s28, s13, s22
	s_cselect_b32 s23, s11, s47
	s_cselect_b32 s22, s19, s46
	v_lshl_add_u64 v[152:153], s[20:21], 0, v[140:141]
	s_add_i32 m0, s31, 0xc000
	ds_read_b128 v[188:191], v158
	ds_read_b128 v[192:195], v158 offset:1024
	ds_read_b128 v[196:199], v158 offset:2048
	ds_read_b128 v[200:203], v158 offset:3072
	ds_read_b128 v[204:207], v158 offset:4096
	ds_read_b128 v[208:211], v158 offset:5120
	ds_read_b128 v[212:215], v158 offset:6144
	ds_read_b128 v[216:219], v158 offset:7168
	global_load_lds_dwordx4 v[152:153], off
	v_lshl_add_u64 v[152:153], s[20:21], 0, v[142:143]
	s_add_i32 m0, s31, 0xe000
	s_nop 0
	global_load_lds_dwordx4 v[152:153], off
	s_waitcnt vmcnt(8)
	s_waitcnt lgkmcnt(0)
	s_barrier
	s_waitcnt lgkmcnt(0)
	v_mfma_f32_16x16x32_bf16 v[124:127], v[148:151], v[188:191], v[124:127]
	v_mfma_f32_16x16x32_bf16 v[120:123], v[164:167], v[188:191], v[120:123]
	v_mfma_f32_16x16x32_bf16 v[108:111], v[148:151], v[196:199], v[108:111]
	v_mfma_f32_16x16x32_bf16 v[104:107], v[164:167], v[196:199], v[104:107]
	v_mfma_f32_16x16x32_bf16 v[92:95], v[148:151], v[204:207], v[92:95]
	v_mfma_f32_16x16x32_bf16 v[88:91], v[164:167], v[204:207], v[88:91]
	v_mfma_f32_16x16x32_bf16 v[76:79], v[148:151], v[212:215], v[76:79]
	v_mfma_f32_16x16x32_bf16 v[72:75], v[164:167], v[212:215], v[72:75]
	v_mfma_f32_16x16x32_bf16 v[124:127], v[160:163], v[192:195], v[124:127]
	v_mfma_f32_16x16x32_bf16 v[120:123], v[168:171], v[192:195], v[120:123]
	v_mfma_f32_16x16x32_bf16 v[108:111], v[160:163], v[200:203], v[108:111]
	v_mfma_f32_16x16x32_bf16 v[104:107], v[168:171], v[200:203], v[104:107]
	v_mfma_f32_16x16x32_bf16 v[92:95], v[160:163], v[208:211], v[92:95]
	v_mfma_f32_16x16x32_bf16 v[88:91], v[168:171], v[208:211], v[88:91]
	v_mfma_f32_16x16x32_bf16 v[76:79], v[160:163], v[216:219], v[76:79]
	v_mfma_f32_16x16x32_bf16 v[72:75], v[168:171], v[216:219], v[72:75]
	v_mfma_f32_16x16x32_bf16 v[116:119], v[172:175], v[188:191], v[116:119]
	v_mfma_f32_16x16x32_bf16 v[112:115], v[180:183], v[188:191], v[112:115]
	v_mfma_f32_16x16x32_bf16 v[100:103], v[172:175], v[196:199], v[100:103]
	v_mfma_f32_16x16x32_bf16 v[96:99], v[180:183], v[196:199], v[96:99]
	v_mfma_f32_16x16x32_bf16 v[84:87], v[172:175], v[204:207], v[84:87]
	v_mfma_f32_16x16x32_bf16 v[80:83], v[180:183], v[204:207], v[80:83]
	v_mfma_f32_16x16x32_bf16 v[68:71], v[172:175], v[212:215], v[68:71]
	v_mfma_f32_16x16x32_bf16 v[64:67], v[180:183], v[212:215], v[64:67]
	v_mfma_f32_16x16x32_bf16 v[116:119], v[176:179], v[192:195], v[116:119]
	v_mfma_f32_16x16x32_bf16 v[112:115], v[184:187], v[192:195], v[112:115]
	v_mfma_f32_16x16x32_bf16 v[100:103], v[176:179], v[200:203], v[100:103]
	v_mfma_f32_16x16x32_bf16 v[96:99], v[184:187], v[200:203], v[96:99]
	v_mfma_f32_16x16x32_bf16 v[84:87], v[176:179], v[208:211], v[84:87]
	v_mfma_f32_16x16x32_bf16 v[80:83], v[184:187], v[208:211], v[80:83]
	v_mfma_f32_16x16x32_bf16 v[68:71], v[176:179], v[216:219], v[68:71]
	v_mfma_f32_16x16x32_bf16 v[64:67], v[184:187], v[216:219], v[64:67]
	s_barrier
	s_add_i32 s49, s42, s30
	v_lshl_add_u64 v[152:153], s[22:23], 0, v[130:131]
	s_mov_b32 m0, s49
	ds_read_b128 v[188:191], v158 offset:16384
	ds_read_b128 v[192:195], v158 offset:17408
	ds_read_b128 v[196:199], v158 offset:18432
	ds_read_b128 v[200:203], v158 offset:19456
	ds_read_b128 v[204:207], v158 offset:20480
	ds_read_b128 v[208:211], v158 offset:21504
	ds_read_b128 v[212:215], v158 offset:22528
	ds_read_b128 v[216:219], v158 offset:23552
	global_load_lds_dwordx4 v[152:153], off
	s_add_i32 m0, s49, 0x2000
	s_add_u32 s50, s22, 0x40000
	v_lshl_add_u64 v[220:221], s[22:23], 0, v[134:135]
	s_addc_u32 s51, s23, 0
	s_add_i32 s49, s43, s30
	global_load_lds_dwordx4 v[220:221], off
	v_lshl_add_u64 v[222:223], s[50:51], 0, v[130:131]
	s_mov_b32 m0, s49
	v_lshl_add_u64 v[224:225], s[28:29], 0, v[132:133]
	global_load_lds_dwordx4 v[222:223], off
	v_lshl_add_u64 v[222:223], s[50:51], 0, v[134:135]
	s_add_i32 m0, s49, 0x2000
	s_nop 0
	global_load_lds_dwordx4 v[222:223], off
	v_lshl_add_u64 v[222:223], s[28:29], 0, v[128:129]
	s_mov_b32 m0, s31
	s_nop 0
	global_load_lds_dwordx4 v[222:223], off
	s_mov_b32 m0, s33
	s_nop 0
	global_load_lds_dwordx4 v[224:225], off
	s_waitcnt vmcnt(8)
	s_waitcnt lgkmcnt(0)
	s_barrier
; #define PG8_STAGE_A(bufoff, gbase, h, nx) do { _Pragma("unroll") for (int _i = 0; _i < 2; ++_i) { \
;         const unsigned vo_ = GA ? ((nx) ? vgn[h][_i] : vgc[h][_i]) : voffA[_i]; \
;         __builtin_amdgcn_global_load_lds((const unsigned*)((const char*)(gbase) + vo_), (PG8_LAS unsigned*)(lds + (bufoff) + ldsw + _i * 8192), 16, 0, 0); } } while (0)
; #define PG8_LDA(dst, b, h) do { _Pragma("unroll") for (int m = 0; m < 4; ++m) _Pragma("unroll") for (int k = 0; k < 2; ++k) dst[m][k] = *(const PG8_LAS bf16x8*)(lds + PG8_SA(b, h) + aoff + m * 2048 + k * 1024); } while (0)
; #define PG8_LDB(dst, b, h) do { _Pragma("unroll") for (int n = 0; n < 2; ++n) _Pragma("unroll") for (int k = 0; k < 2; ++k) dst[n][k] = *(const PG8_LAS bf16x8*)(lds + PG8_SB(b, h) + boff + n * 2048 + k * 1024); } while (0)
; #define PG8_MMA(ai, bj, At, Bt) do { __builtin_amdgcn_s_setprio(1); _Pragma("unroll") for (int m = 0; m < 4; ++m) _Pragma("unroll") for (int n = 0; n < 2; ++n) _Pragma("unroll") for (int k = 0; k < 2; ++k) \
;         acc[ai][bj][m][n] = __builtin_amdgcn_mfma_f32_16x16x32_bf16(Bt[n][k], At[m][k], acc[ai][bj][m][n], 0, 0, 0); __builtin_amdgcn_s_setprio(0); } while (0)
; #define PG8_WAIT_V(n) asm volatile("s_waitcnt vmcnt(" #n ")" ::: "memory")
; #define PG8_WAIT_L(n) asm volatile("s_waitcnt lgkmcnt(" #n ")" ::: "memory")
; #define PG8_BAR __builtin_amdgcn_s_barrier()
; #define PG8_SCHED __builtin_amdgcn_sched_barrier(0)
; template <class Epi, class Sched>
; __device__ __forceinline__ void gemm_phase(const int WID_, PG8_LAS unsigned char* lds, const Sched& S, const Epi& E) {
;     ...
;             PG8_WAIT_V(8); PG8_WAIT_L(0); PG8_BAR; PG8_MMA(1, 0, At, B0); PG8_MMA(1, 1, At, B1); PG8_BAR; PG8_SCHED;
;             PG8_LDB(B0, 1, 0); PG8_LDB(B1, 1, 1); PG8_SCHED; PG8_LDA(At, 1, 0); PG8_STAGE_A(PG8_SA(0, 1), a2 + hstepA, 1, last);
;             PG8_WAIT_V(8); PG8_WAIT_L(0); PG8_BAR; PG8_MMA(0, 0, At, B0); PG8_MMA(0, 1, At, B1); PG8_BAR; PG8_SCHED;
	s_waitcnt lgkmcnt(0)
	v_mfma_f32_16x16x32_bf16 v[60:63], v[148:151], v[188:191], v[60:63]
	v_mfma_f32_16x16x32_bf16 v[56:59], v[164:167], v[188:191], v[56:59]
	v_mfma_f32_16x16x32_bf16 v[44:47], v[148:151], v[196:199], v[44:47]
	v_mfma_f32_16x16x32_bf16 v[40:43], v[164:167], v[196:199], v[40:43]
	v_mfma_f32_16x16x32_bf16 v[28:31], v[148:151], v[204:207], v[28:31]
	v_mfma_f32_16x16x32_bf16 v[24:27], v[164:167], v[204:207], v[24:27]
	v_mfma_f32_16x16x32_bf16 v[12:15], v[148:151], v[212:215], v[12:15]
	v_mfma_f32_16x16x32_bf16 v[8:11], v[164:167], v[212:215], v[8:11]
	v_mfma_f32_16x16x32_bf16 v[60:63], v[160:163], v[192:195], v[60:63]
	v_mfma_f32_16x16x32_bf16 v[56:59], v[168:171], v[192:195], v[56:59]
	v_mfma_f32_16x16x32_bf16 v[44:47], v[160:163], v[200:203], v[44:47]
	v_mfma_f32_16x16x32_bf16 v[40:43], v[168:171], v[200:203], v[40:43]
	v_mfma_f32_16x16x32_bf16 v[28:31], v[160:163], v[208:211], v[28:31]
	v_mfma_f32_16x16x32_bf16 v[24:27], v[168:171], v[208:211], v[24:27]
	v_mfma_f32_16x16x32_bf16 v[12:15], v[160:163], v[216:219], v[12:15]
	v_mfma_f32_16x16x32_bf16 v[8:11], v[168:171], v[216:219], v[8:11]
	v_mfma_f32_16x16x32_bf16 v[52:55], v[172:175], v[188:191], v[52:55]
	v_mfma_f32_16x16x32_bf16 v[48:51], v[180:183], v[188:191], v[48:51]
	v_mfma_f32_16x16x32_bf16 v[36:39], v[172:175], v[196:199], v[36:39]
	v_mfma_f32_16x16x32_bf16 v[32:35], v[180:183], v[196:199], v[32:35]
	v_mfma_f32_16x16x32_bf16 v[20:23], v[172:175], v[204:207], v[20:23]
	v_mfma_f32_16x16x32_bf16 v[16:19], v[180:183], v[204:207], v[16:19]
	v_mfma_f32_16x16x32_bf16 v[4:7], v[172:175], v[212:215], v[4:7]
	v_mfma_f32_16x16x32_bf16 v[0:3], v[180:183], v[212:215], v[0:3]
	v_mfma_f32_16x16x32_bf16 v[52:55], v[176:179], v[192:195], v[52:55]
	v_mfma_f32_16x16x32_bf16 v[48:51], v[184:187], v[192:195], v[48:51]
	v_mfma_f32_16x16x32_bf16 v[36:39], v[176:179], v[200:203], v[36:39]
	v_mfma_f32_16x16x32_bf16 v[32:35], v[184:187], v[200:203], v[32:35]
	v_mfma_f32_16x16x32_bf16 v[20:23], v[176:179], v[208:211], v[20:23]
	v_mfma_f32_16x16x32_bf16 v[16:19], v[184:187], v[208:211], v[16:19]
	v_mfma_f32_16x16x32_bf16 v[4:7], v[176:179], v[216:219], v[4:7]
	v_mfma_f32_16x16x32_bf16 v[0:3], v[184:187], v[216:219], v[0:3]
	s_barrier
	s_add_i32 s49, 0, 0x18000
	v_add_u32_e32 v136, s49, v154
	s_add_i32 s50, 0, 0x1c000
	ds_read_b128 v[148:151], v136
	ds_read_b128 v[160:163], v136 offset:1024
	ds_read_b128 v[164:167], v136 offset:2048
	ds_read_b128 v[168:171], v136 offset:3072
	v_add_u32_e32 v136, s50, v154
	ds_read_b128 v[172:175], v136
	ds_read_b128 v[176:179], v136 offset:1024
	ds_read_b128 v[180:183], v136 offset:2048
	ds_read_b128 v[184:187], v136 offset:3072
	s_add_u32 s28, s28, 0x40000
	s_addc_u32 s29, s29, 0
	s_mov_b32 m0, s34
	v_lshl_add_u64 v[226:227], s[28:29], 0, v[128:129]
	ds_read_b128 v[188:191], v158 offset:32768
	ds_read_b128 v[192:195], v158 offset:33792
	ds_read_b128 v[196:199], v158 offset:34816
	ds_read_b128 v[200:203], v158 offset:35840
	ds_read_b128 v[204:207], v158 offset:36864
	ds_read_b128 v[208:211], v158 offset:37888
	ds_read_b128 v[212:215], v158 offset:38912
	ds_read_b128 v[216:219], v158 offset:39936
	global_load_lds_dwordx4 v[226:227], off
	v_lshl_add_u64 v[226:227], s[28:29], 0, v[132:133]
	s_mov_b32 m0, s35
	s_nop 0
	global_load_lds_dwordx4 v[226:227], off
	s_waitcnt vmcnt(8)
	s_waitcnt lgkmcnt(0)
	s_barrier
	s_waitcnt lgkmcnt(0)
	v_mfma_f32_16x16x32_bf16 v[124:127], v[148:151], v[188:191], v[124:127]
	v_mfma_f32_16x16x32_bf16 v[120:123], v[164:167], v[188:191], v[120:123]
	v_mfma_f32_16x16x32_bf16 v[108:111], v[148:151], v[196:199], v[108:111]
	v_mfma_f32_16x16x32_bf16 v[104:107], v[164:167], v[196:199], v[104:107]
	v_mfma_f32_16x16x32_bf16 v[92:95], v[148:151], v[204:207], v[92:95]
	v_mfma_f32_16x16x32_bf16 v[88:91], v[164:167], v[204:207], v[88:91]
	v_mfma_f32_16x16x32_bf16 v[76:79], v[148:151], v[212:215], v[76:79]
	v_mfma_f32_16x16x32_bf16 v[72:75], v[164:167], v[212:215], v[72:75]
	v_mfma_f32_16x16x32_bf16 v[124:127], v[160:163], v[192:195], v[124:127]
	v_mfma_f32_16x16x32_bf16 v[120:123], v[168:171], v[192:195], v[120:123]
	v_mfma_f32_16x16x32_bf16 v[108:111], v[160:163], v[200:203], v[108:111]
	v_mfma_f32_16x16x32_bf16 v[104:107], v[168:171], v[200:203], v[104:107]
	v_mfma_f32_16x16x32_bf16 v[92:95], v[160:163], v[208:211], v[92:95]
	v_mfma_f32_16x16x32_bf16 v[88:91], v[168:171], v[208:211], v[88:91]
	v_mfma_f32_16x16x32_bf16 v[76:79], v[160:163], v[216:219], v[76:79]
	v_mfma_f32_16x16x32_bf16 v[72:75], v[168:171], v[216:219], v[72:75]
	v_mfma_f32_16x16x32_bf16 v[116:119], v[172:175], v[188:191], v[116:119]
	v_mfma_f32_16x16x32_bf16 v[112:115], v[180:183], v[188:191], v[112:115]
	v_mfma_f32_16x16x32_bf16 v[100:103], v[172:175], v[196:199], v[100:103]
	v_mfma_f32_16x16x32_bf16 v[96:99], v[180:183], v[196:199], v[96:99]
	v_mfma_f32_16x16x32_bf16 v[84:87], v[172:175], v[204:207], v[84:87]
	v_mfma_f32_16x16x32_bf16 v[80:83], v[180:183], v[204:207], v[80:83]
	v_mfma_f32_16x16x32_bf16 v[68:71], v[172:175], v[212:215], v[68:71]
	v_mfma_f32_16x16x32_bf16 v[64:67], v[180:183], v[212:215], v[64:67]
	v_mfma_f32_16x16x32_bf16 v[116:119], v[176:179], v[192:195], v[116:119]
	v_mfma_f32_16x16x32_bf16 v[112:115], v[184:187], v[192:195], v[112:115]
	v_mfma_f32_16x16x32_bf16 v[100:103], v[176:179], v[200:203], v[100:103]
	v_mfma_f32_16x16x32_bf16 v[96:99], v[184:187], v[200:203], v[96:99]
	v_mfma_f32_16x16x32_bf16 v[84:87], v[176:179], v[208:211], v[84:87]
	v_mfma_f32_16x16x32_bf16 v[80:83], v[184:187], v[208:211], v[80:83]
	v_mfma_f32_16x16x32_bf16 v[68:71], v[176:179], v[216:219], v[68:71]
	v_mfma_f32_16x16x32_bf16 v[64:67], v[184:187], v[216:219], v[64:67]
	s_barrier
; #define PG8_STAGE(bufoff, gbase, voff) do { _Pragma("unroll") for (int _i = 0; _i < 2; ++_i) \
;         __builtin_amdgcn_global_load_lds((const unsigned*)((const char*)(gbase) + (voff)[_i]), (PG8_LAS unsigned*)(lds + (bufoff) + ldsw + _i * 8192), 16, 0, 0); } while (0)
; #define PG8_STAGE_A(bufoff, gbase, h, nx) do { _Pragma("unroll") for (int _i = 0; _i < 2; ++_i) { \
;         const unsigned vo_ = GA ? ((nx) ? vgn[h][_i] : vgc[h][_i]) : voffA[_i]; \
;         __builtin_amdgcn_global_load_lds((const unsigned*)((const char*)(gbase) + vo_), (PG8_LAS unsigned*)(lds + (bufoff) + ldsw + _i * 8192), 16, 0, 0); } } while (0)
; #define PG8_LDA(dst, b, h) do { _Pragma("unroll") for (int m = 0; m < 4; ++m) _Pragma("unroll") for (int k = 0; k < 2; ++k) dst[m][k] = *(const PG8_LAS bf16x8*)(lds + PG8_SA(b, h) + aoff + m * 2048 + k * 1024); } while (0)
; #define PG8_MMA(ai, bj, At, Bt) do { __builtin_amdgcn_s_setprio(1); _Pragma("unroll") for (int m = 0; m < 4; ++m) _Pragma("unroll") for (int n = 0; n < 2; ++n) _Pragma("unroll") for (int k = 0; k < 2; ++k) \
;         acc[ai][bj][m][n] = __builtin_amdgcn_mfma_f32_16x16x32_bf16(Bt[n][k], At[m][k], acc[ai][bj][m][n], 0, 0, 0); __builtin_amdgcn_s_setprio(0); } while (0)
; #define PG8_WAIT_V(n) asm volatile("s_waitcnt vmcnt(" #n ")" ::: "memory")
; #define PG8_WAIT_L(n) asm volatile("s_waitcnt lgkmcnt(" #n ")" ::: "memory")
; #define PG8_BAR __builtin_amdgcn_s_barrier()
; #define PG8_SCHED __builtin_amdgcn_sched_barrier(0)
; template <class Epi, class Sched>
; __device__ __forceinline__ void gemm_phase(const int WID_, PG8_LAS unsigned char* lds, const Sched& S, const Epi& E) {
;     ...
;             PG8_LDA(At, 1, 1); PG8_STAGE(PG8_SB(1, 0), b3, voffB); PG8_STAGE(PG8_SB(1, 1), b3 + hstepB, voffB); PG8_STAGE_A(PG8_SA(1, 0), a3, 0, last);
;             PG8_WAIT_V(8); PG8_WAIT_L(0); PG8_BAR; PG8_MMA(1, 0, At, B0); PG8_MMA(1, 1, At, B1); PG8_BAR; PG8_SCHED;
;         }
;         if (wr == 0) PG8_BAR;
	s_add_i32 s28, s49, s30
	v_lshl_add_u64 v[152:153], v[152:153], 0, s[6:7]
	s_mov_b32 m0, s28
	ds_read_b128 v[188:191], v158 offset:49152
	ds_read_b128 v[192:195], v158 offset:50176
	ds_read_b128 v[196:199], v158 offset:51200
	ds_read_b128 v[200:203], v158 offset:52224
	ds_read_b128 v[204:207], v158 offset:53248
	ds_read_b128 v[208:211], v158 offset:54272
	ds_read_b128 v[212:215], v158 offset:55296
	ds_read_b128 v[216:219], v158 offset:56320
	global_load_lds_dwordx4 v[152:153], off
	s_add_i32 m0, s28, 0x2000
	s_add_u32 s22, s22, 0x40080
	v_lshl_add_u64 v[152:153], v[220:221], 0, s[6:7]
	s_addc_u32 s23, s23, 0
	s_add_i32 s28, s50, s30
	global_load_lds_dwordx4 v[152:153], off
	v_lshl_add_u64 v[152:153], s[22:23], 0, v[130:131]
	s_mov_b32 m0, s28
	s_nop 0
	global_load_lds_dwordx4 v[152:153], off
	v_lshl_add_u64 v[152:153], s[22:23], 0, v[134:135]
	s_add_i32 m0, s28, 0x2000
	s_nop 0
	global_load_lds_dwordx4 v[152:153], off
	v_lshl_add_u64 v[152:153], v[222:223], 0, s[6:7]
	s_mov_b32 m0, s37
	s_nop 0
	global_load_lds_dwordx4 v[152:153], off
	v_lshl_add_u64 v[152:153], v[224:225], 0, s[6:7]
	s_mov_b32 m0, s38
	s_nop 0
	global_load_lds_dwordx4 v[152:153], off
	s_waitcnt vmcnt(8)
	s_waitcnt lgkmcnt(0)
	s_barrier
	s_waitcnt lgkmcnt(0)
	v_mfma_f32_16x16x32_bf16 v[60:63], v[148:151], v[188:191], v[60:63]
	v_mfma_f32_16x16x32_bf16 v[56:59], v[164:167], v[188:191], v[56:59]
	v_mfma_f32_16x16x32_bf16 v[44:47], v[148:151], v[196:199], v[44:47]
	v_mfma_f32_16x16x32_bf16 v[40:43], v[164:167], v[196:199], v[40:43]
	v_mfma_f32_16x16x32_bf16 v[28:31], v[148:151], v[204:207], v[28:31]
	v_mfma_f32_16x16x32_bf16 v[24:27], v[164:167], v[204:207], v[24:27]
	v_mfma_f32_16x16x32_bf16 v[12:15], v[148:151], v[212:215], v[12:15]
	v_mfma_f32_16x16x32_bf16 v[8:11], v[164:167], v[212:215], v[8:11]
	v_mfma_f32_16x16x32_bf16 v[60:63], v[160:163], v[192:195], v[60:63]
	v_mfma_f32_16x16x32_bf16 v[56:59], v[168:171], v[192:195], v[56:59]
	v_mfma_f32_16x16x32_bf16 v[44:47], v[160:163], v[200:203], v[44:47]
	v_mfma_f32_16x16x32_bf16 v[40:43], v[168:171], v[200:203], v[40:43]
	v_mfma_f32_16x16x32_bf16 v[28:31], v[160:163], v[208:211], v[28:31]
	v_mfma_f32_16x16x32_bf16 v[24:27], v[168:171], v[208:211], v[24:27]
	v_mfma_f32_16x16x32_bf16 v[12:15], v[160:163], v[216:219], v[12:15]
	v_mfma_f32_16x16x32_bf16 v[8:11], v[168:171], v[216:219], v[8:11]
	v_mfma_f32_16x16x32_bf16 v[52:55], v[172:175], v[188:191], v[52:55]
	v_mfma_f32_16x16x32_bf16 v[48:51], v[180:183], v[188:191], v[48:51]
	v_mfma_f32_16x16x32_bf16 v[36:39], v[172:175], v[196:199], v[36:39]
	v_mfma_f32_16x16x32_bf16 v[32:35], v[180:183], v[196:199], v[32:35]
	v_mfma_f32_16x16x32_bf16 v[20:23], v[172:175], v[204:207], v[20:23]
	v_mfma_f32_16x16x32_bf16 v[16:19], v[180:183], v[204:207], v[16:19]
	v_mfma_f32_16x16x32_bf16 v[4:7], v[172:175], v[212:215], v[4:7]
	v_mfma_f32_16x16x32_bf16 v[0:3], v[180:183], v[212:215], v[0:3]
	v_mfma_f32_16x16x32_bf16 v[52:55], v[176:179], v[192:195], v[52:55]
	v_mfma_f32_16x16x32_bf16 v[48:51], v[184:187], v[192:195], v[48:51]
	v_mfma_f32_16x16x32_bf16 v[36:39], v[176:179], v[200:203], v[36:39]
	v_mfma_f32_16x16x32_bf16 v[32:35], v[184:187], v[200:203], v[32:35]
	v_mfma_f32_16x16x32_bf16 v[20:23], v[176:179], v[208:211], v[20:23]
	v_mfma_f32_16x16x32_bf16 v[16:19], v[184:187], v[208:211], v[16:19]
	v_mfma_f32_16x16x32_bf16 v[4:7], v[176:179], v[216:219], v[4:7]
	v_mfma_f32_16x16x32_bf16 v[0:3], v[184:187], v[216:219], v[0:3]
	s_barrier
	s_add_i32 s48, s48, 2
	s_add_u32 s20, s20, 0x100
	s_addc_u32 s21, s21, 0
	s_add_u32 s46, s46, 0x100
	s_addc_u32 s47, s47, 0
	s_cmp_gt_u32 s48, 13
	s_cbranch_scc0 .LBB0_114
	s_and_b64 vcc, exec, s[8:9]
	s_cbranch_vccz .LBB0_117
	s_barrier

; #define PG8_STAGE(bufoff, gbase, voff) do { _Pragma("unroll") for (int _i = 0; _i < 2; ++_i) \
;         __builtin_amdgcn_global_load_lds((const unsigned*)((const char*)(gbase) + (voff)[_i]), (PG8_LAS unsigned*)(lds + (bufoff) + ldsw + _i * 8192), 16, 0, 0); } while (0)
; #define PG8_STAGE_A(bufoff, gbase, h, nx) do { _Pragma("unroll") for (int _i = 0; _i < 2; ++_i) { \
;         const unsigned vo_ = GA ? ((nx) ? vgn[h][_i] : vgc[h][_i]) : voffA[_i]; \
;         __builtin_amdgcn_global_load_lds((const unsigned*)((const char*)(gbase) + vo_), (PG8_LAS unsigned*)(lds + (bufoff) + ldsw + _i * 8192), 16, 0, 0); } } while (0)
; #define PG8_LDA(dst, b, h) do { _Pragma("unroll") for (int m = 0; m < 4; ++m) _Pragma("unroll") for (int k = 0; k < 2; ++k) dst[m][k] = *(const PG8_LAS bf16x8*)(lds + PG8_SA(b, h) + aoff + m * 2048 + k * 1024); } while (0)
; #define PG8_LDB(dst, b, h) do { _Pragma("unroll") for (int n = 0; n < 2; ++n) _Pragma("unroll") for (int k = 0; k < 2; ++k) dst[n][k] = *(const PG8_LAS bf16x8*)(lds + PG8_SB(b, h) + boff + n * 2048 + k * 1024); } while (0)
; #define PG8_WAIT_V(n) asm volatile("s_waitcnt vmcnt(" #n ")" ::: "memory")
; #define PG8_WAIT_L(n) asm volatile("s_waitcnt lgkmcnt(" #n ")" ::: "memory")
; #define PG8_BAR __builtin_amdgcn_s_barrier()
; #define PG8_SCHED __builtin_amdgcn_sched_barrier(0)
; template <class Epi, class Sched>
; __device__ __forceinline__ void gemm_phase(const int WID_, PG8_LAS unsigned char* lds, const Sched& S, const Epi& E) {
;     ...
;         for (int t = 0; t < nt; t += 2) {
;             const bool last = (t == nt - 2);
;             const char* a1 = cA + (size_t)(t + 1) * kstep;
;             const char* a2 = last ? nA : cA + (size_t)(t + 2) * kstep; const char* b2 = last ? nB : cB + (size_t)(t + 2) * kstep;
;             const char* a3 = a2 + kstep; const char* b3 = b2 + kstep;
;             PG8_LDB(B0, 0, 0); PG8_LDB(B1, 0, 1); PG8_SCHED; PG8_LDA(At, 0, 0); PG8_STAGE_A(PG8_SA(1, 1), a1 + hstepA, 1, false);
;             PG8_WAIT_V(8); PG8_WAIT_L(0); PG8_BAR; PG8_MMA(0, 0, At, B0); PG8_MMA(0, 1, At, B1); PG8_BAR; PG8_SCHED;
;             PG8_LDA(At, 0, 1); PG8_STAGE(PG8_SB(0, 0), b2, voffB); PG8_STAGE(PG8_SB(0, 1), b2 + hstepB, voffB); PG8_STAGE_A(PG8_SA(0, 0), a2, 0, last);
;             PG8_WAIT_V(8); PG8_WAIT_L(0); PG8_BAR; PG8_MMA(1, 0, At, B0); PG8_MMA(1, 1, At, B1); PG8_BAR; PG8_SCHED;
.LBB0_263:
	ds_read_b128 v[138:141], v149
	ds_read_b128 v[142:145], v149 offset:1024
	ds_read_b128 v[152:155], v149 offset:2048
	ds_read_b128 v[156:159], v149 offset:3072
	ds_read_b128 v[160:163], v150
	ds_read_b128 v[164:167], v150 offset:1024
	ds_read_b128 v[168:171], v150 offset:2048
	ds_read_b128 v[172:175], v150 offset:3072
	s_add_u32 s8, s6, 0xfffe0080
	s_addc_u32 s9, s7, -1
	s_cmp_eq_u32 s35, 4
	s_cselect_b32 s11, s23, s9
	s_cselect_b32 s10, s22, s8
	s_cselect_b32 s9, s29, s21
	s_cselect_b32 s8, s28, s5
	v_lshl_add_u64 v[208:209], s[6:7], 0, v[134:135]
	s_add_i32 m0, s38, 0xc000
	ds_read_b128 v[176:179], v151
	ds_read_b128 v[180:183], v151 offset:1024
	ds_read_b128 v[184:187], v151 offset:2048
	ds_read_b128 v[188:191], v151 offset:3072
	ds_read_b128 v[192:195], v151 offset:4096
	ds_read_b128 v[196:199], v151 offset:5120
	ds_read_b128 v[200:203], v151 offset:6144
	ds_read_b128 v[204:207], v151 offset:7168
	global_load_lds_dwordx4 v[208:209], off
	v_lshl_add_u64 v[208:209], s[6:7], 0, v[136:137]
	s_add_i32 m0, s38, 0xe000
	s_nop 0
	global_load_lds_dwordx4 v[208:209], off
	s_waitcnt vmcnt(8)
	s_waitcnt lgkmcnt(0)
	s_barrier
	s_waitcnt lgkmcnt(0)
	v_mfma_f32_16x16x32_bf16 v[124:127], v[138:141], v[176:179], v[124:127]
	v_mfma_f32_16x16x32_bf16 v[120:123], v[152:155], v[176:179], v[120:123]
	v_mfma_f32_16x16x32_bf16 v[108:111], v[138:141], v[184:187], v[108:111]
	v_mfma_f32_16x16x32_bf16 v[104:107], v[152:155], v[184:187], v[104:107]
	v_mfma_f32_16x16x32_bf16 v[92:95], v[138:141], v[192:195], v[92:95]
	v_mfma_f32_16x16x32_bf16 v[88:91], v[152:155], v[192:195], v[88:91]
	v_mfma_f32_16x16x32_bf16 v[76:79], v[138:141], v[200:203], v[76:79]
	v_mfma_f32_16x16x32_bf16 v[72:75], v[152:155], v[200:203], v[72:75]
	v_mfma_f32_16x16x32_bf16 v[124:127], v[142:145], v[180:183], v[124:127]
	v_mfma_f32_16x16x32_bf16 v[120:123], v[156:159], v[180:183], v[120:123]
	v_mfma_f32_16x16x32_bf16 v[108:111], v[142:145], v[188:191], v[108:111]
	v_mfma_f32_16x16x32_bf16 v[104:107], v[156:159], v[188:191], v[104:107]
	v_mfma_f32_16x16x32_bf16 v[92:95], v[142:145], v[196:199], v[92:95]
	v_mfma_f32_16x16x32_bf16 v[88:91], v[156:159], v[196:199], v[88:91]
	v_mfma_f32_16x16x32_bf16 v[76:79], v[142:145], v[204:207], v[76:79]
	v_mfma_f32_16x16x32_bf16 v[72:75], v[156:159], v[204:207], v[72:75]
	v_mfma_f32_16x16x32_bf16 v[116:119], v[160:163], v[176:179], v[116:119]
	v_mfma_f32_16x16x32_bf16 v[112:115], v[168:171], v[176:179], v[112:115]
	v_mfma_f32_16x16x32_bf16 v[100:103], v[160:163], v[184:187], v[100:103]
	v_mfma_f32_16x16x32_bf16 v[96:99], v[168:171], v[184:187], v[96:99]
	v_mfma_f32_16x16x32_bf16 v[84:87], v[160:163], v[192:195], v[84:87]
	v_mfma_f32_16x16x32_bf16 v[80:83], v[168:171], v[192:195], v[80:83]
	v_mfma_f32_16x16x32_bf16 v[68:71], v[160:163], v[200:203], v[68:71]
	v_mfma_f32_16x16x32_bf16 v[64:67], v[168:171], v[200:203], v[64:67]
	v_mfma_f32_16x16x32_bf16 v[116:119], v[164:167], v[180:183], v[116:119]
	v_mfma_f32_16x16x32_bf16 v[112:115], v[172:175], v[180:183], v[112:115]
	v_mfma_f32_16x16x32_bf16 v[100:103], v[164:167], v[188:191], v[100:103]
	v_mfma_f32_16x16x32_bf16 v[96:99], v[172:175], v[188:191], v[96:99]
	v_mfma_f32_16x16x32_bf16 v[84:87], v[164:167], v[196:199], v[84:87]
	v_mfma_f32_16x16x32_bf16 v[80:83], v[172:175], v[196:199], v[80:83]
	v_mfma_f32_16x16x32_bf16 v[68:71], v[164:167], v[204:207], v[68:71]
	v_mfma_f32_16x16x32_bf16 v[64:67], v[172:175], v[204:207], v[64:67]
	s_barrier
	s_add_i32 s36, s47, s33
	v_lshl_add_u64 v[208:209], s[8:9], 0, v[128:129]
	s_mov_b32 m0, s36
	ds_read_b128 v[176:179], v151 offset:16384
	ds_read_b128 v[180:183], v151 offset:17408
	ds_read_b128 v[184:187], v151 offset:18432
	ds_read_b128 v[188:191], v151 offset:19456
	ds_read_b128 v[192:195], v151 offset:20480
	ds_read_b128 v[196:199], v151 offset:21504
	ds_read_b128 v[200:203], v151 offset:22528
	ds_read_b128 v[204:207], v151 offset:23552
	global_load_lds_dwordx4 v[208:209], off
	s_add_i32 m0, s36, 0x2000
	s_add_u32 s36, s8, 0x20000
	v_lshl_add_u64 v[210:211], s[8:9], 0, v[130:131]
	s_addc_u32 s37, s9, 0
	s_add_i32 s52, s48, s33
	global_load_lds_dwordx4 v[210:211], off
	v_lshl_add_u64 v[212:213], s[36:37], 0, v[128:129]
	s_mov_b32 m0, s52
	v_lshl_add_u64 v[214:215], s[10:11], 0, v[130:131]
	global_load_lds_dwordx4 v[212:213], off
	v_lshl_add_u64 v[212:213], s[36:37], 0, v[130:131]
	s_add_i32 m0, s52, 0x2000
	s_nop 0
	global_load_lds_dwordx4 v[212:213], off
	v_lshl_add_u64 v[212:213], s[10:11], 0, v[128:129]
	s_mov_b32 m0, s38
	s_nop 0
	global_load_lds_dwordx4 v[212:213], off
	s_mov_b32 m0, s39
	s_nop 0
	global_load_lds_dwordx4 v[214:215], off
	s_waitcnt vmcnt(8)
	s_waitcnt lgkmcnt(0)
	s_barrier
; #define PG8_STAGE_A(bufoff, gbase, h, nx) do { _Pragma("unroll") for (int _i = 0; _i < 2; ++_i) { \
;         const unsigned vo_ = GA ? ((nx) ? vgn[h][_i] : vgc[h][_i]) : voffA[_i]; \
;         __builtin_amdgcn_global_load_lds((const unsigned*)((const char*)(gbase) + vo_), (PG8_LAS unsigned*)(lds + (bufoff) + ldsw + _i * 8192), 16, 0, 0); } } while (0)
; #define PG8_LDA(dst, b, h) do { _Pragma("unroll") for (int m = 0; m < 4; ++m) _Pragma("unroll") for (int k = 0; k < 2; ++k) dst[m][k] = *(const PG8_LAS bf16x8*)(lds + PG8_SA(b, h) + aoff + m * 2048 + k * 1024); } while (0)
; #define PG8_LDB(dst, b, h) do { _Pragma("unroll") for (int n = 0; n < 2; ++n) _Pragma("unroll") for (int k = 0; k < 2; ++k) dst[n][k] = *(const PG8_LAS bf16x8*)(lds + PG8_SB(b, h) + boff + n * 2048 + k * 1024); } while (0)
; #define PG8_MMA(ai, bj, At, Bt) do { __builtin_amdgcn_s_setprio(1); _Pragma("unroll") for (int m = 0; m < 4; ++m) _Pragma("unroll") for (int n = 0; n < 2; ++n) _Pragma("unroll") for (int k = 0; k < 2; ++k) \
;         acc[ai][bj][m][n] = __builtin_amdgcn_mfma_f32_16x16x32_bf16(Bt[n][k], At[m][k], acc[ai][bj][m][n], 0, 0, 0); __builtin_amdgcn_s_setprio(0); } while (0)
; #define PG8_WAIT_V(n) asm volatile("s_waitcnt vmcnt(" #n ")" ::: "memory")
; #define PG8_WAIT_L(n) asm volatile("s_waitcnt lgkmcnt(" #n ")" ::: "memory")
; #define PG8_BAR __builtin_amdgcn_s_barrier()
; #define PG8_SCHED __builtin_amdgcn_sched_barrier(0)
; template <class Epi, class Sched>
; __device__ __forceinline__ void gemm_phase(const int WID_, PG8_LAS unsigned char* lds, const Sched& S, const Epi& E) {
;     ...
;             PG8_WAIT_V(8); PG8_WAIT_L(0); PG8_BAR; PG8_MMA(1, 0, At, B0); PG8_MMA(1, 1, At, B1); PG8_BAR; PG8_SCHED;
;             PG8_LDB(B0, 1, 0); PG8_LDB(B1, 1, 1); PG8_SCHED; PG8_LDA(At, 1, 0); PG8_STAGE_A(PG8_SA(0, 1), a2 + hstepA, 1, last);
;             PG8_WAIT_V(8); PG8_WAIT_L(0); PG8_BAR; PG8_MMA(0, 0, At, B0); PG8_MMA(0, 1, At, B1); PG8_BAR; PG8_SCHED;
	s_waitcnt lgkmcnt(0)
	v_mfma_f32_16x16x32_bf16 v[60:63], v[138:141], v[176:179], v[60:63]
	v_mfma_f32_16x16x32_bf16 v[56:59], v[152:155], v[176:179], v[56:59]
	v_mfma_f32_16x16x32_bf16 v[44:47], v[138:141], v[184:187], v[44:47]
	v_mfma_f32_16x16x32_bf16 v[40:43], v[152:155], v[184:187], v[40:43]
	v_mfma_f32_16x16x32_bf16 v[28:31], v[138:141], v[192:195], v[28:31]
	v_mfma_f32_16x16x32_bf16 v[24:27], v[152:155], v[192:195], v[24:27]
	v_mfma_f32_16x16x32_bf16 v[12:15], v[138:141], v[200:203], v[12:15]
	v_mfma_f32_16x16x32_bf16 v[8:11], v[152:155], v[200:203], v[8:11]
	v_mfma_f32_16x16x32_bf16 v[60:63], v[142:145], v[180:183], v[60:63]
	v_mfma_f32_16x16x32_bf16 v[56:59], v[156:159], v[180:183], v[56:59]
	v_mfma_f32_16x16x32_bf16 v[44:47], v[142:145], v[188:191], v[44:47]
	v_mfma_f32_16x16x32_bf16 v[40:43], v[156:159], v[188:191], v[40:43]
	v_mfma_f32_16x16x32_bf16 v[28:31], v[142:145], v[196:199], v[28:31]
	v_mfma_f32_16x16x32_bf16 v[24:27], v[156:159], v[196:199], v[24:27]
	v_mfma_f32_16x16x32_bf16 v[12:15], v[142:145], v[204:207], v[12:15]
	v_mfma_f32_16x16x32_bf16 v[8:11], v[156:159], v[204:207], v[8:11]
	v_mfma_f32_16x16x32_bf16 v[52:55], v[160:163], v[176:179], v[52:55]
	v_mfma_f32_16x16x32_bf16 v[48:51], v[168:171], v[176:179], v[48:51]
	v_mfma_f32_16x16x32_bf16 v[36:39], v[160:163], v[184:187], v[36:39]
	v_mfma_f32_16x16x32_bf16 v[32:35], v[168:171], v[184:187], v[32:35]
	v_mfma_f32_16x16x32_bf16 v[20:23], v[160:163], v[192:195], v[20:23]
	v_mfma_f32_16x16x32_bf16 v[16:19], v[168:171], v[192:195], v[16:19]
	v_mfma_f32_16x16x32_bf16 v[4:7], v[160:163], v[200:203], v[4:7]
	v_mfma_f32_16x16x32_bf16 v[0:3], v[168:171], v[200:203], v[0:3]
	v_mfma_f32_16x16x32_bf16 v[52:55], v[164:167], v[180:183], v[52:55]
	v_mfma_f32_16x16x32_bf16 v[48:51], v[172:175], v[180:183], v[48:51]
	v_mfma_f32_16x16x32_bf16 v[36:39], v[164:167], v[188:191], v[36:39]
	v_mfma_f32_16x16x32_bf16 v[32:35], v[172:175], v[188:191], v[32:35]
	v_mfma_f32_16x16x32_bf16 v[20:23], v[164:167], v[196:199], v[20:23]
	v_mfma_f32_16x16x32_bf16 v[16:19], v[172:175], v[196:199], v[16:19]
	v_mfma_f32_16x16x32_bf16 v[4:7], v[164:167], v[204:207], v[4:7]
	v_mfma_f32_16x16x32_bf16 v[0:3], v[172:175], v[204:207], v[0:3]
	s_barrier
	s_add_i32 s36, 0, 0x18000
	v_add_u32_e32 v132, s36, v147
	s_add_i32 s37, 0, 0x1c000
	ds_read_b128 v[138:141], v132
	ds_read_b128 v[142:145], v132 offset:1024
	ds_read_b128 v[152:155], v132 offset:2048
	ds_read_b128 v[156:159], v132 offset:3072
	v_add_u32_e32 v132, s37, v147
	ds_read_b128 v[160:163], v132
	ds_read_b128 v[164:167], v132 offset:1024
	ds_read_b128 v[168:171], v132 offset:2048
	ds_read_b128 v[172:175], v132 offset:3072
	s_add_u32 s10, s10, 0x20000
	s_addc_u32 s11, s11, 0
	s_mov_b32 m0, s40
	v_lshl_add_u64 v[216:217], s[10:11], 0, v[128:129]
	ds_read_b128 v[176:179], v151 offset:32768
	ds_read_b128 v[180:183], v151 offset:33792
	ds_read_b128 v[184:187], v151 offset:34816
	ds_read_b128 v[188:191], v151 offset:35840
	ds_read_b128 v[192:195], v151 offset:36864
	ds_read_b128 v[196:199], v151 offset:37888
	ds_read_b128 v[200:203], v151 offset:38912
	ds_read_b128 v[204:207], v151 offset:39936
	global_load_lds_dwordx4 v[216:217], off
	v_lshl_add_u64 v[216:217], s[10:11], 0, v[130:131]
	s_mov_b32 m0, s41
	s_nop 0
	global_load_lds_dwordx4 v[216:217], off
	s_waitcnt vmcnt(8)
	s_waitcnt lgkmcnt(0)
	s_barrier
	s_waitcnt lgkmcnt(0)
	v_mfma_f32_16x16x32_bf16 v[124:127], v[138:141], v[176:179], v[124:127]
	v_mfma_f32_16x16x32_bf16 v[120:123], v[152:155], v[176:179], v[120:123]
	v_mfma_f32_16x16x32_bf16 v[108:111], v[138:141], v[184:187], v[108:111]
	v_mfma_f32_16x16x32_bf16 v[104:107], v[152:155], v[184:187], v[104:107]
	v_mfma_f32_16x16x32_bf16 v[92:95], v[138:141], v[192:195], v[92:95]
	v_mfma_f32_16x16x32_bf16 v[88:91], v[152:155], v[192:195], v[88:91]
	v_mfma_f32_16x16x32_bf16 v[76:79], v[138:141], v[200:203], v[76:79]
	v_mfma_f32_16x16x32_bf16 v[72:75], v[152:155], v[200:203], v[72:75]
	v_mfma_f32_16x16x32_bf16 v[124:127], v[142:145], v[180:183], v[124:127]
	v_mfma_f32_16x16x32_bf16 v[120:123], v[156:159], v[180:183], v[120:123]
	v_mfma_f32_16x16x32_bf16 v[108:111], v[142:145], v[188:191], v[108:111]
	v_mfma_f32_16x16x32_bf16 v[104:107], v[156:159], v[188:191], v[104:107]
	v_mfma_f32_16x16x32_bf16 v[92:95], v[142:145], v[196:199], v[92:95]
	v_mfma_f32_16x16x32_bf16 v[88:91], v[156:159], v[196:199], v[88:91]
	v_mfma_f32_16x16x32_bf16 v[76:79], v[142:145], v[204:207], v[76:79]
	v_mfma_f32_16x16x32_bf16 v[72:75], v[156:159], v[204:207], v[72:75]
	v_mfma_f32_16x16x32_bf16 v[116:119], v[160:163], v[176:179], v[116:119]
	v_mfma_f32_16x16x32_bf16 v[112:115], v[168:171], v[176:179], v[112:115]
	v_mfma_f32_16x16x32_bf16 v[100:103], v[160:163], v[184:187], v[100:103]
	v_mfma_f32_16x16x32_bf16 v[96:99], v[168:171], v[184:187], v[96:99]
	v_mfma_f32_16x16x32_bf16 v[84:87], v[160:163], v[192:195], v[84:87]
	v_mfma_f32_16x16x32_bf16 v[80:83], v[168:171], v[192:195], v[80:83]
	v_mfma_f32_16x16x32_bf16 v[68:71], v[160:163], v[200:203], v[68:71]
	v_mfma_f32_16x16x32_bf16 v[64:67], v[168:171], v[200:203], v[64:67]
	v_mfma_f32_16x16x32_bf16 v[116:119], v[164:167], v[180:183], v[116:119]
	v_mfma_f32_16x16x32_bf16 v[112:115], v[172:175], v[180:183], v[112:115]
	v_mfma_f32_16x16x32_bf16 v[100:103], v[164:167], v[188:191], v[100:103]
	v_mfma_f32_16x16x32_bf16 v[96:99], v[172:175], v[188:191], v[96:99]
	v_mfma_f32_16x16x32_bf16 v[84:87], v[164:167], v[196:199], v[84:87]
	v_mfma_f32_16x16x32_bf16 v[80:83], v[172:175], v[196:199], v[80:83]
	v_mfma_f32_16x16x32_bf16 v[68:71], v[164:167], v[204:207], v[68:71]
	v_mfma_f32_16x16x32_bf16 v[64:67], v[172:175], v[204:207], v[64:67]
	s_barrier
; #define PG8_STAGE(bufoff, gbase, voff) do { _Pragma("unroll") for (int _i = 0; _i < 2; ++_i) \
;         __builtin_amdgcn_global_load_lds((const unsigned*)((const char*)(gbase) + (voff)[_i]), (PG8_LAS unsigned*)(lds + (bufoff) + ldsw + _i * 8192), 16, 0, 0); } while (0)
; #define PG8_STAGE_A(bufoff, gbase, h, nx) do { _Pragma("unroll") for (int _i = 0; _i < 2; ++_i) { \
;         const unsigned vo_ = GA ? ((nx) ? vgn[h][_i] : vgc[h][_i]) : voffA[_i]; \
;         __builtin_amdgcn_global_load_lds((const unsigned*)((const char*)(gbase) + vo_), (PG8_LAS unsigned*)(lds + (bufoff) + ldsw + _i * 8192), 16, 0, 0); } } while (0)
; #define PG8_LDA(dst, b, h) do { _Pragma("unroll") for (int m = 0; m < 4; ++m) _Pragma("unroll") for (int k = 0; k < 2; ++k) dst[m][k] = *(const PG8_LAS bf16x8*)(lds + PG8_SA(b, h) + aoff + m * 2048 + k * 1024); } while (0)
; #define PG8_MMA(ai, bj, At, Bt) do { __builtin_amdgcn_s_setprio(1); _Pragma("unroll") for (int m = 0; m < 4; ++m) _Pragma("unroll") for (int n = 0; n < 2; ++n) _Pragma("unroll") for (int k = 0; k < 2; ++k) \
;         acc[ai][bj][m][n] = __builtin_amdgcn_mfma_f32_16x16x32_bf16(Bt[n][k], At[m][k], acc[ai][bj][m][n], 0, 0, 0); __builtin_amdgcn_s_setprio(0); } while (0)
; #define PG8_WAIT_V(n) asm volatile("s_waitcnt vmcnt(" #n ")" ::: "memory")
; #define PG8_WAIT_L(n) asm volatile("s_waitcnt lgkmcnt(" #n ")" ::: "memory")
; #define PG8_BAR __builtin_amdgcn_s_barrier()
; #define PG8_SCHED __builtin_amdgcn_sched_barrier(0)
; template <class Epi, class Sched>
; __device__ __forceinline__ void gemm_phase(const int WID_, PG8_LAS unsigned char* lds, const Sched& S, const Epi& E) {
;     ...
;             PG8_LDA(At, 1, 1); PG8_STAGE(PG8_SB(1, 0), b3, voffB); PG8_STAGE(PG8_SB(1, 1), b3 + hstepB, voffB); PG8_STAGE_A(PG8_SA(1, 0), a3, 0, last);
;             PG8_WAIT_V(8); PG8_WAIT_L(0); PG8_BAR; PG8_MMA(1, 0, At, B0); PG8_MMA(1, 1, At, B1); PG8_BAR; PG8_SCHED;
;         }
;         if (wr == 0) PG8_BAR;
	s_add_i32 s10, s36, s33
	v_lshl_add_u64 v[208:209], v[208:209], 0, s[16:17]
	s_mov_b32 m0, s10
	ds_read_b128 v[176:179], v151 offset:49152
	ds_read_b128 v[180:183], v151 offset:50176
	ds_read_b128 v[184:187], v151 offset:51200
	ds_read_b128 v[188:191], v151 offset:52224
	ds_read_b128 v[192:195], v151 offset:53248
	ds_read_b128 v[196:199], v151 offset:54272
	ds_read_b128 v[200:203], v151 offset:55296
	ds_read_b128 v[204:207], v151 offset:56320
	global_load_lds_dwordx4 v[208:209], off
	s_add_i32 m0, s10, 0x2000
	s_add_u32 s8, s8, 0x20080
	v_lshl_add_u64 v[208:209], v[210:211], 0, s[16:17]
	s_addc_u32 s9, s9, 0
	s_add_i32 s10, s37, s33
	global_load_lds_dwordx4 v[208:209], off
	v_lshl_add_u64 v[208:209], s[8:9], 0, v[128:129]
	s_mov_b32 m0, s10
	s_nop 0
	global_load_lds_dwordx4 v[208:209], off
	v_lshl_add_u64 v[208:209], s[8:9], 0, v[130:131]
	s_add_i32 m0, s10, 0x2000
	s_nop 0
	global_load_lds_dwordx4 v[208:209], off
	v_lshl_add_u64 v[208:209], v[212:213], 0, s[16:17]
	s_mov_b32 m0, s43
	s_nop 0
	global_load_lds_dwordx4 v[208:209], off
	v_lshl_add_u64 v[208:209], v[214:215], 0, s[16:17]
	s_mov_b32 m0, s44
	s_nop 0
	global_load_lds_dwordx4 v[208:209], off
	s_waitcnt vmcnt(8)
	s_waitcnt lgkmcnt(0)
	s_barrier
	s_waitcnt lgkmcnt(0)
	v_mfma_f32_16x16x32_bf16 v[60:63], v[138:141], v[176:179], v[60:63]
	v_mfma_f32_16x16x32_bf16 v[56:59], v[152:155], v[176:179], v[56:59]
	v_mfma_f32_16x16x32_bf16 v[44:47], v[138:141], v[184:187], v[44:47]
	v_mfma_f32_16x16x32_bf16 v[40:43], v[152:155], v[184:187], v[40:43]
	v_mfma_f32_16x16x32_bf16 v[28:31], v[138:141], v[192:195], v[28:31]
	v_mfma_f32_16x16x32_bf16 v[24:27], v[152:155], v[192:195], v[24:27]
	v_mfma_f32_16x16x32_bf16 v[12:15], v[138:141], v[200:203], v[12:15]
	v_mfma_f32_16x16x32_bf16 v[8:11], v[152:155], v[200:203], v[8:11]
	v_mfma_f32_16x16x32_bf16 v[60:63], v[142:145], v[180:183], v[60:63]
	v_mfma_f32_16x16x32_bf16 v[56:59], v[156:159], v[180:183], v[56:59]
	v_mfma_f32_16x16x32_bf16 v[44:47], v[142:145], v[188:191], v[44:47]
	v_mfma_f32_16x16x32_bf16 v[40:43], v[156:159], v[188:191], v[40:43]
	v_mfma_f32_16x16x32_bf16 v[28:31], v[142:145], v[196:199], v[28:31]
	v_mfma_f32_16x16x32_bf16 v[24:27], v[156:159], v[196:199], v[24:27]
	v_mfma_f32_16x16x32_bf16 v[12:15], v[142:145], v[204:207], v[12:15]
	v_mfma_f32_16x16x32_bf16 v[8:11], v[156:159], v[204:207], v[8:11]
	v_mfma_f32_16x16x32_bf16 v[52:55], v[160:163], v[176:179], v[52:55]
	v_mfma_f32_16x16x32_bf16 v[48:51], v[168:171], v[176:179], v[48:51]
	v_mfma_f32_16x16x32_bf16 v[36:39], v[160:163], v[184:187], v[36:39]
	v_mfma_f32_16x16x32_bf16 v[32:35], v[168:171], v[184:187], v[32:35]
	v_mfma_f32_16x16x32_bf16 v[20:23], v[160:163], v[192:195], v[20:23]
	v_mfma_f32_16x16x32_bf16 v[16:19], v[168:171], v[192:195], v[16:19]
	v_mfma_f32_16x16x32_bf16 v[4:7], v[160:163], v[200:203], v[4:7]
	v_mfma_f32_16x16x32_bf16 v[0:3], v[168:171], v[200:203], v[0:3]
	v_mfma_f32_16x16x32_bf16 v[52:55], v[164:167], v[180:183], v[52:55]
	v_mfma_f32_16x16x32_bf16 v[48:51], v[172:175], v[180:183], v[48:51]
	v_mfma_f32_16x16x32_bf16 v[36:39], v[164:167], v[188:191], v[36:39]
	v_mfma_f32_16x16x32_bf16 v[32:35], v[172:175], v[188:191], v[32:35]
	v_mfma_f32_16x16x32_bf16 v[20:23], v[164:167], v[196:199], v[20:23]
	v_mfma_f32_16x16x32_bf16 v[16:19], v[172:175], v[196:199], v[16:19]
	v_mfma_f32_16x16x32_bf16 v[4:7], v[164:167], v[204:207], v[4:7]
	v_mfma_f32_16x16x32_bf16 v[0:3], v[172:175], v[204:207], v[0:3]
	s_barrier
	s_add_i32 s35, s35, 2
	s_add_u32 s6, s6, 0x100
	s_addc_u32 s7, s7, 0
	s_add_u32 s5, s5, 0x100
	s_addc_u32 s21, s21, 0
	s_cmp_gt_u32 s35, 5
	s_cbranch_scc0 .LBB0_263
	s_and_b64 vcc, exec, s[18:19]
	s_cbranch_vccz .LBB0_266
	s_barrier

; #define PG8_STAGE(bufoff, gbase, voff) do { _Pragma("unroll") for (int _i = 0; _i < 2; ++_i) \
;         __builtin_amdgcn_global_load_lds((const unsigned*)((const char*)(gbase) + (voff)[_i]), (PG8_LAS unsigned*)(lds + (bufoff) + ldsw + _i * 8192), 16, 0, 0); } while (0)
; #define PG8_STAGE_A(bufoff, gbase, h, nx) do { _Pragma("unroll") for (int _i = 0; _i < 2; ++_i) { \
;         const unsigned vo_ = GA ? ((nx) ? vgn[h][_i] : vgc[h][_i]) : voffA[_i]; \
;         __builtin_amdgcn_global_load_lds((const unsigned*)((const char*)(gbase) + vo_), (PG8_LAS unsigned*)(lds + (bufoff) + ldsw + _i * 8192), 16, 0, 0); } } while (0)
; #define PG8_LDA(dst, b, h) do { _Pragma("unroll") for (int m = 0; m < 4; ++m) _Pragma("unroll") for (int k = 0; k < 2; ++k) dst[m][k] = *(const PG8_LAS bf16x8*)(lds + PG8_SA(b, h) + aoff + m * 2048 + k * 1024); } while (0)
; #define PG8_LDB(dst, b, h) do { _Pragma("unroll") for (int n = 0; n < 2; ++n) _Pragma("unroll") for (int k = 0; k < 2; ++k) dst[n][k] = *(const PG8_LAS bf16x8*)(lds + PG8_SB(b, h) + boff + n * 2048 + k * 1024); } while (0)
; #define PG8_WAIT_V(n) asm volatile("s_waitcnt vmcnt(" #n ")" ::: "memory")
; #define PG8_WAIT_L(n) asm volatile("s_waitcnt lgkmcnt(" #n ")" ::: "memory")
; #define PG8_BAR __builtin_amdgcn_s_barrier()
; #define PG8_SCHED __builtin_amdgcn_sched_barrier(0)
; template <class Epi, class Sched>
; __device__ __forceinline__ void gemm_phase(const int WID_, PG8_LAS unsigned char* lds, const Sched& S, const Epi& E) {
;     ...
;         for (int t = 0; t < nt; t += 2) {
;             const bool last = (t == nt - 2);
;             const char* a1 = cA + (size_t)(t + 1) * kstep;
;             const char* a2 = last ? nA : cA + (size_t)(t + 2) * kstep; const char* b2 = last ? nB : cB + (size_t)(t + 2) * kstep;
;             const char* a3 = a2 + kstep; const char* b3 = b2 + kstep;
;             PG8_LDB(B0, 0, 0); PG8_LDB(B1, 0, 1); PG8_SCHED; PG8_LDA(At, 0, 0); PG8_STAGE_A(PG8_SA(1, 1), a1 + hstepA, 1, false);
;             PG8_WAIT_V(8); PG8_WAIT_L(0); PG8_BAR; PG8_MMA(0, 0, At, B0); PG8_MMA(0, 1, At, B1); PG8_BAR; PG8_SCHED;
;             PG8_LDA(At, 0, 1); PG8_STAGE(PG8_SB(0, 0), b2, voffB); PG8_STAGE(PG8_SB(0, 1), b2 + hstepB, voffB); PG8_STAGE_A(PG8_SA(0, 0), a2, 0, last);
;             PG8_WAIT_V(8); PG8_WAIT_L(0); PG8_BAR; PG8_MMA(1, 0, At, B0); PG8_MMA(1, 1, At, B1); PG8_BAR; PG8_SCHED;
.LBB0_568:
	s_add_i32 s62, s2, 2
	s_add_u32 s3, s0, 0xffff0080
	s_addc_u32 s4, s1, -1
	s_add_i32 s63, 0, 0x10000
	s_cmp_eq_u32 s11, s2
	s_cselect_b32 s5, s53, s4
	s_cselect_b32 s4, s52, s3
	v_add_u32_e32 v136, s63, v153
	s_cselect_b32 s3, s61, s51
	s_cselect_b32 s2, s60, s49
	s_add_i32 s69, 0, 0x14000
	ds_read_b128 v[80:83], v136
	ds_read_b128 v[88:91], v136 offset:1024
	ds_read_b128 v[156:159], v136 offset:2048
	ds_read_b128 v[160:163], v136 offset:3072
	v_add_u32_e32 v136, s69, v153
	ds_read_b128 v[164:167], v136
	ds_read_b128 v[168:171], v136 offset:1024
	ds_read_b128 v[172:175], v136 offset:2048
	ds_read_b128 v[176:179], v136 offset:3072
	v_lshl_add_u64 v[212:213], s[0:1], 0, v[146:147]
	s_add_i32 m0, s37, 0xc000
	ds_read_b128 v[180:183], v155
	ds_read_b128 v[184:187], v155 offset:1024
	ds_read_b128 v[188:191], v155 offset:2048
	ds_read_b128 v[192:195], v155 offset:3072
	ds_read_b128 v[196:199], v155 offset:4096
	ds_read_b128 v[200:203], v155 offset:5120
	ds_read_b128 v[204:207], v155 offset:6144
	ds_read_b128 v[208:211], v155 offset:7168
	global_load_lds_dwordx4 v[212:213], off
	v_lshl_add_u64 v[212:213], s[0:1], 0, v[148:149]
	s_add_i32 m0, s37, 0xe000
	s_nop 0
	global_load_lds_dwordx4 v[212:213], off
	s_waitcnt vmcnt(8)
	s_waitcnt lgkmcnt(0)
	s_barrier
	s_waitcnt lgkmcnt(0)
	v_mfma_f32_16x16x32_bf16 v[132:135], v[80:83], v[180:183], v[132:135]
	v_mfma_f32_16x16x32_bf16 v[128:131], v[156:159], v[180:183], v[128:131]
	v_mfma_f32_16x16x32_bf16 v[124:127], v[80:83], v[188:191], v[124:127]
	v_mfma_f32_16x16x32_bf16 v[120:123], v[156:159], v[188:191], v[120:123]
	v_mfma_f32_16x16x32_bf16 v[116:119], v[80:83], v[196:199], v[116:119]
	v_mfma_f32_16x16x32_bf16 v[112:115], v[156:159], v[196:199], v[112:115]
	v_mfma_f32_16x16x32_bf16 v[108:111], v[80:83], v[204:207], v[108:111]
	v_mfma_f32_16x16x32_bf16 v[104:107], v[156:159], v[204:207], v[104:107]
	v_mfma_f32_16x16x32_bf16 v[132:135], v[88:91], v[184:187], v[132:135]
	v_mfma_f32_16x16x32_bf16 v[128:131], v[160:163], v[184:187], v[128:131]
	v_mfma_f32_16x16x32_bf16 v[124:127], v[88:91], v[192:195], v[124:127]
	v_mfma_f32_16x16x32_bf16 v[120:123], v[160:163], v[192:195], v[120:123]
	v_mfma_f32_16x16x32_bf16 v[116:119], v[88:91], v[200:203], v[116:119]
	v_mfma_f32_16x16x32_bf16 v[112:115], v[160:163], v[200:203], v[112:115]
	v_mfma_f32_16x16x32_bf16 v[108:111], v[88:91], v[208:211], v[108:111]
	v_mfma_f32_16x16x32_bf16 v[104:107], v[160:163], v[208:211], v[104:107]
	v_mfma_f32_16x16x32_bf16 v[60:63], v[164:167], v[180:183], v[60:63]
	v_mfma_f32_16x16x32_bf16 v[56:59], v[172:175], v[180:183], v[56:59]
	v_mfma_f32_16x16x32_bf16 v[52:55], v[164:167], v[188:191], v[52:55]
	v_mfma_f32_16x16x32_bf16 v[48:51], v[172:175], v[188:191], v[48:51]
	v_mfma_f32_16x16x32_bf16 v[44:47], v[164:167], v[196:199], v[44:47]
	v_mfma_f32_16x16x32_bf16 v[40:43], v[172:175], v[196:199], v[40:43]
	v_mfma_f32_16x16x32_bf16 v[36:39], v[164:167], v[204:207], v[36:39]
	v_mfma_f32_16x16x32_bf16 v[32:35], v[172:175], v[204:207], v[32:35]
	v_mfma_f32_16x16x32_bf16 v[60:63], v[168:171], v[184:187], v[60:63]
	v_mfma_f32_16x16x32_bf16 v[56:59], v[176:179], v[184:187], v[56:59]
	v_mfma_f32_16x16x32_bf16 v[52:55], v[168:171], v[192:195], v[52:55]
	v_mfma_f32_16x16x32_bf16 v[48:51], v[176:179], v[192:195], v[48:51]
	v_mfma_f32_16x16x32_bf16 v[44:47], v[168:171], v[200:203], v[44:47]
	v_mfma_f32_16x16x32_bf16 v[40:43], v[176:179], v[200:203], v[40:43]
	v_mfma_f32_16x16x32_bf16 v[36:39], v[168:171], v[208:211], v[36:39]
	v_mfma_f32_16x16x32_bf16 v[32:35], v[176:179], v[208:211], v[32:35]
	s_barrier
	s_add_i32 s63, s63, s35
	v_lshl_add_u64 v[212:213], s[2:3], 0, v[140:141]
	s_mov_b32 m0, s63
	ds_read_b128 v[180:183], v155 offset:16384
	ds_read_b128 v[184:187], v155 offset:17408
	ds_read_b128 v[188:191], v155 offset:18432
	ds_read_b128 v[192:195], v155 offset:19456
	ds_read_b128 v[196:199], v155 offset:20480
	ds_read_b128 v[200:203], v155 offset:21504
	ds_read_b128 v[204:207], v155 offset:22528
	ds_read_b128 v[208:211], v155 offset:23552
	global_load_lds_dwordx4 v[212:213], off
	s_add_i32 m0, s63, 0x2000
	s_add_u32 s76, s2, 0x10000
	v_lshl_add_u64 v[214:215], s[2:3], 0, v[144:145]
	s_addc_u32 s77, s3, 0
	s_add_i32 s63, s69, s35
	global_load_lds_dwordx4 v[214:215], off
	v_lshl_add_u64 v[216:217], s[76:77], 0, v[140:141]
	s_mov_b32 m0, s63
	v_lshl_add_u64 v[218:219], s[4:5], 0, v[142:143]
	global_load_lds_dwordx4 v[216:217], off
	v_lshl_add_u64 v[216:217], s[76:77], 0, v[144:145]
	s_add_i32 m0, s63, 0x2000
	s_nop 0
	global_load_lds_dwordx4 v[216:217], off
	v_lshl_add_u64 v[216:217], s[4:5], 0, v[138:139]
	s_mov_b32 m0, s37
	s_nop 0
	global_load_lds_dwordx4 v[216:217], off
	s_mov_b32 m0, s39
	s_nop 0
	global_load_lds_dwordx4 v[218:219], off
	s_waitcnt vmcnt(8)
	s_waitcnt lgkmcnt(0)
	s_barrier
; #define PG8_STAGE_A(bufoff, gbase, h, nx) do { _Pragma("unroll") for (int _i = 0; _i < 2; ++_i) { \
;         const unsigned vo_ = GA ? ((nx) ? vgn[h][_i] : vgc[h][_i]) : voffA[_i]; \
;         __builtin_amdgcn_global_load_lds((const unsigned*)((const char*)(gbase) + vo_), (PG8_LAS unsigned*)(lds + (bufoff) + ldsw + _i * 8192), 16, 0, 0); } } while (0)
; #define PG8_LDA(dst, b, h) do { _Pragma("unroll") for (int m = 0; m < 4; ++m) _Pragma("unroll") for (int k = 0; k < 2; ++k) dst[m][k] = *(const PG8_LAS bf16x8*)(lds + PG8_SA(b, h) + aoff + m * 2048 + k * 1024); } while (0)
; #define PG8_LDB(dst, b, h) do { _Pragma("unroll") for (int n = 0; n < 2; ++n) _Pragma("unroll") for (int k = 0; k < 2; ++k) dst[n][k] = *(const PG8_LAS bf16x8*)(lds + PG8_SB(b, h) + boff + n * 2048 + k * 1024); } while (0)
; #define PG8_MMA(ai, bj, At, Bt) do { __builtin_amdgcn_s_setprio(1); _Pragma("unroll") for (int m = 0; m < 4; ++m) _Pragma("unroll") for (int n = 0; n < 2; ++n) _Pragma("unroll") for (int k = 0; k < 2; ++k) \
;         acc[ai][bj][m][n] = __builtin_amdgcn_mfma_f32_16x16x32_bf16(Bt[n][k], At[m][k], acc[ai][bj][m][n], 0, 0, 0); __builtin_amdgcn_s_setprio(0); } while (0)
; #define PG8_WAIT_V(n) asm volatile("s_waitcnt vmcnt(" #n ")" ::: "memory")
; #define PG8_WAIT_L(n) asm volatile("s_waitcnt lgkmcnt(" #n ")" ::: "memory")
; #define PG8_BAR __builtin_amdgcn_s_barrier()
; #define PG8_SCHED __builtin_amdgcn_sched_barrier(0)
; template <class Epi, class Sched>
; __device__ __forceinline__ void gemm_phase(const int WID_, PG8_LAS unsigned char* lds, const Sched& S, const Epi& E) {
;     ...
;             PG8_WAIT_V(8); PG8_WAIT_L(0); PG8_BAR; PG8_MMA(1, 0, At, B0); PG8_MMA(1, 1, At, B1); PG8_BAR; PG8_SCHED;
;             PG8_LDB(B0, 1, 0); PG8_LDB(B1, 1, 1); PG8_SCHED; PG8_LDA(At, 1, 0); PG8_STAGE_A(PG8_SA(0, 1), a2 + hstepA, 1, last);
;             PG8_WAIT_V(8); PG8_WAIT_L(0); PG8_BAR; PG8_MMA(0, 0, At, B0); PG8_MMA(0, 1, At, B1); PG8_BAR; PG8_SCHED;
	s_waitcnt lgkmcnt(0)
	v_mfma_f32_16x16x32_bf16 v[100:103], v[80:83], v[180:183], v[100:103]
	v_mfma_f32_16x16x32_bf16 v[96:99], v[156:159], v[180:183], v[96:99]
	v_mfma_f32_16x16x32_bf16 v[92:95], v[80:83], v[188:191], v[92:95]
	v_mfma_f32_16x16x32_bf16 v[84:87], v[156:159], v[188:191], v[84:87]
	v_mfma_f32_16x16x32_bf16 v[76:79], v[80:83], v[196:199], v[76:79]
	v_mfma_f32_16x16x32_bf16 v[72:75], v[156:159], v[196:199], v[72:75]
	v_mfma_f32_16x16x32_bf16 v[68:71], v[80:83], v[204:207], v[68:71]
	v_mfma_f32_16x16x32_bf16 v[64:67], v[156:159], v[204:207], v[64:67]
	v_mfma_f32_16x16x32_bf16 v[100:103], v[88:91], v[184:187], v[100:103]
	v_mfma_f32_16x16x32_bf16 v[96:99], v[160:163], v[184:187], v[96:99]
	v_mfma_f32_16x16x32_bf16 v[92:95], v[88:91], v[192:195], v[92:95]
	v_mfma_f32_16x16x32_bf16 v[84:87], v[160:163], v[192:195], v[84:87]
	v_mfma_f32_16x16x32_bf16 v[76:79], v[88:91], v[200:203], v[76:79]
	v_mfma_f32_16x16x32_bf16 v[72:75], v[160:163], v[200:203], v[72:75]
	v_mfma_f32_16x16x32_bf16 v[68:71], v[88:91], v[208:211], v[68:71]
	v_mfma_f32_16x16x32_bf16 v[64:67], v[160:163], v[208:211], v[64:67]
	v_mfma_f32_16x16x32_bf16 v[28:31], v[164:167], v[180:183], v[28:31]
	v_mfma_f32_16x16x32_bf16 v[24:27], v[172:175], v[180:183], v[24:27]
	v_mfma_f32_16x16x32_bf16 v[20:23], v[164:167], v[188:191], v[20:23]
	v_mfma_f32_16x16x32_bf16 v[16:19], v[172:175], v[188:191], v[16:19]
	v_mfma_f32_16x16x32_bf16 v[12:15], v[164:167], v[196:199], v[12:15]
	v_mfma_f32_16x16x32_bf16 v[8:11], v[172:175], v[196:199], v[8:11]
	v_mfma_f32_16x16x32_bf16 v[4:7], v[164:167], v[204:207], v[4:7]
	v_mfma_f32_16x16x32_bf16 v[0:3], v[172:175], v[204:207], v[0:3]
	v_mfma_f32_16x16x32_bf16 v[28:31], v[168:171], v[184:187], v[28:31]
	v_mfma_f32_16x16x32_bf16 v[24:27], v[176:179], v[184:187], v[24:27]
	v_mfma_f32_16x16x32_bf16 v[20:23], v[168:171], v[192:195], v[20:23]
	v_mfma_f32_16x16x32_bf16 v[16:19], v[176:179], v[192:195], v[16:19]
	v_mfma_f32_16x16x32_bf16 v[12:15], v[168:171], v[200:203], v[12:15]
	v_mfma_f32_16x16x32_bf16 v[8:11], v[176:179], v[200:203], v[8:11]
	v_mfma_f32_16x16x32_bf16 v[4:7], v[168:171], v[208:211], v[4:7]
	v_mfma_f32_16x16x32_bf16 v[0:3], v[176:179], v[208:211], v[0:3]
	s_barrier
	s_add_i32 s63, 0, 0x18000
	v_add_u32_e32 v136, s63, v153
	s_add_i32 s69, 0, 0x1c000
	ds_read_b128 v[80:83], v136
	ds_read_b128 v[88:91], v136 offset:1024
	ds_read_b128 v[156:159], v136 offset:2048
	ds_read_b128 v[160:163], v136 offset:3072
	v_add_u32_e32 v136, s69, v153
	ds_read_b128 v[164:167], v136
	ds_read_b128 v[168:171], v136 offset:1024
	ds_read_b128 v[172:175], v136 offset:2048
	ds_read_b128 v[176:179], v136 offset:3072
	s_add_u32 s4, s4, 0x10000
	s_addc_u32 s5, s5, 0
	s_mov_b32 m0, s41
	v_lshl_add_u64 v[220:221], s[4:5], 0, v[138:139]
	ds_read_b128 v[180:183], v155 offset:32768
	ds_read_b128 v[184:187], v155 offset:33792
	ds_read_b128 v[188:191], v155 offset:34816
	ds_read_b128 v[192:195], v155 offset:35840
	ds_read_b128 v[196:199], v155 offset:36864
	ds_read_b128 v[200:203], v155 offset:37888
	ds_read_b128 v[204:207], v155 offset:38912
	ds_read_b128 v[208:211], v155 offset:39936
	global_load_lds_dwordx4 v[220:221], off
	v_lshl_add_u64 v[220:221], s[4:5], 0, v[142:143]
	s_mov_b32 m0, s84
	s_nop 0
	global_load_lds_dwordx4 v[220:221], off
	s_waitcnt vmcnt(8)
	s_waitcnt lgkmcnt(0)
	s_barrier
	s_waitcnt lgkmcnt(0)
	v_mfma_f32_16x16x32_bf16 v[132:135], v[80:83], v[180:183], v[132:135]
	v_mfma_f32_16x16x32_bf16 v[128:131], v[156:159], v[180:183], v[128:131]
	v_mfma_f32_16x16x32_bf16 v[124:127], v[80:83], v[188:191], v[124:127]
	v_mfma_f32_16x16x32_bf16 v[120:123], v[156:159], v[188:191], v[120:123]
	v_mfma_f32_16x16x32_bf16 v[116:119], v[80:83], v[196:199], v[116:119]
	v_mfma_f32_16x16x32_bf16 v[112:115], v[156:159], v[196:199], v[112:115]
	v_mfma_f32_16x16x32_bf16 v[108:111], v[80:83], v[204:207], v[108:111]
	v_mfma_f32_16x16x32_bf16 v[104:107], v[156:159], v[204:207], v[104:107]
	v_mfma_f32_16x16x32_bf16 v[132:135], v[88:91], v[184:187], v[132:135]
	v_mfma_f32_16x16x32_bf16 v[128:131], v[160:163], v[184:187], v[128:131]
	v_mfma_f32_16x16x32_bf16 v[124:127], v[88:91], v[192:195], v[124:127]
	v_mfma_f32_16x16x32_bf16 v[120:123], v[160:163], v[192:195], v[120:123]
	v_mfma_f32_16x16x32_bf16 v[116:119], v[88:91], v[200:203], v[116:119]
	v_mfma_f32_16x16x32_bf16 v[112:115], v[160:163], v[200:203], v[112:115]
	v_mfma_f32_16x16x32_bf16 v[108:111], v[88:91], v[208:211], v[108:111]
	v_mfma_f32_16x16x32_bf16 v[104:107], v[160:163], v[208:211], v[104:107]
	v_mfma_f32_16x16x32_bf16 v[60:63], v[164:167], v[180:183], v[60:63]
	v_mfma_f32_16x16x32_bf16 v[56:59], v[172:175], v[180:183], v[56:59]
	v_mfma_f32_16x16x32_bf16 v[52:55], v[164:167], v[188:191], v[52:55]
	v_mfma_f32_16x16x32_bf16 v[48:51], v[172:175], v[188:191], v[48:51]
	v_mfma_f32_16x16x32_bf16 v[44:47], v[164:167], v[196:199], v[44:47]
	v_mfma_f32_16x16x32_bf16 v[40:43], v[172:175], v[196:199], v[40:43]
	v_mfma_f32_16x16x32_bf16 v[36:39], v[164:167], v[204:207], v[36:39]
	v_mfma_f32_16x16x32_bf16 v[32:35], v[172:175], v[204:207], v[32:35]
	v_mfma_f32_16x16x32_bf16 v[60:63], v[168:171], v[184:187], v[60:63]
	v_mfma_f32_16x16x32_bf16 v[56:59], v[176:179], v[184:187], v[56:59]
	v_mfma_f32_16x16x32_bf16 v[52:55], v[168:171], v[192:195], v[52:55]
	v_mfma_f32_16x16x32_bf16 v[48:51], v[176:179], v[192:195], v[48:51]
	v_mfma_f32_16x16x32_bf16 v[44:47], v[168:171], v[200:203], v[44:47]
	v_mfma_f32_16x16x32_bf16 v[40:43], v[176:179], v[200:203], v[40:43]
	v_mfma_f32_16x16x32_bf16 v[36:39], v[168:171], v[208:211], v[36:39]
	v_mfma_f32_16x16x32_bf16 v[32:35], v[176:179], v[208:211], v[32:35]
	s_barrier
; #define PG8_STAGE(bufoff, gbase, voff) do { _Pragma("unroll") for (int _i = 0; _i < 2; ++_i) \
;         __builtin_amdgcn_global_load_lds((const unsigned*)((const char*)(gbase) + (voff)[_i]), (PG8_LAS unsigned*)(lds + (bufoff) + ldsw + _i * 8192), 16, 0, 0); } while (0)
; #define PG8_STAGE_A(bufoff, gbase, h, nx) do { _Pragma("unroll") for (int _i = 0; _i < 2; ++_i) { \
;         const unsigned vo_ = GA ? ((nx) ? vgn[h][_i] : vgc[h][_i]) : voffA[_i]; \
;         __builtin_amdgcn_global_load_lds((const unsigned*)((const char*)(gbase) + vo_), (PG8_LAS unsigned*)(lds + (bufoff) + ldsw + _i * 8192), 16, 0, 0); } } while (0)
; #define PG8_LDA(dst, b, h) do { _Pragma("unroll") for (int m = 0; m < 4; ++m) _Pragma("unroll") for (int k = 0; k < 2; ++k) dst[m][k] = *(const PG8_LAS bf16x8*)(lds + PG8_SA(b, h) + aoff + m * 2048 + k * 1024); } while (0)
; #define PG8_MMA(ai, bj, At, Bt) do { __builtin_amdgcn_s_setprio(1); _Pragma("unroll") for (int m = 0; m < 4; ++m) _Pragma("unroll") for (int n = 0; n < 2; ++n) _Pragma("unroll") for (int k = 0; k < 2; ++k) \
;         acc[ai][bj][m][n] = __builtin_amdgcn_mfma_f32_16x16x32_bf16(Bt[n][k], At[m][k], acc[ai][bj][m][n], 0, 0, 0); __builtin_amdgcn_s_setprio(0); } while (0)
; #define PG8_WAIT_V(n) asm volatile("s_waitcnt vmcnt(" #n ")" ::: "memory")
; #define PG8_WAIT_L(n) asm volatile("s_waitcnt lgkmcnt(" #n ")" ::: "memory")
; #define PG8_BAR __builtin_amdgcn_s_barrier()
; #define PG8_SCHED __builtin_amdgcn_sched_barrier(0)
; template <class Epi, class Sched>
; __device__ __forceinline__ void gemm_phase(const int WID_, PG8_LAS unsigned char* lds, const Sched& S, const Epi& E) {
;     ...
;             PG8_LDA(At, 1, 1); PG8_STAGE(PG8_SB(1, 0), b3, voffB); PG8_STAGE(PG8_SB(1, 1), b3 + hstepB, voffB); PG8_STAGE_A(PG8_SA(1, 0), a3, 0, last);
;             PG8_WAIT_V(8); PG8_WAIT_L(0); PG8_BAR; PG8_MMA(1, 0, At, B0); PG8_MMA(1, 1, At, B1); PG8_BAR; PG8_SCHED;
;         }
	s_add_i32 s4, s63, s35
	v_lshl_add_u64 v[212:213], v[212:213], 0, s[42:43]
	s_mov_b32 m0, s4
	ds_read_b128 v[180:183], v155 offset:49152
	ds_read_b128 v[184:187], v155 offset:50176
	ds_read_b128 v[188:191], v155 offset:51200
	ds_read_b128 v[192:195], v155 offset:52224
	ds_read_b128 v[196:199], v155 offset:53248
	ds_read_b128 v[200:203], v155 offset:54272
	ds_read_b128 v[204:207], v155 offset:55296
	ds_read_b128 v[208:211], v155 offset:56320
	global_load_lds_dwordx4 v[212:213], off
	s_add_i32 m0, s4, 0x2000
	s_add_u32 s2, s2, 0x10080
	v_lshl_add_u64 v[212:213], v[214:215], 0, s[42:43]
	s_addc_u32 s3, s3, 0
	s_add_i32 s4, s69, s35
	global_load_lds_dwordx4 v[212:213], off
	v_lshl_add_u64 v[212:213], s[2:3], 0, v[140:141]
	s_mov_b32 m0, s4
	s_nop 0
	global_load_lds_dwordx4 v[212:213], off
	v_lshl_add_u64 v[212:213], s[2:3], 0, v[144:145]
	s_add_i32 m0, s4, 0x2000
	s_nop 0
	global_load_lds_dwordx4 v[212:213], off
	v_lshl_add_u64 v[212:213], v[216:217], 0, s[42:43]
	s_mov_b32 m0, s6
	s_nop 0
	global_load_lds_dwordx4 v[212:213], off
	v_lshl_add_u64 v[212:213], v[218:219], 0, s[42:43]
	s_mov_b32 m0, s10
	s_nop 0
	global_load_lds_dwordx4 v[212:213], off
	s_waitcnt vmcnt(8)
	s_waitcnt lgkmcnt(0)
	s_barrier
	s_waitcnt lgkmcnt(0)
	v_mfma_f32_16x16x32_bf16 v[100:103], v[80:83], v[180:183], v[100:103]
	v_mfma_f32_16x16x32_bf16 v[96:99], v[156:159], v[180:183], v[96:99]
	v_mfma_f32_16x16x32_bf16 v[92:95], v[80:83], v[188:191], v[92:95]
	v_mfma_f32_16x16x32_bf16 v[84:87], v[156:159], v[188:191], v[84:87]
	v_mfma_f32_16x16x32_bf16 v[76:79], v[80:83], v[196:199], v[76:79]
	v_mfma_f32_16x16x32_bf16 v[72:75], v[156:159], v[196:199], v[72:75]
	v_mfma_f32_16x16x32_bf16 v[68:71], v[80:83], v[204:207], v[68:71]
	v_mfma_f32_16x16x32_bf16 v[64:67], v[156:159], v[204:207], v[64:67]
	v_mfma_f32_16x16x32_bf16 v[100:103], v[88:91], v[184:187], v[100:103]
	v_mfma_f32_16x16x32_bf16 v[96:99], v[160:163], v[184:187], v[96:99]
	v_mfma_f32_16x16x32_bf16 v[92:95], v[88:91], v[192:195], v[92:95]
	v_mfma_f32_16x16x32_bf16 v[84:87], v[160:163], v[192:195], v[84:87]
	v_mfma_f32_16x16x32_bf16 v[76:79], v[88:91], v[200:203], v[76:79]
	v_mfma_f32_16x16x32_bf16 v[72:75], v[160:163], v[200:203], v[72:75]
	v_mfma_f32_16x16x32_bf16 v[68:71], v[88:91], v[208:211], v[68:71]
	v_mfma_f32_16x16x32_bf16 v[64:67], v[160:163], v[208:211], v[64:67]
	v_mfma_f32_16x16x32_bf16 v[28:31], v[164:167], v[180:183], v[28:31]
	v_mfma_f32_16x16x32_bf16 v[24:27], v[172:175], v[180:183], v[24:27]
	v_mfma_f32_16x16x32_bf16 v[20:23], v[164:167], v[188:191], v[20:23]
	v_mfma_f32_16x16x32_bf16 v[16:19], v[172:175], v[188:191], v[16:19]
	v_mfma_f32_16x16x32_bf16 v[12:15], v[164:167], v[196:199], v[12:15]
	v_mfma_f32_16x16x32_bf16 v[8:11], v[172:175], v[196:199], v[8:11]
	v_mfma_f32_16x16x32_bf16 v[4:7], v[164:167], v[204:207], v[4:7]
	v_mfma_f32_16x16x32_bf16 v[0:3], v[172:175], v[204:207], v[0:3]
	v_mfma_f32_16x16x32_bf16 v[28:31], v[168:171], v[184:187], v[28:31]
	v_mfma_f32_16x16x32_bf16 v[24:27], v[176:179], v[184:187], v[24:27]
	v_mfma_f32_16x16x32_bf16 v[20:23], v[168:171], v[192:195], v[20:23]
	v_mfma_f32_16x16x32_bf16 v[16:19], v[176:179], v[192:195], v[16:19]
	v_mfma_f32_16x16x32_bf16 v[12:15], v[168:171], v[200:203], v[12:15]
	v_mfma_f32_16x16x32_bf16 v[8:11], v[176:179], v[200:203], v[8:11]
	v_mfma_f32_16x16x32_bf16 v[4:7], v[168:171], v[208:211], v[4:7]
	v_mfma_f32_16x16x32_bf16 v[0:3], v[176:179], v[208:211], v[0:3]
	s_barrier
	s_add_u32 s0, s0, 0x100
	s_addc_u32 s1, s1, 0
	s_add_u32 s49, s49, 0x100
	s_addc_u32 s51, s51, 0
	s_cmp_ge_i32 s62, s58
	s_mov_b32 s2, s62
	s_cbranch_scc0 .LBB0_568

; #define PG8_STAGE(bufoff, gbase, voff) do { _Pragma("unroll") for (int _i = 0; _i < 2; ++_i) \
;         __builtin_amdgcn_global_load_lds((const unsigned*)((const char*)(gbase) + (voff)[_i]), (PG8_LAS unsigned*)(lds + (bufoff) + ldsw + _i * 8192), 16, 0, 0); } while (0)
; #define PG8_STAGE_A(bufoff, gbase, h, nx) do { _Pragma("unroll") for (int _i = 0; _i < 2; ++_i) { \
;         const unsigned vo_ = GA ? ((nx) ? vgn[h][_i] : vgc[h][_i]) : voffA[_i]; \
;         __builtin_amdgcn_global_load_lds((const unsigned*)((const char*)(gbase) + vo_), (PG8_LAS unsigned*)(lds + (bufoff) + ldsw + _i * 8192), 16, 0, 0); } } while (0)
; #define PG8_LDA(dst, b, h) do { _Pragma("unroll") for (int m = 0; m < 4; ++m) _Pragma("unroll") for (int k = 0; k < 2; ++k) dst[m][k] = *(const PG8_LAS bf16x8*)(lds + PG8_SA(b, h) + aoff + m * 2048 + k * 1024); } while (0)
; #define PG8_LDB(dst, b, h) do { _Pragma("unroll") for (int n = 0; n < 2; ++n) _Pragma("unroll") for (int k = 0; k < 2; ++k) dst[n][k] = *(const PG8_LAS bf16x8*)(lds + PG8_SB(b, h) + boff + n * 2048 + k * 1024); } while (0)
; #define PG8_WAIT_V(n) asm volatile("s_waitcnt vmcnt(" #n ")" ::: "memory")
; #define PG8_WAIT_L(n) asm volatile("s_waitcnt lgkmcnt(" #n ")" ::: "memory")
; #define PG8_BAR __builtin_amdgcn_s_barrier()
; #define PG8_SCHED __builtin_amdgcn_sched_barrier(0)
; template <class Epi, class Sched>
; __device__ __forceinline__ void gemm_phase(const int WID_, PG8_LAS unsigned char* lds, const Sched& S, const Epi& E) {
;     ...
;         for (int t = 0; t < nt; t += 2) {
;             const bool last = (t == nt - 2);
;             const char* a1 = cA + (size_t)(t + 1) * kstep;
;             const char* a2 = last ? nA : cA + (size_t)(t + 2) * kstep; const char* b2 = last ? nB : cB + (size_t)(t + 2) * kstep;
;             const char* a3 = a2 + kstep; const char* b3 = b2 + kstep;
;             PG8_LDB(B0, 0, 0); PG8_LDB(B1, 0, 1); PG8_SCHED; PG8_LDA(At, 0, 0); PG8_STAGE_A(PG8_SA(1, 1), a1 + hstepA, 1, false);
;             PG8_WAIT_V(8); PG8_WAIT_L(0); PG8_BAR; PG8_MMA(0, 0, At, B0); PG8_MMA(0, 1, At, B1); PG8_BAR; PG8_SCHED;
;             PG8_LDA(At, 0, 1); PG8_STAGE(PG8_SB(0, 0), b2, voffB); PG8_STAGE(PG8_SB(0, 1), b2 + hstepB, voffB); PG8_STAGE_A(PG8_SA(0, 0), a2, 0, last);
;             PG8_WAIT_V(8); PG8_WAIT_L(0); PG8_BAR; PG8_MMA(1, 0, At, B0); PG8_MMA(1, 1, At, B1); PG8_BAR; PG8_SCHED;
.LBB0_1563:
	ds_read_b128 v[146:149], v143
	ds_read_b128 v[150:153], v143 offset:1024
	ds_read_b128 v[154:157], v143 offset:2048
	ds_read_b128 v[158:161], v143 offset:3072
	ds_read_b128 v[162:165], v144
	ds_read_b128 v[166:169], v144 offset:1024
	ds_read_b128 v[170:173], v144 offset:2048
	ds_read_b128 v[174:177], v144 offset:3072
	s_add_u32 s48, s46, 0xfffc0080
	s_addc_u32 s49, s47, -1
	s_cmp_eq_u32 s71, 12
	s_cselect_b32 s51, s37, s49
	s_cselect_b32 s50, s67, s48
	s_cselect_b32 s49, s39, s70
	s_cselect_b32 s48, s68, s69
	v_lshl_add_u64 v[210:211], s[46:47], 0, v[136:137]
	s_add_i32 m0, s52, 0xc000
	ds_read_b128 v[178:181], v145
	ds_read_b128 v[182:185], v145 offset:1024
	ds_read_b128 v[186:189], v145 offset:2048
	ds_read_b128 v[190:193], v145 offset:3072
	ds_read_b128 v[194:197], v145 offset:4096
	ds_read_b128 v[198:201], v145 offset:5120
	ds_read_b128 v[202:205], v145 offset:6144
	ds_read_b128 v[206:209], v145 offset:7168
	global_load_lds_dwordx4 v[210:211], off
	v_lshl_add_u64 v[210:211], s[46:47], 0, v[138:139]
	s_add_i32 m0, s52, 0xe000
	s_nop 0
	global_load_lds_dwordx4 v[210:211], off
	s_waitcnt vmcnt(8)
	s_waitcnt lgkmcnt(0)
	s_barrier
	s_waitcnt lgkmcnt(0)
	v_mfma_f32_16x16x32_bf16 v[124:127], v[146:149], v[178:181], v[124:127]
	v_mfma_f32_16x16x32_bf16 v[120:123], v[154:157], v[178:181], v[120:123]
	v_mfma_f32_16x16x32_bf16 v[116:119], v[146:149], v[186:189], v[116:119]
	v_mfma_f32_16x16x32_bf16 v[112:115], v[154:157], v[186:189], v[112:115]
	v_mfma_f32_16x16x32_bf16 v[100:103], v[146:149], v[194:197], v[100:103]
	v_mfma_f32_16x16x32_bf16 v[96:99], v[154:157], v[194:197], v[96:99]
	v_mfma_f32_16x16x32_bf16 v[84:87], v[146:149], v[202:205], v[84:87]
	v_mfma_f32_16x16x32_bf16 v[80:83], v[154:157], v[202:205], v[80:83]
	v_mfma_f32_16x16x32_bf16 v[124:127], v[150:153], v[182:185], v[124:127]
	v_mfma_f32_16x16x32_bf16 v[120:123], v[158:161], v[182:185], v[120:123]
	v_mfma_f32_16x16x32_bf16 v[116:119], v[150:153], v[190:193], v[116:119]
	v_mfma_f32_16x16x32_bf16 v[112:115], v[158:161], v[190:193], v[112:115]
	v_mfma_f32_16x16x32_bf16 v[100:103], v[150:153], v[198:201], v[100:103]
	v_mfma_f32_16x16x32_bf16 v[96:99], v[158:161], v[198:201], v[96:99]
	v_mfma_f32_16x16x32_bf16 v[84:87], v[150:153], v[206:209], v[84:87]
	v_mfma_f32_16x16x32_bf16 v[80:83], v[158:161], v[206:209], v[80:83]
	v_mfma_f32_16x16x32_bf16 v[108:111], v[162:165], v[178:181], v[108:111]
	v_mfma_f32_16x16x32_bf16 v[104:107], v[170:173], v[178:181], v[104:107]
	v_mfma_f32_16x16x32_bf16 v[92:95], v[162:165], v[186:189], v[92:95]
	v_mfma_f32_16x16x32_bf16 v[88:91], v[170:173], v[186:189], v[88:91]
	v_mfma_f32_16x16x32_bf16 v[76:79], v[162:165], v[194:197], v[76:79]
	v_mfma_f32_16x16x32_bf16 v[72:75], v[170:173], v[194:197], v[72:75]
	v_mfma_f32_16x16x32_bf16 v[68:71], v[162:165], v[202:205], v[68:71]
	v_mfma_f32_16x16x32_bf16 v[64:67], v[170:173], v[202:205], v[64:67]
	v_mfma_f32_16x16x32_bf16 v[108:111], v[166:169], v[182:185], v[108:111]
	v_mfma_f32_16x16x32_bf16 v[104:107], v[174:177], v[182:185], v[104:107]
	v_mfma_f32_16x16x32_bf16 v[92:95], v[166:169], v[190:193], v[92:95]
	v_mfma_f32_16x16x32_bf16 v[88:91], v[174:177], v[190:193], v[88:91]
	v_mfma_f32_16x16x32_bf16 v[76:79], v[166:169], v[198:201], v[76:79]
	v_mfma_f32_16x16x32_bf16 v[72:75], v[174:177], v[198:201], v[72:75]
	v_mfma_f32_16x16x32_bf16 v[68:71], v[166:169], v[206:209], v[68:71]
	v_mfma_f32_16x16x32_bf16 v[64:67], v[174:177], v[206:209], v[64:67]
	s_barrier
	s_add_i32 s76, s63, s33
	v_lshl_add_u64 v[210:211], s[48:49], 0, v[130:131]
	s_mov_b32 m0, s76
	ds_read_b128 v[178:181], v145 offset:16384
	ds_read_b128 v[182:185], v145 offset:17408
	ds_read_b128 v[186:189], v145 offset:18432
	ds_read_b128 v[190:193], v145 offset:19456
	ds_read_b128 v[194:197], v145 offset:20480
	ds_read_b128 v[198:201], v145 offset:21504
	ds_read_b128 v[202:205], v145 offset:22528
	ds_read_b128 v[206:209], v145 offset:23552
	global_load_lds_dwordx4 v[210:211], off
	s_add_i32 m0, s76, 0x2000
	s_add_u32 s76, s48, 0x40000
	v_lshl_add_u64 v[212:213], s[48:49], 0, v[134:135]
	s_addc_u32 s77, s49, 0
	s_add_i32 s78, s66, s33
	global_load_lds_dwordx4 v[212:213], off
	v_lshl_add_u64 v[214:215], s[76:77], 0, v[130:131]
	s_mov_b32 m0, s78
	v_lshl_add_u64 v[216:217], s[50:51], 0, v[132:133]
	global_load_lds_dwordx4 v[214:215], off
	v_lshl_add_u64 v[214:215], s[76:77], 0, v[134:135]
	s_add_i32 m0, s78, 0x2000
	s_nop 0
	global_load_lds_dwordx4 v[214:215], off
	v_lshl_add_u64 v[214:215], s[50:51], 0, v[128:129]
	s_mov_b32 m0, s52
	s_nop 0
	global_load_lds_dwordx4 v[214:215], off
	s_mov_b32 m0, s53
	s_nop 0
	global_load_lds_dwordx4 v[216:217], off
	s_waitcnt vmcnt(8)
	s_waitcnt lgkmcnt(0)
	s_barrier
; #define PG8_STAGE_A(bufoff, gbase, h, nx) do { _Pragma("unroll") for (int _i = 0; _i < 2; ++_i) { \
;         const unsigned vo_ = GA ? ((nx) ? vgn[h][_i] : vgc[h][_i]) : voffA[_i]; \
;         __builtin_amdgcn_global_load_lds((const unsigned*)((const char*)(gbase) + vo_), (PG8_LAS unsigned*)(lds + (bufoff) + ldsw + _i * 8192), 16, 0, 0); } } while (0)
; #define PG8_LDA(dst, b, h) do { _Pragma("unroll") for (int m = 0; m < 4; ++m) _Pragma("unroll") for (int k = 0; k < 2; ++k) dst[m][k] = *(const PG8_LAS bf16x8*)(lds + PG8_SA(b, h) + aoff + m * 2048 + k * 1024); } while (0)
; #define PG8_LDB(dst, b, h) do { _Pragma("unroll") for (int n = 0; n < 2; ++n) _Pragma("unroll") for (int k = 0; k < 2; ++k) dst[n][k] = *(const PG8_LAS bf16x8*)(lds + PG8_SB(b, h) + boff + n * 2048 + k * 1024); } while (0)
; #define PG8_MMA(ai, bj, At, Bt) do { __builtin_amdgcn_s_setprio(1); _Pragma("unroll") for (int m = 0; m < 4; ++m) _Pragma("unroll") for (int n = 0; n < 2; ++n) _Pragma("unroll") for (int k = 0; k < 2; ++k) \
;         acc[ai][bj][m][n] = __builtin_amdgcn_mfma_f32_16x16x32_bf16(Bt[n][k], At[m][k], acc[ai][bj][m][n], 0, 0, 0); __builtin_amdgcn_s_setprio(0); } while (0)
; #define PG8_WAIT_V(n) asm volatile("s_waitcnt vmcnt(" #n ")" ::: "memory")
; #define PG8_WAIT_L(n) asm volatile("s_waitcnt lgkmcnt(" #n ")" ::: "memory")
; #define PG8_BAR __builtin_amdgcn_s_barrier()
; #define PG8_SCHED __builtin_amdgcn_sched_barrier(0)
; template <class Epi, class Sched>
; __device__ __forceinline__ void gemm_phase(const int WID_, PG8_LAS unsigned char* lds, const Sched& S, const Epi& E) {
;     ...
;             PG8_WAIT_V(8); PG8_WAIT_L(0); PG8_BAR; PG8_MMA(1, 0, At, B0); PG8_MMA(1, 1, At, B1); PG8_BAR; PG8_SCHED;
;             PG8_LDB(B0, 1, 0); PG8_LDB(B1, 1, 1); PG8_SCHED; PG8_LDA(At, 1, 0); PG8_STAGE_A(PG8_SA(0, 1), a2 + hstepA, 1, last);
;             PG8_WAIT_V(8); PG8_WAIT_L(0); PG8_BAR; PG8_MMA(0, 0, At, B0); PG8_MMA(0, 1, At, B1); PG8_BAR; PG8_SCHED;
	s_waitcnt lgkmcnt(0)
	v_mfma_f32_16x16x32_bf16 v[60:63], v[146:149], v[178:181], v[60:63]
	v_mfma_f32_16x16x32_bf16 v[56:59], v[154:157], v[178:181], v[56:59]
	v_mfma_f32_16x16x32_bf16 v[52:55], v[146:149], v[186:189], v[52:55]
	v_mfma_f32_16x16x32_bf16 v[48:51], v[154:157], v[186:189], v[48:51]
	v_mfma_f32_16x16x32_bf16 v[36:39], v[146:149], v[194:197], v[36:39]
	v_mfma_f32_16x16x32_bf16 v[32:35], v[154:157], v[194:197], v[32:35]
	v_mfma_f32_16x16x32_bf16 v[20:23], v[146:149], v[202:205], v[20:23]
	v_mfma_f32_16x16x32_bf16 v[16:19], v[154:157], v[202:205], v[16:19]
	v_mfma_f32_16x16x32_bf16 v[60:63], v[150:153], v[182:185], v[60:63]
	v_mfma_f32_16x16x32_bf16 v[56:59], v[158:161], v[182:185], v[56:59]
	v_mfma_f32_16x16x32_bf16 v[52:55], v[150:153], v[190:193], v[52:55]
	v_mfma_f32_16x16x32_bf16 v[48:51], v[158:161], v[190:193], v[48:51]
	v_mfma_f32_16x16x32_bf16 v[36:39], v[150:153], v[198:201], v[36:39]
	v_mfma_f32_16x16x32_bf16 v[32:35], v[158:161], v[198:201], v[32:35]
	v_mfma_f32_16x16x32_bf16 v[20:23], v[150:153], v[206:209], v[20:23]
	v_mfma_f32_16x16x32_bf16 v[16:19], v[158:161], v[206:209], v[16:19]
	v_mfma_f32_16x16x32_bf16 v[44:47], v[162:165], v[178:181], v[44:47]
	v_mfma_f32_16x16x32_bf16 v[40:43], v[170:173], v[178:181], v[40:43]
	v_mfma_f32_16x16x32_bf16 v[28:31], v[162:165], v[186:189], v[28:31]
	v_mfma_f32_16x16x32_bf16 v[24:27], v[170:173], v[186:189], v[24:27]
	v_mfma_f32_16x16x32_bf16 v[12:15], v[162:165], v[194:197], v[12:15]
	v_mfma_f32_16x16x32_bf16 v[8:11], v[170:173], v[194:197], v[8:11]
	v_mfma_f32_16x16x32_bf16 v[4:7], v[162:165], v[202:205], v[4:7]
	v_mfma_f32_16x16x32_bf16 v[0:3], v[170:173], v[202:205], v[0:3]
	v_mfma_f32_16x16x32_bf16 v[44:47], v[166:169], v[182:185], v[44:47]
	v_mfma_f32_16x16x32_bf16 v[40:43], v[174:177], v[182:185], v[40:43]
	v_mfma_f32_16x16x32_bf16 v[28:31], v[166:169], v[190:193], v[28:31]
	v_mfma_f32_16x16x32_bf16 v[24:27], v[174:177], v[190:193], v[24:27]
	v_mfma_f32_16x16x32_bf16 v[12:15], v[166:169], v[198:201], v[12:15]
	v_mfma_f32_16x16x32_bf16 v[8:11], v[174:177], v[198:201], v[8:11]
	v_mfma_f32_16x16x32_bf16 v[4:7], v[166:169], v[206:209], v[4:7]
	v_mfma_f32_16x16x32_bf16 v[0:3], v[174:177], v[206:209], v[0:3]
	s_barrier
	s_add_i32 s76, 0, 0x18000
	s_add_i32 s77, 0, 0x1c000
	v_add_u32_e32 v158, s76, v141
	v_add_u32_e32 v174, s77, v141
	ds_read_b128 v[146:149], v158
	ds_read_b128 v[150:153], v158 offset:1024
	ds_read_b128 v[154:157], v158 offset:2048
	ds_read_b128 v[158:161], v158 offset:3072
	ds_read_b128 v[162:165], v174
	ds_read_b128 v[166:169], v174 offset:1024
	ds_read_b128 v[170:173], v174 offset:2048
	ds_read_b128 v[174:177], v174 offset:3072
	s_add_u32 s50, s50, 0x40000
	s_addc_u32 s51, s51, 0
	s_mov_b32 m0, s58
	v_lshl_add_u64 v[218:219], s[50:51], 0, v[128:129]
	ds_read_b128 v[178:181], v145 offset:32768
	ds_read_b128 v[182:185], v145 offset:33792
	ds_read_b128 v[186:189], v145 offset:34816
	ds_read_b128 v[190:193], v145 offset:35840
	ds_read_b128 v[194:197], v145 offset:36864
	ds_read_b128 v[198:201], v145 offset:37888
	ds_read_b128 v[202:205], v145 offset:38912
	ds_read_b128 v[206:209], v145 offset:39936
	global_load_lds_dwordx4 v[218:219], off
	v_lshl_add_u64 v[218:219], s[50:51], 0, v[132:133]
	s_mov_b32 m0, s59
	s_nop 0
	global_load_lds_dwordx4 v[218:219], off
	s_waitcnt vmcnt(8)
	s_waitcnt lgkmcnt(0)
	s_barrier
	s_waitcnt lgkmcnt(0)
	v_mfma_f32_16x16x32_bf16 v[124:127], v[146:149], v[178:181], v[124:127]
	v_mfma_f32_16x16x32_bf16 v[120:123], v[154:157], v[178:181], v[120:123]
	v_mfma_f32_16x16x32_bf16 v[116:119], v[146:149], v[186:189], v[116:119]
	v_mfma_f32_16x16x32_bf16 v[112:115], v[154:157], v[186:189], v[112:115]
	v_mfma_f32_16x16x32_bf16 v[100:103], v[146:149], v[194:197], v[100:103]
	v_mfma_f32_16x16x32_bf16 v[96:99], v[154:157], v[194:197], v[96:99]
	v_mfma_f32_16x16x32_bf16 v[84:87], v[146:149], v[202:205], v[84:87]
	v_mfma_f32_16x16x32_bf16 v[80:83], v[154:157], v[202:205], v[80:83]
	v_mfma_f32_16x16x32_bf16 v[124:127], v[150:153], v[182:185], v[124:127]
	v_mfma_f32_16x16x32_bf16 v[120:123], v[158:161], v[182:185], v[120:123]
	v_mfma_f32_16x16x32_bf16 v[116:119], v[150:153], v[190:193], v[116:119]
	v_mfma_f32_16x16x32_bf16 v[112:115], v[158:161], v[190:193], v[112:115]
	v_mfma_f32_16x16x32_bf16 v[100:103], v[150:153], v[198:201], v[100:103]
	v_mfma_f32_16x16x32_bf16 v[96:99], v[158:161], v[198:201], v[96:99]
	v_mfma_f32_16x16x32_bf16 v[84:87], v[150:153], v[206:209], v[84:87]
	v_mfma_f32_16x16x32_bf16 v[80:83], v[158:161], v[206:209], v[80:83]
	v_mfma_f32_16x16x32_bf16 v[108:111], v[162:165], v[178:181], v[108:111]
	v_mfma_f32_16x16x32_bf16 v[104:107], v[170:173], v[178:181], v[104:107]
	v_mfma_f32_16x16x32_bf16 v[92:95], v[162:165], v[186:189], v[92:95]
	v_mfma_f32_16x16x32_bf16 v[88:91], v[170:173], v[186:189], v[88:91]
	v_mfma_f32_16x16x32_bf16 v[76:79], v[162:165], v[194:197], v[76:79]
	v_mfma_f32_16x16x32_bf16 v[72:75], v[170:173], v[194:197], v[72:75]
	v_mfma_f32_16x16x32_bf16 v[68:71], v[162:165], v[202:205], v[68:71]
	v_mfma_f32_16x16x32_bf16 v[64:67], v[170:173], v[202:205], v[64:67]
	v_mfma_f32_16x16x32_bf16 v[108:111], v[166:169], v[182:185], v[108:111]
	v_mfma_f32_16x16x32_bf16 v[104:107], v[174:177], v[182:185], v[104:107]
	v_mfma_f32_16x16x32_bf16 v[92:95], v[166:169], v[190:193], v[92:95]
	v_mfma_f32_16x16x32_bf16 v[88:91], v[174:177], v[190:193], v[88:91]
	v_mfma_f32_16x16x32_bf16 v[76:79], v[166:169], v[198:201], v[76:79]
	v_mfma_f32_16x16x32_bf16 v[72:75], v[174:177], v[198:201], v[72:75]
	v_mfma_f32_16x16x32_bf16 v[68:71], v[166:169], v[206:209], v[68:71]
	v_mfma_f32_16x16x32_bf16 v[64:67], v[174:177], v[206:209], v[64:67]
	s_barrier
; #define PG8_STAGE(bufoff, gbase, voff) do { _Pragma("unroll") for (int _i = 0; _i < 2; ++_i) \
;         __builtin_amdgcn_global_load_lds((const unsigned*)((const char*)(gbase) + (voff)[_i]), (PG8_LAS unsigned*)(lds + (bufoff) + ldsw + _i * 8192), 16, 0, 0); } while (0)
; #define PG8_STAGE_A(bufoff, gbase, h, nx) do { _Pragma("unroll") for (int _i = 0; _i < 2; ++_i) { \
;         const unsigned vo_ = GA ? ((nx) ? vgn[h][_i] : vgc[h][_i]) : voffA[_i]; \
;         __builtin_amdgcn_global_load_lds((const unsigned*)((const char*)(gbase) + vo_), (PG8_LAS unsigned*)(lds + (bufoff) + ldsw + _i * 8192), 16, 0, 0); } } while (0)
; #define PG8_LDA(dst, b, h) do { _Pragma("unroll") for (int m = 0; m < 4; ++m) _Pragma("unroll") for (int k = 0; k < 2; ++k) dst[m][k] = *(const PG8_LAS bf16x8*)(lds + PG8_SA(b, h) + aoff + m * 2048 + k * 1024); } while (0)
; #define PG8_MMA(ai, bj, At, Bt) do { __builtin_amdgcn_s_setprio(1); _Pragma("unroll") for (int m = 0; m < 4; ++m) _Pragma("unroll") for (int n = 0; n < 2; ++n) _Pragma("unroll") for (int k = 0; k < 2; ++k) \
;         acc[ai][bj][m][n] = __builtin_amdgcn_mfma_f32_16x16x32_bf16(Bt[n][k], At[m][k], acc[ai][bj][m][n], 0, 0, 0); __builtin_amdgcn_s_setprio(0); } while (0)
; #define PG8_WAIT_V(n) asm volatile("s_waitcnt vmcnt(" #n ")" ::: "memory")
; #define PG8_WAIT_L(n) asm volatile("s_waitcnt lgkmcnt(" #n ")" ::: "memory")
; #define PG8_BAR __builtin_amdgcn_s_barrier()
; #define PG8_SCHED __builtin_amdgcn_sched_barrier(0)
; template <class Epi, class Sched>
; __device__ __forceinline__ void gemm_phase(const int WID_, PG8_LAS unsigned char* lds, const Sched& S, const Epi& E) {
;     ...
;             PG8_LDA(At, 1, 1); PG8_STAGE(PG8_SB(1, 0), b3, voffB); PG8_STAGE(PG8_SB(1, 1), b3 + hstepB, voffB); PG8_STAGE_A(PG8_SA(1, 0), a3, 0, last);
;             PG8_WAIT_V(8); PG8_WAIT_L(0); PG8_BAR; PG8_MMA(1, 0, At, B0); PG8_MMA(1, 1, At, B1); PG8_BAR; PG8_SCHED;
;         }
;         if (wr == 0) PG8_BAR;
	s_add_i32 s50, s76, s33
	v_lshl_add_u64 v[210:211], v[210:211], 0, s[4:5]
	s_mov_b32 m0, s50
	ds_read_b128 v[178:181], v145 offset:49152
	ds_read_b128 v[182:185], v145 offset:50176
	ds_read_b128 v[186:189], v145 offset:51200
	ds_read_b128 v[190:193], v145 offset:52224
	ds_read_b128 v[194:197], v145 offset:53248
	ds_read_b128 v[198:201], v145 offset:54272
	ds_read_b128 v[202:205], v145 offset:55296
	ds_read_b128 v[206:209], v145 offset:56320
	global_load_lds_dwordx4 v[210:211], off
	s_add_i32 m0, s50, 0x2000
	s_add_u32 s48, s48, 0x40080
	v_lshl_add_u64 v[210:211], v[212:213], 0, s[4:5]
	s_addc_u32 s49, s49, 0
	s_add_i32 s50, s77, s33
	global_load_lds_dwordx4 v[210:211], off
	v_lshl_add_u64 v[210:211], s[48:49], 0, v[130:131]
	s_mov_b32 m0, s50
	s_nop 0
	global_load_lds_dwordx4 v[210:211], off
	v_lshl_add_u64 v[210:211], s[48:49], 0, v[134:135]
	s_add_i32 m0, s50, 0x2000
	s_nop 0
	global_load_lds_dwordx4 v[210:211], off
	v_lshl_add_u64 v[210:211], v[214:215], 0, s[4:5]
	s_mov_b32 m0, s60
	s_nop 0
	global_load_lds_dwordx4 v[210:211], off
	v_lshl_add_u64 v[210:211], v[216:217], 0, s[4:5]
	s_mov_b32 m0, s61
	s_nop 0
	global_load_lds_dwordx4 v[210:211], off
	s_waitcnt vmcnt(8)
	s_waitcnt lgkmcnt(0)
	s_barrier
	s_waitcnt lgkmcnt(0)
	v_mfma_f32_16x16x32_bf16 v[60:63], v[146:149], v[178:181], v[60:63]
	v_mfma_f32_16x16x32_bf16 v[56:59], v[154:157], v[178:181], v[56:59]
	v_mfma_f32_16x16x32_bf16 v[52:55], v[146:149], v[186:189], v[52:55]
	v_mfma_f32_16x16x32_bf16 v[48:51], v[154:157], v[186:189], v[48:51]
	v_mfma_f32_16x16x32_bf16 v[36:39], v[146:149], v[194:197], v[36:39]
	v_mfma_f32_16x16x32_bf16 v[32:35], v[154:157], v[194:197], v[32:35]
	v_mfma_f32_16x16x32_bf16 v[20:23], v[146:149], v[202:205], v[20:23]
	v_mfma_f32_16x16x32_bf16 v[16:19], v[154:157], v[202:205], v[16:19]
	v_mfma_f32_16x16x32_bf16 v[60:63], v[150:153], v[182:185], v[60:63]
	v_mfma_f32_16x16x32_bf16 v[56:59], v[158:161], v[182:185], v[56:59]
	v_mfma_f32_16x16x32_bf16 v[52:55], v[150:153], v[190:193], v[52:55]
	v_mfma_f32_16x16x32_bf16 v[48:51], v[158:161], v[190:193], v[48:51]
	v_mfma_f32_16x16x32_bf16 v[36:39], v[150:153], v[198:201], v[36:39]
	v_mfma_f32_16x16x32_bf16 v[32:35], v[158:161], v[198:201], v[32:35]
	v_mfma_f32_16x16x32_bf16 v[20:23], v[150:153], v[206:209], v[20:23]
	v_mfma_f32_16x16x32_bf16 v[16:19], v[158:161], v[206:209], v[16:19]
	v_mfma_f32_16x16x32_bf16 v[44:47], v[162:165], v[178:181], v[44:47]
	v_mfma_f32_16x16x32_bf16 v[40:43], v[170:173], v[178:181], v[40:43]
	v_mfma_f32_16x16x32_bf16 v[28:31], v[162:165], v[186:189], v[28:31]
	v_mfma_f32_16x16x32_bf16 v[24:27], v[170:173], v[186:189], v[24:27]
	v_mfma_f32_16x16x32_bf16 v[12:15], v[162:165], v[194:197], v[12:15]
	v_mfma_f32_16x16x32_bf16 v[8:11], v[170:173], v[194:197], v[8:11]
	v_mfma_f32_16x16x32_bf16 v[4:7], v[162:165], v[202:205], v[4:7]
	v_mfma_f32_16x16x32_bf16 v[0:3], v[170:173], v[202:205], v[0:3]
	v_mfma_f32_16x16x32_bf16 v[44:47], v[166:169], v[182:185], v[44:47]
	v_mfma_f32_16x16x32_bf16 v[40:43], v[174:177], v[182:185], v[40:43]
	v_mfma_f32_16x16x32_bf16 v[28:31], v[166:169], v[190:193], v[28:31]
	v_mfma_f32_16x16x32_bf16 v[24:27], v[174:177], v[190:193], v[24:27]
	v_mfma_f32_16x16x32_bf16 v[12:15], v[166:169], v[198:201], v[12:15]
	v_mfma_f32_16x16x32_bf16 v[8:11], v[174:177], v[198:201], v[8:11]
	v_mfma_f32_16x16x32_bf16 v[4:7], v[166:169], v[206:209], v[4:7]
	v_mfma_f32_16x16x32_bf16 v[0:3], v[174:177], v[206:209], v[0:3]
	s_barrier
	s_add_i32 s71, s71, 2
	s_add_u32 s46, s46, 0x100
	s_addc_u32 s47, s47, 0
	s_add_u32 s69, s69, 0x100
	s_addc_u32 s70, s70, 0
	s_cmp_gt_u32 s71, 13
	s_cbranch_scc0 .LBB0_1563
	s_and_b64 vcc, exec, s[18:19]
	s_cbranch_vccz .LBB0_1566
	s_barrier

; __device__ __forceinline__ void phase2(const int WID_, const char* items, float* Y, char* lds, const int vblk, const int nvblk) {
;     ...
;     for (int item = vblk; item < NB * 8 * 2; item += nvblk) {
;     ...
;         __builtin_amdgcn_s_setprio(0);
.LBB0_1606:
	s_setprio 0
	v_readlane_b32 s98, v243, 44
	s_nop 3
	s_cmp_lt_u32 s98, 4
	s_cbranch_scc1 .Lprio_pa
	s_setprio 1
.Lprio_pa:
	s_add_i32 s36, s46, 0x80
	s_cmp_gt_i32 s46, -1
	s_mov_b32 s46, s36
	s_cbranch_scc1 .LBB0_1667

; __device__ __forceinline__ void phase2(const int WID_, const char* items, float* Y, char* lds, const int vblk, const int nvblk) {
;     ...
;     for (int item = vblk; item < NB * 8 * 2; item += nvblk) {
.Lprio_pb:
	s_add_i32 s45, s45, s94
	s_add_i32 s44, s44, s94
	s_cmpk_gt_i32 s45, 0x7f
	s_cbranch_scc1 .LBB0_1732

; #define PG8_STAGE(bufoff, gbase, voff) do { _Pragma("unroll") for (int _i = 0; _i < 2; ++_i) \
;         __builtin_amdgcn_global_load_lds((const unsigned*)((const char*)(gbase) + (voff)[_i]), (PG8_LAS unsigned*)(lds + (bufoff) + ldsw + _i * 8192), 16, 0, 0); } while (0)
; #define PG8_STAGE_A(bufoff, gbase, h, nx) do { _Pragma("unroll") for (int _i = 0; _i < 2; ++_i) { \
;         const unsigned vo_ = GA ? ((nx) ? vgn[h][_i] : vgc[h][_i]) : voffA[_i]; \
;         __builtin_amdgcn_global_load_lds((const unsigned*)((const char*)(gbase) + vo_), (PG8_LAS unsigned*)(lds + (bufoff) + ldsw + _i * 8192), 16, 0, 0); } } while (0)
; #define PG8_LDA(dst, b, h) do { _Pragma("unroll") for (int m = 0; m < 4; ++m) _Pragma("unroll") for (int k = 0; k < 2; ++k) dst[m][k] = *(const PG8_LAS bf16x8*)(lds + PG8_SA(b, h) + aoff + m * 2048 + k * 1024); } while (0)
; #define PG8_LDB(dst, b, h) do { _Pragma("unroll") for (int n = 0; n < 2; ++n) _Pragma("unroll") for (int k = 0; k < 2; ++k) dst[n][k] = *(const PG8_LAS bf16x8*)(lds + PG8_SB(b, h) + boff + n * 2048 + k * 1024); } while (0)
; #define PG8_WAIT_V(n) asm volatile("s_waitcnt vmcnt(" #n ")" ::: "memory")
; #define PG8_WAIT_L(n) asm volatile("s_waitcnt lgkmcnt(" #n ")" ::: "memory")
; #define PG8_BAR __builtin_amdgcn_s_barrier()
; #define PG8_SCHED __builtin_amdgcn_sched_barrier(0)
; template <class Epi, class Sched>
; __device__ __forceinline__ void gemm_phase(const int WID_, PG8_LAS unsigned char* lds, const Sched& S, const Epi& E) {
;     ...
;         for (int t = 0; t < nt; t += 2) {
;             const bool last = (t == nt - 2);
;             const char* a1 = cA + (size_t)(t + 1) * kstep;
;             const char* a2 = last ? nA : cA + (size_t)(t + 2) * kstep; const char* b2 = last ? nB : cB + (size_t)(t + 2) * kstep;
;             const char* a3 = a2 + kstep; const char* b3 = b2 + kstep;
;             PG8_LDB(B0, 0, 0); PG8_LDB(B1, 0, 1); PG8_SCHED; PG8_LDA(At, 0, 0); PG8_STAGE_A(PG8_SA(1, 1), a1 + hstepA, 1, false);
;             PG8_WAIT_V(8); PG8_WAIT_L(0); PG8_BAR; PG8_MMA(0, 0, At, B0); PG8_MMA(0, 1, At, B1); PG8_BAR; PG8_SCHED;
;             PG8_LDA(At, 0, 1); PG8_STAGE(PG8_SB(0, 0), b2, voffB); PG8_STAGE(PG8_SB(0, 1), b2 + hstepB, voffB); PG8_STAGE_A(PG8_SA(0, 0), a2, 0, last);
;             PG8_WAIT_V(8); PG8_WAIT_L(0); PG8_BAR; PG8_MMA(1, 0, At, B0); PG8_MMA(1, 1, At, B1); PG8_BAR; PG8_SCHED;
.LBB0_1786:
	ds_read_b128 v[146:149], v143
	ds_read_b128 v[150:153], v143 offset:1024
	ds_read_b128 v[154:157], v143 offset:2048
	ds_read_b128 v[158:161], v143 offset:3072
	ds_read_b128 v[162:165], v144
	ds_read_b128 v[166:169], v144 offset:1024
	ds_read_b128 v[170:173], v144 offset:2048
	ds_read_b128 v[174:177], v144 offset:3072
	s_add_u32 s44, s42, 0xfffc0080
	s_addc_u32 s45, s43, -1
	s_cmp_eq_u32 s67, 12
	s_cselect_b32 s47, s37, s45
	s_cselect_b32 s46, s61, s44
	s_cselect_b32 s45, s23, s66
	s_cselect_b32 s44, s62, s63
	v_lshl_add_u64 v[210:211], s[42:43], 0, v[136:137]
	s_add_i32 m0, s33, 0xc000
	ds_read_b128 v[178:181], v145
	ds_read_b128 v[182:185], v145 offset:1024
	ds_read_b128 v[186:189], v145 offset:2048
	ds_read_b128 v[190:193], v145 offset:3072
	ds_read_b128 v[194:197], v145 offset:4096
	ds_read_b128 v[198:201], v145 offset:5120
	ds_read_b128 v[202:205], v145 offset:6144
	ds_read_b128 v[206:209], v145 offset:7168
	global_load_lds_dwordx4 v[210:211], off
	v_lshl_add_u64 v[210:211], s[42:43], 0, v[138:139]
	s_add_i32 m0, s33, 0xe000
	s_nop 0
	global_load_lds_dwordx4 v[210:211], off
	s_waitcnt vmcnt(8)
	s_waitcnt lgkmcnt(0)
	s_barrier
	s_waitcnt lgkmcnt(0)
	v_mfma_f32_16x16x32_bf16 v[124:127], v[146:149], v[178:181], v[124:127]
	v_mfma_f32_16x16x32_bf16 v[120:123], v[154:157], v[178:181], v[120:123]
	v_mfma_f32_16x16x32_bf16 v[116:119], v[146:149], v[186:189], v[116:119]
	v_mfma_f32_16x16x32_bf16 v[112:115], v[154:157], v[186:189], v[112:115]
	v_mfma_f32_16x16x32_bf16 v[100:103], v[146:149], v[194:197], v[100:103]
	v_mfma_f32_16x16x32_bf16 v[96:99], v[154:157], v[194:197], v[96:99]
	v_mfma_f32_16x16x32_bf16 v[84:87], v[146:149], v[202:205], v[84:87]
	v_mfma_f32_16x16x32_bf16 v[80:83], v[154:157], v[202:205], v[80:83]
	v_mfma_f32_16x16x32_bf16 v[124:127], v[150:153], v[182:185], v[124:127]
	v_mfma_f32_16x16x32_bf16 v[120:123], v[158:161], v[182:185], v[120:123]
	v_mfma_f32_16x16x32_bf16 v[116:119], v[150:153], v[190:193], v[116:119]
	v_mfma_f32_16x16x32_bf16 v[112:115], v[158:161], v[190:193], v[112:115]
	v_mfma_f32_16x16x32_bf16 v[100:103], v[150:153], v[198:201], v[100:103]
	v_mfma_f32_16x16x32_bf16 v[96:99], v[158:161], v[198:201], v[96:99]
	v_mfma_f32_16x16x32_bf16 v[84:87], v[150:153], v[206:209], v[84:87]
	v_mfma_f32_16x16x32_bf16 v[80:83], v[158:161], v[206:209], v[80:83]
	v_mfma_f32_16x16x32_bf16 v[108:111], v[162:165], v[178:181], v[108:111]
	v_mfma_f32_16x16x32_bf16 v[104:107], v[170:173], v[178:181], v[104:107]
	v_mfma_f32_16x16x32_bf16 v[92:95], v[162:165], v[186:189], v[92:95]
	v_mfma_f32_16x16x32_bf16 v[88:91], v[170:173], v[186:189], v[88:91]
	v_mfma_f32_16x16x32_bf16 v[76:79], v[162:165], v[194:197], v[76:79]
	v_mfma_f32_16x16x32_bf16 v[72:75], v[170:173], v[194:197], v[72:75]
	v_mfma_f32_16x16x32_bf16 v[68:71], v[162:165], v[202:205], v[68:71]
	v_mfma_f32_16x16x32_bf16 v[64:67], v[170:173], v[202:205], v[64:67]
	v_mfma_f32_16x16x32_bf16 v[108:111], v[166:169], v[182:185], v[108:111]
	v_mfma_f32_16x16x32_bf16 v[104:107], v[174:177], v[182:185], v[104:107]
	v_mfma_f32_16x16x32_bf16 v[92:95], v[166:169], v[190:193], v[92:95]
	v_mfma_f32_16x16x32_bf16 v[88:91], v[174:177], v[190:193], v[88:91]
	v_mfma_f32_16x16x32_bf16 v[76:79], v[166:169], v[198:201], v[76:79]
	v_mfma_f32_16x16x32_bf16 v[72:75], v[174:177], v[198:201], v[72:75]
	v_mfma_f32_16x16x32_bf16 v[68:71], v[166:169], v[206:209], v[68:71]
	v_mfma_f32_16x16x32_bf16 v[64:67], v[174:177], v[206:209], v[64:67]
	s_barrier
	s_add_i32 s68, s59, s9
	v_lshl_add_u64 v[210:211], s[44:45], 0, v[130:131]
	s_mov_b32 m0, s68
	ds_read_b128 v[178:181], v145 offset:16384
	ds_read_b128 v[182:185], v145 offset:17408
	ds_read_b128 v[186:189], v145 offset:18432
	ds_read_b128 v[190:193], v145 offset:19456
	ds_read_b128 v[194:197], v145 offset:20480
	ds_read_b128 v[198:201], v145 offset:21504
	ds_read_b128 v[202:205], v145 offset:22528
	ds_read_b128 v[206:209], v145 offset:23552
	global_load_lds_dwordx4 v[210:211], off
	s_add_i32 m0, s68, 0x2000
	s_add_u32 s68, s44, 0x40000
	v_lshl_add_u64 v[212:213], s[44:45], 0, v[134:135]
	s_addc_u32 s69, s45, 0
	s_add_i32 s70, s60, s9
	global_load_lds_dwordx4 v[212:213], off
	v_lshl_add_u64 v[214:215], s[68:69], 0, v[130:131]
	s_mov_b32 m0, s70
	v_lshl_add_u64 v[216:217], s[46:47], 0, v[132:133]
	global_load_lds_dwordx4 v[214:215], off
	v_lshl_add_u64 v[214:215], s[68:69], 0, v[134:135]
	s_add_i32 m0, s70, 0x2000
	s_nop 0
	global_load_lds_dwordx4 v[214:215], off
	v_lshl_add_u64 v[214:215], s[46:47], 0, v[128:129]
	s_mov_b32 m0, s33
	s_nop 0
	global_load_lds_dwordx4 v[214:215], off
	s_mov_b32 m0, s48
	s_nop 0
	global_load_lds_dwordx4 v[216:217], off
	s_waitcnt vmcnt(8)
	s_waitcnt lgkmcnt(0)
	s_barrier
; #define PG8_STAGE_A(bufoff, gbase, h, nx) do { _Pragma("unroll") for (int _i = 0; _i < 2; ++_i) { \
;         const unsigned vo_ = GA ? ((nx) ? vgn[h][_i] : vgc[h][_i]) : voffA[_i]; \
;         __builtin_amdgcn_global_load_lds((const unsigned*)((const char*)(gbase) + vo_), (PG8_LAS unsigned*)(lds + (bufoff) + ldsw + _i * 8192), 16, 0, 0); } } while (0)
; #define PG8_LDA(dst, b, h) do { _Pragma("unroll") for (int m = 0; m < 4; ++m) _Pragma("unroll") for (int k = 0; k < 2; ++k) dst[m][k] = *(const PG8_LAS bf16x8*)(lds + PG8_SA(b, h) + aoff + m * 2048 + k * 1024); } while (0)
; #define PG8_LDB(dst, b, h) do { _Pragma("unroll") for (int n = 0; n < 2; ++n) _Pragma("unroll") for (int k = 0; k < 2; ++k) dst[n][k] = *(const PG8_LAS bf16x8*)(lds + PG8_SB(b, h) + boff + n * 2048 + k * 1024); } while (0)
; #define PG8_MMA(ai, bj, At, Bt) do { __builtin_amdgcn_s_setprio(1); _Pragma("unroll") for (int m = 0; m < 4; ++m) _Pragma("unroll") for (int n = 0; n < 2; ++n) _Pragma("unroll") for (int k = 0; k < 2; ++k) \
;         acc[ai][bj][m][n] = __builtin_amdgcn_mfma_f32_16x16x32_bf16(Bt[n][k], At[m][k], acc[ai][bj][m][n], 0, 0, 0); __builtin_amdgcn_s_setprio(0); } while (0)
; #define PG8_WAIT_V(n) asm volatile("s_waitcnt vmcnt(" #n ")" ::: "memory")
; #define PG8_WAIT_L(n) asm volatile("s_waitcnt lgkmcnt(" #n ")" ::: "memory")
; #define PG8_BAR __builtin_amdgcn_s_barrier()
; #define PG8_SCHED __builtin_amdgcn_sched_barrier(0)
; template <class Epi, class Sched>
; __device__ __forceinline__ void gemm_phase(const int WID_, PG8_LAS unsigned char* lds, const Sched& S, const Epi& E) {
;     ...
;             PG8_WAIT_V(8); PG8_WAIT_L(0); PG8_BAR; PG8_MMA(1, 0, At, B0); PG8_MMA(1, 1, At, B1); PG8_BAR; PG8_SCHED;
;             PG8_LDB(B0, 1, 0); PG8_LDB(B1, 1, 1); PG8_SCHED; PG8_LDA(At, 1, 0); PG8_STAGE_A(PG8_SA(0, 1), a2 + hstepA, 1, last);
;             PG8_WAIT_V(8); PG8_WAIT_L(0); PG8_BAR; PG8_MMA(0, 0, At, B0); PG8_MMA(0, 1, At, B1); PG8_BAR; PG8_SCHED;
	s_waitcnt lgkmcnt(0)
	v_mfma_f32_16x16x32_bf16 v[60:63], v[146:149], v[178:181], v[60:63]
	v_mfma_f32_16x16x32_bf16 v[56:59], v[154:157], v[178:181], v[56:59]
	v_mfma_f32_16x16x32_bf16 v[52:55], v[146:149], v[186:189], v[52:55]
	v_mfma_f32_16x16x32_bf16 v[48:51], v[154:157], v[186:189], v[48:51]
	v_mfma_f32_16x16x32_bf16 v[36:39], v[146:149], v[194:197], v[36:39]
	v_mfma_f32_16x16x32_bf16 v[32:35], v[154:157], v[194:197], v[32:35]
	v_mfma_f32_16x16x32_bf16 v[20:23], v[146:149], v[202:205], v[20:23]
	v_mfma_f32_16x16x32_bf16 v[16:19], v[154:157], v[202:205], v[16:19]
	v_mfma_f32_16x16x32_bf16 v[60:63], v[150:153], v[182:185], v[60:63]
	v_mfma_f32_16x16x32_bf16 v[56:59], v[158:161], v[182:185], v[56:59]
	v_mfma_f32_16x16x32_bf16 v[52:55], v[150:153], v[190:193], v[52:55]
	v_mfma_f32_16x16x32_bf16 v[48:51], v[158:161], v[190:193], v[48:51]
	v_mfma_f32_16x16x32_bf16 v[36:39], v[150:153], v[198:201], v[36:39]
	v_mfma_f32_16x16x32_bf16 v[32:35], v[158:161], v[198:201], v[32:35]
	v_mfma_f32_16x16x32_bf16 v[20:23], v[150:153], v[206:209], v[20:23]
	v_mfma_f32_16x16x32_bf16 v[16:19], v[158:161], v[206:209], v[16:19]
	v_mfma_f32_16x16x32_bf16 v[44:47], v[162:165], v[178:181], v[44:47]
	v_mfma_f32_16x16x32_bf16 v[40:43], v[170:173], v[178:181], v[40:43]
	v_mfma_f32_16x16x32_bf16 v[28:31], v[162:165], v[186:189], v[28:31]
	v_mfma_f32_16x16x32_bf16 v[24:27], v[170:173], v[186:189], v[24:27]
	v_mfma_f32_16x16x32_bf16 v[12:15], v[162:165], v[194:197], v[12:15]
	v_mfma_f32_16x16x32_bf16 v[8:11], v[170:173], v[194:197], v[8:11]
	v_mfma_f32_16x16x32_bf16 v[4:7], v[162:165], v[202:205], v[4:7]
	v_mfma_f32_16x16x32_bf16 v[0:3], v[170:173], v[202:205], v[0:3]
	v_mfma_f32_16x16x32_bf16 v[44:47], v[166:169], v[182:185], v[44:47]
	v_mfma_f32_16x16x32_bf16 v[40:43], v[174:177], v[182:185], v[40:43]
	v_mfma_f32_16x16x32_bf16 v[28:31], v[166:169], v[190:193], v[28:31]
	v_mfma_f32_16x16x32_bf16 v[24:27], v[174:177], v[190:193], v[24:27]
	v_mfma_f32_16x16x32_bf16 v[12:15], v[166:169], v[198:201], v[12:15]
	v_mfma_f32_16x16x32_bf16 v[8:11], v[174:177], v[198:201], v[8:11]
	v_mfma_f32_16x16x32_bf16 v[4:7], v[166:169], v[206:209], v[4:7]
	v_mfma_f32_16x16x32_bf16 v[0:3], v[174:177], v[206:209], v[0:3]
	s_barrier
	s_add_i32 s68, 0, 0x18000
	s_add_i32 s69, 0, 0x1c000
	v_add_u32_e32 v158, s68, v141
	v_add_u32_e32 v174, s69, v141
	ds_read_b128 v[146:149], v158
	ds_read_b128 v[150:153], v158 offset:1024
	ds_read_b128 v[154:157], v158 offset:2048
	ds_read_b128 v[158:161], v158 offset:3072
	ds_read_b128 v[162:165], v174
	ds_read_b128 v[166:169], v174 offset:1024
	ds_read_b128 v[170:173], v174 offset:2048
	ds_read_b128 v[174:177], v174 offset:3072
	s_add_u32 s46, s46, 0x40000
	s_addc_u32 s47, s47, 0
	s_mov_b32 m0, s49
	v_lshl_add_u64 v[218:219], s[46:47], 0, v[128:129]
	ds_read_b128 v[178:181], v145 offset:32768
	ds_read_b128 v[182:185], v145 offset:33792
	ds_read_b128 v[186:189], v145 offset:34816
	ds_read_b128 v[190:193], v145 offset:35840
	ds_read_b128 v[194:197], v145 offset:36864
	ds_read_b128 v[198:201], v145 offset:37888
	ds_read_b128 v[202:205], v145 offset:38912
	ds_read_b128 v[206:209], v145 offset:39936
	global_load_lds_dwordx4 v[218:219], off
	v_lshl_add_u64 v[218:219], s[46:47], 0, v[132:133]
	s_mov_b32 m0, s50
	s_nop 0
	global_load_lds_dwordx4 v[218:219], off
	s_waitcnt vmcnt(8)
	s_waitcnt lgkmcnt(0)
	s_barrier
	s_waitcnt lgkmcnt(0)
	v_mfma_f32_16x16x32_bf16 v[124:127], v[146:149], v[178:181], v[124:127]
	v_mfma_f32_16x16x32_bf16 v[120:123], v[154:157], v[178:181], v[120:123]
	v_mfma_f32_16x16x32_bf16 v[116:119], v[146:149], v[186:189], v[116:119]
	v_mfma_f32_16x16x32_bf16 v[112:115], v[154:157], v[186:189], v[112:115]
	v_mfma_f32_16x16x32_bf16 v[100:103], v[146:149], v[194:197], v[100:103]
	v_mfma_f32_16x16x32_bf16 v[96:99], v[154:157], v[194:197], v[96:99]
	v_mfma_f32_16x16x32_bf16 v[84:87], v[146:149], v[202:205], v[84:87]
	v_mfma_f32_16x16x32_bf16 v[80:83], v[154:157], v[202:205], v[80:83]
	v_mfma_f32_16x16x32_bf16 v[124:127], v[150:153], v[182:185], v[124:127]
	v_mfma_f32_16x16x32_bf16 v[120:123], v[158:161], v[182:185], v[120:123]
	v_mfma_f32_16x16x32_bf16 v[116:119], v[150:153], v[190:193], v[116:119]
	v_mfma_f32_16x16x32_bf16 v[112:115], v[158:161], v[190:193], v[112:115]
	v_mfma_f32_16x16x32_bf16 v[100:103], v[150:153], v[198:201], v[100:103]
	v_mfma_f32_16x16x32_bf16 v[96:99], v[158:161], v[198:201], v[96:99]
	v_mfma_f32_16x16x32_bf16 v[84:87], v[150:153], v[206:209], v[84:87]
	v_mfma_f32_16x16x32_bf16 v[80:83], v[158:161], v[206:209], v[80:83]
	v_mfma_f32_16x16x32_bf16 v[108:111], v[162:165], v[178:181], v[108:111]
	v_mfma_f32_16x16x32_bf16 v[104:107], v[170:173], v[178:181], v[104:107]
	v_mfma_f32_16x16x32_bf16 v[92:95], v[162:165], v[186:189], v[92:95]
	v_mfma_f32_16x16x32_bf16 v[88:91], v[170:173], v[186:189], v[88:91]
	v_mfma_f32_16x16x32_bf16 v[76:79], v[162:165], v[194:197], v[76:79]
	v_mfma_f32_16x16x32_bf16 v[72:75], v[170:173], v[194:197], v[72:75]
	v_mfma_f32_16x16x32_bf16 v[68:71], v[162:165], v[202:205], v[68:71]
	v_mfma_f32_16x16x32_bf16 v[64:67], v[170:173], v[202:205], v[64:67]
	v_mfma_f32_16x16x32_bf16 v[108:111], v[166:169], v[182:185], v[108:111]
	v_mfma_f32_16x16x32_bf16 v[104:107], v[174:177], v[182:185], v[104:107]
	v_mfma_f32_16x16x32_bf16 v[92:95], v[166:169], v[190:193], v[92:95]
	v_mfma_f32_16x16x32_bf16 v[88:91], v[174:177], v[190:193], v[88:91]
	v_mfma_f32_16x16x32_bf16 v[76:79], v[166:169], v[198:201], v[76:79]
	v_mfma_f32_16x16x32_bf16 v[72:75], v[174:177], v[198:201], v[72:75]
	v_mfma_f32_16x16x32_bf16 v[68:71], v[166:169], v[206:209], v[68:71]
	v_mfma_f32_16x16x32_bf16 v[64:67], v[174:177], v[206:209], v[64:67]
	s_barrier
; #define PG8_STAGE(bufoff, gbase, voff) do { _Pragma("unroll") for (int _i = 0; _i < 2; ++_i) \
;         __builtin_amdgcn_global_load_lds((const unsigned*)((const char*)(gbase) + (voff)[_i]), (PG8_LAS unsigned*)(lds + (bufoff) + ldsw + _i * 8192), 16, 0, 0); } while (0)
; #define PG8_STAGE_A(bufoff, gbase, h, nx) do { _Pragma("unroll") for (int _i = 0; _i < 2; ++_i) { \
;         const unsigned vo_ = GA ? ((nx) ? vgn[h][_i] : vgc[h][_i]) : voffA[_i]; \
;         __builtin_amdgcn_global_load_lds((const unsigned*)((const char*)(gbase) + vo_), (PG8_LAS unsigned*)(lds + (bufoff) + ldsw + _i * 8192), 16, 0, 0); } } while (0)
; #define PG8_LDA(dst, b, h) do { _Pragma("unroll") for (int m = 0; m < 4; ++m) _Pragma("unroll") for (int k = 0; k < 2; ++k) dst[m][k] = *(const PG8_LAS bf16x8*)(lds + PG8_SA(b, h) + aoff + m * 2048 + k * 1024); } while (0)
; #define PG8_MMA(ai, bj, At, Bt) do { __builtin_amdgcn_s_setprio(1); _Pragma("unroll") for (int m = 0; m < 4; ++m) _Pragma("unroll") for (int n = 0; n < 2; ++n) _Pragma("unroll") for (int k = 0; k < 2; ++k) \
;         acc[ai][bj][m][n] = __builtin_amdgcn_mfma_f32_16x16x32_bf16(Bt[n][k], At[m][k], acc[ai][bj][m][n], 0, 0, 0); __builtin_amdgcn_s_setprio(0); } while (0)
; #define PG8_WAIT_V(n) asm volatile("s_waitcnt vmcnt(" #n ")" ::: "memory")
; #define PG8_WAIT_L(n) asm volatile("s_waitcnt lgkmcnt(" #n ")" ::: "memory")
; #define PG8_BAR __builtin_amdgcn_s_barrier()
; #define PG8_SCHED __builtin_amdgcn_sched_barrier(0)
; template <class Epi, class Sched>
; __device__ __forceinline__ void gemm_phase(const int WID_, PG8_LAS unsigned char* lds, const Sched& S, const Epi& E) {
;     ...
;             PG8_LDA(At, 1, 1); PG8_STAGE(PG8_SB(1, 0), b3, voffB); PG8_STAGE(PG8_SB(1, 1), b3 + hstepB, voffB); PG8_STAGE_A(PG8_SA(1, 0), a3, 0, last);
;             PG8_WAIT_V(8); PG8_WAIT_L(0); PG8_BAR; PG8_MMA(1, 0, At, B0); PG8_MMA(1, 1, At, B1); PG8_BAR; PG8_SCHED;
;         }
;         if (wr == 0) PG8_BAR;
	s_add_i32 s46, s68, s9
	v_lshl_add_u64 v[210:211], v[210:211], 0, s[2:3]
	s_mov_b32 m0, s46
	ds_read_b128 v[178:181], v145 offset:49152
	ds_read_b128 v[182:185], v145 offset:50176
	ds_read_b128 v[186:189], v145 offset:51200
	ds_read_b128 v[190:193], v145 offset:52224
	ds_read_b128 v[194:197], v145 offset:53248
	ds_read_b128 v[198:201], v145 offset:54272
	ds_read_b128 v[202:205], v145 offset:55296
	ds_read_b128 v[206:209], v145 offset:56320
	global_load_lds_dwordx4 v[210:211], off
	s_add_i32 m0, s46, 0x2000
	s_add_u32 s44, s44, 0x40080
	v_lshl_add_u64 v[210:211], v[212:213], 0, s[2:3]
	s_addc_u32 s45, s45, 0
	s_add_i32 s46, s69, s9
	global_load_lds_dwordx4 v[210:211], off
	v_lshl_add_u64 v[210:211], s[44:45], 0, v[130:131]
	s_mov_b32 m0, s46
	s_nop 0
	global_load_lds_dwordx4 v[210:211], off
	v_lshl_add_u64 v[210:211], s[44:45], 0, v[134:135]
	s_add_i32 m0, s46, 0x2000
	s_nop 0
	global_load_lds_dwordx4 v[210:211], off
	v_lshl_add_u64 v[210:211], v[214:215], 0, s[2:3]
	s_mov_b32 m0, s52
	s_nop 0
	global_load_lds_dwordx4 v[210:211], off
	v_lshl_add_u64 v[210:211], v[216:217], 0, s[2:3]
	s_mov_b32 m0, s53
	s_nop 0
	global_load_lds_dwordx4 v[210:211], off
	s_waitcnt vmcnt(8)
	s_waitcnt lgkmcnt(0)
	s_barrier
	s_waitcnt lgkmcnt(0)
	v_mfma_f32_16x16x32_bf16 v[60:63], v[146:149], v[178:181], v[60:63]
	v_mfma_f32_16x16x32_bf16 v[56:59], v[154:157], v[178:181], v[56:59]
	v_mfma_f32_16x16x32_bf16 v[52:55], v[146:149], v[186:189], v[52:55]
	v_mfma_f32_16x16x32_bf16 v[48:51], v[154:157], v[186:189], v[48:51]
	v_mfma_f32_16x16x32_bf16 v[36:39], v[146:149], v[194:197], v[36:39]
	v_mfma_f32_16x16x32_bf16 v[32:35], v[154:157], v[194:197], v[32:35]
	v_mfma_f32_16x16x32_bf16 v[20:23], v[146:149], v[202:205], v[20:23]
	v_mfma_f32_16x16x32_bf16 v[16:19], v[154:157], v[202:205], v[16:19]
	v_mfma_f32_16x16x32_bf16 v[60:63], v[150:153], v[182:185], v[60:63]
	v_mfma_f32_16x16x32_bf16 v[56:59], v[158:161], v[182:185], v[56:59]
	v_mfma_f32_16x16x32_bf16 v[52:55], v[150:153], v[190:193], v[52:55]
	v_mfma_f32_16x16x32_bf16 v[48:51], v[158:161], v[190:193], v[48:51]
	v_mfma_f32_16x16x32_bf16 v[36:39], v[150:153], v[198:201], v[36:39]
	v_mfma_f32_16x16x32_bf16 v[32:35], v[158:161], v[198:201], v[32:35]
	v_mfma_f32_16x16x32_bf16 v[20:23], v[150:153], v[206:209], v[20:23]
	v_mfma_f32_16x16x32_bf16 v[16:19], v[158:161], v[206:209], v[16:19]
	v_mfma_f32_16x16x32_bf16 v[44:47], v[162:165], v[178:181], v[44:47]
	v_mfma_f32_16x16x32_bf16 v[40:43], v[170:173], v[178:181], v[40:43]
	v_mfma_f32_16x16x32_bf16 v[28:31], v[162:165], v[186:189], v[28:31]
	v_mfma_f32_16x16x32_bf16 v[24:27], v[170:173], v[186:189], v[24:27]
	v_mfma_f32_16x16x32_bf16 v[12:15], v[162:165], v[194:197], v[12:15]
	v_mfma_f32_16x16x32_bf16 v[8:11], v[170:173], v[194:197], v[8:11]
	v_mfma_f32_16x16x32_bf16 v[4:7], v[162:165], v[202:205], v[4:7]
	v_mfma_f32_16x16x32_bf16 v[0:3], v[170:173], v[202:205], v[0:3]
	v_mfma_f32_16x16x32_bf16 v[44:47], v[166:169], v[182:185], v[44:47]
	v_mfma_f32_16x16x32_bf16 v[40:43], v[174:177], v[182:185], v[40:43]
	v_mfma_f32_16x16x32_bf16 v[28:31], v[166:169], v[190:193], v[28:31]
	v_mfma_f32_16x16x32_bf16 v[24:27], v[174:177], v[190:193], v[24:27]
	v_mfma_f32_16x16x32_bf16 v[12:15], v[166:169], v[198:201], v[12:15]
	v_mfma_f32_16x16x32_bf16 v[8:11], v[174:177], v[198:201], v[8:11]
	v_mfma_f32_16x16x32_bf16 v[4:7], v[166:169], v[206:209], v[4:7]
	v_mfma_f32_16x16x32_bf16 v[0:3], v[174:177], v[206:209], v[0:3]
	s_barrier
	s_add_i32 s67, s67, 2
	s_add_u32 s42, s42, 0x100
	s_addc_u32 s43, s43, 0
	s_add_u32 s63, s63, 0x100
	s_addc_u32 s66, s66, 0
	s_cmp_gt_u32 s67, 13
	s_cbranch_scc0 .LBB0_1786
	s_and_b64 vcc, exec, s[4:5]
	s_cbranch_vccz .LBB0_1789
	s_barrier

; #define PG8_STAGE(bufoff, gbase, voff) do { _Pragma("unroll") for (int _i = 0; _i < 2; ++_i) \
;         __builtin_amdgcn_global_load_lds((const unsigned*)((const char*)(gbase) + (voff)[_i]), (PG8_LAS unsigned*)(lds + (bufoff) + ldsw + _i * 8192), 16, 0, 0); } while (0)
; #define PG8_STAGE_A(bufoff, gbase, h, nx) do { _Pragma("unroll") for (int _i = 0; _i < 2; ++_i) { \
;         const unsigned vo_ = GA ? ((nx) ? vgn[h][_i] : vgc[h][_i]) : voffA[_i]; \
;         __builtin_amdgcn_global_load_lds((const unsigned*)((const char*)(gbase) + vo_), (PG8_LAS unsigned*)(lds + (bufoff) + ldsw + _i * 8192), 16, 0, 0); } } while (0)
; #define PG8_LDA(dst, b, h) do { _Pragma("unroll") for (int m = 0; m < 4; ++m) _Pragma("unroll") for (int k = 0; k < 2; ++k) dst[m][k] = *(const PG8_LAS bf16x8*)(lds + PG8_SA(b, h) + aoff + m * 2048 + k * 1024); } while (0)
; #define PG8_LDB(dst, b, h) do { _Pragma("unroll") for (int n = 0; n < 2; ++n) _Pragma("unroll") for (int k = 0; k < 2; ++k) dst[n][k] = *(const PG8_LAS bf16x8*)(lds + PG8_SB(b, h) + boff + n * 2048 + k * 1024); } while (0)
; #define PG8_WAIT_V(n) asm volatile("s_waitcnt vmcnt(" #n ")" ::: "memory")
; #define PG8_WAIT_L(n) asm volatile("s_waitcnt lgkmcnt(" #n ")" ::: "memory")
; #define PG8_BAR __builtin_amdgcn_s_barrier()
; #define PG8_SCHED __builtin_amdgcn_sched_barrier(0)
; template <class Epi, class Sched>
; __device__ __forceinline__ void gemm_phase(const int WID_, PG8_LAS unsigned char* lds, const Sched& S, const Epi& E) {
;     ...
;         for (int t = 0; t < nt; t += 2) {
;             const bool last = (t == nt - 2);
;             const char* a1 = cA + (size_t)(t + 1) * kstep;
;             const char* a2 = last ? nA : cA + (size_t)(t + 2) * kstep; const char* b2 = last ? nB : cB + (size_t)(t + 2) * kstep;
;             const char* a3 = a2 + kstep; const char* b3 = b2 + kstep;
;             PG8_LDB(B0, 0, 0); PG8_LDB(B1, 0, 1); PG8_SCHED; PG8_LDA(At, 0, 0); PG8_STAGE_A(PG8_SA(1, 1), a1 + hstepA, 1, false);
;             PG8_WAIT_V(8); PG8_WAIT_L(0); PG8_BAR; PG8_MMA(0, 0, At, B0); PG8_MMA(0, 1, At, B1); PG8_BAR; PG8_SCHED;
;             PG8_LDA(At, 0, 1); PG8_STAGE(PG8_SB(0, 0), b2, voffB); PG8_STAGE(PG8_SB(0, 1), b2 + hstepB, voffB); PG8_STAGE_A(PG8_SA(0, 0), a2, 0, last);
;             PG8_WAIT_V(8); PG8_WAIT_L(0); PG8_BAR; PG8_MMA(1, 0, At, B0); PG8_MMA(1, 1, At, B1); PG8_BAR; PG8_SCHED;
.LBB0_1810:
	ds_read_b128 v[146:149], v143
	ds_read_b128 v[150:153], v143 offset:1024
	ds_read_b128 v[154:157], v143 offset:2048
	ds_read_b128 v[158:161], v143 offset:3072
	ds_read_b128 v[162:165], v144
	ds_read_b128 v[166:169], v144 offset:1024
	ds_read_b128 v[170:173], v144 offset:2048
	ds_read_b128 v[174:177], v144 offset:3072
	s_add_u32 s44, s42, 0xfffc0080
	s_addc_u32 s45, s43, -1
	s_cmp_eq_u32 s68, 12
	s_cselect_b32 s47, s37, s45
	s_cselect_b32 s46, s62, s44
	s_cselect_b32 s45, s23, s67
	s_cselect_b32 s44, s63, s66
	v_lshl_add_u64 v[210:211], s[42:43], 0, v[136:137]
	s_add_i32 m0, s48, 0xc000
	ds_read_b128 v[178:181], v145
	ds_read_b128 v[182:185], v145 offset:1024
	ds_read_b128 v[186:189], v145 offset:2048
	ds_read_b128 v[190:193], v145 offset:3072
	ds_read_b128 v[194:197], v145 offset:4096
	ds_read_b128 v[198:201], v145 offset:5120
	ds_read_b128 v[202:205], v145 offset:6144
	ds_read_b128 v[206:209], v145 offset:7168
	global_load_lds_dwordx4 v[210:211], off
	v_lshl_add_u64 v[210:211], s[42:43], 0, v[138:139]
	s_add_i32 m0, s48, 0xe000
	s_nop 0
	global_load_lds_dwordx4 v[210:211], off
	s_waitcnt vmcnt(8)
	s_waitcnt lgkmcnt(0)
	s_barrier
	s_waitcnt lgkmcnt(0)
	v_mfma_f32_16x16x32_bf16 v[124:127], v[146:149], v[178:181], v[124:127]
	v_mfma_f32_16x16x32_bf16 v[120:123], v[154:157], v[178:181], v[120:123]
	v_mfma_f32_16x16x32_bf16 v[116:119], v[146:149], v[186:189], v[116:119]
	v_mfma_f32_16x16x32_bf16 v[112:115], v[154:157], v[186:189], v[112:115]
	v_mfma_f32_16x16x32_bf16 v[100:103], v[146:149], v[194:197], v[100:103]
	v_mfma_f32_16x16x32_bf16 v[96:99], v[154:157], v[194:197], v[96:99]
	v_mfma_f32_16x16x32_bf16 v[84:87], v[146:149], v[202:205], v[84:87]
	v_mfma_f32_16x16x32_bf16 v[80:83], v[154:157], v[202:205], v[80:83]
	v_mfma_f32_16x16x32_bf16 v[124:127], v[150:153], v[182:185], v[124:127]
	v_mfma_f32_16x16x32_bf16 v[120:123], v[158:161], v[182:185], v[120:123]
	v_mfma_f32_16x16x32_bf16 v[116:119], v[150:153], v[190:193], v[116:119]
	v_mfma_f32_16x16x32_bf16 v[112:115], v[158:161], v[190:193], v[112:115]
	v_mfma_f32_16x16x32_bf16 v[100:103], v[150:153], v[198:201], v[100:103]
	v_mfma_f32_16x16x32_bf16 v[96:99], v[158:161], v[198:201], v[96:99]
	v_mfma_f32_16x16x32_bf16 v[84:87], v[150:153], v[206:209], v[84:87]
	v_mfma_f32_16x16x32_bf16 v[80:83], v[158:161], v[206:209], v[80:83]
	v_mfma_f32_16x16x32_bf16 v[108:111], v[162:165], v[178:181], v[108:111]
	v_mfma_f32_16x16x32_bf16 v[104:107], v[170:173], v[178:181], v[104:107]
	v_mfma_f32_16x16x32_bf16 v[92:95], v[162:165], v[186:189], v[92:95]
	v_mfma_f32_16x16x32_bf16 v[88:91], v[170:173], v[186:189], v[88:91]
	v_mfma_f32_16x16x32_bf16 v[76:79], v[162:165], v[194:197], v[76:79]
	v_mfma_f32_16x16x32_bf16 v[72:75], v[170:173], v[194:197], v[72:75]
	v_mfma_f32_16x16x32_bf16 v[68:71], v[162:165], v[202:205], v[68:71]
	v_mfma_f32_16x16x32_bf16 v[64:67], v[170:173], v[202:205], v[64:67]
	v_mfma_f32_16x16x32_bf16 v[108:111], v[166:169], v[182:185], v[108:111]
	v_mfma_f32_16x16x32_bf16 v[104:107], v[174:177], v[182:185], v[104:107]
	v_mfma_f32_16x16x32_bf16 v[92:95], v[166:169], v[190:193], v[92:95]
	v_mfma_f32_16x16x32_bf16 v[88:91], v[174:177], v[190:193], v[88:91]
	v_mfma_f32_16x16x32_bf16 v[76:79], v[166:169], v[198:201], v[76:79]
	v_mfma_f32_16x16x32_bf16 v[72:75], v[174:177], v[198:201], v[72:75]
	v_mfma_f32_16x16x32_bf16 v[68:71], v[166:169], v[206:209], v[68:71]
	v_mfma_f32_16x16x32_bf16 v[64:67], v[174:177], v[206:209], v[64:67]
	s_barrier
	s_add_i32 s69, s60, s33
	v_lshl_add_u64 v[210:211], s[44:45], 0, v[130:131]
	s_mov_b32 m0, s69
	ds_read_b128 v[178:181], v145 offset:16384
	ds_read_b128 v[182:185], v145 offset:17408
	ds_read_b128 v[186:189], v145 offset:18432
	ds_read_b128 v[190:193], v145 offset:19456
	ds_read_b128 v[194:197], v145 offset:20480
	ds_read_b128 v[198:201], v145 offset:21504
	ds_read_b128 v[202:205], v145 offset:22528
	ds_read_b128 v[206:209], v145 offset:23552
	global_load_lds_dwordx4 v[210:211], off
	s_add_i32 m0, s69, 0x2000
	s_add_u32 s70, s44, 0x40000
	v_lshl_add_u64 v[212:213], s[44:45], 0, v[134:135]
	s_addc_u32 s71, s45, 0
	s_add_i32 s69, s61, s33
	global_load_lds_dwordx4 v[212:213], off
	v_lshl_add_u64 v[214:215], s[70:71], 0, v[130:131]
	s_mov_b32 m0, s69
	v_lshl_add_u64 v[216:217], s[46:47], 0, v[132:133]
	global_load_lds_dwordx4 v[214:215], off
	v_lshl_add_u64 v[214:215], s[70:71], 0, v[134:135]
	s_add_i32 m0, s69, 0x2000
	s_nop 0
	global_load_lds_dwordx4 v[214:215], off
	v_lshl_add_u64 v[214:215], s[46:47], 0, v[128:129]
	s_mov_b32 m0, s48
	s_nop 0
	global_load_lds_dwordx4 v[214:215], off
	s_mov_b32 m0, s49
	s_nop 0
	global_load_lds_dwordx4 v[216:217], off
	s_waitcnt vmcnt(8)
	s_waitcnt lgkmcnt(0)
	s_barrier
; #define PG8_STAGE_A(bufoff, gbase, h, nx) do { _Pragma("unroll") for (int _i = 0; _i < 2; ++_i) { \
;         const unsigned vo_ = GA ? ((nx) ? vgn[h][_i] : vgc[h][_i]) : voffA[_i]; \
;         __builtin_amdgcn_global_load_lds((const unsigned*)((const char*)(gbase) + vo_), (PG8_LAS unsigned*)(lds + (bufoff) + ldsw + _i * 8192), 16, 0, 0); } } while (0)
; #define PG8_LDA(dst, b, h) do { _Pragma("unroll") for (int m = 0; m < 4; ++m) _Pragma("unroll") for (int k = 0; k < 2; ++k) dst[m][k] = *(const PG8_LAS bf16x8*)(lds + PG8_SA(b, h) + aoff + m * 2048 + k * 1024); } while (0)
; #define PG8_LDB(dst, b, h) do { _Pragma("unroll") for (int n = 0; n < 2; ++n) _Pragma("unroll") for (int k = 0; k < 2; ++k) dst[n][k] = *(const PG8_LAS bf16x8*)(lds + PG8_SB(b, h) + boff + n * 2048 + k * 1024); } while (0)
; #define PG8_MMA(ai, bj, At, Bt) do { __builtin_amdgcn_s_setprio(1); _Pragma("unroll") for (int m = 0; m < 4; ++m) _Pragma("unroll") for (int n = 0; n < 2; ++n) _Pragma("unroll") for (int k = 0; k < 2; ++k) \
;         acc[ai][bj][m][n] = __builtin_amdgcn_mfma_f32_16x16x32_bf16(Bt[n][k], At[m][k], acc[ai][bj][m][n], 0, 0, 0); __builtin_amdgcn_s_setprio(0); } while (0)
; #define PG8_WAIT_V(n) asm volatile("s_waitcnt vmcnt(" #n ")" ::: "memory")
; #define PG8_WAIT_L(n) asm volatile("s_waitcnt lgkmcnt(" #n ")" ::: "memory")
; #define PG8_BAR __builtin_amdgcn_s_barrier()
; #define PG8_SCHED __builtin_amdgcn_sched_barrier(0)
; template <class Epi, class Sched>
; __device__ __forceinline__ void gemm_phase(const int WID_, PG8_LAS unsigned char* lds, const Sched& S, const Epi& E) {
;     ...
;             PG8_WAIT_V(8); PG8_WAIT_L(0); PG8_BAR; PG8_MMA(1, 0, At, B0); PG8_MMA(1, 1, At, B1); PG8_BAR; PG8_SCHED;
;             PG8_LDB(B0, 1, 0); PG8_LDB(B1, 1, 1); PG8_SCHED; PG8_LDA(At, 1, 0); PG8_STAGE_A(PG8_SA(0, 1), a2 + hstepA, 1, last);
;             PG8_WAIT_V(8); PG8_WAIT_L(0); PG8_BAR; PG8_MMA(0, 0, At, B0); PG8_MMA(0, 1, At, B1); PG8_BAR; PG8_SCHED;
	s_waitcnt lgkmcnt(0)
	v_mfma_f32_16x16x32_bf16 v[60:63], v[146:149], v[178:181], v[60:63]
	v_mfma_f32_16x16x32_bf16 v[56:59], v[154:157], v[178:181], v[56:59]
	v_mfma_f32_16x16x32_bf16 v[52:55], v[146:149], v[186:189], v[52:55]
	v_mfma_f32_16x16x32_bf16 v[48:51], v[154:157], v[186:189], v[48:51]
	v_mfma_f32_16x16x32_bf16 v[36:39], v[146:149], v[194:197], v[36:39]
	v_mfma_f32_16x16x32_bf16 v[32:35], v[154:157], v[194:197], v[32:35]
	v_mfma_f32_16x16x32_bf16 v[20:23], v[146:149], v[202:205], v[20:23]
	v_mfma_f32_16x16x32_bf16 v[16:19], v[154:157], v[202:205], v[16:19]
	v_mfma_f32_16x16x32_bf16 v[60:63], v[150:153], v[182:185], v[60:63]
	v_mfma_f32_16x16x32_bf16 v[56:59], v[158:161], v[182:185], v[56:59]
	v_mfma_f32_16x16x32_bf16 v[52:55], v[150:153], v[190:193], v[52:55]
	v_mfma_f32_16x16x32_bf16 v[48:51], v[158:161], v[190:193], v[48:51]
	v_mfma_f32_16x16x32_bf16 v[36:39], v[150:153], v[198:201], v[36:39]
	v_mfma_f32_16x16x32_bf16 v[32:35], v[158:161], v[198:201], v[32:35]
	v_mfma_f32_16x16x32_bf16 v[20:23], v[150:153], v[206:209], v[20:23]
	v_mfma_f32_16x16x32_bf16 v[16:19], v[158:161], v[206:209], v[16:19]
	v_mfma_f32_16x16x32_bf16 v[44:47], v[162:165], v[178:181], v[44:47]
	v_mfma_f32_16x16x32_bf16 v[40:43], v[170:173], v[178:181], v[40:43]
	v_mfma_f32_16x16x32_bf16 v[28:31], v[162:165], v[186:189], v[28:31]
	v_mfma_f32_16x16x32_bf16 v[24:27], v[170:173], v[186:189], v[24:27]
	v_mfma_f32_16x16x32_bf16 v[12:15], v[162:165], v[194:197], v[12:15]
	v_mfma_f32_16x16x32_bf16 v[8:11], v[170:173], v[194:197], v[8:11]
	v_mfma_f32_16x16x32_bf16 v[4:7], v[162:165], v[202:205], v[4:7]
	v_mfma_f32_16x16x32_bf16 v[0:3], v[170:173], v[202:205], v[0:3]
	v_mfma_f32_16x16x32_bf16 v[44:47], v[166:169], v[182:185], v[44:47]
	v_mfma_f32_16x16x32_bf16 v[40:43], v[174:177], v[182:185], v[40:43]
	v_mfma_f32_16x16x32_bf16 v[28:31], v[166:169], v[190:193], v[28:31]
	v_mfma_f32_16x16x32_bf16 v[24:27], v[174:177], v[190:193], v[24:27]
	v_mfma_f32_16x16x32_bf16 v[12:15], v[166:169], v[198:201], v[12:15]
	v_mfma_f32_16x16x32_bf16 v[8:11], v[174:177], v[198:201], v[8:11]
	v_mfma_f32_16x16x32_bf16 v[4:7], v[166:169], v[206:209], v[4:7]
	v_mfma_f32_16x16x32_bf16 v[0:3], v[174:177], v[206:209], v[0:3]
	s_barrier
	s_add_i32 s69, 0, 0x18000
	s_add_i32 s70, 0, 0x1c000
	v_add_u32_e32 v158, s69, v141
	v_add_u32_e32 v174, s70, v141
	ds_read_b128 v[146:149], v158
	ds_read_b128 v[150:153], v158 offset:1024
	ds_read_b128 v[154:157], v158 offset:2048
	ds_read_b128 v[158:161], v158 offset:3072
	ds_read_b128 v[162:165], v174
	ds_read_b128 v[166:169], v174 offset:1024
	ds_read_b128 v[170:173], v174 offset:2048
	ds_read_b128 v[174:177], v174 offset:3072
	s_add_u32 s46, s46, 0x40000
	s_addc_u32 s47, s47, 0
	s_mov_b32 m0, s50
	v_lshl_add_u64 v[218:219], s[46:47], 0, v[128:129]
	ds_read_b128 v[178:181], v145 offset:32768
	ds_read_b128 v[182:185], v145 offset:33792
	ds_read_b128 v[186:189], v145 offset:34816
	ds_read_b128 v[190:193], v145 offset:35840
	ds_read_b128 v[194:197], v145 offset:36864
	ds_read_b128 v[198:201], v145 offset:37888
	ds_read_b128 v[202:205], v145 offset:38912
	ds_read_b128 v[206:209], v145 offset:39936
	global_load_lds_dwordx4 v[218:219], off
	v_lshl_add_u64 v[218:219], s[46:47], 0, v[132:133]
	s_mov_b32 m0, s51
	s_nop 0
	global_load_lds_dwordx4 v[218:219], off
	s_waitcnt vmcnt(8)
	s_waitcnt lgkmcnt(0)
	s_barrier
	s_waitcnt lgkmcnt(0)
	v_mfma_f32_16x16x32_bf16 v[124:127], v[146:149], v[178:181], v[124:127]
	v_mfma_f32_16x16x32_bf16 v[120:123], v[154:157], v[178:181], v[120:123]
	v_mfma_f32_16x16x32_bf16 v[116:119], v[146:149], v[186:189], v[116:119]
	v_mfma_f32_16x16x32_bf16 v[112:115], v[154:157], v[186:189], v[112:115]
	v_mfma_f32_16x16x32_bf16 v[100:103], v[146:149], v[194:197], v[100:103]
	v_mfma_f32_16x16x32_bf16 v[96:99], v[154:157], v[194:197], v[96:99]
	v_mfma_f32_16x16x32_bf16 v[84:87], v[146:149], v[202:205], v[84:87]
	v_mfma_f32_16x16x32_bf16 v[80:83], v[154:157], v[202:205], v[80:83]
	v_mfma_f32_16x16x32_bf16 v[124:127], v[150:153], v[182:185], v[124:127]
	v_mfma_f32_16x16x32_bf16 v[120:123], v[158:161], v[182:185], v[120:123]
	v_mfma_f32_16x16x32_bf16 v[116:119], v[150:153], v[190:193], v[116:119]
	v_mfma_f32_16x16x32_bf16 v[112:115], v[158:161], v[190:193], v[112:115]
	v_mfma_f32_16x16x32_bf16 v[100:103], v[150:153], v[198:201], v[100:103]
	v_mfma_f32_16x16x32_bf16 v[96:99], v[158:161], v[198:201], v[96:99]
	v_mfma_f32_16x16x32_bf16 v[84:87], v[150:153], v[206:209], v[84:87]
	v_mfma_f32_16x16x32_bf16 v[80:83], v[158:161], v[206:209], v[80:83]
	v_mfma_f32_16x16x32_bf16 v[108:111], v[162:165], v[178:181], v[108:111]
	v_mfma_f32_16x16x32_bf16 v[104:107], v[170:173], v[178:181], v[104:107]
	v_mfma_f32_16x16x32_bf16 v[92:95], v[162:165], v[186:189], v[92:95]
	v_mfma_f32_16x16x32_bf16 v[88:91], v[170:173], v[186:189], v[88:91]
	v_mfma_f32_16x16x32_bf16 v[76:79], v[162:165], v[194:197], v[76:79]
	v_mfma_f32_16x16x32_bf16 v[72:75], v[170:173], v[194:197], v[72:75]
	v_mfma_f32_16x16x32_bf16 v[68:71], v[162:165], v[202:205], v[68:71]
	v_mfma_f32_16x16x32_bf16 v[64:67], v[170:173], v[202:205], v[64:67]
	v_mfma_f32_16x16x32_bf16 v[108:111], v[166:169], v[182:185], v[108:111]
	v_mfma_f32_16x16x32_bf16 v[104:107], v[174:177], v[182:185], v[104:107]
	v_mfma_f32_16x16x32_bf16 v[92:95], v[166:169], v[190:193], v[92:95]
	v_mfma_f32_16x16x32_bf16 v[88:91], v[174:177], v[190:193], v[88:91]
	v_mfma_f32_16x16x32_bf16 v[76:79], v[166:169], v[198:201], v[76:79]
	v_mfma_f32_16x16x32_bf16 v[72:75], v[174:177], v[198:201], v[72:75]
	v_mfma_f32_16x16x32_bf16 v[68:71], v[166:169], v[206:209], v[68:71]
	v_mfma_f32_16x16x32_bf16 v[64:67], v[174:177], v[206:209], v[64:67]
	s_barrier
; #define PG8_STAGE(bufoff, gbase, voff) do { _Pragma("unroll") for (int _i = 0; _i < 2; ++_i) \
;         __builtin_amdgcn_global_load_lds((const unsigned*)((const char*)(gbase) + (voff)[_i]), (PG8_LAS unsigned*)(lds + (bufoff) + ldsw + _i * 8192), 16, 0, 0); } while (0)
; #define PG8_STAGE_A(bufoff, gbase, h, nx) do { _Pragma("unroll") for (int _i = 0; _i < 2; ++_i) { \
;         const unsigned vo_ = GA ? ((nx) ? vgn[h][_i] : vgc[h][_i]) : voffA[_i]; \
;         __builtin_amdgcn_global_load_lds((const unsigned*)((const char*)(gbase) + vo_), (PG8_LAS unsigned*)(lds + (bufoff) + ldsw + _i * 8192), 16, 0, 0); } } while (0)
; #define PG8_LDA(dst, b, h) do { _Pragma("unroll") for (int m = 0; m < 4; ++m) _Pragma("unroll") for (int k = 0; k < 2; ++k) dst[m][k] = *(const PG8_LAS bf16x8*)(lds + PG8_SA(b, h) + aoff + m * 2048 + k * 1024); } while (0)
; #define PG8_MMA(ai, bj, At, Bt) do { __builtin_amdgcn_s_setprio(1); _Pragma("unroll") for (int m = 0; m < 4; ++m) _Pragma("unroll") for (int n = 0; n < 2; ++n) _Pragma("unroll") for (int k = 0; k < 2; ++k) \
;         acc[ai][bj][m][n] = __builtin_amdgcn_mfma_f32_16x16x32_bf16(Bt[n][k], At[m][k], acc[ai][bj][m][n], 0, 0, 0); __builtin_amdgcn_s_setprio(0); } while (0)
; #define PG8_WAIT_V(n) asm volatile("s_waitcnt vmcnt(" #n ")" ::: "memory")
; #define PG8_WAIT_L(n) asm volatile("s_waitcnt lgkmcnt(" #n ")" ::: "memory")
; #define PG8_BAR __builtin_amdgcn_s_barrier()
; #define PG8_SCHED __builtin_amdgcn_sched_barrier(0)
; template <class Epi, class Sched>
; __device__ __forceinline__ void gemm_phase(const int WID_, PG8_LAS unsigned char* lds, const Sched& S, const Epi& E) {
;     ...
;             PG8_LDA(At, 1, 1); PG8_STAGE(PG8_SB(1, 0), b3, voffB); PG8_STAGE(PG8_SB(1, 1), b3 + hstepB, voffB); PG8_STAGE_A(PG8_SA(1, 0), a3, 0, last);
;             PG8_WAIT_V(8); PG8_WAIT_L(0); PG8_BAR; PG8_MMA(1, 0, At, B0); PG8_MMA(1, 1, At, B1); PG8_BAR; PG8_SCHED;
;         }
;         if (wr == 0) PG8_BAR;
	s_add_i32 s46, s69, s33
	v_lshl_add_u64 v[210:211], v[210:211], 0, s[2:3]
	s_mov_b32 m0, s46
	ds_read_b128 v[178:181], v145 offset:49152
	ds_read_b128 v[182:185], v145 offset:50176
	ds_read_b128 v[186:189], v145 offset:51200
	ds_read_b128 v[190:193], v145 offset:52224
	ds_read_b128 v[194:197], v145 offset:53248
	ds_read_b128 v[198:201], v145 offset:54272
	ds_read_b128 v[202:205], v145 offset:55296
	ds_read_b128 v[206:209], v145 offset:56320
	global_load_lds_dwordx4 v[210:211], off
	s_add_i32 m0, s46, 0x2000
	s_add_u32 s44, s44, 0x40080
	v_lshl_add_u64 v[210:211], v[212:213], 0, s[2:3]
	s_addc_u32 s45, s45, 0
	s_add_i32 s46, s70, s33
	global_load_lds_dwordx4 v[210:211], off
	v_lshl_add_u64 v[210:211], s[44:45], 0, v[130:131]
	s_mov_b32 m0, s46
	s_nop 0
	global_load_lds_dwordx4 v[210:211], off
	v_lshl_add_u64 v[210:211], s[44:45], 0, v[134:135]
	s_add_i32 m0, s46, 0x2000
	s_nop 0
	global_load_lds_dwordx4 v[210:211], off
	v_lshl_add_u64 v[210:211], v[214:215], 0, s[2:3]
	s_mov_b32 m0, s53
	s_nop 0
	global_load_lds_dwordx4 v[210:211], off
	v_lshl_add_u64 v[210:211], v[216:217], 0, s[2:3]
	s_mov_b32 m0, s58
	s_nop 0
	global_load_lds_dwordx4 v[210:211], off
	s_waitcnt vmcnt(8)
	s_waitcnt lgkmcnt(0)
	s_barrier
	s_waitcnt lgkmcnt(0)
	v_mfma_f32_16x16x32_bf16 v[60:63], v[146:149], v[178:181], v[60:63]
	v_mfma_f32_16x16x32_bf16 v[56:59], v[154:157], v[178:181], v[56:59]
	v_mfma_f32_16x16x32_bf16 v[52:55], v[146:149], v[186:189], v[52:55]
	v_mfma_f32_16x16x32_bf16 v[48:51], v[154:157], v[186:189], v[48:51]
	v_mfma_f32_16x16x32_bf16 v[36:39], v[146:149], v[194:197], v[36:39]
	v_mfma_f32_16x16x32_bf16 v[32:35], v[154:157], v[194:197], v[32:35]
	v_mfma_f32_16x16x32_bf16 v[20:23], v[146:149], v[202:205], v[20:23]
	v_mfma_f32_16x16x32_bf16 v[16:19], v[154:157], v[202:205], v[16:19]
	v_mfma_f32_16x16x32_bf16 v[60:63], v[150:153], v[182:185], v[60:63]
	v_mfma_f32_16x16x32_bf16 v[56:59], v[158:161], v[182:185], v[56:59]
	v_mfma_f32_16x16x32_bf16 v[52:55], v[150:153], v[190:193], v[52:55]
	v_mfma_f32_16x16x32_bf16 v[48:51], v[158:161], v[190:193], v[48:51]
	v_mfma_f32_16x16x32_bf16 v[36:39], v[150:153], v[198:201], v[36:39]
	v_mfma_f32_16x16x32_bf16 v[32:35], v[158:161], v[198:201], v[32:35]
	v_mfma_f32_16x16x32_bf16 v[20:23], v[150:153], v[206:209], v[20:23]
	v_mfma_f32_16x16x32_bf16 v[16:19], v[158:161], v[206:209], v[16:19]
	v_mfma_f32_16x16x32_bf16 v[44:47], v[162:165], v[178:181], v[44:47]
	v_mfma_f32_16x16x32_bf16 v[40:43], v[170:173], v[178:181], v[40:43]
	v_mfma_f32_16x16x32_bf16 v[28:31], v[162:165], v[186:189], v[28:31]
	v_mfma_f32_16x16x32_bf16 v[24:27], v[170:173], v[186:189], v[24:27]
	v_mfma_f32_16x16x32_bf16 v[12:15], v[162:165], v[194:197], v[12:15]
	v_mfma_f32_16x16x32_bf16 v[8:11], v[170:173], v[194:197], v[8:11]
	v_mfma_f32_16x16x32_bf16 v[4:7], v[162:165], v[202:205], v[4:7]
	v_mfma_f32_16x16x32_bf16 v[0:3], v[170:173], v[202:205], v[0:3]
	v_mfma_f32_16x16x32_bf16 v[44:47], v[166:169], v[182:185], v[44:47]
	v_mfma_f32_16x16x32_bf16 v[40:43], v[174:177], v[182:185], v[40:43]
	v_mfma_f32_16x16x32_bf16 v[28:31], v[166:169], v[190:193], v[28:31]
	v_mfma_f32_16x16x32_bf16 v[24:27], v[174:177], v[190:193], v[24:27]
	v_mfma_f32_16x16x32_bf16 v[12:15], v[166:169], v[198:201], v[12:15]
	v_mfma_f32_16x16x32_bf16 v[8:11], v[174:177], v[198:201], v[8:11]
	v_mfma_f32_16x16x32_bf16 v[4:7], v[166:169], v[206:209], v[4:7]
	v_mfma_f32_16x16x32_bf16 v[0:3], v[174:177], v[206:209], v[0:3]
	s_barrier
	s_add_i32 s68, s68, 2
	s_add_u32 s42, s42, 0x100
	s_addc_u32 s43, s43, 0
	s_add_u32 s66, s66, 0x100
	s_addc_u32 s67, s67, 0
	s_cmp_gt_u32 s68, 13
	s_cbranch_scc0 .LBB0_1810
	s_and_b64 vcc, exec, s[4:5]
	s_cbranch_vccz .LBB0_1813
	s_barrier

; #define PG8_STAGE(bufoff, gbase, voff) do { _Pragma("unroll") for (int _i = 0; _i < 2; ++_i) \
;         __builtin_amdgcn_global_load_lds((const unsigned*)((const char*)(gbase) + (voff)[_i]), (PG8_LAS unsigned*)(lds + (bufoff) + ldsw + _i * 8192), 16, 0, 0); } while (0)
; #define PG8_STAGE_A(bufoff, gbase, h, nx) do { _Pragma("unroll") for (int _i = 0; _i < 2; ++_i) { \
;         const unsigned vo_ = GA ? ((nx) ? vgn[h][_i] : vgc[h][_i]) : voffA[_i]; \
;         __builtin_amdgcn_global_load_lds((const unsigned*)((const char*)(gbase) + vo_), (PG8_LAS unsigned*)(lds + (bufoff) + ldsw + _i * 8192), 16, 0, 0); } } while (0)
; #define PG8_LDA(dst, b, h) do { _Pragma("unroll") for (int m = 0; m < 4; ++m) _Pragma("unroll") for (int k = 0; k < 2; ++k) dst[m][k] = *(const PG8_LAS bf16x8*)(lds + PG8_SA(b, h) + aoff + m * 2048 + k * 1024); } while (0)
; #define PG8_LDB(dst, b, h) do { _Pragma("unroll") for (int n = 0; n < 2; ++n) _Pragma("unroll") for (int k = 0; k < 2; ++k) dst[n][k] = *(const PG8_LAS bf16x8*)(lds + PG8_SB(b, h) + boff + n * 2048 + k * 1024); } while (0)
; #define PG8_WAIT_V(n) asm volatile("s_waitcnt vmcnt(" #n ")" ::: "memory")
; #define PG8_WAIT_L(n) asm volatile("s_waitcnt lgkmcnt(" #n ")" ::: "memory")
; #define PG8_BAR __builtin_amdgcn_s_barrier()
; #define PG8_SCHED __builtin_amdgcn_sched_barrier(0)
; template <class Epi, class Sched>
; __device__ __forceinline__ void gemm_phase(const int WID_, PG8_LAS unsigned char* lds, const Sched& S, const Epi& E) {
;     ...
;         for (int t = 0; t < nt; t += 2) {
;             const bool last = (t == nt - 2);
;             const char* a1 = cA + (size_t)(t + 1) * kstep;
;             const char* a2 = last ? nA : cA + (size_t)(t + 2) * kstep; const char* b2 = last ? nB : cB + (size_t)(t + 2) * kstep;
;             const char* a3 = a2 + kstep; const char* b3 = b2 + kstep;
;             PG8_LDB(B0, 0, 0); PG8_LDB(B1, 0, 1); PG8_SCHED; PG8_LDA(At, 0, 0); PG8_STAGE_A(PG8_SA(1, 1), a1 + hstepA, 1, false);
;             PG8_WAIT_V(8); PG8_WAIT_L(0); PG8_BAR; PG8_MMA(0, 0, At, B0); PG8_MMA(0, 1, At, B1); PG8_BAR; PG8_SCHED;
;             PG8_LDA(At, 0, 1); PG8_STAGE(PG8_SB(0, 0), b2, voffB); PG8_STAGE(PG8_SB(0, 1), b2 + hstepB, voffB); PG8_STAGE_A(PG8_SA(0, 0), a2, 0, last);
;             PG8_WAIT_V(8); PG8_WAIT_L(0); PG8_BAR; PG8_MMA(1, 0, At, B0); PG8_MMA(1, 1, At, B1); PG8_BAR; PG8_SCHED;
.LBB0_1892:
	s_add_u32 s47, s50, s41
	s_addc_u32 s70, s51, 0
	s_add_u32 s66, s47, 0x100
	s_addc_u32 s67, s70, 0
	s_and_b64 s[62:63], s[60:61], exec
	s_cselect_b32 s67, s43, s67
	s_cselect_b32 s66, s42, s66
	s_add_u32 s41, s48, s41
	s_addc_u32 s62, s49, 0
	s_add_u32 s41, s41, 0x100
	s_addc_u32 s62, s62, 0
	s_and_b64 s[60:61], s[60:61], exec
	ds_read_b128 v[128:131], v157
	ds_read_b128 v[142:145], v157 offset:1024
	ds_read_b128 v[146:149], v157 offset:2048
	ds_read_b128 v[150:153], v157 offset:3072
	ds_read_b128 v[160:163], v158
	ds_read_b128 v[164:167], v158 offset:1024
	ds_read_b128 v[168:171], v158 offset:2048
	ds_read_b128 v[172:175], v158 offset:3072
	s_cselect_b32 s69, s45, s62
	s_cselect_b32 s68, s44, s41
	s_add_u32 s72, s47, 0x10080
	s_addc_u32 s73, s70, 0
	s_add_u32 s70, s68, 0x10000
	s_addc_u32 s71, s69, 0
	s_add_i32 s86, s80, 0x2000
	s_add_i32 s85, 0, 0x18000
	s_add_i32 s84, 0, 0x1c000
	s_add_u32 s62, s66, 0x10000
	s_addc_u32 s63, s67, 0
	s_add_i32 s83, s85, s8
	s_add_i32 s47, s83, 0x2000
	s_add_u32 s60, s68, 0x10080
	s_addc_u32 s61, s69, 0
	s_add_i32 s82, s84, s8
	s_add_i32 s41, s82, 0x2000
	s_mov_b32 m0, s76
	v_lshl_add_u64 v[208:209], s[72:73], 0, v[138:139]
	ds_read_b128 v[176:179], v159
	ds_read_b128 v[180:183], v159 offset:1024
	ds_read_b128 v[184:187], v159 offset:2048
	ds_read_b128 v[188:191], v159 offset:3072
	ds_read_b128 v[192:195], v159 offset:4096
	ds_read_b128 v[196:199], v159 offset:5120
	ds_read_b128 v[200:203], v159 offset:6144
	ds_read_b128 v[204:207], v159 offset:7168
	global_load_lds_dwordx4 v[208:209], off
	v_lshl_add_u64 v[208:209], s[72:73], 0, v[134:135]
	s_mov_b32 m0, s77
	s_nop 0
	global_load_lds_dwordx4 v[208:209], off
	s_waitcnt vmcnt(8)
	s_waitcnt lgkmcnt(0)
	s_barrier
	s_waitcnt lgkmcnt(0)
	v_mfma_f32_16x16x32_bf16 v[124:127], v[128:131], v[176:179], v[124:127]
	v_mfma_f32_16x16x32_bf16 v[120:123], v[146:149], v[176:179], v[120:123]
	v_mfma_f32_16x16x32_bf16 v[108:111], v[128:131], v[184:187], v[108:111]
	v_mfma_f32_16x16x32_bf16 v[104:107], v[146:149], v[184:187], v[104:107]
	v_mfma_f32_16x16x32_bf16 v[92:95], v[128:131], v[192:195], v[92:95]
	v_mfma_f32_16x16x32_bf16 v[88:91], v[146:149], v[192:195], v[88:91]
	v_mfma_f32_16x16x32_bf16 v[76:79], v[128:131], v[200:203], v[76:79]
	v_mfma_f32_16x16x32_bf16 v[72:75], v[146:149], v[200:203], v[72:75]
	v_mfma_f32_16x16x32_bf16 v[124:127], v[142:145], v[180:183], v[124:127]
	v_mfma_f32_16x16x32_bf16 v[120:123], v[150:153], v[180:183], v[120:123]
	v_mfma_f32_16x16x32_bf16 v[108:111], v[142:145], v[188:191], v[108:111]
	v_mfma_f32_16x16x32_bf16 v[104:107], v[150:153], v[188:191], v[104:107]
	v_mfma_f32_16x16x32_bf16 v[92:95], v[142:145], v[196:199], v[92:95]
	v_mfma_f32_16x16x32_bf16 v[88:91], v[150:153], v[196:199], v[88:91]
	v_mfma_f32_16x16x32_bf16 v[76:79], v[142:145], v[204:207], v[76:79]
	v_mfma_f32_16x16x32_bf16 v[72:75], v[150:153], v[204:207], v[72:75]
	v_mfma_f32_16x16x32_bf16 v[116:119], v[160:163], v[176:179], v[116:119]
	v_mfma_f32_16x16x32_bf16 v[112:115], v[168:171], v[176:179], v[112:115]
	v_mfma_f32_16x16x32_bf16 v[100:103], v[160:163], v[184:187], v[100:103]
	v_mfma_f32_16x16x32_bf16 v[96:99], v[168:171], v[184:187], v[96:99]
	v_mfma_f32_16x16x32_bf16 v[84:87], v[160:163], v[192:195], v[84:87]
	v_mfma_f32_16x16x32_bf16 v[80:83], v[168:171], v[192:195], v[80:83]
	v_mfma_f32_16x16x32_bf16 v[68:71], v[160:163], v[200:203], v[68:71]
	v_mfma_f32_16x16x32_bf16 v[64:67], v[168:171], v[200:203], v[64:67]
	v_mfma_f32_16x16x32_bf16 v[116:119], v[164:167], v[180:183], v[116:119]
	v_mfma_f32_16x16x32_bf16 v[112:115], v[172:175], v[180:183], v[112:115]
	v_mfma_f32_16x16x32_bf16 v[100:103], v[164:167], v[188:191], v[100:103]
	v_mfma_f32_16x16x32_bf16 v[96:99], v[172:175], v[188:191], v[96:99]
	v_mfma_f32_16x16x32_bf16 v[84:87], v[164:167], v[196:199], v[84:87]
	v_mfma_f32_16x16x32_bf16 v[80:83], v[172:175], v[196:199], v[80:83]
	v_mfma_f32_16x16x32_bf16 v[68:71], v[164:167], v[204:207], v[68:71]
	v_mfma_f32_16x16x32_bf16 v[64:67], v[172:175], v[204:207], v[64:67]
	s_barrier
	s_mov_b32 m0, s78
	v_lshl_add_u64 v[208:209], s[68:69], 0, v[136:137]
	ds_read_b128 v[176:179], v159 offset:16384
	ds_read_b128 v[180:183], v159 offset:17408
	ds_read_b128 v[184:187], v159 offset:18432
	ds_read_b128 v[188:191], v159 offset:19456
	ds_read_b128 v[192:195], v159 offset:20480
	ds_read_b128 v[196:199], v159 offset:21504
	ds_read_b128 v[200:203], v159 offset:22528
	ds_read_b128 v[204:207], v159 offset:23552
	global_load_lds_dwordx4 v[208:209], off
	v_lshl_add_u64 v[210:211], s[68:69], 0, v[132:133]
	s_mov_b32 m0, s79
	v_lshl_add_u64 v[212:213], s[70:71], 0, v[136:137]
	global_load_lds_dwordx4 v[210:211], off
	s_mov_b32 m0, s80
	v_lshl_add_u64 v[214:215], s[66:67], 0, v[134:135]
	global_load_lds_dwordx4 v[212:213], off
	v_lshl_add_u64 v[212:213], s[70:71], 0, v[132:133]
	s_mov_b32 m0, s86
	s_nop 0
	global_load_lds_dwordx4 v[212:213], off
	v_lshl_add_u64 v[212:213], s[66:67], 0, v[138:139]
	s_mov_b32 m0, s9
	s_nop 0
	global_load_lds_dwordx4 v[212:213], off
	s_mov_b32 m0, s34
	s_nop 0
	global_load_lds_dwordx4 v[214:215], off
	s_waitcnt vmcnt(8)
	s_waitcnt lgkmcnt(0)
	s_barrier
; #define PG8_STAGE_A(bufoff, gbase, h, nx) do { _Pragma("unroll") for (int _i = 0; _i < 2; ++_i) { \
;         const unsigned vo_ = GA ? ((nx) ? vgn[h][_i] : vgc[h][_i]) : voffA[_i]; \
;         __builtin_amdgcn_global_load_lds((const unsigned*)((const char*)(gbase) + vo_), (PG8_LAS unsigned*)(lds + (bufoff) + ldsw + _i * 8192), 16, 0, 0); } } while (0)
; #define PG8_LDA(dst, b, h) do { _Pragma("unroll") for (int m = 0; m < 4; ++m) _Pragma("unroll") for (int k = 0; k < 2; ++k) dst[m][k] = *(const PG8_LAS bf16x8*)(lds + PG8_SA(b, h) + aoff + m * 2048 + k * 1024); } while (0)
; #define PG8_LDB(dst, b, h) do { _Pragma("unroll") for (int n = 0; n < 2; ++n) _Pragma("unroll") for (int k = 0; k < 2; ++k) dst[n][k] = *(const PG8_LAS bf16x8*)(lds + PG8_SB(b, h) + boff + n * 2048 + k * 1024); } while (0)
; #define PG8_MMA(ai, bj, At, Bt) do { __builtin_amdgcn_s_setprio(1); _Pragma("unroll") for (int m = 0; m < 4; ++m) _Pragma("unroll") for (int n = 0; n < 2; ++n) _Pragma("unroll") for (int k = 0; k < 2; ++k) \
;         acc[ai][bj][m][n] = __builtin_amdgcn_mfma_f32_16x16x32_bf16(Bt[n][k], At[m][k], acc[ai][bj][m][n], 0, 0, 0); __builtin_amdgcn_s_setprio(0); } while (0)
; #define PG8_WAIT_V(n) asm volatile("s_waitcnt vmcnt(" #n ")" ::: "memory")
; #define PG8_WAIT_L(n) asm volatile("s_waitcnt lgkmcnt(" #n ")" ::: "memory")
; #define PG8_BAR __builtin_amdgcn_s_barrier()
; #define PG8_SCHED __builtin_amdgcn_sched_barrier(0)
; template <class Epi, class Sched>
; __device__ __forceinline__ void gemm_phase(const int WID_, PG8_LAS unsigned char* lds, const Sched& S, const Epi& E) {
;     ...
;             PG8_WAIT_V(8); PG8_WAIT_L(0); PG8_BAR; PG8_MMA(1, 0, At, B0); PG8_MMA(1, 1, At, B1); PG8_BAR; PG8_SCHED;
;             PG8_LDB(B0, 1, 0); PG8_LDB(B1, 1, 1); PG8_SCHED; PG8_LDA(At, 1, 0); PG8_STAGE_A(PG8_SA(0, 1), a2 + hstepA, 1, last);
;             PG8_WAIT_V(8); PG8_WAIT_L(0); PG8_BAR; PG8_MMA(0, 0, At, B0); PG8_MMA(0, 1, At, B1); PG8_BAR; PG8_SCHED;
	s_waitcnt lgkmcnt(0)
	v_mfma_f32_16x16x32_bf16 v[60:63], v[128:131], v[176:179], v[60:63]
	v_mfma_f32_16x16x32_bf16 v[56:59], v[146:149], v[176:179], v[56:59]
	v_mfma_f32_16x16x32_bf16 v[44:47], v[128:131], v[184:187], v[44:47]
	v_mfma_f32_16x16x32_bf16 v[40:43], v[146:149], v[184:187], v[40:43]
	v_mfma_f32_16x16x32_bf16 v[28:31], v[128:131], v[192:195], v[28:31]
	v_mfma_f32_16x16x32_bf16 v[24:27], v[146:149], v[192:195], v[24:27]
	v_mfma_f32_16x16x32_bf16 v[12:15], v[128:131], v[200:203], v[12:15]
	v_mfma_f32_16x16x32_bf16 v[8:11], v[146:149], v[200:203], v[8:11]
	v_mfma_f32_16x16x32_bf16 v[60:63], v[142:145], v[180:183], v[60:63]
	v_mfma_f32_16x16x32_bf16 v[56:59], v[150:153], v[180:183], v[56:59]
	v_mfma_f32_16x16x32_bf16 v[44:47], v[142:145], v[188:191], v[44:47]
	v_mfma_f32_16x16x32_bf16 v[40:43], v[150:153], v[188:191], v[40:43]
	v_mfma_f32_16x16x32_bf16 v[28:31], v[142:145], v[196:199], v[28:31]
	v_mfma_f32_16x16x32_bf16 v[24:27], v[150:153], v[196:199], v[24:27]
	v_mfma_f32_16x16x32_bf16 v[12:15], v[142:145], v[204:207], v[12:15]
	v_mfma_f32_16x16x32_bf16 v[8:11], v[150:153], v[204:207], v[8:11]
	v_mfma_f32_16x16x32_bf16 v[52:55], v[160:163], v[176:179], v[52:55]
	v_mfma_f32_16x16x32_bf16 v[48:51], v[168:171], v[176:179], v[48:51]
	v_mfma_f32_16x16x32_bf16 v[36:39], v[160:163], v[184:187], v[36:39]
	v_mfma_f32_16x16x32_bf16 v[32:35], v[168:171], v[184:187], v[32:35]
	v_mfma_f32_16x16x32_bf16 v[20:23], v[160:163], v[192:195], v[20:23]
	v_mfma_f32_16x16x32_bf16 v[16:19], v[168:171], v[192:195], v[16:19]
	v_mfma_f32_16x16x32_bf16 v[4:7], v[160:163], v[200:203], v[4:7]
	v_mfma_f32_16x16x32_bf16 v[0:3], v[168:171], v[200:203], v[0:3]
	v_mfma_f32_16x16x32_bf16 v[52:55], v[164:167], v[180:183], v[52:55]
	v_mfma_f32_16x16x32_bf16 v[48:51], v[172:175], v[180:183], v[48:51]
	v_mfma_f32_16x16x32_bf16 v[36:39], v[164:167], v[188:191], v[36:39]
	v_mfma_f32_16x16x32_bf16 v[32:35], v[172:175], v[188:191], v[32:35]
	v_mfma_f32_16x16x32_bf16 v[20:23], v[164:167], v[196:199], v[20:23]
	v_mfma_f32_16x16x32_bf16 v[16:19], v[172:175], v[196:199], v[16:19]
	v_mfma_f32_16x16x32_bf16 v[4:7], v[164:167], v[204:207], v[4:7]
	v_mfma_f32_16x16x32_bf16 v[0:3], v[172:175], v[204:207], v[0:3]
	s_barrier
	v_add_u32_e32 v150, s85, v155
	v_add_u32_e32 v172, s84, v155
	ds_read_b128 v[128:131], v150
	ds_read_b128 v[142:145], v150 offset:1024
	ds_read_b128 v[146:149], v150 offset:2048
	ds_read_b128 v[150:153], v150 offset:3072
	ds_read_b128 v[160:163], v172
	ds_read_b128 v[164:167], v172 offset:1024
	ds_read_b128 v[168:171], v172 offset:2048
	ds_read_b128 v[172:175], v172 offset:3072
	s_mov_b32 m0, s35
	v_lshl_add_u64 v[216:217], s[62:63], 0, v[138:139]
	ds_read_b128 v[176:179], v159 offset:32768
	ds_read_b128 v[180:183], v159 offset:33792
	ds_read_b128 v[184:187], v159 offset:34816
	ds_read_b128 v[188:191], v159 offset:35840
	ds_read_b128 v[192:195], v159 offset:36864
	ds_read_b128 v[196:199], v159 offset:37888
	ds_read_b128 v[200:203], v159 offset:38912
	ds_read_b128 v[204:207], v159 offset:39936
	global_load_lds_dwordx4 v[216:217], off
	v_lshl_add_u64 v[216:217], s[62:63], 0, v[134:135]
	s_mov_b32 m0, s58
	s_nop 0
	global_load_lds_dwordx4 v[216:217], off
	s_waitcnt vmcnt(8)
	s_waitcnt lgkmcnt(0)
	s_barrier
	s_waitcnt lgkmcnt(0)
	v_mfma_f32_16x16x32_bf16 v[124:127], v[128:131], v[176:179], v[124:127]
	v_mfma_f32_16x16x32_bf16 v[120:123], v[146:149], v[176:179], v[120:123]
	v_mfma_f32_16x16x32_bf16 v[108:111], v[128:131], v[184:187], v[108:111]
	v_mfma_f32_16x16x32_bf16 v[104:107], v[146:149], v[184:187], v[104:107]
	v_mfma_f32_16x16x32_bf16 v[92:95], v[128:131], v[192:195], v[92:95]
	v_mfma_f32_16x16x32_bf16 v[88:91], v[146:149], v[192:195], v[88:91]
	v_mfma_f32_16x16x32_bf16 v[76:79], v[128:131], v[200:203], v[76:79]
	v_mfma_f32_16x16x32_bf16 v[72:75], v[146:149], v[200:203], v[72:75]
	v_mfma_f32_16x16x32_bf16 v[124:127], v[142:145], v[180:183], v[124:127]
	v_mfma_f32_16x16x32_bf16 v[120:123], v[150:153], v[180:183], v[120:123]
	v_mfma_f32_16x16x32_bf16 v[108:111], v[142:145], v[188:191], v[108:111]
	v_mfma_f32_16x16x32_bf16 v[104:107], v[150:153], v[188:191], v[104:107]
	v_mfma_f32_16x16x32_bf16 v[92:95], v[142:145], v[196:199], v[92:95]
	v_mfma_f32_16x16x32_bf16 v[88:91], v[150:153], v[196:199], v[88:91]
	v_mfma_f32_16x16x32_bf16 v[76:79], v[142:145], v[204:207], v[76:79]
	v_mfma_f32_16x16x32_bf16 v[72:75], v[150:153], v[204:207], v[72:75]
	v_mfma_f32_16x16x32_bf16 v[116:119], v[160:163], v[176:179], v[116:119]
	v_mfma_f32_16x16x32_bf16 v[112:115], v[168:171], v[176:179], v[112:115]
	v_mfma_f32_16x16x32_bf16 v[100:103], v[160:163], v[184:187], v[100:103]
	v_mfma_f32_16x16x32_bf16 v[96:99], v[168:171], v[184:187], v[96:99]
	v_mfma_f32_16x16x32_bf16 v[84:87], v[160:163], v[192:195], v[84:87]
	v_mfma_f32_16x16x32_bf16 v[80:83], v[168:171], v[192:195], v[80:83]
	v_mfma_f32_16x16x32_bf16 v[68:71], v[160:163], v[200:203], v[68:71]
	v_mfma_f32_16x16x32_bf16 v[64:67], v[168:171], v[200:203], v[64:67]
	v_mfma_f32_16x16x32_bf16 v[116:119], v[164:167], v[180:183], v[116:119]
	v_mfma_f32_16x16x32_bf16 v[112:115], v[172:175], v[180:183], v[112:115]
	v_mfma_f32_16x16x32_bf16 v[100:103], v[164:167], v[188:191], v[100:103]
	v_mfma_f32_16x16x32_bf16 v[96:99], v[172:175], v[188:191], v[96:99]
	v_mfma_f32_16x16x32_bf16 v[84:87], v[164:167], v[196:199], v[84:87]
	v_mfma_f32_16x16x32_bf16 v[80:83], v[172:175], v[196:199], v[80:83]
	v_mfma_f32_16x16x32_bf16 v[68:71], v[164:167], v[204:207], v[68:71]
	v_mfma_f32_16x16x32_bf16 v[64:67], v[172:175], v[204:207], v[64:67]
	s_barrier
; #define PG8_STAGE(bufoff, gbase, voff) do { _Pragma("unroll") for (int _i = 0; _i < 2; ++_i) \
;         __builtin_amdgcn_global_load_lds((const unsigned*)((const char*)(gbase) + (voff)[_i]), (PG8_LAS unsigned*)(lds + (bufoff) + ldsw + _i * 8192), 16, 0, 0); } while (0)
; #define PG8_STAGE_A(bufoff, gbase, h, nx) do { _Pragma("unroll") for (int _i = 0; _i < 2; ++_i) { \
;         const unsigned vo_ = GA ? ((nx) ? vgn[h][_i] : vgc[h][_i]) : voffA[_i]; \
;         __builtin_amdgcn_global_load_lds((const unsigned*)((const char*)(gbase) + vo_), (PG8_LAS unsigned*)(lds + (bufoff) + ldsw + _i * 8192), 16, 0, 0); } } while (0)
; #define PG8_LDA(dst, b, h) do { _Pragma("unroll") for (int m = 0; m < 4; ++m) _Pragma("unroll") for (int k = 0; k < 2; ++k) dst[m][k] = *(const PG8_LAS bf16x8*)(lds + PG8_SA(b, h) + aoff + m * 2048 + k * 1024); } while (0)
; #define PG8_MMA(ai, bj, At, Bt) do { __builtin_amdgcn_s_setprio(1); _Pragma("unroll") for (int m = 0; m < 4; ++m) _Pragma("unroll") for (int n = 0; n < 2; ++n) _Pragma("unroll") for (int k = 0; k < 2; ++k) \
;         acc[ai][bj][m][n] = __builtin_amdgcn_mfma_f32_16x16x32_bf16(Bt[n][k], At[m][k], acc[ai][bj][m][n], 0, 0, 0); __builtin_amdgcn_s_setprio(0); } while (0)
; #define PG8_WAIT_V(n) asm volatile("s_waitcnt vmcnt(" #n ")" ::: "memory")
; #define PG8_WAIT_L(n) asm volatile("s_waitcnt lgkmcnt(" #n ")" ::: "memory")
; #define PG8_BAR __builtin_amdgcn_s_barrier()
; #define PG8_SCHED __builtin_amdgcn_sched_barrier(0)
; template <class Epi, class Sched>
; __device__ __forceinline__ void gemm_phase(const int WID_, PG8_LAS unsigned char* lds, const Sched& S, const Epi& E) {
;     ...
;             PG8_LDA(At, 1, 1); PG8_STAGE(PG8_SB(1, 0), b3, voffB); PG8_STAGE(PG8_SB(1, 1), b3 + hstepB, voffB); PG8_STAGE_A(PG8_SA(1, 0), a3, 0, last);
;             PG8_WAIT_V(8); PG8_WAIT_L(0); PG8_BAR; PG8_MMA(1, 0, At, B0); PG8_MMA(1, 1, At, B1); PG8_BAR; PG8_SCHED;
;         }
;         if (wr == 0) PG8_BAR;
	s_mov_b32 m0, s83
	v_lshl_add_u64 v[208:209], v[208:209], 0, s[22:23]
	ds_read_b128 v[176:179], v159 offset:49152
	ds_read_b128 v[180:183], v159 offset:50176
	ds_read_b128 v[184:187], v159 offset:51200
	ds_read_b128 v[188:191], v159 offset:52224
	ds_read_b128 v[192:195], v159 offset:53248
	ds_read_b128 v[196:199], v159 offset:54272
	ds_read_b128 v[200:203], v159 offset:55296
	ds_read_b128 v[204:207], v159 offset:56320
	global_load_lds_dwordx4 v[208:209], off
	v_lshl_add_u64 v[208:209], v[210:211], 0, s[22:23]
	s_mov_b32 m0, s47
	s_nop 0
	global_load_lds_dwordx4 v[208:209], off
	v_lshl_add_u64 v[208:209], s[60:61], 0, v[136:137]
	s_mov_b32 m0, s82
	s_nop 0
	global_load_lds_dwordx4 v[208:209], off
	v_lshl_add_u64 v[208:209], s[60:61], 0, v[132:133]
	s_mov_b32 m0, s41
	s_nop 0
	global_load_lds_dwordx4 v[208:209], off
	v_lshl_add_u64 v[208:209], v[212:213], 0, s[22:23]
	s_mov_b32 m0, s74
	s_nop 0
	global_load_lds_dwordx4 v[208:209], off
	v_lshl_add_u64 v[208:209], v[214:215], 0, s[22:23]
	s_mov_b32 m0, s75
	s_nop 0
	global_load_lds_dwordx4 v[208:209], off
	s_waitcnt vmcnt(8)
	s_waitcnt lgkmcnt(0)
	s_barrier
	s_waitcnt lgkmcnt(0)
	v_mfma_f32_16x16x32_bf16 v[60:63], v[128:131], v[176:179], v[60:63]
	v_mfma_f32_16x16x32_bf16 v[56:59], v[146:149], v[176:179], v[56:59]
	v_mfma_f32_16x16x32_bf16 v[44:47], v[128:131], v[184:187], v[44:47]
	v_mfma_f32_16x16x32_bf16 v[40:43], v[146:149], v[184:187], v[40:43]
	v_mfma_f32_16x16x32_bf16 v[28:31], v[128:131], v[192:195], v[28:31]
	v_mfma_f32_16x16x32_bf16 v[24:27], v[146:149], v[192:195], v[24:27]
	v_mfma_f32_16x16x32_bf16 v[12:15], v[128:131], v[200:203], v[12:15]
	v_mfma_f32_16x16x32_bf16 v[8:11], v[146:149], v[200:203], v[8:11]
	v_mfma_f32_16x16x32_bf16 v[60:63], v[142:145], v[180:183], v[60:63]
	v_mfma_f32_16x16x32_bf16 v[56:59], v[150:153], v[180:183], v[56:59]
	v_mfma_f32_16x16x32_bf16 v[44:47], v[142:145], v[188:191], v[44:47]
	v_mfma_f32_16x16x32_bf16 v[40:43], v[150:153], v[188:191], v[40:43]
	v_mfma_f32_16x16x32_bf16 v[28:31], v[142:145], v[196:199], v[28:31]
	v_mfma_f32_16x16x32_bf16 v[24:27], v[150:153], v[196:199], v[24:27]
	v_mfma_f32_16x16x32_bf16 v[12:15], v[142:145], v[204:207], v[12:15]
	v_mfma_f32_16x16x32_bf16 v[8:11], v[150:153], v[204:207], v[8:11]
	v_mfma_f32_16x16x32_bf16 v[52:55], v[160:163], v[176:179], v[52:55]
	v_mfma_f32_16x16x32_bf16 v[48:51], v[168:171], v[176:179], v[48:51]
	v_mfma_f32_16x16x32_bf16 v[36:39], v[160:163], v[184:187], v[36:39]
	v_mfma_f32_16x16x32_bf16 v[32:35], v[168:171], v[184:187], v[32:35]
	v_mfma_f32_16x16x32_bf16 v[20:23], v[160:163], v[192:195], v[20:23]
	v_mfma_f32_16x16x32_bf16 v[16:19], v[168:171], v[192:195], v[16:19]
	v_mfma_f32_16x16x32_bf16 v[4:7], v[160:163], v[200:203], v[4:7]
	v_mfma_f32_16x16x32_bf16 v[0:3], v[168:171], v[200:203], v[0:3]
	v_mfma_f32_16x16x32_bf16 v[52:55], v[164:167], v[180:183], v[52:55]
	v_mfma_f32_16x16x32_bf16 v[48:51], v[172:175], v[180:183], v[48:51]
	v_mfma_f32_16x16x32_bf16 v[36:39], v[164:167], v[188:191], v[36:39]
	v_mfma_f32_16x16x32_bf16 v[32:35], v[172:175], v[188:191], v[32:35]
	v_mfma_f32_16x16x32_bf16 v[20:23], v[164:167], v[196:199], v[20:23]
	v_mfma_f32_16x16x32_bf16 v[16:19], v[172:175], v[196:199], v[16:19]
	v_mfma_f32_16x16x32_bf16 v[4:7], v[164:167], v[204:207], v[4:7]
	v_mfma_f32_16x16x32_bf16 v[0:3], v[172:175], v[204:207], v[0:3]
	s_barrier
	s_movk_i32 s41, 0x100
	s_andn2_b64 vcc, exec, s[52:53]
	s_mov_b64 s[60:61], -1
	s_mov_b64 s[52:53], 0
	s_cbranch_vccz .LBB0_1892
	s_and_b64 vcc, exec, s[38:39]
	s_cbranch_vccz .LBB0_1895
	s_barrier

; #define PG8_STAGE(bufoff, gbase, voff) do { _Pragma("unroll") for (int _i = 0; _i < 2; ++_i) \
;         __builtin_amdgcn_global_load_lds((const unsigned*)((const char*)(gbase) + (voff)[_i]), (PG8_LAS unsigned*)(lds + (bufoff) + ldsw + _i * 8192), 16, 0, 0); } while (0)
; #define PG8_STAGE_A(bufoff, gbase, h, nx) do { _Pragma("unroll") for (int _i = 0; _i < 2; ++_i) { \
;         const unsigned vo_ = GA ? ((nx) ? vgn[h][_i] : vgc[h][_i]) : voffA[_i]; \
;         __builtin_amdgcn_global_load_lds((const unsigned*)((const char*)(gbase) + vo_), (PG8_LAS unsigned*)(lds + (bufoff) + ldsw + _i * 8192), 16, 0, 0); } } while (0)
; #define PG8_LDA(dst, b, h) do { _Pragma("unroll") for (int m = 0; m < 4; ++m) _Pragma("unroll") for (int k = 0; k < 2; ++k) dst[m][k] = *(const PG8_LAS bf16x8*)(lds + PG8_SA(b, h) + aoff + m * 2048 + k * 1024); } while (0)
; #define PG8_LDB(dst, b, h) do { _Pragma("unroll") for (int n = 0; n < 2; ++n) _Pragma("unroll") for (int k = 0; k < 2; ++k) dst[n][k] = *(const PG8_LAS bf16x8*)(lds + PG8_SB(b, h) + boff + n * 2048 + k * 1024); } while (0)
; #define PG8_WAIT_V(n) asm volatile("s_waitcnt vmcnt(" #n ")" ::: "memory")
; #define PG8_WAIT_L(n) asm volatile("s_waitcnt lgkmcnt(" #n ")" ::: "memory")
; #define PG8_BAR __builtin_amdgcn_s_barrier()
; #define PG8_SCHED __builtin_amdgcn_sched_barrier(0)
; template <class Epi, class Sched>
; __device__ __forceinline__ void gemm_phase(const int WID_, PG8_LAS unsigned char* lds, const Sched& S, const Epi& E) {
;     ...
;         for (int t = 0; t < nt; t += 2) {
;             const bool last = (t == nt - 2);
;             const char* a1 = cA + (size_t)(t + 1) * kstep;
;             const char* a2 = last ? nA : cA + (size_t)(t + 2) * kstep; const char* b2 = last ? nB : cB + (size_t)(t + 2) * kstep;
;             const char* a3 = a2 + kstep; const char* b3 = b2 + kstep;
;             PG8_LDB(B0, 0, 0); PG8_LDB(B1, 0, 1); PG8_SCHED; PG8_LDA(At, 0, 0); PG8_STAGE_A(PG8_SA(1, 1), a1 + hstepA, 1, false);
;             PG8_WAIT_V(8); PG8_WAIT_L(0); PG8_BAR; PG8_MMA(0, 0, At, B0); PG8_MMA(0, 1, At, B1); PG8_BAR; PG8_SCHED;
;             PG8_LDA(At, 0, 1); PG8_STAGE(PG8_SB(0, 0), b2, voffB); PG8_STAGE(PG8_SB(0, 1), b2 + hstepB, voffB); PG8_STAGE_A(PG8_SA(0, 0), a2, 0, last);
;             PG8_WAIT_V(8); PG8_WAIT_L(0); PG8_BAR; PG8_MMA(1, 0, At, B0); PG8_MMA(1, 1, At, B1); PG8_BAR; PG8_SCHED;
.LBB0_1928:
	s_add_u32 s66, s20, s43
	s_addc_u32 s67, s21, 0
	s_add_u32 s60, s66, 0x100
	s_addc_u32 s61, s67, 0
	s_and_b64 s[52:53], s[50:51], exec
	s_cselect_b32 s61, s45, s61
	s_cselect_b32 s60, s44, s60
	s_add_u32 s43, s38, s43
	s_addc_u32 s52, s39, 0
	s_add_u32 s43, s43, 0x100
	s_addc_u32 s52, s52, 0
	s_and_b64 s[50:51], s[50:51], exec
	s_cselect_b32 s63, s47, s52
	s_cselect_b32 s62, s46, s43
	s_add_u32 s68, s66, 0x40080
	s_addc_u32 s69, s67, 0
	s_add_i32 s84, s73, s9
	ds_read_b128 v[142:145], v139
	ds_read_b128 v[146:149], v139 offset:1024
	ds_read_b128 v[150:153], v139 offset:2048
	ds_read_b128 v[154:157], v139 offset:3072
	ds_read_b128 v[158:161], v140
	ds_read_b128 v[162:165], v140 offset:1024
	ds_read_b128 v[166:169], v140 offset:2048
	ds_read_b128 v[170:173], v140 offset:3072
	s_add_i32 m0, s33, 0xc000
	s_add_i32 s85, s33, 0xe000
	s_add_i32 s81, s84, 0x2000
	s_add_u32 s66, s62, 0x40000
	s_addc_u32 s67, s63, 0
	s_add_i32 s83, s74, s9
	s_add_i32 s82, s83, 0x2000
	s_add_i32 s80, 0, 0x18000
	s_add_i32 s79, 0, 0x1c000
	s_add_u32 s52, s60, 0x40000
	s_addc_u32 s53, s61, 0
	s_add_i32 s78, s80, s9
	s_add_i32 s76, s78, 0x2000
	s_add_u32 s50, s62, 0x40080
	s_addc_u32 s51, s63, 0
	s_add_i32 s77, s79, s9
	s_add_i32 s43, s77, 0x2000
	v_lshl_add_u64 v[206:207], s[68:69], 0, v[128:129]
	ds_read_b128 v[174:177], v141
	ds_read_b128 v[178:181], v141 offset:1024
	ds_read_b128 v[182:185], v141 offset:2048
	ds_read_b128 v[186:189], v141 offset:3072
	ds_read_b128 v[190:193], v141 offset:4096
	ds_read_b128 v[194:197], v141 offset:5120
	ds_read_b128 v[198:201], v141 offset:6144
	ds_read_b128 v[202:205], v141 offset:7168
	global_load_lds_dwordx4 v[206:207], off
	v_lshl_add_u64 v[206:207], s[68:69], 0, v[132:133]
	s_mov_b32 m0, s85
	s_nop 0
	global_load_lds_dwordx4 v[206:207], off
	s_waitcnt vmcnt(8)
	s_waitcnt lgkmcnt(0)
	s_barrier
	s_waitcnt lgkmcnt(0)
	v_mfma_f32_16x16x32_bf16 v[124:127], v[142:145], v[174:177], v[124:127]
	v_mfma_f32_16x16x32_bf16 v[120:123], v[150:153], v[174:177], v[120:123]
	v_mfma_f32_16x16x32_bf16 v[116:119], v[142:145], v[182:185], v[116:119]
	v_mfma_f32_16x16x32_bf16 v[112:115], v[150:153], v[182:185], v[112:115]
	v_mfma_f32_16x16x32_bf16 v[100:103], v[142:145], v[190:193], v[100:103]
	v_mfma_f32_16x16x32_bf16 v[96:99], v[150:153], v[190:193], v[96:99]
	v_mfma_f32_16x16x32_bf16 v[84:87], v[142:145], v[198:201], v[84:87]
	v_mfma_f32_16x16x32_bf16 v[80:83], v[150:153], v[198:201], v[80:83]
	v_mfma_f32_16x16x32_bf16 v[124:127], v[146:149], v[178:181], v[124:127]
	v_mfma_f32_16x16x32_bf16 v[120:123], v[154:157], v[178:181], v[120:123]
	v_mfma_f32_16x16x32_bf16 v[116:119], v[146:149], v[186:189], v[116:119]
	v_mfma_f32_16x16x32_bf16 v[112:115], v[154:157], v[186:189], v[112:115]
	v_mfma_f32_16x16x32_bf16 v[100:103], v[146:149], v[194:197], v[100:103]
	v_mfma_f32_16x16x32_bf16 v[96:99], v[154:157], v[194:197], v[96:99]
	v_mfma_f32_16x16x32_bf16 v[84:87], v[146:149], v[202:205], v[84:87]
	v_mfma_f32_16x16x32_bf16 v[80:83], v[154:157], v[202:205], v[80:83]
	v_mfma_f32_16x16x32_bf16 v[108:111], v[158:161], v[174:177], v[108:111]
	v_mfma_f32_16x16x32_bf16 v[104:107], v[166:169], v[174:177], v[104:107]
	v_mfma_f32_16x16x32_bf16 v[92:95], v[158:161], v[182:185], v[92:95]
	v_mfma_f32_16x16x32_bf16 v[88:91], v[166:169], v[182:185], v[88:91]
	v_mfma_f32_16x16x32_bf16 v[76:79], v[158:161], v[190:193], v[76:79]
	v_mfma_f32_16x16x32_bf16 v[72:75], v[166:169], v[190:193], v[72:75]
	v_mfma_f32_16x16x32_bf16 v[68:71], v[158:161], v[198:201], v[68:71]
	v_mfma_f32_16x16x32_bf16 v[64:67], v[166:169], v[198:201], v[64:67]
	v_mfma_f32_16x16x32_bf16 v[108:111], v[162:165], v[178:181], v[108:111]
	v_mfma_f32_16x16x32_bf16 v[104:107], v[170:173], v[178:181], v[104:107]
	v_mfma_f32_16x16x32_bf16 v[92:95], v[162:165], v[186:189], v[92:95]
	v_mfma_f32_16x16x32_bf16 v[88:91], v[170:173], v[186:189], v[88:91]
	v_mfma_f32_16x16x32_bf16 v[76:79], v[162:165], v[194:197], v[76:79]
	v_mfma_f32_16x16x32_bf16 v[72:75], v[170:173], v[194:197], v[72:75]
	v_mfma_f32_16x16x32_bf16 v[68:71], v[162:165], v[202:205], v[68:71]
	v_mfma_f32_16x16x32_bf16 v[64:67], v[170:173], v[202:205], v[64:67]
	s_barrier
	s_mov_b32 m0, s84
	v_lshl_add_u64 v[206:207], s[62:63], 0, v[130:131]
	ds_read_b128 v[174:177], v141 offset:16384
	ds_read_b128 v[178:181], v141 offset:17408
	ds_read_b128 v[182:185], v141 offset:18432
	ds_read_b128 v[186:189], v141 offset:19456
	ds_read_b128 v[190:193], v141 offset:20480
	ds_read_b128 v[194:197], v141 offset:21504
	ds_read_b128 v[198:201], v141 offset:22528
	ds_read_b128 v[202:205], v141 offset:23552
	global_load_lds_dwordx4 v[206:207], off
	v_lshl_add_u64 v[208:209], s[62:63], 0, v[134:135]
	s_mov_b32 m0, s81
	v_lshl_add_u64 v[210:211], s[66:67], 0, v[130:131]
	global_load_lds_dwordx4 v[208:209], off
	s_mov_b32 m0, s83
	v_lshl_add_u64 v[212:213], s[60:61], 0, v[132:133]
	global_load_lds_dwordx4 v[210:211], off
	v_lshl_add_u64 v[210:211], s[66:67], 0, v[134:135]
	s_mov_b32 m0, s82
	s_nop 0
	global_load_lds_dwordx4 v[210:211], off
	v_lshl_add_u64 v[210:211], s[60:61], 0, v[128:129]
	s_mov_b32 m0, s33
	s_nop 0
	global_load_lds_dwordx4 v[210:211], off
	s_mov_b32 m0, s34
	s_nop 0
	global_load_lds_dwordx4 v[212:213], off
	s_waitcnt vmcnt(8)
	s_waitcnt lgkmcnt(0)
	s_barrier
; #define PG8_STAGE_A(bufoff, gbase, h, nx) do { _Pragma("unroll") for (int _i = 0; _i < 2; ++_i) { \
;         const unsigned vo_ = GA ? ((nx) ? vgn[h][_i] : vgc[h][_i]) : voffA[_i]; \
;         __builtin_amdgcn_global_load_lds((const unsigned*)((const char*)(gbase) + vo_), (PG8_LAS unsigned*)(lds + (bufoff) + ldsw + _i * 8192), 16, 0, 0); } } while (0)
; #define PG8_LDA(dst, b, h) do { _Pragma("unroll") for (int m = 0; m < 4; ++m) _Pragma("unroll") for (int k = 0; k < 2; ++k) dst[m][k] = *(const PG8_LAS bf16x8*)(lds + PG8_SA(b, h) + aoff + m * 2048 + k * 1024); } while (0)
; #define PG8_LDB(dst, b, h) do { _Pragma("unroll") for (int n = 0; n < 2; ++n) _Pragma("unroll") for (int k = 0; k < 2; ++k) dst[n][k] = *(const PG8_LAS bf16x8*)(lds + PG8_SB(b, h) + boff + n * 2048 + k * 1024); } while (0)
; #define PG8_MMA(ai, bj, At, Bt) do { __builtin_amdgcn_s_setprio(1); _Pragma("unroll") for (int m = 0; m < 4; ++m) _Pragma("unroll") for (int n = 0; n < 2; ++n) _Pragma("unroll") for (int k = 0; k < 2; ++k) \
;         acc[ai][bj][m][n] = __builtin_amdgcn_mfma_f32_16x16x32_bf16(Bt[n][k], At[m][k], acc[ai][bj][m][n], 0, 0, 0); __builtin_amdgcn_s_setprio(0); } while (0)
; #define PG8_WAIT_V(n) asm volatile("s_waitcnt vmcnt(" #n ")" ::: "memory")
; #define PG8_WAIT_L(n) asm volatile("s_waitcnt lgkmcnt(" #n ")" ::: "memory")
; #define PG8_BAR __builtin_amdgcn_s_barrier()
; #define PG8_SCHED __builtin_amdgcn_sched_barrier(0)
; template <class Epi, class Sched>
; __device__ __forceinline__ void gemm_phase(const int WID_, PG8_LAS unsigned char* lds, const Sched& S, const Epi& E) {
;     ...
;             PG8_WAIT_V(8); PG8_WAIT_L(0); PG8_BAR; PG8_MMA(1, 0, At, B0); PG8_MMA(1, 1, At, B1); PG8_BAR; PG8_SCHED;
;             PG8_LDB(B0, 1, 0); PG8_LDB(B1, 1, 1); PG8_SCHED; PG8_LDA(At, 1, 0); PG8_STAGE_A(PG8_SA(0, 1), a2 + hstepA, 1, last);
;             PG8_WAIT_V(8); PG8_WAIT_L(0); PG8_BAR; PG8_MMA(0, 0, At, B0); PG8_MMA(0, 1, At, B1); PG8_BAR; PG8_SCHED;
	s_waitcnt lgkmcnt(0)
	v_mfma_f32_16x16x32_bf16 v[60:63], v[142:145], v[174:177], v[60:63]
	v_mfma_f32_16x16x32_bf16 v[56:59], v[150:153], v[174:177], v[56:59]
	v_mfma_f32_16x16x32_bf16 v[52:55], v[142:145], v[182:185], v[52:55]
	v_mfma_f32_16x16x32_bf16 v[48:51], v[150:153], v[182:185], v[48:51]
	v_mfma_f32_16x16x32_bf16 v[36:39], v[142:145], v[190:193], v[36:39]
	v_mfma_f32_16x16x32_bf16 v[32:35], v[150:153], v[190:193], v[32:35]
	v_mfma_f32_16x16x32_bf16 v[20:23], v[142:145], v[198:201], v[20:23]
	v_mfma_f32_16x16x32_bf16 v[16:19], v[150:153], v[198:201], v[16:19]
	v_mfma_f32_16x16x32_bf16 v[60:63], v[146:149], v[178:181], v[60:63]
	v_mfma_f32_16x16x32_bf16 v[56:59], v[154:157], v[178:181], v[56:59]
	v_mfma_f32_16x16x32_bf16 v[52:55], v[146:149], v[186:189], v[52:55]
	v_mfma_f32_16x16x32_bf16 v[48:51], v[154:157], v[186:189], v[48:51]
	v_mfma_f32_16x16x32_bf16 v[36:39], v[146:149], v[194:197], v[36:39]
	v_mfma_f32_16x16x32_bf16 v[32:35], v[154:157], v[194:197], v[32:35]
	v_mfma_f32_16x16x32_bf16 v[20:23], v[146:149], v[202:205], v[20:23]
	v_mfma_f32_16x16x32_bf16 v[16:19], v[154:157], v[202:205], v[16:19]
	v_mfma_f32_16x16x32_bf16 v[44:47], v[158:161], v[174:177], v[44:47]
	v_mfma_f32_16x16x32_bf16 v[40:43], v[166:169], v[174:177], v[40:43]
	v_mfma_f32_16x16x32_bf16 v[28:31], v[158:161], v[182:185], v[28:31]
	v_mfma_f32_16x16x32_bf16 v[24:27], v[166:169], v[182:185], v[24:27]
	v_mfma_f32_16x16x32_bf16 v[12:15], v[158:161], v[190:193], v[12:15]
	v_mfma_f32_16x16x32_bf16 v[8:11], v[166:169], v[190:193], v[8:11]
	v_mfma_f32_16x16x32_bf16 v[4:7], v[158:161], v[198:201], v[4:7]
	v_mfma_f32_16x16x32_bf16 v[0:3], v[166:169], v[198:201], v[0:3]
	v_mfma_f32_16x16x32_bf16 v[44:47], v[162:165], v[178:181], v[44:47]
	v_mfma_f32_16x16x32_bf16 v[40:43], v[170:173], v[178:181], v[40:43]
	v_mfma_f32_16x16x32_bf16 v[28:31], v[162:165], v[186:189], v[28:31]
	v_mfma_f32_16x16x32_bf16 v[24:27], v[170:173], v[186:189], v[24:27]
	v_mfma_f32_16x16x32_bf16 v[12:15], v[162:165], v[194:197], v[12:15]
	v_mfma_f32_16x16x32_bf16 v[8:11], v[170:173], v[194:197], v[8:11]
	v_mfma_f32_16x16x32_bf16 v[4:7], v[162:165], v[202:205], v[4:7]
	v_mfma_f32_16x16x32_bf16 v[0:3], v[170:173], v[202:205], v[0:3]
	s_barrier
	v_add_u32_e32 v154, s80, v137
	v_add_u32_e32 v170, s79, v137
	ds_read_b128 v[142:145], v154
	ds_read_b128 v[146:149], v154 offset:1024
	ds_read_b128 v[150:153], v154 offset:2048
	ds_read_b128 v[154:157], v154 offset:3072
	ds_read_b128 v[158:161], v170
	ds_read_b128 v[162:165], v170 offset:1024
	ds_read_b128 v[166:169], v170 offset:2048
	ds_read_b128 v[170:173], v170 offset:3072
	s_mov_b32 m0, s35
	v_lshl_add_u64 v[214:215], s[52:53], 0, v[128:129]
	ds_read_b128 v[174:177], v141 offset:32768
	ds_read_b128 v[178:181], v141 offset:33792
	ds_read_b128 v[182:185], v141 offset:34816
	ds_read_b128 v[186:189], v141 offset:35840
	ds_read_b128 v[190:193], v141 offset:36864
	ds_read_b128 v[194:197], v141 offset:37888
	ds_read_b128 v[198:201], v141 offset:38912
	ds_read_b128 v[202:205], v141 offset:39936
	global_load_lds_dwordx4 v[214:215], off
	v_lshl_add_u64 v[214:215], s[52:53], 0, v[132:133]
	s_mov_b32 m0, s59
	s_nop 0
	global_load_lds_dwordx4 v[214:215], off
	s_waitcnt vmcnt(8)
	s_waitcnt lgkmcnt(0)
	s_barrier
	s_waitcnt lgkmcnt(0)
	v_mfma_f32_16x16x32_bf16 v[124:127], v[142:145], v[174:177], v[124:127]
	v_mfma_f32_16x16x32_bf16 v[120:123], v[150:153], v[174:177], v[120:123]
	v_mfma_f32_16x16x32_bf16 v[116:119], v[142:145], v[182:185], v[116:119]
	v_mfma_f32_16x16x32_bf16 v[112:115], v[150:153], v[182:185], v[112:115]
	v_mfma_f32_16x16x32_bf16 v[100:103], v[142:145], v[190:193], v[100:103]
	v_mfma_f32_16x16x32_bf16 v[96:99], v[150:153], v[190:193], v[96:99]
	v_mfma_f32_16x16x32_bf16 v[84:87], v[142:145], v[198:201], v[84:87]
	v_mfma_f32_16x16x32_bf16 v[80:83], v[150:153], v[198:201], v[80:83]
	v_mfma_f32_16x16x32_bf16 v[124:127], v[146:149], v[178:181], v[124:127]
	v_mfma_f32_16x16x32_bf16 v[120:123], v[154:157], v[178:181], v[120:123]
	v_mfma_f32_16x16x32_bf16 v[116:119], v[146:149], v[186:189], v[116:119]
	v_mfma_f32_16x16x32_bf16 v[112:115], v[154:157], v[186:189], v[112:115]
	v_mfma_f32_16x16x32_bf16 v[100:103], v[146:149], v[194:197], v[100:103]
	v_mfma_f32_16x16x32_bf16 v[96:99], v[154:157], v[194:197], v[96:99]
	v_mfma_f32_16x16x32_bf16 v[84:87], v[146:149], v[202:205], v[84:87]
	v_mfma_f32_16x16x32_bf16 v[80:83], v[154:157], v[202:205], v[80:83]
	v_mfma_f32_16x16x32_bf16 v[108:111], v[158:161], v[174:177], v[108:111]
	v_mfma_f32_16x16x32_bf16 v[104:107], v[166:169], v[174:177], v[104:107]
	v_mfma_f32_16x16x32_bf16 v[92:95], v[158:161], v[182:185], v[92:95]
	v_mfma_f32_16x16x32_bf16 v[88:91], v[166:169], v[182:185], v[88:91]
	v_mfma_f32_16x16x32_bf16 v[76:79], v[158:161], v[190:193], v[76:79]
	v_mfma_f32_16x16x32_bf16 v[72:75], v[166:169], v[190:193], v[72:75]
	v_mfma_f32_16x16x32_bf16 v[68:71], v[158:161], v[198:201], v[68:71]
	v_mfma_f32_16x16x32_bf16 v[64:67], v[166:169], v[198:201], v[64:67]
	v_mfma_f32_16x16x32_bf16 v[108:111], v[162:165], v[178:181], v[108:111]
	v_mfma_f32_16x16x32_bf16 v[104:107], v[170:173], v[178:181], v[104:107]
	v_mfma_f32_16x16x32_bf16 v[92:95], v[162:165], v[186:189], v[92:95]
	v_mfma_f32_16x16x32_bf16 v[88:91], v[170:173], v[186:189], v[88:91]
	v_mfma_f32_16x16x32_bf16 v[76:79], v[162:165], v[194:197], v[76:79]
	v_mfma_f32_16x16x32_bf16 v[72:75], v[170:173], v[194:197], v[72:75]
	v_mfma_f32_16x16x32_bf16 v[68:71], v[162:165], v[202:205], v[68:71]
	v_mfma_f32_16x16x32_bf16 v[64:67], v[170:173], v[202:205], v[64:67]
	s_barrier
; #define PG8_STAGE(bufoff, gbase, voff) do { _Pragma("unroll") for (int _i = 0; _i < 2; ++_i) \
;         __builtin_amdgcn_global_load_lds((const unsigned*)((const char*)(gbase) + (voff)[_i]), (PG8_LAS unsigned*)(lds + (bufoff) + ldsw + _i * 8192), 16, 0, 0); } while (0)
; #define PG8_STAGE_A(bufoff, gbase, h, nx) do { _Pragma("unroll") for (int _i = 0; _i < 2; ++_i) { \
;         const unsigned vo_ = GA ? ((nx) ? vgn[h][_i] : vgc[h][_i]) : voffA[_i]; \
;         __builtin_amdgcn_global_load_lds((const unsigned*)((const char*)(gbase) + vo_), (PG8_LAS unsigned*)(lds + (bufoff) + ldsw + _i * 8192), 16, 0, 0); } } while (0)
; #define PG8_LDA(dst, b, h) do { _Pragma("unroll") for (int m = 0; m < 4; ++m) _Pragma("unroll") for (int k = 0; k < 2; ++k) dst[m][k] = *(const PG8_LAS bf16x8*)(lds + PG8_SA(b, h) + aoff + m * 2048 + k * 1024); } while (0)
; #define PG8_MMA(ai, bj, At, Bt) do { __builtin_amdgcn_s_setprio(1); _Pragma("unroll") for (int m = 0; m < 4; ++m) _Pragma("unroll") for (int n = 0; n < 2; ++n) _Pragma("unroll") for (int k = 0; k < 2; ++k) \
;         acc[ai][bj][m][n] = __builtin_amdgcn_mfma_f32_16x16x32_bf16(Bt[n][k], At[m][k], acc[ai][bj][m][n], 0, 0, 0); __builtin_amdgcn_s_setprio(0); } while (0)
; #define PG8_WAIT_V(n) asm volatile("s_waitcnt vmcnt(" #n ")" ::: "memory")
; #define PG8_WAIT_L(n) asm volatile("s_waitcnt lgkmcnt(" #n ")" ::: "memory")
; #define PG8_BAR __builtin_amdgcn_s_barrier()
; #define PG8_SCHED __builtin_amdgcn_sched_barrier(0)
; template <class Epi, class Sched>
; __device__ __forceinline__ void gemm_phase(const int WID_, PG8_LAS unsigned char* lds, const Sched& S, const Epi& E) {
;     ...
;             PG8_LDA(At, 1, 1); PG8_STAGE(PG8_SB(1, 0), b3, voffB); PG8_STAGE(PG8_SB(1, 1), b3 + hstepB, voffB); PG8_STAGE_A(PG8_SA(1, 0), a3, 0, last);
;             PG8_WAIT_V(8); PG8_WAIT_L(0); PG8_BAR; PG8_MMA(1, 0, At, B0); PG8_MMA(1, 1, At, B1); PG8_BAR; PG8_SCHED;
;         }
;         if (wr == 0) PG8_BAR;
	s_mov_b32 m0, s78
	v_lshl_add_u64 v[206:207], v[206:207], 0, s[22:23]
	ds_read_b128 v[174:177], v141 offset:49152
	ds_read_b128 v[178:181], v141 offset:50176
	ds_read_b128 v[182:185], v141 offset:51200
	ds_read_b128 v[186:189], v141 offset:52224
	ds_read_b128 v[190:193], v141 offset:53248
	ds_read_b128 v[194:197], v141 offset:54272
	ds_read_b128 v[198:201], v141 offset:55296
	ds_read_b128 v[202:205], v141 offset:56320
	global_load_lds_dwordx4 v[206:207], off
	v_lshl_add_u64 v[206:207], v[208:209], 0, s[22:23]
	s_mov_b32 m0, s76
	s_nop 0
	global_load_lds_dwordx4 v[206:207], off
	v_lshl_add_u64 v[206:207], s[50:51], 0, v[130:131]
	s_mov_b32 m0, s77
	s_nop 0
	global_load_lds_dwordx4 v[206:207], off
	v_lshl_add_u64 v[206:207], s[50:51], 0, v[134:135]
	s_mov_b32 m0, s43
	s_nop 0
	global_load_lds_dwordx4 v[206:207], off
	v_lshl_add_u64 v[206:207], v[210:211], 0, s[22:23]
	s_mov_b32 m0, s71
	s_nop 0
	global_load_lds_dwordx4 v[206:207], off
	v_lshl_add_u64 v[206:207], v[212:213], 0, s[22:23]
	s_mov_b32 m0, s72
	s_nop 0
	global_load_lds_dwordx4 v[206:207], off
	s_waitcnt vmcnt(8)
	s_waitcnt lgkmcnt(0)
	s_barrier
	s_waitcnt lgkmcnt(0)
	v_mfma_f32_16x16x32_bf16 v[60:63], v[142:145], v[174:177], v[60:63]
	v_mfma_f32_16x16x32_bf16 v[56:59], v[150:153], v[174:177], v[56:59]
	v_mfma_f32_16x16x32_bf16 v[52:55], v[142:145], v[182:185], v[52:55]
	v_mfma_f32_16x16x32_bf16 v[48:51], v[150:153], v[182:185], v[48:51]
	v_mfma_f32_16x16x32_bf16 v[36:39], v[142:145], v[190:193], v[36:39]
	v_mfma_f32_16x16x32_bf16 v[32:35], v[150:153], v[190:193], v[32:35]
	v_mfma_f32_16x16x32_bf16 v[20:23], v[142:145], v[198:201], v[20:23]
	v_mfma_f32_16x16x32_bf16 v[16:19], v[150:153], v[198:201], v[16:19]
	v_mfma_f32_16x16x32_bf16 v[60:63], v[146:149], v[178:181], v[60:63]
	v_mfma_f32_16x16x32_bf16 v[56:59], v[154:157], v[178:181], v[56:59]
	v_mfma_f32_16x16x32_bf16 v[52:55], v[146:149], v[186:189], v[52:55]
	v_mfma_f32_16x16x32_bf16 v[48:51], v[154:157], v[186:189], v[48:51]
	v_mfma_f32_16x16x32_bf16 v[36:39], v[146:149], v[194:197], v[36:39]
	v_mfma_f32_16x16x32_bf16 v[32:35], v[154:157], v[194:197], v[32:35]
	v_mfma_f32_16x16x32_bf16 v[20:23], v[146:149], v[202:205], v[20:23]
	v_mfma_f32_16x16x32_bf16 v[16:19], v[154:157], v[202:205], v[16:19]
	v_mfma_f32_16x16x32_bf16 v[44:47], v[158:161], v[174:177], v[44:47]
	v_mfma_f32_16x16x32_bf16 v[40:43], v[166:169], v[174:177], v[40:43]
	v_mfma_f32_16x16x32_bf16 v[28:31], v[158:161], v[182:185], v[28:31]
	v_mfma_f32_16x16x32_bf16 v[24:27], v[166:169], v[182:185], v[24:27]
	v_mfma_f32_16x16x32_bf16 v[12:15], v[158:161], v[190:193], v[12:15]
	v_mfma_f32_16x16x32_bf16 v[8:11], v[166:169], v[190:193], v[8:11]
	v_mfma_f32_16x16x32_bf16 v[4:7], v[158:161], v[198:201], v[4:7]
	v_mfma_f32_16x16x32_bf16 v[0:3], v[166:169], v[198:201], v[0:3]
	v_mfma_f32_16x16x32_bf16 v[44:47], v[162:165], v[178:181], v[44:47]
	v_mfma_f32_16x16x32_bf16 v[40:43], v[170:173], v[178:181], v[40:43]
	v_mfma_f32_16x16x32_bf16 v[28:31], v[162:165], v[186:189], v[28:31]
	v_mfma_f32_16x16x32_bf16 v[24:27], v[170:173], v[186:189], v[24:27]
	v_mfma_f32_16x16x32_bf16 v[12:15], v[162:165], v[194:197], v[12:15]
	v_mfma_f32_16x16x32_bf16 v[8:11], v[170:173], v[194:197], v[8:11]
	v_mfma_f32_16x16x32_bf16 v[4:7], v[162:165], v[202:205], v[4:7]
	v_mfma_f32_16x16x32_bf16 v[0:3], v[170:173], v[202:205], v[0:3]
	s_barrier
	s_movk_i32 s43, 0x100
	s_andn2_b64 vcc, exec, s[48:49]
	s_mov_b64 s[50:51], -1
	s_mov_b64 s[48:49], 0
	s_cbranch_vccz .LBB0_1928
	s_and_b64 vcc, exec, s[40:41]
	s_cbranch_vccz .LBB0_1931
	s_barrier

; #define PG8_STAGE(bufoff, gbase, voff) do { _Pragma("unroll") for (int _i = 0; _i < 2; ++_i) \
;         __builtin_amdgcn_global_load_lds((const unsigned*)((const char*)(gbase) + (voff)[_i]), (PG8_LAS unsigned*)(lds + (bufoff) + ldsw + _i * 8192), 16, 0, 0); } while (0)
; #define PG8_STAGE_A(bufoff, gbase, h, nx) do { _Pragma("unroll") for (int _i = 0; _i < 2; ++_i) { \
;         const unsigned vo_ = GA ? ((nx) ? vgn[h][_i] : vgc[h][_i]) : voffA[_i]; \
;         __builtin_amdgcn_global_load_lds((const unsigned*)((const char*)(gbase) + vo_), (PG8_LAS unsigned*)(lds + (bufoff) + ldsw + _i * 8192), 16, 0, 0); } } while (0)
; #define PG8_LDA(dst, b, h) do { _Pragma("unroll") for (int m = 0; m < 4; ++m) _Pragma("unroll") for (int k = 0; k < 2; ++k) dst[m][k] = *(const PG8_LAS bf16x8*)(lds + PG8_SA(b, h) + aoff + m * 2048 + k * 1024); } while (0)
; #define PG8_LDB(dst, b, h) do { _Pragma("unroll") for (int n = 0; n < 2; ++n) _Pragma("unroll") for (int k = 0; k < 2; ++k) dst[n][k] = *(const PG8_LAS bf16x8*)(lds + PG8_SB(b, h) + boff + n * 2048 + k * 1024); } while (0)
; #define PG8_WAIT_V(n) asm volatile("s_waitcnt vmcnt(" #n ")" ::: "memory")
; #define PG8_WAIT_L(n) asm volatile("s_waitcnt lgkmcnt(" #n ")" ::: "memory")
; #define PG8_BAR __builtin_amdgcn_s_barrier()
; #define PG8_SCHED __builtin_amdgcn_sched_barrier(0)
; template <class Epi, class Sched>
; __device__ __forceinline__ void gemm_phase(const int WID_, PG8_LAS unsigned char* lds, const Sched& S, const Epi& E) {
;     ...
;         for (int t = 0; t < nt; t += 2) {
;             const bool last = (t == nt - 2);
;             const char* a1 = cA + (size_t)(t + 1) * kstep;
;             const char* a2 = last ? nA : cA + (size_t)(t + 2) * kstep; const char* b2 = last ? nB : cB + (size_t)(t + 2) * kstep;
;             const char* a3 = a2 + kstep; const char* b3 = b2 + kstep;
;             PG8_LDB(B0, 0, 0); PG8_LDB(B1, 0, 1); PG8_SCHED; PG8_LDA(At, 0, 0); PG8_STAGE_A(PG8_SA(1, 1), a1 + hstepA, 1, false);
;             PG8_WAIT_V(8); PG8_WAIT_L(0); PG8_BAR; PG8_MMA(0, 0, At, B0); PG8_MMA(0, 1, At, B1); PG8_BAR; PG8_SCHED;
;             PG8_LDA(At, 0, 1); PG8_STAGE(PG8_SB(0, 0), b2, voffB); PG8_STAGE(PG8_SB(0, 1), b2 + hstepB, voffB); PG8_STAGE_A(PG8_SA(0, 0), a2, 0, last);
;             PG8_WAIT_V(8); PG8_WAIT_L(0); PG8_BAR; PG8_MMA(1, 0, At, B0); PG8_MMA(1, 1, At, B1); PG8_BAR; PG8_SCHED;
.LBB0_2018:
	s_add_u32 s18, s16, 0xfffe0080
	s_addc_u32 s19, s17, -1
	s_add_i32 s43, 0, 0x10000
	s_cmp_eq_u32 s60, 4
	s_cselect_b32 s21, s9, s19
	s_cselect_b32 s20, s33, s18
	v_add_u32_e32 v148, s43, v151
	s_cselect_b32 s19, s44, s51
	s_cselect_b32 s18, s49, s50
	s_add_i32 s67, 0, 0x14000
	ds_read_b128 v[140:143], v148
	ds_read_b128 v[144:147], v148 offset:1024
	ds_read_b128 v[154:157], v148 offset:2048
	ds_read_b128 v[158:161], v148 offset:3072
	v_add_u32_e32 v148, s67, v151
	ds_read_b128 v[162:165], v148
	ds_read_b128 v[166:169], v148 offset:1024
	ds_read_b128 v[170:173], v148 offset:2048
	ds_read_b128 v[174:177], v148 offset:3072
	v_lshl_add_u64 v[148:149], s[16:17], 0, v[136:137]
	s_add_i32 m0, s23, 0xc000
	ds_read_b128 v[178:181], v153
	ds_read_b128 v[182:185], v153 offset:1024
	ds_read_b128 v[186:189], v153 offset:2048
	ds_read_b128 v[190:193], v153 offset:3072
	ds_read_b128 v[198:201], v153 offset:4096
	ds_read_b128 v[202:205], v153 offset:5120
	ds_read_b128 v[206:209], v153 offset:6144
	ds_read_b128 v[210:213], v153 offset:7168
	global_load_lds_dwordx4 v[148:149], off
	v_lshl_add_u64 v[148:149], s[16:17], 0, v[138:139]
	s_add_i32 m0, s23, 0xe000
	s_nop 0
	global_load_lds_dwordx4 v[148:149], off
	s_waitcnt vmcnt(8)
	s_waitcnt lgkmcnt(0)
	s_barrier
	s_waitcnt lgkmcnt(0)
	v_mfma_f32_16x16x32_bf16 v[124:127], v[140:143], v[178:181], v[124:127]
	v_mfma_f32_16x16x32_bf16 v[120:123], v[154:157], v[178:181], v[120:123]
	v_mfma_f32_16x16x32_bf16 v[108:111], v[140:143], v[186:189], v[108:111]
	v_mfma_f32_16x16x32_bf16 v[104:107], v[154:157], v[186:189], v[104:107]
	v_mfma_f32_16x16x32_bf16 v[92:95], v[140:143], v[198:201], v[92:95]
	v_mfma_f32_16x16x32_bf16 v[88:91], v[154:157], v[198:201], v[88:91]
	v_mfma_f32_16x16x32_bf16 v[76:79], v[140:143], v[206:209], v[76:79]
	v_mfma_f32_16x16x32_bf16 v[72:75], v[154:157], v[206:209], v[72:75]
	v_mfma_f32_16x16x32_bf16 v[124:127], v[144:147], v[182:185], v[124:127]
	v_mfma_f32_16x16x32_bf16 v[120:123], v[158:161], v[182:185], v[120:123]
	v_mfma_f32_16x16x32_bf16 v[108:111], v[144:147], v[190:193], v[108:111]
	v_mfma_f32_16x16x32_bf16 v[104:107], v[158:161], v[190:193], v[104:107]
	v_mfma_f32_16x16x32_bf16 v[92:95], v[144:147], v[202:205], v[92:95]
	v_mfma_f32_16x16x32_bf16 v[88:91], v[158:161], v[202:205], v[88:91]
	v_mfma_f32_16x16x32_bf16 v[76:79], v[144:147], v[210:213], v[76:79]
	v_mfma_f32_16x16x32_bf16 v[72:75], v[158:161], v[210:213], v[72:75]
	v_mfma_f32_16x16x32_bf16 v[116:119], v[162:165], v[178:181], v[116:119]
	v_mfma_f32_16x16x32_bf16 v[112:115], v[170:173], v[178:181], v[112:115]
	v_mfma_f32_16x16x32_bf16 v[100:103], v[162:165], v[186:189], v[100:103]
	v_mfma_f32_16x16x32_bf16 v[96:99], v[170:173], v[186:189], v[96:99]
	v_mfma_f32_16x16x32_bf16 v[84:87], v[162:165], v[198:201], v[84:87]
	v_mfma_f32_16x16x32_bf16 v[80:83], v[170:173], v[198:201], v[80:83]
	v_mfma_f32_16x16x32_bf16 v[68:71], v[162:165], v[206:209], v[68:71]
	v_mfma_f32_16x16x32_bf16 v[64:67], v[170:173], v[206:209], v[64:67]
	v_mfma_f32_16x16x32_bf16 v[116:119], v[166:169], v[182:185], v[116:119]
	v_mfma_f32_16x16x32_bf16 v[112:115], v[174:177], v[182:185], v[112:115]
	v_mfma_f32_16x16x32_bf16 v[100:103], v[166:169], v[190:193], v[100:103]
	v_mfma_f32_16x16x32_bf16 v[96:99], v[174:177], v[190:193], v[96:99]
	v_mfma_f32_16x16x32_bf16 v[84:87], v[166:169], v[202:205], v[84:87]
	v_mfma_f32_16x16x32_bf16 v[80:83], v[174:177], v[202:205], v[80:83]
	v_mfma_f32_16x16x32_bf16 v[68:71], v[166:169], v[210:213], v[68:71]
	v_mfma_f32_16x16x32_bf16 v[64:67], v[174:177], v[210:213], v[64:67]
	s_barrier
	s_add_i32 s46, s43, s22
	v_lshl_add_u64 v[148:149], s[18:19], 0, v[128:129]
	s_mov_b32 m0, s46
	ds_read_b128 v[178:181], v153 offset:16384
	ds_read_b128 v[182:185], v153 offset:17408
	ds_read_b128 v[186:189], v153 offset:18432
	ds_read_b128 v[190:193], v153 offset:19456
	ds_read_b128 v[198:201], v153 offset:20480
	ds_read_b128 v[202:205], v153 offset:21504
	ds_read_b128 v[206:209], v153 offset:22528
	ds_read_b128 v[210:213], v153 offset:23552
	global_load_lds_dwordx4 v[148:149], off
	s_add_i32 m0, s46, 0x2000
	s_add_u32 s62, s18, 0x20000
	v_lshl_add_u64 v[214:215], s[18:19], 0, v[130:131]
	s_addc_u32 s63, s19, 0
	s_add_i32 s46, s67, s22
	global_load_lds_dwordx4 v[214:215], off
	v_lshl_add_u64 v[216:217], s[62:63], 0, v[128:129]
	s_mov_b32 m0, s46
	v_lshl_add_u64 v[218:219], s[20:21], 0, v[132:133]
	global_load_lds_dwordx4 v[216:217], off
	v_lshl_add_u64 v[216:217], s[62:63], 0, v[130:131]
	s_add_i32 m0, s46, 0x2000
	s_nop 0
	global_load_lds_dwordx4 v[216:217], off
	v_lshl_add_u64 v[216:217], s[20:21], 0, v[134:135]
	s_mov_b32 m0, s23
	s_nop 0
	global_load_lds_dwordx4 v[216:217], off
	s_mov_b32 m0, s78
	s_nop 0
	global_load_lds_dwordx4 v[218:219], off
	s_waitcnt vmcnt(8)
	s_waitcnt lgkmcnt(0)
	s_barrier
; #define PG8_STAGE_A(bufoff, gbase, h, nx) do { _Pragma("unroll") for (int _i = 0; _i < 2; ++_i) { \
;         const unsigned vo_ = GA ? ((nx) ? vgn[h][_i] : vgc[h][_i]) : voffA[_i]; \
;         __builtin_amdgcn_global_load_lds((const unsigned*)((const char*)(gbase) + vo_), (PG8_LAS unsigned*)(lds + (bufoff) + ldsw + _i * 8192), 16, 0, 0); } } while (0)
; #define PG8_LDA(dst, b, h) do { _Pragma("unroll") for (int m = 0; m < 4; ++m) _Pragma("unroll") for (int k = 0; k < 2; ++k) dst[m][k] = *(const PG8_LAS bf16x8*)(lds + PG8_SA(b, h) + aoff + m * 2048 + k * 1024); } while (0)
; #define PG8_LDB(dst, b, h) do { _Pragma("unroll") for (int n = 0; n < 2; ++n) _Pragma("unroll") for (int k = 0; k < 2; ++k) dst[n][k] = *(const PG8_LAS bf16x8*)(lds + PG8_SB(b, h) + boff + n * 2048 + k * 1024); } while (0)
; #define PG8_MMA(ai, bj, At, Bt) do { __builtin_amdgcn_s_setprio(1); _Pragma("unroll") for (int m = 0; m < 4; ++m) _Pragma("unroll") for (int n = 0; n < 2; ++n) _Pragma("unroll") for (int k = 0; k < 2; ++k) \
;         acc[ai][bj][m][n] = __builtin_amdgcn_mfma_f32_16x16x32_bf16(Bt[n][k], At[m][k], acc[ai][bj][m][n], 0, 0, 0); __builtin_amdgcn_s_setprio(0); } while (0)
; #define PG8_WAIT_V(n) asm volatile("s_waitcnt vmcnt(" #n ")" ::: "memory")
; #define PG8_WAIT_L(n) asm volatile("s_waitcnt lgkmcnt(" #n ")" ::: "memory")
; #define PG8_BAR __builtin_amdgcn_s_barrier()
; #define PG8_SCHED __builtin_amdgcn_sched_barrier(0)
; template <class Epi, class Sched>
; __device__ __forceinline__ void gemm_phase(const int WID_, PG8_LAS unsigned char* lds, const Sched& S, const Epi& E) {
;     ...
;             PG8_WAIT_V(8); PG8_WAIT_L(0); PG8_BAR; PG8_MMA(1, 0, At, B0); PG8_MMA(1, 1, At, B1); PG8_BAR; PG8_SCHED;
;             PG8_LDB(B0, 1, 0); PG8_LDB(B1, 1, 1); PG8_SCHED; PG8_LDA(At, 1, 0); PG8_STAGE_A(PG8_SA(0, 1), a2 + hstepA, 1, last);
;             PG8_WAIT_V(8); PG8_WAIT_L(0); PG8_BAR; PG8_MMA(0, 0, At, B0); PG8_MMA(0, 1, At, B1); PG8_BAR; PG8_SCHED;
	s_waitcnt lgkmcnt(0)
	v_mfma_f32_16x16x32_bf16 v[60:63], v[140:143], v[178:181], v[60:63]
	v_mfma_f32_16x16x32_bf16 v[56:59], v[154:157], v[178:181], v[56:59]
	v_mfma_f32_16x16x32_bf16 v[44:47], v[140:143], v[186:189], v[44:47]
	v_mfma_f32_16x16x32_bf16 v[40:43], v[154:157], v[186:189], v[40:43]
	v_mfma_f32_16x16x32_bf16 v[28:31], v[140:143], v[198:201], v[28:31]
	v_mfma_f32_16x16x32_bf16 v[24:27], v[154:157], v[198:201], v[24:27]
	v_mfma_f32_16x16x32_bf16 v[12:15], v[140:143], v[206:209], v[12:15]
	v_mfma_f32_16x16x32_bf16 v[8:11], v[154:157], v[206:209], v[8:11]
	v_mfma_f32_16x16x32_bf16 v[60:63], v[144:147], v[182:185], v[60:63]
	v_mfma_f32_16x16x32_bf16 v[56:59], v[158:161], v[182:185], v[56:59]
	v_mfma_f32_16x16x32_bf16 v[44:47], v[144:147], v[190:193], v[44:47]
	v_mfma_f32_16x16x32_bf16 v[40:43], v[158:161], v[190:193], v[40:43]
	v_mfma_f32_16x16x32_bf16 v[28:31], v[144:147], v[202:205], v[28:31]
	v_mfma_f32_16x16x32_bf16 v[24:27], v[158:161], v[202:205], v[24:27]
	v_mfma_f32_16x16x32_bf16 v[12:15], v[144:147], v[210:213], v[12:15]
	v_mfma_f32_16x16x32_bf16 v[8:11], v[158:161], v[210:213], v[8:11]
	v_mfma_f32_16x16x32_bf16 v[52:55], v[162:165], v[178:181], v[52:55]
	v_mfma_f32_16x16x32_bf16 v[48:51], v[170:173], v[178:181], v[48:51]
	v_mfma_f32_16x16x32_bf16 v[36:39], v[162:165], v[186:189], v[36:39]
	v_mfma_f32_16x16x32_bf16 v[32:35], v[170:173], v[186:189], v[32:35]
	v_mfma_f32_16x16x32_bf16 v[20:23], v[162:165], v[198:201], v[20:23]
	v_mfma_f32_16x16x32_bf16 v[16:19], v[170:173], v[198:201], v[16:19]
	v_mfma_f32_16x16x32_bf16 v[0:3], v[162:165], v[206:209], v[0:3]
	v_mfma_f32_16x16x32_bf16 v[4:7], v[170:173], v[206:209], v[4:7]
	v_mfma_f32_16x16x32_bf16 v[52:55], v[166:169], v[182:185], v[52:55]
	v_mfma_f32_16x16x32_bf16 v[48:51], v[174:177], v[182:185], v[48:51]
	v_mfma_f32_16x16x32_bf16 v[36:39], v[166:169], v[190:193], v[36:39]
	v_mfma_f32_16x16x32_bf16 v[32:35], v[174:177], v[190:193], v[32:35]
	v_mfma_f32_16x16x32_bf16 v[20:23], v[166:169], v[202:205], v[20:23]
	v_mfma_f32_16x16x32_bf16 v[16:19], v[174:177], v[202:205], v[16:19]
	v_mfma_f32_16x16x32_bf16 v[0:3], v[166:169], v[210:213], v[0:3]
	v_mfma_f32_16x16x32_bf16 v[4:7], v[174:177], v[210:213], v[4:7]
	s_barrier
	s_add_i32 s82, 0, 0x18000
	s_add_i32 s83, 0, 0x1c000
	v_add_u32_e32 v158, s82, v151
	v_add_u32_e32 v174, s83, v151
	ds_read_b128 v[140:143], v158
	ds_read_b128 v[144:147], v158 offset:1024
	ds_read_b128 v[154:157], v158 offset:2048
	ds_read_b128 v[158:161], v158 offset:3072
	ds_read_b128 v[162:165], v174
	ds_read_b128 v[166:169], v174 offset:1024
	ds_read_b128 v[170:173], v174 offset:2048
	ds_read_b128 v[174:177], v174 offset:3072
	s_add_u32 s20, s20, 0x20000
	s_addc_u32 s21, s21, 0
	s_mov_b32 m0, s79
	v_lshl_add_u64 v[220:221], s[20:21], 0, v[134:135]
	ds_read_b128 v[178:181], v153 offset:32768
	ds_read_b128 v[182:185], v153 offset:33792
	ds_read_b128 v[186:189], v153 offset:34816
	ds_read_b128 v[190:193], v153 offset:35840
	ds_read_b128 v[198:201], v153 offset:36864
	ds_read_b128 v[202:205], v153 offset:37888
	ds_read_b128 v[206:209], v153 offset:38912
	ds_read_b128 v[210:213], v153 offset:39936
	global_load_lds_dwordx4 v[220:221], off
	v_lshl_add_u64 v[220:221], s[20:21], 0, v[132:133]
	s_mov_b32 m0, s80
	s_nop 0
	global_load_lds_dwordx4 v[220:221], off
	s_waitcnt vmcnt(8)
	s_waitcnt lgkmcnt(0)
	s_barrier
	s_waitcnt lgkmcnt(0)
	v_mfma_f32_16x16x32_bf16 v[124:127], v[140:143], v[178:181], v[124:127]
	v_mfma_f32_16x16x32_bf16 v[120:123], v[154:157], v[178:181], v[120:123]
	v_mfma_f32_16x16x32_bf16 v[108:111], v[140:143], v[186:189], v[108:111]
	v_mfma_f32_16x16x32_bf16 v[104:107], v[154:157], v[186:189], v[104:107]
	v_mfma_f32_16x16x32_bf16 v[92:95], v[140:143], v[198:201], v[92:95]
	v_mfma_f32_16x16x32_bf16 v[88:91], v[154:157], v[198:201], v[88:91]
	v_mfma_f32_16x16x32_bf16 v[76:79], v[140:143], v[206:209], v[76:79]
	v_mfma_f32_16x16x32_bf16 v[72:75], v[154:157], v[206:209], v[72:75]
	v_mfma_f32_16x16x32_bf16 v[124:127], v[144:147], v[182:185], v[124:127]
	v_mfma_f32_16x16x32_bf16 v[120:123], v[158:161], v[182:185], v[120:123]
	v_mfma_f32_16x16x32_bf16 v[108:111], v[144:147], v[190:193], v[108:111]
	v_mfma_f32_16x16x32_bf16 v[104:107], v[158:161], v[190:193], v[104:107]
	v_mfma_f32_16x16x32_bf16 v[92:95], v[144:147], v[202:205], v[92:95]
	v_mfma_f32_16x16x32_bf16 v[88:91], v[158:161], v[202:205], v[88:91]
	v_mfma_f32_16x16x32_bf16 v[76:79], v[144:147], v[210:213], v[76:79]
	v_mfma_f32_16x16x32_bf16 v[72:75], v[158:161], v[210:213], v[72:75]
	v_mfma_f32_16x16x32_bf16 v[116:119], v[162:165], v[178:181], v[116:119]
	v_mfma_f32_16x16x32_bf16 v[112:115], v[170:173], v[178:181], v[112:115]
	v_mfma_f32_16x16x32_bf16 v[100:103], v[162:165], v[186:189], v[100:103]
	v_mfma_f32_16x16x32_bf16 v[96:99], v[170:173], v[186:189], v[96:99]
	v_mfma_f32_16x16x32_bf16 v[84:87], v[162:165], v[198:201], v[84:87]
	v_mfma_f32_16x16x32_bf16 v[80:83], v[170:173], v[198:201], v[80:83]
	v_mfma_f32_16x16x32_bf16 v[68:71], v[162:165], v[206:209], v[68:71]
	v_mfma_f32_16x16x32_bf16 v[64:67], v[170:173], v[206:209], v[64:67]
	v_mfma_f32_16x16x32_bf16 v[116:119], v[166:169], v[182:185], v[116:119]
	v_mfma_f32_16x16x32_bf16 v[112:115], v[174:177], v[182:185], v[112:115]
	v_mfma_f32_16x16x32_bf16 v[100:103], v[166:169], v[190:193], v[100:103]
	v_mfma_f32_16x16x32_bf16 v[96:99], v[174:177], v[190:193], v[96:99]
	v_mfma_f32_16x16x32_bf16 v[84:87], v[166:169], v[202:205], v[84:87]
	v_mfma_f32_16x16x32_bf16 v[80:83], v[174:177], v[202:205], v[80:83]
	v_mfma_f32_16x16x32_bf16 v[68:71], v[166:169], v[210:213], v[68:71]
	v_mfma_f32_16x16x32_bf16 v[64:67], v[174:177], v[210:213], v[64:67]
	s_barrier
; #define PG8_STAGE(bufoff, gbase, voff) do { _Pragma("unroll") for (int _i = 0; _i < 2; ++_i) \
;         __builtin_amdgcn_global_load_lds((const unsigned*)((const char*)(gbase) + (voff)[_i]), (PG8_LAS unsigned*)(lds + (bufoff) + ldsw + _i * 8192), 16, 0, 0); } while (0)
; #define PG8_STAGE_A(bufoff, gbase, h, nx) do { _Pragma("unroll") for (int _i = 0; _i < 2; ++_i) { \
;         const unsigned vo_ = GA ? ((nx) ? vgn[h][_i] : vgc[h][_i]) : voffA[_i]; \
;         __builtin_amdgcn_global_load_lds((const unsigned*)((const char*)(gbase) + vo_), (PG8_LAS unsigned*)(lds + (bufoff) + ldsw + _i * 8192), 16, 0, 0); } } while (0)
; #define PG8_LDA(dst, b, h) do { _Pragma("unroll") for (int m = 0; m < 4; ++m) _Pragma("unroll") for (int k = 0; k < 2; ++k) dst[m][k] = *(const PG8_LAS bf16x8*)(lds + PG8_SA(b, h) + aoff + m * 2048 + k * 1024); } while (0)
; #define PG8_MMA(ai, bj, At, Bt) do { __builtin_amdgcn_s_setprio(1); _Pragma("unroll") for (int m = 0; m < 4; ++m) _Pragma("unroll") for (int n = 0; n < 2; ++n) _Pragma("unroll") for (int k = 0; k < 2; ++k) \
;         acc[ai][bj][m][n] = __builtin_amdgcn_mfma_f32_16x16x32_bf16(Bt[n][k], At[m][k], acc[ai][bj][m][n], 0, 0, 0); __builtin_amdgcn_s_setprio(0); } while (0)
; #define PG8_WAIT_V(n) asm volatile("s_waitcnt vmcnt(" #n ")" ::: "memory")
; #define PG8_WAIT_L(n) asm volatile("s_waitcnt lgkmcnt(" #n ")" ::: "memory")
; #define PG8_BAR __builtin_amdgcn_s_barrier()
; #define PG8_SCHED __builtin_amdgcn_sched_barrier(0)
; template <class Epi, class Sched>
; __device__ __forceinline__ void gemm_phase(const int WID_, PG8_LAS unsigned char* lds, const Sched& S, const Epi& E) {
;     ...
;             PG8_LDA(At, 1, 1); PG8_STAGE(PG8_SB(1, 0), b3, voffB); PG8_STAGE(PG8_SB(1, 1), b3 + hstepB, voffB); PG8_STAGE_A(PG8_SA(1, 0), a3, 0, last);
;             PG8_WAIT_V(8); PG8_WAIT_L(0); PG8_BAR; PG8_MMA(1, 0, At, B0); PG8_MMA(1, 1, At, B1); PG8_BAR; PG8_SCHED;
;         }
;         if (wr == 0) PG8_BAR;
	s_add_i32 s20, s82, s22
	v_lshl_add_u64 v[148:149], v[148:149], 0, s[68:69]
	s_mov_b32 m0, s20
	ds_read_b128 v[178:181], v153 offset:49152
	ds_read_b128 v[182:185], v153 offset:50176
	ds_read_b128 v[186:189], v153 offset:51200
	ds_read_b128 v[190:193], v153 offset:52224
	ds_read_b128 v[198:201], v153 offset:53248
	ds_read_b128 v[202:205], v153 offset:54272
	ds_read_b128 v[206:209], v153 offset:55296
	ds_read_b128 v[210:213], v153 offset:56320
	global_load_lds_dwordx4 v[148:149], off
	s_add_i32 m0, s20, 0x2000
	s_add_u32 s18, s18, 0x20080
	v_lshl_add_u64 v[148:149], v[214:215], 0, s[68:69]
	s_addc_u32 s19, s19, 0
	s_add_i32 s20, s83, s22
	global_load_lds_dwordx4 v[148:149], off
	v_lshl_add_u64 v[148:149], s[18:19], 0, v[128:129]
	s_mov_b32 m0, s20
	s_nop 0
	global_load_lds_dwordx4 v[148:149], off
	v_lshl_add_u64 v[148:149], s[18:19], 0, v[130:131]
	s_add_i32 m0, s20, 0x2000
	s_nop 0
	global_load_lds_dwordx4 v[148:149], off
	v_lshl_add_u64 v[148:149], v[216:217], 0, s[68:69]
	s_mov_b32 m0, s81
	s_nop 0
	global_load_lds_dwordx4 v[148:149], off
	v_lshl_add_u64 v[148:149], v[218:219], 0, s[68:69]
	s_mov_b32 m0, s48
	s_nop 0
	global_load_lds_dwordx4 v[148:149], off
	s_waitcnt vmcnt(8)
	s_waitcnt lgkmcnt(0)
	s_barrier
	s_waitcnt lgkmcnt(0)
	v_mfma_f32_16x16x32_bf16 v[60:63], v[140:143], v[178:181], v[60:63]
	v_mfma_f32_16x16x32_bf16 v[56:59], v[154:157], v[178:181], v[56:59]
	v_mfma_f32_16x16x32_bf16 v[44:47], v[140:143], v[186:189], v[44:47]
	v_mfma_f32_16x16x32_bf16 v[40:43], v[154:157], v[186:189], v[40:43]
	v_mfma_f32_16x16x32_bf16 v[28:31], v[140:143], v[198:201], v[28:31]
	v_mfma_f32_16x16x32_bf16 v[24:27], v[154:157], v[198:201], v[24:27]
	v_mfma_f32_16x16x32_bf16 v[12:15], v[140:143], v[206:209], v[12:15]
	v_mfma_f32_16x16x32_bf16 v[8:11], v[154:157], v[206:209], v[8:11]
	v_mfma_f32_16x16x32_bf16 v[60:63], v[144:147], v[182:185], v[60:63]
	v_mfma_f32_16x16x32_bf16 v[56:59], v[158:161], v[182:185], v[56:59]
	v_mfma_f32_16x16x32_bf16 v[44:47], v[144:147], v[190:193], v[44:47]
	v_mfma_f32_16x16x32_bf16 v[40:43], v[158:161], v[190:193], v[40:43]
	v_mfma_f32_16x16x32_bf16 v[28:31], v[144:147], v[202:205], v[28:31]
	v_mfma_f32_16x16x32_bf16 v[24:27], v[158:161], v[202:205], v[24:27]
	v_mfma_f32_16x16x32_bf16 v[12:15], v[144:147], v[210:213], v[12:15]
	v_mfma_f32_16x16x32_bf16 v[8:11], v[158:161], v[210:213], v[8:11]
	v_mfma_f32_16x16x32_bf16 v[52:55], v[162:165], v[178:181], v[52:55]
	v_mfma_f32_16x16x32_bf16 v[48:51], v[170:173], v[178:181], v[48:51]
	v_mfma_f32_16x16x32_bf16 v[36:39], v[162:165], v[186:189], v[36:39]
	v_mfma_f32_16x16x32_bf16 v[32:35], v[170:173], v[186:189], v[32:35]
	v_mfma_f32_16x16x32_bf16 v[20:23], v[162:165], v[198:201], v[20:23]
	v_mfma_f32_16x16x32_bf16 v[16:19], v[170:173], v[198:201], v[16:19]
	v_mfma_f32_16x16x32_bf16 v[0:3], v[162:165], v[206:209], v[0:3]
	v_mfma_f32_16x16x32_bf16 v[4:7], v[170:173], v[206:209], v[4:7]
	v_mfma_f32_16x16x32_bf16 v[52:55], v[166:169], v[182:185], v[52:55]
	v_mfma_f32_16x16x32_bf16 v[48:51], v[174:177], v[182:185], v[48:51]
	v_mfma_f32_16x16x32_bf16 v[36:39], v[166:169], v[190:193], v[36:39]
	v_mfma_f32_16x16x32_bf16 v[32:35], v[174:177], v[190:193], v[32:35]
	v_mfma_f32_16x16x32_bf16 v[20:23], v[166:169], v[202:205], v[20:23]
	v_mfma_f32_16x16x32_bf16 v[16:19], v[174:177], v[202:205], v[16:19]
	v_mfma_f32_16x16x32_bf16 v[0:3], v[166:169], v[210:213], v[0:3]
	v_mfma_f32_16x16x32_bf16 v[4:7], v[174:177], v[210:213], v[4:7]
	s_barrier
	s_add_i32 s60, s60, 2
	s_add_u32 s16, s16, 0x100
	s_addc_u32 s17, s17, 0
	s_add_u32 s50, s50, 0x100
	s_addc_u32 s51, s51, 0
	s_cmp_gt_u32 s60, 5
	s_cbranch_scc0 .LBB0_2018
	s_and_b64 vcc, exec, s[28:29]
	s_cbranch_vccz .LBB0_2021
	s_barrier

; #define PG8_STAGE(bufoff, gbase, voff) do { _Pragma("unroll") for (int _i = 0; _i < 2; ++_i) \
;         __builtin_amdgcn_global_load_lds((const unsigned*)((const char*)(gbase) + (voff)[_i]), (PG8_LAS unsigned*)(lds + (bufoff) + ldsw + _i * 8192), 16, 0, 0); } while (0)
; #define PG8_STAGE_A(bufoff, gbase, h, nx) do { _Pragma("unroll") for (int _i = 0; _i < 2; ++_i) { \
;         const unsigned vo_ = GA ? ((nx) ? vgn[h][_i] : vgc[h][_i]) : voffA[_i]; \
;         __builtin_amdgcn_global_load_lds((const unsigned*)((const char*)(gbase) + vo_), (PG8_LAS unsigned*)(lds + (bufoff) + ldsw + _i * 8192), 16, 0, 0); } } while (0)
; #define PG8_LDA(dst, b, h) do { _Pragma("unroll") for (int m = 0; m < 4; ++m) _Pragma("unroll") for (int k = 0; k < 2; ++k) dst[m][k] = *(const PG8_LAS bf16x8*)(lds + PG8_SA(b, h) + aoff + m * 2048 + k * 1024); } while (0)
; #define PG8_LDB(dst, b, h) do { _Pragma("unroll") for (int n = 0; n < 2; ++n) _Pragma("unroll") for (int k = 0; k < 2; ++k) dst[n][k] = *(const PG8_LAS bf16x8*)(lds + PG8_SB(b, h) + boff + n * 2048 + k * 1024); } while (0)
; #define PG8_WAIT_V(n) asm volatile("s_waitcnt vmcnt(" #n ")" ::: "memory")
; #define PG8_WAIT_L(n) asm volatile("s_waitcnt lgkmcnt(" #n ")" ::: "memory")
; #define PG8_BAR __builtin_amdgcn_s_barrier()
; #define PG8_SCHED __builtin_amdgcn_sched_barrier(0)
; template <class Epi, class Sched>
; __device__ __forceinline__ void gemm_phase(const int WID_, PG8_LAS unsigned char* lds, const Sched& S, const Epi& E) {
;     ...
;         for (int t = 0; t < nt; t += 2) {
;             const bool last = (t == nt - 2);
;             const char* a1 = cA + (size_t)(t + 1) * kstep;
;             const char* a2 = last ? nA : cA + (size_t)(t + 2) * kstep; const char* b2 = last ? nB : cB + (size_t)(t + 2) * kstep;
;             const char* a3 = a2 + kstep; const char* b3 = b2 + kstep;
;             PG8_LDB(B0, 0, 0); PG8_LDB(B1, 0, 1); PG8_SCHED; PG8_LDA(At, 0, 0); PG8_STAGE_A(PG8_SA(1, 1), a1 + hstepA, 1, false);
;             PG8_WAIT_V(8); PG8_WAIT_L(0); PG8_BAR; PG8_MMA(0, 0, At, B0); PG8_MMA(0, 1, At, B1); PG8_BAR; PG8_SCHED;
;             PG8_LDA(At, 0, 1); PG8_STAGE(PG8_SB(0, 0), b2, voffB); PG8_STAGE(PG8_SB(0, 1), b2 + hstepB, voffB); PG8_STAGE_A(PG8_SA(0, 0), a2, 0, last);
;             PG8_WAIT_V(8); PG8_WAIT_L(0); PG8_BAR; PG8_MMA(1, 0, At, B0); PG8_MMA(1, 1, At, B1); PG8_BAR; PG8_SCHED;
.LBB0_2036:
	v_add_u32_e32 v149, s43, v145
	ds_read_b128 v[140:143], v149
	ds_read_b128 v[150:153], v149 offset:1024
	ds_read_b128 v[154:157], v149 offset:2048
	ds_read_b128 v[158:161], v149 offset:3072
	v_add_u32_e32 v149, s67, v145
	ds_read_b128 v[162:165], v149
	ds_read_b128 v[166:169], v149 offset:1024
	ds_read_b128 v[170:173], v149 offset:2048
	ds_read_b128 v[174:177], v149 offset:3072
	s_add_u32 s20, s18, 0xfffc0080
	s_addc_u32 s21, s19, -1
	s_cmp_eq_u32 s63, 12
	s_cselect_b32 s23, s13, s21
	s_cselect_b32 s22, s12, s20
	s_cselect_b32 s21, s15, s11
	s_cselect_b32 s20, s14, s9
	v_lshl_add_u64 v[214:215], s[18:19], 0, v[136:137]
	s_add_i32 m0, s44, 0xc000
	ds_read_b128 v[178:181], v148
	ds_read_b128 v[182:185], v148 offset:1024
	ds_read_b128 v[186:189], v148 offset:2048
	ds_read_b128 v[190:193], v148 offset:3072
	ds_read_b128 v[198:201], v148 offset:4096
	ds_read_b128 v[202:205], v148 offset:5120
	ds_read_b128 v[206:209], v148 offset:6144
	ds_read_b128 v[210:213], v148 offset:7168
	global_load_lds_dwordx4 v[214:215], off
	v_lshl_add_u64 v[214:215], s[18:19], 0, v[138:139]
	s_add_i32 m0, s44, 0xe000
	s_nop 0
	global_load_lds_dwordx4 v[214:215], off
	s_waitcnt vmcnt(8)
	s_waitcnt lgkmcnt(0)
	s_barrier
	s_waitcnt lgkmcnt(0)
	v_mfma_f32_16x16x32_bf16 v[124:127], v[140:143], v[178:181], v[124:127]
	v_mfma_f32_16x16x32_bf16 v[120:123], v[154:157], v[178:181], v[120:123]
	v_mfma_f32_16x16x32_bf16 v[108:111], v[140:143], v[186:189], v[108:111]
	v_mfma_f32_16x16x32_bf16 v[104:107], v[154:157], v[186:189], v[104:107]
	v_mfma_f32_16x16x32_bf16 v[92:95], v[140:143], v[198:201], v[92:95]
	v_mfma_f32_16x16x32_bf16 v[88:91], v[154:157], v[198:201], v[88:91]
	v_mfma_f32_16x16x32_bf16 v[76:79], v[140:143], v[206:209], v[76:79]
	v_mfma_f32_16x16x32_bf16 v[72:75], v[154:157], v[206:209], v[72:75]
	v_mfma_f32_16x16x32_bf16 v[124:127], v[150:153], v[182:185], v[124:127]
	v_mfma_f32_16x16x32_bf16 v[120:123], v[158:161], v[182:185], v[120:123]
	v_mfma_f32_16x16x32_bf16 v[108:111], v[150:153], v[190:193], v[108:111]
	v_mfma_f32_16x16x32_bf16 v[104:107], v[158:161], v[190:193], v[104:107]
	v_mfma_f32_16x16x32_bf16 v[92:95], v[150:153], v[202:205], v[92:95]
	v_mfma_f32_16x16x32_bf16 v[88:91], v[158:161], v[202:205], v[88:91]
	v_mfma_f32_16x16x32_bf16 v[76:79], v[150:153], v[210:213], v[76:79]
	v_mfma_f32_16x16x32_bf16 v[72:75], v[158:161], v[210:213], v[72:75]
	v_mfma_f32_16x16x32_bf16 v[116:119], v[162:165], v[178:181], v[116:119]
	v_mfma_f32_16x16x32_bf16 v[112:115], v[170:173], v[178:181], v[112:115]
	v_mfma_f32_16x16x32_bf16 v[100:103], v[162:165], v[186:189], v[100:103]
	v_mfma_f32_16x16x32_bf16 v[96:99], v[170:173], v[186:189], v[96:99]
	v_mfma_f32_16x16x32_bf16 v[84:87], v[162:165], v[198:201], v[84:87]
	v_mfma_f32_16x16x32_bf16 v[80:83], v[170:173], v[198:201], v[80:83]
	v_mfma_f32_16x16x32_bf16 v[68:71], v[162:165], v[206:209], v[68:71]
	v_mfma_f32_16x16x32_bf16 v[64:67], v[170:173], v[206:209], v[64:67]
	v_mfma_f32_16x16x32_bf16 v[116:119], v[166:169], v[182:185], v[116:119]
	v_mfma_f32_16x16x32_bf16 v[112:115], v[174:177], v[182:185], v[112:115]
	v_mfma_f32_16x16x32_bf16 v[100:103], v[166:169], v[190:193], v[100:103]
	v_mfma_f32_16x16x32_bf16 v[96:99], v[174:177], v[190:193], v[96:99]
	v_mfma_f32_16x16x32_bf16 v[84:87], v[166:169], v[202:205], v[84:87]
	v_mfma_f32_16x16x32_bf16 v[80:83], v[174:177], v[202:205], v[80:83]
	v_mfma_f32_16x16x32_bf16 v[68:71], v[166:169], v[210:213], v[68:71]
	v_mfma_f32_16x16x32_bf16 v[64:67], v[174:177], v[210:213], v[64:67]
	s_barrier
	s_add_i32 s46, s43, s33
	v_lshl_add_u64 v[214:215], s[20:21], 0, v[128:129]
	s_mov_b32 m0, s46
	ds_read_b128 v[178:181], v148 offset:16384
	ds_read_b128 v[182:185], v148 offset:17408
	ds_read_b128 v[186:189], v148 offset:18432
	ds_read_b128 v[190:193], v148 offset:19456
	ds_read_b128 v[198:201], v148 offset:20480
	ds_read_b128 v[202:205], v148 offset:21504
	ds_read_b128 v[206:209], v148 offset:22528
	ds_read_b128 v[210:213], v148 offset:23552
	global_load_lds_dwordx4 v[214:215], off
	s_add_i32 m0, s46, 0x2000
	s_add_u32 s78, s20, 0x40000
	v_lshl_add_u64 v[216:217], s[20:21], 0, v[134:135]
	s_addc_u32 s79, s21, 0
	s_add_i32 s46, s67, s33
	global_load_lds_dwordx4 v[216:217], off
	v_lshl_add_u64 v[218:219], s[78:79], 0, v[128:129]
	s_mov_b32 m0, s46
	v_lshl_add_u64 v[220:221], s[22:23], 0, v[132:133]
	global_load_lds_dwordx4 v[218:219], off
	v_lshl_add_u64 v[218:219], s[78:79], 0, v[134:135]
	s_add_i32 m0, s46, 0x2000
	s_nop 0
	global_load_lds_dwordx4 v[218:219], off
	v_lshl_add_u64 v[218:219], s[22:23], 0, v[130:131]
	s_mov_b32 m0, s44
	s_nop 0
	global_load_lds_dwordx4 v[218:219], off
	s_mov_b32 m0, s48
	s_nop 0
	global_load_lds_dwordx4 v[220:221], off
	s_waitcnt vmcnt(8)
	s_waitcnt lgkmcnt(0)
	s_barrier
; #define PG8_STAGE_A(bufoff, gbase, h, nx) do { _Pragma("unroll") for (int _i = 0; _i < 2; ++_i) { \
;         const unsigned vo_ = GA ? ((nx) ? vgn[h][_i] : vgc[h][_i]) : voffA[_i]; \
;         __builtin_amdgcn_global_load_lds((const unsigned*)((const char*)(gbase) + vo_), (PG8_LAS unsigned*)(lds + (bufoff) + ldsw + _i * 8192), 16, 0, 0); } } while (0)
; #define PG8_LDA(dst, b, h) do { _Pragma("unroll") for (int m = 0; m < 4; ++m) _Pragma("unroll") for (int k = 0; k < 2; ++k) dst[m][k] = *(const PG8_LAS bf16x8*)(lds + PG8_SA(b, h) + aoff + m * 2048 + k * 1024); } while (0)
; #define PG8_LDB(dst, b, h) do { _Pragma("unroll") for (int n = 0; n < 2; ++n) _Pragma("unroll") for (int k = 0; k < 2; ++k) dst[n][k] = *(const PG8_LAS bf16x8*)(lds + PG8_SB(b, h) + boff + n * 2048 + k * 1024); } while (0)
; #define PG8_MMA(ai, bj, At, Bt) do { __builtin_amdgcn_s_setprio(1); _Pragma("unroll") for (int m = 0; m < 4; ++m) _Pragma("unroll") for (int n = 0; n < 2; ++n) _Pragma("unroll") for (int k = 0; k < 2; ++k) \
;         acc[ai][bj][m][n] = __builtin_amdgcn_mfma_f32_16x16x32_bf16(Bt[n][k], At[m][k], acc[ai][bj][m][n], 0, 0, 0); __builtin_amdgcn_s_setprio(0); } while (0)
; #define PG8_WAIT_V(n) asm volatile("s_waitcnt vmcnt(" #n ")" ::: "memory")
; #define PG8_WAIT_L(n) asm volatile("s_waitcnt lgkmcnt(" #n ")" ::: "memory")
; #define PG8_BAR __builtin_amdgcn_s_barrier()
; #define PG8_SCHED __builtin_amdgcn_sched_barrier(0)
; template <class Epi, class Sched>
; __device__ __forceinline__ void gemm_phase(const int WID_, PG8_LAS unsigned char* lds, const Sched& S, const Epi& E) {
;     ...
;             PG8_WAIT_V(8); PG8_WAIT_L(0); PG8_BAR; PG8_MMA(1, 0, At, B0); PG8_MMA(1, 1, At, B1); PG8_BAR; PG8_SCHED;
;             PG8_LDB(B0, 1, 0); PG8_LDB(B1, 1, 1); PG8_SCHED; PG8_LDA(At, 1, 0); PG8_STAGE_A(PG8_SA(0, 1), a2 + hstepA, 1, last);
;             PG8_WAIT_V(8); PG8_WAIT_L(0); PG8_BAR; PG8_MMA(0, 0, At, B0); PG8_MMA(0, 1, At, B1); PG8_BAR; PG8_SCHED;
	s_waitcnt lgkmcnt(0)
	v_mfma_f32_16x16x32_bf16 v[60:63], v[140:143], v[178:181], v[60:63]
	v_mfma_f32_16x16x32_bf16 v[56:59], v[154:157], v[178:181], v[56:59]
	v_mfma_f32_16x16x32_bf16 v[44:47], v[140:143], v[186:189], v[44:47]
	v_mfma_f32_16x16x32_bf16 v[40:43], v[154:157], v[186:189], v[40:43]
	v_mfma_f32_16x16x32_bf16 v[28:31], v[140:143], v[198:201], v[28:31]
	v_mfma_f32_16x16x32_bf16 v[24:27], v[154:157], v[198:201], v[24:27]
	v_mfma_f32_16x16x32_bf16 v[12:15], v[140:143], v[206:209], v[12:15]
	v_mfma_f32_16x16x32_bf16 v[8:11], v[154:157], v[206:209], v[8:11]
	v_mfma_f32_16x16x32_bf16 v[60:63], v[150:153], v[182:185], v[60:63]
	v_mfma_f32_16x16x32_bf16 v[56:59], v[158:161], v[182:185], v[56:59]
	v_mfma_f32_16x16x32_bf16 v[44:47], v[150:153], v[190:193], v[44:47]
	v_mfma_f32_16x16x32_bf16 v[40:43], v[158:161], v[190:193], v[40:43]
	v_mfma_f32_16x16x32_bf16 v[28:31], v[150:153], v[202:205], v[28:31]
	v_mfma_f32_16x16x32_bf16 v[24:27], v[158:161], v[202:205], v[24:27]
	v_mfma_f32_16x16x32_bf16 v[12:15], v[150:153], v[210:213], v[12:15]
	v_mfma_f32_16x16x32_bf16 v[8:11], v[158:161], v[210:213], v[8:11]
	v_mfma_f32_16x16x32_bf16 v[52:55], v[162:165], v[178:181], v[52:55]
	v_mfma_f32_16x16x32_bf16 v[48:51], v[170:173], v[178:181], v[48:51]
	v_mfma_f32_16x16x32_bf16 v[36:39], v[162:165], v[186:189], v[36:39]
	v_mfma_f32_16x16x32_bf16 v[32:35], v[170:173], v[186:189], v[32:35]
	v_mfma_f32_16x16x32_bf16 v[20:23], v[162:165], v[198:201], v[20:23]
	v_mfma_f32_16x16x32_bf16 v[16:19], v[170:173], v[198:201], v[16:19]
	v_mfma_f32_16x16x32_bf16 v[4:7], v[162:165], v[206:209], v[4:7]
	v_mfma_f32_16x16x32_bf16 v[0:3], v[170:173], v[206:209], v[0:3]
	v_mfma_f32_16x16x32_bf16 v[52:55], v[166:169], v[182:185], v[52:55]
	v_mfma_f32_16x16x32_bf16 v[48:51], v[174:177], v[182:185], v[48:51]
	v_mfma_f32_16x16x32_bf16 v[36:39], v[166:169], v[190:193], v[36:39]
	v_mfma_f32_16x16x32_bf16 v[32:35], v[174:177], v[190:193], v[32:35]
	v_mfma_f32_16x16x32_bf16 v[20:23], v[166:169], v[202:205], v[20:23]
	v_mfma_f32_16x16x32_bf16 v[16:19], v[174:177], v[202:205], v[16:19]
	v_mfma_f32_16x16x32_bf16 v[4:7], v[166:169], v[210:213], v[4:7]
	v_mfma_f32_16x16x32_bf16 v[0:3], v[174:177], v[210:213], v[0:3]
	s_barrier
	v_add_u32_e32 v149, s82, v145
	ds_read_b128 v[140:143], v149
	ds_read_b128 v[150:153], v149 offset:1024
	ds_read_b128 v[154:157], v149 offset:2048
	ds_read_b128 v[158:161], v149 offset:3072
	v_add_u32_e32 v149, s83, v145
	ds_read_b128 v[162:165], v149
	ds_read_b128 v[166:169], v149 offset:1024
	ds_read_b128 v[170:173], v149 offset:2048
	ds_read_b128 v[174:177], v149 offset:3072
	s_add_u32 s22, s22, 0x40000
	s_addc_u32 s23, s23, 0
	s_mov_b32 m0, s49
	v_lshl_add_u64 v[222:223], s[22:23], 0, v[130:131]
	ds_read_b128 v[178:181], v148 offset:32768
	ds_read_b128 v[182:185], v148 offset:33792
	ds_read_b128 v[186:189], v148 offset:34816
	ds_read_b128 v[190:193], v148 offset:35840
	ds_read_b128 v[198:201], v148 offset:36864
	ds_read_b128 v[202:205], v148 offset:37888
	ds_read_b128 v[206:209], v148 offset:38912
	ds_read_b128 v[210:213], v148 offset:39936
	global_load_lds_dwordx4 v[222:223], off
	v_lshl_add_u64 v[222:223], s[22:23], 0, v[132:133]
	s_mov_b32 m0, s50
	s_nop 0
	global_load_lds_dwordx4 v[222:223], off
	s_waitcnt vmcnt(8)
	s_waitcnt lgkmcnt(0)
	s_barrier
	s_waitcnt lgkmcnt(0)
	v_mfma_f32_16x16x32_bf16 v[124:127], v[140:143], v[178:181], v[124:127]
	v_mfma_f32_16x16x32_bf16 v[120:123], v[154:157], v[178:181], v[120:123]
	v_mfma_f32_16x16x32_bf16 v[108:111], v[140:143], v[186:189], v[108:111]
	v_mfma_f32_16x16x32_bf16 v[104:107], v[154:157], v[186:189], v[104:107]
	v_mfma_f32_16x16x32_bf16 v[92:95], v[140:143], v[198:201], v[92:95]
	v_mfma_f32_16x16x32_bf16 v[88:91], v[154:157], v[198:201], v[88:91]
	v_mfma_f32_16x16x32_bf16 v[76:79], v[140:143], v[206:209], v[76:79]
	v_mfma_f32_16x16x32_bf16 v[72:75], v[154:157], v[206:209], v[72:75]
	v_mfma_f32_16x16x32_bf16 v[124:127], v[150:153], v[182:185], v[124:127]
	v_mfma_f32_16x16x32_bf16 v[120:123], v[158:161], v[182:185], v[120:123]
	v_mfma_f32_16x16x32_bf16 v[108:111], v[150:153], v[190:193], v[108:111]
	v_mfma_f32_16x16x32_bf16 v[104:107], v[158:161], v[190:193], v[104:107]
	v_mfma_f32_16x16x32_bf16 v[92:95], v[150:153], v[202:205], v[92:95]
	v_mfma_f32_16x16x32_bf16 v[88:91], v[158:161], v[202:205], v[88:91]
	v_mfma_f32_16x16x32_bf16 v[76:79], v[150:153], v[210:213], v[76:79]
	v_mfma_f32_16x16x32_bf16 v[72:75], v[158:161], v[210:213], v[72:75]
	v_mfma_f32_16x16x32_bf16 v[116:119], v[162:165], v[178:181], v[116:119]
	v_mfma_f32_16x16x32_bf16 v[112:115], v[170:173], v[178:181], v[112:115]
	v_mfma_f32_16x16x32_bf16 v[100:103], v[162:165], v[186:189], v[100:103]
	v_mfma_f32_16x16x32_bf16 v[96:99], v[170:173], v[186:189], v[96:99]
	v_mfma_f32_16x16x32_bf16 v[84:87], v[162:165], v[198:201], v[84:87]
	v_mfma_f32_16x16x32_bf16 v[80:83], v[170:173], v[198:201], v[80:83]
	v_mfma_f32_16x16x32_bf16 v[68:71], v[162:165], v[206:209], v[68:71]
	v_mfma_f32_16x16x32_bf16 v[64:67], v[170:173], v[206:209], v[64:67]
	v_mfma_f32_16x16x32_bf16 v[116:119], v[166:169], v[182:185], v[116:119]
	v_mfma_f32_16x16x32_bf16 v[112:115], v[174:177], v[182:185], v[112:115]
	v_mfma_f32_16x16x32_bf16 v[100:103], v[166:169], v[190:193], v[100:103]
	v_mfma_f32_16x16x32_bf16 v[96:99], v[174:177], v[190:193], v[96:99]
	v_mfma_f32_16x16x32_bf16 v[84:87], v[166:169], v[202:205], v[84:87]
	v_mfma_f32_16x16x32_bf16 v[80:83], v[174:177], v[202:205], v[80:83]
	v_mfma_f32_16x16x32_bf16 v[68:71], v[166:169], v[210:213], v[68:71]
	v_mfma_f32_16x16x32_bf16 v[64:67], v[174:177], v[210:213], v[64:67]
	s_barrier
; #define PG8_STAGE(bufoff, gbase, voff) do { _Pragma("unroll") for (int _i = 0; _i < 2; ++_i) \
;         __builtin_amdgcn_global_load_lds((const unsigned*)((const char*)(gbase) + (voff)[_i]), (PG8_LAS unsigned*)(lds + (bufoff) + ldsw + _i * 8192), 16, 0, 0); } while (0)
; #define PG8_STAGE_A(bufoff, gbase, h, nx) do { _Pragma("unroll") for (int _i = 0; _i < 2; ++_i) { \
;         const unsigned vo_ = GA ? ((nx) ? vgn[h][_i] : vgc[h][_i]) : voffA[_i]; \
;         __builtin_amdgcn_global_load_lds((const unsigned*)((const char*)(gbase) + vo_), (PG8_LAS unsigned*)(lds + (bufoff) + ldsw + _i * 8192), 16, 0, 0); } } while (0)
; #define PG8_LDA(dst, b, h) do { _Pragma("unroll") for (int m = 0; m < 4; ++m) _Pragma("unroll") for (int k = 0; k < 2; ++k) dst[m][k] = *(const PG8_LAS bf16x8*)(lds + PG8_SA(b, h) + aoff + m * 2048 + k * 1024); } while (0)
; #define PG8_MMA(ai, bj, At, Bt) do { __builtin_amdgcn_s_setprio(1); _Pragma("unroll") for (int m = 0; m < 4; ++m) _Pragma("unroll") for (int n = 0; n < 2; ++n) _Pragma("unroll") for (int k = 0; k < 2; ++k) \
;         acc[ai][bj][m][n] = __builtin_amdgcn_mfma_f32_16x16x32_bf16(Bt[n][k], At[m][k], acc[ai][bj][m][n], 0, 0, 0); __builtin_amdgcn_s_setprio(0); } while (0)
; #define PG8_WAIT_V(n) asm volatile("s_waitcnt vmcnt(" #n ")" ::: "memory")
; #define PG8_WAIT_L(n) asm volatile("s_waitcnt lgkmcnt(" #n ")" ::: "memory")
; #define PG8_BAR __builtin_amdgcn_s_barrier()
; #define PG8_SCHED __builtin_amdgcn_sched_barrier(0)
; template <class Epi, class Sched>
; __device__ __forceinline__ void gemm_phase(const int WID_, PG8_LAS unsigned char* lds, const Sched& S, const Epi& E) {
;     ...
;             PG8_LDA(At, 1, 1); PG8_STAGE(PG8_SB(1, 0), b3, voffB); PG8_STAGE(PG8_SB(1, 1), b3 + hstepB, voffB); PG8_STAGE_A(PG8_SA(1, 0), a3, 0, last);
;             PG8_WAIT_V(8); PG8_WAIT_L(0); PG8_BAR; PG8_MMA(1, 0, At, B0); PG8_MMA(1, 1, At, B1); PG8_BAR; PG8_SCHED;
;         }
;         if (wr == 0) PG8_BAR;
	s_add_i32 s22, s82, s33
	v_lshl_add_u64 v[214:215], v[214:215], 0, s[68:69]
	s_mov_b32 m0, s22
	ds_read_b128 v[178:181], v148 offset:49152
	ds_read_b128 v[182:185], v148 offset:50176
	ds_read_b128 v[186:189], v148 offset:51200
	ds_read_b128 v[190:193], v148 offset:52224
	ds_read_b128 v[198:201], v148 offset:53248
	ds_read_b128 v[202:205], v148 offset:54272
	ds_read_b128 v[206:209], v148 offset:55296
	ds_read_b128 v[210:213], v148 offset:56320
	global_load_lds_dwordx4 v[214:215], off
	s_add_i32 m0, s22, 0x2000
	s_add_u32 s20, s20, 0x40080
	v_lshl_add_u64 v[214:215], v[216:217], 0, s[68:69]
	s_addc_u32 s21, s21, 0
	s_add_i32 s22, s83, s33
	global_load_lds_dwordx4 v[214:215], off
	v_lshl_add_u64 v[214:215], s[20:21], 0, v[128:129]
	s_mov_b32 m0, s22
	s_nop 0
	global_load_lds_dwordx4 v[214:215], off
	v_lshl_add_u64 v[214:215], s[20:21], 0, v[134:135]
	s_add_i32 m0, s22, 0x2000
	s_nop 0
	global_load_lds_dwordx4 v[214:215], off
	v_lshl_add_u64 v[214:215], v[218:219], 0, s[68:69]
	s_mov_b32 m0, s51
	s_nop 0
	global_load_lds_dwordx4 v[214:215], off
	v_lshl_add_u64 v[214:215], v[220:221], 0, s[68:69]
	s_mov_b32 m0, s60
	s_nop 0
	global_load_lds_dwordx4 v[214:215], off
	s_waitcnt vmcnt(8)
	s_waitcnt lgkmcnt(0)
	s_barrier
	s_waitcnt lgkmcnt(0)
	v_mfma_f32_16x16x32_bf16 v[60:63], v[140:143], v[178:181], v[60:63]
	v_mfma_f32_16x16x32_bf16 v[56:59], v[154:157], v[178:181], v[56:59]
	v_mfma_f32_16x16x32_bf16 v[44:47], v[140:143], v[186:189], v[44:47]
	v_mfma_f32_16x16x32_bf16 v[40:43], v[154:157], v[186:189], v[40:43]
	v_mfma_f32_16x16x32_bf16 v[28:31], v[140:143], v[198:201], v[28:31]
	v_mfma_f32_16x16x32_bf16 v[24:27], v[154:157], v[198:201], v[24:27]
	v_mfma_f32_16x16x32_bf16 v[12:15], v[140:143], v[206:209], v[12:15]
	v_mfma_f32_16x16x32_bf16 v[8:11], v[154:157], v[206:209], v[8:11]
	v_mfma_f32_16x16x32_bf16 v[60:63], v[150:153], v[182:185], v[60:63]
	v_mfma_f32_16x16x32_bf16 v[56:59], v[158:161], v[182:185], v[56:59]
	v_mfma_f32_16x16x32_bf16 v[44:47], v[150:153], v[190:193], v[44:47]
	v_mfma_f32_16x16x32_bf16 v[40:43], v[158:161], v[190:193], v[40:43]
	v_mfma_f32_16x16x32_bf16 v[28:31], v[150:153], v[202:205], v[28:31]
	v_mfma_f32_16x16x32_bf16 v[24:27], v[158:161], v[202:205], v[24:27]
	v_mfma_f32_16x16x32_bf16 v[12:15], v[150:153], v[210:213], v[12:15]
	v_mfma_f32_16x16x32_bf16 v[8:11], v[158:161], v[210:213], v[8:11]
	v_mfma_f32_16x16x32_bf16 v[52:55], v[162:165], v[178:181], v[52:55]
	v_mfma_f32_16x16x32_bf16 v[48:51], v[170:173], v[178:181], v[48:51]
	v_mfma_f32_16x16x32_bf16 v[36:39], v[162:165], v[186:189], v[36:39]
	v_mfma_f32_16x16x32_bf16 v[32:35], v[170:173], v[186:189], v[32:35]
	v_mfma_f32_16x16x32_bf16 v[20:23], v[162:165], v[198:201], v[20:23]
	v_mfma_f32_16x16x32_bf16 v[16:19], v[170:173], v[198:201], v[16:19]
	v_mfma_f32_16x16x32_bf16 v[4:7], v[162:165], v[206:209], v[4:7]
	v_mfma_f32_16x16x32_bf16 v[0:3], v[170:173], v[206:209], v[0:3]
	v_mfma_f32_16x16x32_bf16 v[52:55], v[166:169], v[182:185], v[52:55]
	v_mfma_f32_16x16x32_bf16 v[48:51], v[174:177], v[182:185], v[48:51]
	v_mfma_f32_16x16x32_bf16 v[36:39], v[166:169], v[190:193], v[36:39]
	v_mfma_f32_16x16x32_bf16 v[32:35], v[174:177], v[190:193], v[32:35]
	v_mfma_f32_16x16x32_bf16 v[20:23], v[166:169], v[202:205], v[20:23]
	v_mfma_f32_16x16x32_bf16 v[16:19], v[174:177], v[202:205], v[16:19]
	v_mfma_f32_16x16x32_bf16 v[4:7], v[166:169], v[210:213], v[4:7]
	v_mfma_f32_16x16x32_bf16 v[0:3], v[174:177], v[210:213], v[0:3]
	s_barrier
	s_add_i32 s63, s63, 2
	s_add_u32 s18, s18, 0x100
	s_addc_u32 s19, s19, 0
	s_add_u32 s9, s9, 0x100
	s_addc_u32 s11, s11, 0
	s_cmp_gt_u32 s63, 13
	s_cbranch_scc0 .LBB0_2036
	s_and_b64 vcc, exec, s[6:7]
	s_cbranch_vccz .LBB0_2039
	s_barrier

; #define PG8_STAGE(bufoff, gbase, voff) do { _Pragma("unroll") for (int _i = 0; _i < 2; ++_i) \
;         __builtin_amdgcn_global_load_lds((const unsigned*)((const char*)(gbase) + (voff)[_i]), (PG8_LAS unsigned*)(lds + (bufoff) + ldsw + _i * 8192), 16, 0, 0); } while (0)
; #define PG8_STAGE_A(bufoff, gbase, h, nx) do { _Pragma("unroll") for (int _i = 0; _i < 2; ++_i) { \
;         const unsigned vo_ = GA ? ((nx) ? vgn[h][_i] : vgc[h][_i]) : voffA[_i]; \
;         __builtin_amdgcn_global_load_lds((const unsigned*)((const char*)(gbase) + vo_), (PG8_LAS unsigned*)(lds + (bufoff) + ldsw + _i * 8192), 16, 0, 0); } } while (0)
; #define PG8_LDA(dst, b, h) do { _Pragma("unroll") for (int m = 0; m < 4; ++m) _Pragma("unroll") for (int k = 0; k < 2; ++k) dst[m][k] = *(const PG8_LAS bf16x8*)(lds + PG8_SA(b, h) + aoff + m * 2048 + k * 1024); } while (0)
; #define PG8_LDB(dst, b, h) do { _Pragma("unroll") for (int n = 0; n < 2; ++n) _Pragma("unroll") for (int k = 0; k < 2; ++k) dst[n][k] = *(const PG8_LAS bf16x8*)(lds + PG8_SB(b, h) + boff + n * 2048 + k * 1024); } while (0)
; #define PG8_WAIT_V(n) asm volatile("s_waitcnt vmcnt(" #n ")" ::: "memory")
; #define PG8_WAIT_L(n) asm volatile("s_waitcnt lgkmcnt(" #n ")" ::: "memory")
; #define PG8_BAR __builtin_amdgcn_s_barrier()
; #define PG8_SCHED __builtin_amdgcn_sched_barrier(0)
; template <class Epi, class Sched>
; __device__ __forceinline__ void gemm_phase(const int WID_, PG8_LAS unsigned char* lds, const Sched& S, const Epi& E) {
;     ...
;         for (int t = 0; t < nt; t += 2) {
;             const bool last = (t == nt - 2);
;             const char* a1 = cA + (size_t)(t + 1) * kstep;
;             const char* a2 = last ? nA : cA + (size_t)(t + 2) * kstep; const char* b2 = last ? nB : cB + (size_t)(t + 2) * kstep;
;             const char* a3 = a2 + kstep; const char* b3 = b2 + kstep;
;             PG8_LDB(B0, 0, 0); PG8_LDB(B1, 0, 1); PG8_SCHED; PG8_LDA(At, 0, 0); PG8_STAGE_A(PG8_SA(1, 1), a1 + hstepA, 1, false);
;             PG8_WAIT_V(8); PG8_WAIT_L(0); PG8_BAR; PG8_MMA(0, 0, At, B0); PG8_MMA(0, 1, At, B1); PG8_BAR; PG8_SCHED;
;             PG8_LDA(At, 0, 1); PG8_STAGE(PG8_SB(0, 0), b2, voffB); PG8_STAGE(PG8_SB(0, 1), b2 + hstepB, voffB); PG8_STAGE_A(PG8_SA(0, 0), a2, 0, last);
;             PG8_WAIT_V(8); PG8_WAIT_L(0); PG8_BAR; PG8_MMA(1, 0, At, B0); PG8_MMA(1, 1, At, B1); PG8_BAR; PG8_SCHED;
.LBB0_2070:
	v_add_u32_e32 v152, s43, v199
	v_add_u32_e32 v168, s67, v199
	ds_read_b128 v[140:143], v152
	ds_read_b128 v[144:147], v152 offset:1024
	ds_read_b128 v[148:151], v152 offset:2048
	ds_read_b128 v[152:155], v152 offset:3072
	ds_read_b128 v[156:159], v168
	ds_read_b128 v[160:163], v168 offset:1024
	ds_read_b128 v[164:167], v168 offset:2048
	ds_read_b128 v[168:171], v168 offset:3072
	s_add_u32 s46, s22, 0xfffc0080
	s_addc_u32 s47, s23, -1
	s_cmp_eq_u32 vcc_lo, 12
	s_cselect_b32 s81, s17, s47
	s_cselect_b32 s80, s16, s46
	s_cselect_b32 s79, s19, s15
	s_cselect_b32 s78, s18, s13
	v_lshl_add_u64 v[192:193], s[22:23], 0, v[136:137]
	s_add_i32 m0, s51, 0xc000
	ds_read_b128 v[172:175], v219
	ds_read_b128 v[176:179], v219 offset:1024
	ds_read_b128 v[180:183], v219 offset:2048
	ds_read_b128 v[184:187], v219 offset:3072
	ds_read_b128 v[188:191], v219 offset:4096
	ds_read_b128 v[222:225], v219 offset:5120
	ds_read_b128 v[226:229], v219 offset:6144
	ds_read_b128 v[230:233], v219 offset:7168
	global_load_lds_dwordx4 v[192:193], off
	v_lshl_add_u64 v[192:193], s[22:23], 0, v[138:139]
	s_add_i32 m0, s51, 0xe000
	s_nop 0
	global_load_lds_dwordx4 v[192:193], off
	s_waitcnt vmcnt(8)
	s_waitcnt lgkmcnt(0)
	s_barrier
	s_waitcnt lgkmcnt(0)
	v_mfma_f32_16x16x32_bf16 v[124:127], v[140:143], v[172:175], v[124:127]
	v_mfma_f32_16x16x32_bf16 v[120:123], v[148:151], v[172:175], v[120:123]
	v_mfma_f32_16x16x32_bf16 v[108:111], v[140:143], v[180:183], v[108:111]
	v_mfma_f32_16x16x32_bf16 v[104:107], v[148:151], v[180:183], v[104:107]
	v_mfma_f32_16x16x32_bf16 v[92:95], v[140:143], v[188:191], v[92:95]
	v_mfma_f32_16x16x32_bf16 v[88:91], v[148:151], v[188:191], v[88:91]
	v_mfma_f32_16x16x32_bf16 v[76:79], v[140:143], v[226:229], v[76:79]
	v_mfma_f32_16x16x32_bf16 v[72:75], v[148:151], v[226:229], v[72:75]
	v_mfma_f32_16x16x32_bf16 v[124:127], v[144:147], v[176:179], v[124:127]
	v_mfma_f32_16x16x32_bf16 v[120:123], v[152:155], v[176:179], v[120:123]
	v_mfma_f32_16x16x32_bf16 v[108:111], v[144:147], v[184:187], v[108:111]
	v_mfma_f32_16x16x32_bf16 v[104:107], v[152:155], v[184:187], v[104:107]
	v_mfma_f32_16x16x32_bf16 v[92:95], v[144:147], v[222:225], v[92:95]
	v_mfma_f32_16x16x32_bf16 v[88:91], v[152:155], v[222:225], v[88:91]
	v_mfma_f32_16x16x32_bf16 v[76:79], v[144:147], v[230:233], v[76:79]
	v_mfma_f32_16x16x32_bf16 v[72:75], v[152:155], v[230:233], v[72:75]
	v_mfma_f32_16x16x32_bf16 v[116:119], v[156:159], v[172:175], v[116:119]
	v_mfma_f32_16x16x32_bf16 v[112:115], v[164:167], v[172:175], v[112:115]
	v_mfma_f32_16x16x32_bf16 v[100:103], v[156:159], v[180:183], v[100:103]
	v_mfma_f32_16x16x32_bf16 v[96:99], v[164:167], v[180:183], v[96:99]
	v_mfma_f32_16x16x32_bf16 v[84:87], v[156:159], v[188:191], v[84:87]
	v_mfma_f32_16x16x32_bf16 v[80:83], v[164:167], v[188:191], v[80:83]
	v_mfma_f32_16x16x32_bf16 v[68:71], v[156:159], v[226:229], v[68:71]
	v_mfma_f32_16x16x32_bf16 v[64:67], v[164:167], v[226:229], v[64:67]
	v_mfma_f32_16x16x32_bf16 v[116:119], v[160:163], v[176:179], v[116:119]
	v_mfma_f32_16x16x32_bf16 v[112:115], v[168:171], v[176:179], v[112:115]
	v_mfma_f32_16x16x32_bf16 v[100:103], v[160:163], v[184:187], v[100:103]
	v_mfma_f32_16x16x32_bf16 v[96:99], v[168:171], v[184:187], v[96:99]
	v_mfma_f32_16x16x32_bf16 v[84:87], v[160:163], v[222:225], v[84:87]
	v_mfma_f32_16x16x32_bf16 v[80:83], v[168:171], v[222:225], v[80:83]
	v_mfma_f32_16x16x32_bf16 v[68:71], v[160:163], v[230:233], v[68:71]
	v_mfma_f32_16x16x32_bf16 v[64:67], v[168:171], v[230:233], v[64:67]
	s_barrier
	s_add_i32 s46, s43, s50
	v_lshl_add_u64 v[192:193], s[78:79], 0, v[128:129]
	s_mov_b32 m0, s46
	ds_read_b128 v[172:175], v219 offset:16384
	ds_read_b128 v[176:179], v219 offset:17408
	ds_read_b128 v[180:183], v219 offset:18432
	ds_read_b128 v[184:187], v219 offset:19456
	ds_read_b128 v[188:191], v219 offset:20480
	ds_read_b128 v[222:225], v219 offset:21504
	ds_read_b128 v[226:229], v219 offset:22528
	ds_read_b128 v[230:233], v219 offset:23552
	global_load_lds_dwordx4 v[192:193], off
	s_add_i32 m0, s46, 0x2000
	s_add_u32 s46, s78, 0x40000
	v_lshl_add_u64 v[234:235], s[78:79], 0, v[134:135]
	s_addc_u32 s47, s79, 0
	s_add_i32 vcc_hi, s67, s50
	global_load_lds_dwordx4 v[234:235], off
	v_lshl_add_u64 v[236:237], s[46:47], 0, v[128:129]
	s_mov_b32 m0, vcc_hi
	v_lshl_add_u64 v[238:239], s[80:81], 0, v[132:133]
	global_load_lds_dwordx4 v[236:237], off
	v_lshl_add_u64 v[236:237], s[46:47], 0, v[134:135]
	s_add_i32 m0, vcc_hi, 0x2000
	s_nop 0
	global_load_lds_dwordx4 v[236:237], off
	v_lshl_add_u64 v[236:237], s[80:81], 0, v[130:131]
	s_mov_b32 m0, s51
	s_nop 0
	global_load_lds_dwordx4 v[236:237], off
	s_mov_b32 m0, s60
	s_nop 0
	global_load_lds_dwordx4 v[238:239], off
	s_waitcnt vmcnt(8)
	s_waitcnt lgkmcnt(0)
	s_barrier
; #define PG8_STAGE_A(bufoff, gbase, h, nx) do { _Pragma("unroll") for (int _i = 0; _i < 2; ++_i) { \
;         const unsigned vo_ = GA ? ((nx) ? vgn[h][_i] : vgc[h][_i]) : voffA[_i]; \
;         __builtin_amdgcn_global_load_lds((const unsigned*)((const char*)(gbase) + vo_), (PG8_LAS unsigned*)(lds + (bufoff) + ldsw + _i * 8192), 16, 0, 0); } } while (0)
; #define PG8_LDA(dst, b, h) do { _Pragma("unroll") for (int m = 0; m < 4; ++m) _Pragma("unroll") for (int k = 0; k < 2; ++k) dst[m][k] = *(const PG8_LAS bf16x8*)(lds + PG8_SA(b, h) + aoff + m * 2048 + k * 1024); } while (0)
; #define PG8_LDB(dst, b, h) do { _Pragma("unroll") for (int n = 0; n < 2; ++n) _Pragma("unroll") for (int k = 0; k < 2; ++k) dst[n][k] = *(const PG8_LAS bf16x8*)(lds + PG8_SB(b, h) + boff + n * 2048 + k * 1024); } while (0)
; #define PG8_MMA(ai, bj, At, Bt) do { __builtin_amdgcn_s_setprio(1); _Pragma("unroll") for (int m = 0; m < 4; ++m) _Pragma("unroll") for (int n = 0; n < 2; ++n) _Pragma("unroll") for (int k = 0; k < 2; ++k) \
;         acc[ai][bj][m][n] = __builtin_amdgcn_mfma_f32_16x16x32_bf16(Bt[n][k], At[m][k], acc[ai][bj][m][n], 0, 0, 0); __builtin_amdgcn_s_setprio(0); } while (0)
; #define PG8_WAIT_V(n) asm volatile("s_waitcnt vmcnt(" #n ")" ::: "memory")
; #define PG8_WAIT_L(n) asm volatile("s_waitcnt lgkmcnt(" #n ")" ::: "memory")
; #define PG8_BAR __builtin_amdgcn_s_barrier()
; #define PG8_SCHED __builtin_amdgcn_sched_barrier(0)
; template <class Epi, class Sched>
; __device__ __forceinline__ void gemm_phase(const int WID_, PG8_LAS unsigned char* lds, const Sched& S, const Epi& E) {
;     ...
;             PG8_WAIT_V(8); PG8_WAIT_L(0); PG8_BAR; PG8_MMA(1, 0, At, B0); PG8_MMA(1, 1, At, B1); PG8_BAR; PG8_SCHED;
;             PG8_LDB(B0, 1, 0); PG8_LDB(B1, 1, 1); PG8_SCHED; PG8_LDA(At, 1, 0); PG8_STAGE_A(PG8_SA(0, 1), a2 + hstepA, 1, last);
;             PG8_WAIT_V(8); PG8_WAIT_L(0); PG8_BAR; PG8_MMA(0, 0, At, B0); PG8_MMA(0, 1, At, B1); PG8_BAR; PG8_SCHED;
	s_waitcnt lgkmcnt(0)
	v_mfma_f32_16x16x32_bf16 v[60:63], v[140:143], v[172:175], v[60:63]
	v_mfma_f32_16x16x32_bf16 v[56:59], v[148:151], v[172:175], v[56:59]
	v_mfma_f32_16x16x32_bf16 v[44:47], v[140:143], v[180:183], v[44:47]
	v_mfma_f32_16x16x32_bf16 v[40:43], v[148:151], v[180:183], v[40:43]
	v_mfma_f32_16x16x32_bf16 v[28:31], v[140:143], v[188:191], v[28:31]
	v_mfma_f32_16x16x32_bf16 v[24:27], v[148:151], v[188:191], v[24:27]
	v_mfma_f32_16x16x32_bf16 v[12:15], v[140:143], v[226:229], v[12:15]
	v_mfma_f32_16x16x32_bf16 v[8:11], v[148:151], v[226:229], v[8:11]
	v_mfma_f32_16x16x32_bf16 v[60:63], v[144:147], v[176:179], v[60:63]
	v_mfma_f32_16x16x32_bf16 v[56:59], v[152:155], v[176:179], v[56:59]
	v_mfma_f32_16x16x32_bf16 v[44:47], v[144:147], v[184:187], v[44:47]
	v_mfma_f32_16x16x32_bf16 v[40:43], v[152:155], v[184:187], v[40:43]
	v_mfma_f32_16x16x32_bf16 v[28:31], v[144:147], v[222:225], v[28:31]
	v_mfma_f32_16x16x32_bf16 v[24:27], v[152:155], v[222:225], v[24:27]
	v_mfma_f32_16x16x32_bf16 v[12:15], v[144:147], v[230:233], v[12:15]
	v_mfma_f32_16x16x32_bf16 v[8:11], v[152:155], v[230:233], v[8:11]
	v_mfma_f32_16x16x32_bf16 v[52:55], v[156:159], v[172:175], v[52:55]
	v_mfma_f32_16x16x32_bf16 v[48:51], v[164:167], v[172:175], v[48:51]
	v_mfma_f32_16x16x32_bf16 v[36:39], v[156:159], v[180:183], v[36:39]
	v_mfma_f32_16x16x32_bf16 v[32:35], v[164:167], v[180:183], v[32:35]
	v_mfma_f32_16x16x32_bf16 v[20:23], v[156:159], v[188:191], v[20:23]
	v_mfma_f32_16x16x32_bf16 v[16:19], v[164:167], v[188:191], v[16:19]
	v_mfma_f32_16x16x32_bf16 v[4:7], v[156:159], v[226:229], v[4:7]
	v_mfma_f32_16x16x32_bf16 v[0:3], v[164:167], v[226:229], v[0:3]
	v_mfma_f32_16x16x32_bf16 v[52:55], v[160:163], v[176:179], v[52:55]
	v_mfma_f32_16x16x32_bf16 v[48:51], v[168:171], v[176:179], v[48:51]
	v_mfma_f32_16x16x32_bf16 v[36:39], v[160:163], v[184:187], v[36:39]
	v_mfma_f32_16x16x32_bf16 v[32:35], v[168:171], v[184:187], v[32:35]
	v_mfma_f32_16x16x32_bf16 v[20:23], v[160:163], v[222:225], v[20:23]
	v_mfma_f32_16x16x32_bf16 v[16:19], v[168:171], v[222:225], v[16:19]
	v_mfma_f32_16x16x32_bf16 v[4:7], v[160:163], v[230:233], v[4:7]
	v_mfma_f32_16x16x32_bf16 v[0:3], v[168:171], v[230:233], v[0:3]
	s_barrier
	v_add_u32_e32 v152, s82, v199
	v_add_u32_e32 v168, s83, v199
	ds_read_b128 v[140:143], v152
	ds_read_b128 v[144:147], v152 offset:1024
	ds_read_b128 v[148:151], v152 offset:2048
	ds_read_b128 v[152:155], v152 offset:3072
	ds_read_b128 v[156:159], v168
	ds_read_b128 v[160:163], v168 offset:1024
	ds_read_b128 v[164:167], v168 offset:2048
	ds_read_b128 v[168:171], v168 offset:3072
	s_add_u32 s46, s80, 0x40000
	s_addc_u32 s47, s81, 0
	s_mov_b32 m0, s61
	v_lshl_add_u64 v[240:241], s[46:47], 0, v[130:131]
	ds_read_b128 v[172:175], v219 offset:32768
	ds_read_b128 v[176:179], v219 offset:33792
	ds_read_b128 v[180:183], v219 offset:34816
	ds_read_b128 v[184:187], v219 offset:35840
	ds_read_b128 v[188:191], v219 offset:36864
	ds_read_b128 v[222:225], v219 offset:37888
	ds_read_b128 v[226:229], v219 offset:38912
	ds_read_b128 v[230:233], v219 offset:39936
	global_load_lds_dwordx4 v[240:241], off
	v_lshl_add_u64 v[240:241], s[46:47], 0, v[132:133]
	s_mov_b32 m0, s62
	s_nop 0
	global_load_lds_dwordx4 v[240:241], off
	s_waitcnt vmcnt(8)
	s_waitcnt lgkmcnt(0)
	s_barrier
	s_waitcnt lgkmcnt(0)
	v_mfma_f32_16x16x32_bf16 v[124:127], v[140:143], v[172:175], v[124:127]
	v_mfma_f32_16x16x32_bf16 v[120:123], v[148:151], v[172:175], v[120:123]
	v_mfma_f32_16x16x32_bf16 v[108:111], v[140:143], v[180:183], v[108:111]
	v_mfma_f32_16x16x32_bf16 v[104:107], v[148:151], v[180:183], v[104:107]
	v_mfma_f32_16x16x32_bf16 v[92:95], v[140:143], v[188:191], v[92:95]
	v_mfma_f32_16x16x32_bf16 v[88:91], v[148:151], v[188:191], v[88:91]
	v_mfma_f32_16x16x32_bf16 v[76:79], v[140:143], v[226:229], v[76:79]
	v_mfma_f32_16x16x32_bf16 v[72:75], v[148:151], v[226:229], v[72:75]
	v_mfma_f32_16x16x32_bf16 v[124:127], v[144:147], v[176:179], v[124:127]
	v_mfma_f32_16x16x32_bf16 v[120:123], v[152:155], v[176:179], v[120:123]
	v_mfma_f32_16x16x32_bf16 v[108:111], v[144:147], v[184:187], v[108:111]
	v_mfma_f32_16x16x32_bf16 v[104:107], v[152:155], v[184:187], v[104:107]
	v_mfma_f32_16x16x32_bf16 v[92:95], v[144:147], v[222:225], v[92:95]
	v_mfma_f32_16x16x32_bf16 v[88:91], v[152:155], v[222:225], v[88:91]
	v_mfma_f32_16x16x32_bf16 v[76:79], v[144:147], v[230:233], v[76:79]
	v_mfma_f32_16x16x32_bf16 v[72:75], v[152:155], v[230:233], v[72:75]
	v_mfma_f32_16x16x32_bf16 v[116:119], v[156:159], v[172:175], v[116:119]
	v_mfma_f32_16x16x32_bf16 v[112:115], v[164:167], v[172:175], v[112:115]
	v_mfma_f32_16x16x32_bf16 v[100:103], v[156:159], v[180:183], v[100:103]
	v_mfma_f32_16x16x32_bf16 v[96:99], v[164:167], v[180:183], v[96:99]
	v_mfma_f32_16x16x32_bf16 v[84:87], v[156:159], v[188:191], v[84:87]
	v_mfma_f32_16x16x32_bf16 v[80:83], v[164:167], v[188:191], v[80:83]
	v_mfma_f32_16x16x32_bf16 v[68:71], v[156:159], v[226:229], v[68:71]
	v_mfma_f32_16x16x32_bf16 v[64:67], v[164:167], v[226:229], v[64:67]
	v_mfma_f32_16x16x32_bf16 v[116:119], v[160:163], v[176:179], v[116:119]
	v_mfma_f32_16x16x32_bf16 v[112:115], v[168:171], v[176:179], v[112:115]
	v_mfma_f32_16x16x32_bf16 v[100:103], v[160:163], v[184:187], v[100:103]
	v_mfma_f32_16x16x32_bf16 v[96:99], v[168:171], v[184:187], v[96:99]
	v_mfma_f32_16x16x32_bf16 v[84:87], v[160:163], v[222:225], v[84:87]
	v_mfma_f32_16x16x32_bf16 v[80:83], v[168:171], v[222:225], v[80:83]
	v_mfma_f32_16x16x32_bf16 v[68:71], v[160:163], v[230:233], v[68:71]
	v_mfma_f32_16x16x32_bf16 v[64:67], v[168:171], v[230:233], v[64:67]
	s_barrier
; #define PG8_STAGE(bufoff, gbase, voff) do { _Pragma("unroll") for (int _i = 0; _i < 2; ++_i) \
;         __builtin_amdgcn_global_load_lds((const unsigned*)((const char*)(gbase) + (voff)[_i]), (PG8_LAS unsigned*)(lds + (bufoff) + ldsw + _i * 8192), 16, 0, 0); } while (0)
; #define PG8_STAGE_A(bufoff, gbase, h, nx) do { _Pragma("unroll") for (int _i = 0; _i < 2; ++_i) { \
;         const unsigned vo_ = GA ? ((nx) ? vgn[h][_i] : vgc[h][_i]) : voffA[_i]; \
;         __builtin_amdgcn_global_load_lds((const unsigned*)((const char*)(gbase) + vo_), (PG8_LAS unsigned*)(lds + (bufoff) + ldsw + _i * 8192), 16, 0, 0); } } while (0)
; #define PG8_LDA(dst, b, h) do { _Pragma("unroll") for (int m = 0; m < 4; ++m) _Pragma("unroll") for (int k = 0; k < 2; ++k) dst[m][k] = *(const PG8_LAS bf16x8*)(lds + PG8_SA(b, h) + aoff + m * 2048 + k * 1024); } while (0)
; #define PG8_MMA(ai, bj, At, Bt) do { __builtin_amdgcn_s_setprio(1); _Pragma("unroll") for (int m = 0; m < 4; ++m) _Pragma("unroll") for (int n = 0; n < 2; ++n) _Pragma("unroll") for (int k = 0; k < 2; ++k) \
;         acc[ai][bj][m][n] = __builtin_amdgcn_mfma_f32_16x16x32_bf16(Bt[n][k], At[m][k], acc[ai][bj][m][n], 0, 0, 0); __builtin_amdgcn_s_setprio(0); } while (0)
; #define PG8_WAIT_V(n) asm volatile("s_waitcnt vmcnt(" #n ")" ::: "memory")
; #define PG8_WAIT_L(n) asm volatile("s_waitcnt lgkmcnt(" #n ")" ::: "memory")
; #define PG8_BAR __builtin_amdgcn_s_barrier()
; #define PG8_SCHED __builtin_amdgcn_sched_barrier(0)
; template <class Epi, class Sched>
; __device__ __forceinline__ void gemm_phase(const int WID_, PG8_LAS unsigned char* lds, const Sched& S, const Epi& E) {
;     ...
;             PG8_LDA(At, 1, 1); PG8_STAGE(PG8_SB(1, 0), b3, voffB); PG8_STAGE(PG8_SB(1, 1), b3 + hstepB, voffB); PG8_STAGE_A(PG8_SA(1, 0), a3, 0, last);
;             PG8_WAIT_V(8); PG8_WAIT_L(0); PG8_BAR; PG8_MMA(1, 0, At, B0); PG8_MMA(1, 1, At, B1); PG8_BAR; PG8_SCHED;
;         }
;         if (wr == 0) PG8_BAR;
	s_add_i32 s46, s82, s50
	v_lshl_add_u64 v[192:193], v[192:193], 0, s[68:69]
	s_mov_b32 m0, s46
	ds_read_b128 v[172:175], v219 offset:49152
	ds_read_b128 v[176:179], v219 offset:50176
	ds_read_b128 v[180:183], v219 offset:51200
	ds_read_b128 v[184:187], v219 offset:52224
	ds_read_b128 v[188:191], v219 offset:53248
	ds_read_b128 v[222:225], v219 offset:54272
	ds_read_b128 v[226:229], v219 offset:55296
	ds_read_b128 v[230:233], v219 offset:56320
	global_load_lds_dwordx4 v[192:193], off
	s_add_i32 m0, s46, 0x2000
	s_add_u32 s46, s78, 0x40080
	v_lshl_add_u64 v[192:193], v[234:235], 0, s[68:69]
	s_addc_u32 s47, s79, 0
	s_add_i32 s78, s83, s50
	global_load_lds_dwordx4 v[192:193], off
	v_lshl_add_u64 v[192:193], s[46:47], 0, v[128:129]
	s_mov_b32 m0, s78
	s_nop 0
	global_load_lds_dwordx4 v[192:193], off
	v_lshl_add_u64 v[192:193], s[46:47], 0, v[134:135]
	s_add_i32 m0, s78, 0x2000
	s_nop 0
	global_load_lds_dwordx4 v[192:193], off
	v_lshl_add_u64 v[192:193], v[236:237], 0, s[68:69]
	s_mov_b32 m0, s63
	s_nop 0
	global_load_lds_dwordx4 v[192:193], off
	v_lshl_add_u64 v[192:193], v[238:239], 0, s[68:69]
	s_mov_b32 m0, s86
	s_nop 0
	global_load_lds_dwordx4 v[192:193], off
	s_waitcnt vmcnt(8)
	s_waitcnt lgkmcnt(0)
	s_barrier
	s_waitcnt lgkmcnt(0)
	v_mfma_f32_16x16x32_bf16 v[60:63], v[140:143], v[172:175], v[60:63]
	v_mfma_f32_16x16x32_bf16 v[56:59], v[148:151], v[172:175], v[56:59]
	v_mfma_f32_16x16x32_bf16 v[44:47], v[140:143], v[180:183], v[44:47]
	v_mfma_f32_16x16x32_bf16 v[40:43], v[148:151], v[180:183], v[40:43]
	v_mfma_f32_16x16x32_bf16 v[28:31], v[140:143], v[188:191], v[28:31]
	v_mfma_f32_16x16x32_bf16 v[24:27], v[148:151], v[188:191], v[24:27]
	v_mfma_f32_16x16x32_bf16 v[12:15], v[140:143], v[226:229], v[12:15]
	v_mfma_f32_16x16x32_bf16 v[8:11], v[148:151], v[226:229], v[8:11]
	v_mfma_f32_16x16x32_bf16 v[60:63], v[144:147], v[176:179], v[60:63]
	v_mfma_f32_16x16x32_bf16 v[56:59], v[152:155], v[176:179], v[56:59]
	v_mfma_f32_16x16x32_bf16 v[44:47], v[144:147], v[184:187], v[44:47]
	v_mfma_f32_16x16x32_bf16 v[40:43], v[152:155], v[184:187], v[40:43]
	v_mfma_f32_16x16x32_bf16 v[28:31], v[144:147], v[222:225], v[28:31]
	v_mfma_f32_16x16x32_bf16 v[24:27], v[152:155], v[222:225], v[24:27]
	v_mfma_f32_16x16x32_bf16 v[12:15], v[144:147], v[230:233], v[12:15]
	v_mfma_f32_16x16x32_bf16 v[8:11], v[152:155], v[230:233], v[8:11]
	v_mfma_f32_16x16x32_bf16 v[52:55], v[156:159], v[172:175], v[52:55]
	v_mfma_f32_16x16x32_bf16 v[48:51], v[164:167], v[172:175], v[48:51]
	v_mfma_f32_16x16x32_bf16 v[36:39], v[156:159], v[180:183], v[36:39]
	v_mfma_f32_16x16x32_bf16 v[32:35], v[164:167], v[180:183], v[32:35]
	v_mfma_f32_16x16x32_bf16 v[20:23], v[156:159], v[188:191], v[20:23]
	v_mfma_f32_16x16x32_bf16 v[16:19], v[164:167], v[188:191], v[16:19]
	v_mfma_f32_16x16x32_bf16 v[4:7], v[156:159], v[226:229], v[4:7]
	v_mfma_f32_16x16x32_bf16 v[0:3], v[164:167], v[226:229], v[0:3]
	v_mfma_f32_16x16x32_bf16 v[52:55], v[160:163], v[176:179], v[52:55]
	v_mfma_f32_16x16x32_bf16 v[48:51], v[168:171], v[176:179], v[48:51]
	v_mfma_f32_16x16x32_bf16 v[36:39], v[160:163], v[184:187], v[36:39]
	v_mfma_f32_16x16x32_bf16 v[32:35], v[168:171], v[184:187], v[32:35]
	v_mfma_f32_16x16x32_bf16 v[20:23], v[160:163], v[222:225], v[20:23]
	v_mfma_f32_16x16x32_bf16 v[16:19], v[168:171], v[222:225], v[16:19]
	v_mfma_f32_16x16x32_bf16 v[4:7], v[160:163], v[230:233], v[4:7]
	v_mfma_f32_16x16x32_bf16 v[0:3], v[168:171], v[230:233], v[0:3]
	s_barrier
	s_add_i32 vcc_lo, vcc_lo, 2
	s_add_u32 s22, s22, 0x100
	s_addc_u32 s23, s23, 0
	s_add_u32 s13, s13, 0x100
	s_addc_u32 s15, s15, 0
	s_cmp_gt_u32 vcc_lo, 13
	s_cbranch_scc0 .LBB0_2070
	s_and_b64 vcc, exec, s[10:11]
	s_cbranch_vccz .LBB0_2073
	s_barrier

; #define PG8_STAGE(bufoff, gbase, voff) do { _Pragma("unroll") for (int _i = 0; _i < 2; ++_i) \
;         __builtin_amdgcn_global_load_lds((const unsigned*)((const char*)(gbase) + (voff)[_i]), (PG8_LAS unsigned*)(lds + (bufoff) + ldsw + _i * 8192), 16, 0, 0); } while (0)
; #define PG8_STAGE_A(bufoff, gbase, h, nx) do { _Pragma("unroll") for (int _i = 0; _i < 2; ++_i) { \
;         const unsigned vo_ = GA ? ((nx) ? vgn[h][_i] : vgc[h][_i]) : voffA[_i]; \
;         __builtin_amdgcn_global_load_lds((const unsigned*)((const char*)(gbase) + vo_), (PG8_LAS unsigned*)(lds + (bufoff) + ldsw + _i * 8192), 16, 0, 0); } } while (0)
; #define PG8_LDA(dst, b, h) do { _Pragma("unroll") for (int m = 0; m < 4; ++m) _Pragma("unroll") for (int k = 0; k < 2; ++k) dst[m][k] = *(const PG8_LAS bf16x8*)(lds + PG8_SA(b, h) + aoff + m * 2048 + k * 1024); } while (0)
; #define PG8_LDB(dst, b, h) do { _Pragma("unroll") for (int n = 0; n < 2; ++n) _Pragma("unroll") for (int k = 0; k < 2; ++k) dst[n][k] = *(const PG8_LAS bf16x8*)(lds + PG8_SB(b, h) + boff + n * 2048 + k * 1024); } while (0)
; #define PG8_MMA(ai, bj, At, Bt) do { __builtin_amdgcn_s_setprio(1); _Pragma("unroll") for (int m = 0; m < 4; ++m) _Pragma("unroll") for (int n = 0; n < 2; ++n) _Pragma("unroll") for (int k = 0; k < 2; ++k) \
;         acc[ai][bj][m][n] = __builtin_amdgcn_mfma_f32_16x16x32_bf16(Bt[n][k], At[m][k], acc[ai][bj][m][n], 0, 0, 0); __builtin_amdgcn_s_setprio(0); } while (0)
; template <class Epi, class Sched>
; __device__ __forceinline__ void gemm_phase(const int WID_, PG8_LAS unsigned char* lds, const Sched& S, const Epi& E) {
;     ...
;         for (int t = 0; t < nt; t += 2) {
;             const bool last = (t == nt - 2);
;             const char* a1 = cA + (size_t)(t + 1) * kstep;
;             const char* a2 = last ? nA : cA + (size_t)(t + 2) * kstep; const char* b2 = last ? nB : cB + (size_t)(t + 2) * kstep;
;             const char* a3 = a2 + kstep; const char* b3 = b2 + kstep;
;             PG8_LDB(B0, 0, 0); PG8_LDB(B1, 0, 1); PG8_SCHED; PG8_LDA(At, 0, 0); PG8_STAGE_A(PG8_SA(1, 1), a1 + hstepA, 1, false);
;             PG8_WAIT_V(8); PG8_WAIT_L(0); PG8_BAR; PG8_MMA(0, 0, At, B0); PG8_MMA(0, 1, At, B1); PG8_BAR; PG8_SCHED;
;             PG8_LDA(At, 0, 1); PG8_STAGE(PG8_SB(0, 0), b2, voffB); PG8_STAGE(PG8_SB(0, 1), b2 + hstepB, voffB); PG8_STAGE_A(PG8_SA(0, 0), a2, 0, last);
.LBB0_2120:
	v_add_u32_e32 v144, s43, v147
	ds_read_b128 v[140:143], v144
	ds_read_b128 v[150:153], v144 offset:1024
	ds_read_b128 v[154:157], v144 offset:2048
	ds_read_b128 v[158:161], v144 offset:3072
	v_add_u32_e32 v144, s67, v147
	ds_read_b128 v[162:165], v144
	ds_read_b128 v[166:169], v144 offset:1024
	ds_read_b128 v[170:173], v144 offset:2048
	ds_read_b128 v[174:177], v144 offset:3072
	s_add_u32 s20, s18, 0xfffc0080
	s_addc_u32 s21, s19, -1
	s_cmp_eq_u32 s79, 12
	s_cselect_b32 s23, s13, s21
	s_cselect_b32 s22, s12, s20
	s_cselect_b32 s21, s15, s11
	s_cselect_b32 s20, s14, s9
	v_lshl_add_u64 v[144:145], s[18:19], 0, v[136:137]
	s_add_i32 m0, s49, 0xc000
	ds_read_b128 v[178:181], v149
	ds_read_b128 v[182:185], v149 offset:1024
	ds_read_b128 v[186:189], v149 offset:2048
	ds_read_b128 v[190:193], v149 offset:3072
	ds_read_b128 v[198:201], v149 offset:4096
	ds_read_b128 v[202:205], v149 offset:5120
	ds_read_b128 v[206:209], v149 offset:6144
	ds_read_b128 v[210:213], v149 offset:7168
	global_load_lds_dwordx4 v[144:145], off
	v_lshl_add_u64 v[144:145], s[18:19], 0, v[138:139]
	s_add_i32 m0, s49, 0xe000
	s_nop 0
	global_load_lds_dwordx4 v[144:145], off
	s_waitcnt vmcnt(8)
	s_waitcnt lgkmcnt(0)
	s_barrier
	s_waitcnt lgkmcnt(0)
	v_mfma_f32_16x16x32_bf16 v[124:127], v[140:143], v[178:181], v[124:127]
	v_mfma_f32_16x16x32_bf16 v[120:123], v[154:157], v[178:181], v[120:123]
	v_mfma_f32_16x16x32_bf16 v[108:111], v[140:143], v[186:189], v[108:111]
	v_mfma_f32_16x16x32_bf16 v[104:107], v[154:157], v[186:189], v[104:107]
	v_mfma_f32_16x16x32_bf16 v[92:95], v[140:143], v[198:201], v[92:95]
	v_mfma_f32_16x16x32_bf16 v[88:91], v[154:157], v[198:201], v[88:91]
	v_mfma_f32_16x16x32_bf16 v[76:79], v[140:143], v[206:209], v[76:79]
	v_mfma_f32_16x16x32_bf16 v[72:75], v[154:157], v[206:209], v[72:75]
	v_mfma_f32_16x16x32_bf16 v[124:127], v[150:153], v[182:185], v[124:127]
	v_mfma_f32_16x16x32_bf16 v[120:123], v[158:161], v[182:185], v[120:123]
	v_mfma_f32_16x16x32_bf16 v[108:111], v[150:153], v[190:193], v[108:111]
	v_mfma_f32_16x16x32_bf16 v[104:107], v[158:161], v[190:193], v[104:107]
	v_mfma_f32_16x16x32_bf16 v[92:95], v[150:153], v[202:205], v[92:95]
	v_mfma_f32_16x16x32_bf16 v[88:91], v[158:161], v[202:205], v[88:91]
	v_mfma_f32_16x16x32_bf16 v[76:79], v[150:153], v[210:213], v[76:79]
	v_mfma_f32_16x16x32_bf16 v[72:75], v[158:161], v[210:213], v[72:75]
	v_mfma_f32_16x16x32_bf16 v[116:119], v[162:165], v[178:181], v[116:119]
	v_mfma_f32_16x16x32_bf16 v[112:115], v[170:173], v[178:181], v[112:115]
	v_mfma_f32_16x16x32_bf16 v[100:103], v[162:165], v[186:189], v[100:103]
	v_mfma_f32_16x16x32_bf16 v[96:99], v[170:173], v[186:189], v[96:99]
	v_mfma_f32_16x16x32_bf16 v[84:87], v[162:165], v[198:201], v[84:87]
	v_mfma_f32_16x16x32_bf16 v[80:83], v[170:173], v[198:201], v[80:83]
	v_mfma_f32_16x16x32_bf16 v[68:71], v[162:165], v[206:209], v[68:71]
	v_mfma_f32_16x16x32_bf16 v[64:67], v[170:173], v[206:209], v[64:67]
	v_mfma_f32_16x16x32_bf16 v[116:119], v[166:169], v[182:185], v[116:119]
	v_mfma_f32_16x16x32_bf16 v[112:115], v[174:177], v[182:185], v[112:115]
	v_mfma_f32_16x16x32_bf16 v[100:103], v[166:169], v[190:193], v[100:103]
	v_mfma_f32_16x16x32_bf16 v[96:99], v[174:177], v[190:193], v[96:99]
	v_mfma_f32_16x16x32_bf16 v[84:87], v[166:169], v[202:205], v[84:87]
	v_mfma_f32_16x16x32_bf16 v[80:83], v[174:177], v[202:205], v[80:83]
	v_mfma_f32_16x16x32_bf16 v[68:71], v[166:169], v[210:213], v[68:71]
	v_mfma_f32_16x16x32_bf16 v[64:67], v[174:177], v[210:213], v[64:67]
	s_barrier
	s_add_i32 s46, s43, s48
	v_lshl_add_u64 v[144:145], s[20:21], 0, v[128:129]
	s_mov_b32 m0, s46
	ds_read_b128 v[178:181], v149 offset:16384
	ds_read_b128 v[182:185], v149 offset:17408
	ds_read_b128 v[186:189], v149 offset:18432
	ds_read_b128 v[190:193], v149 offset:19456
	ds_read_b128 v[198:201], v149 offset:20480
	ds_read_b128 v[202:205], v149 offset:21504
	ds_read_b128 v[206:209], v149 offset:22528
	ds_read_b128 v[210:213], v149 offset:23552
	global_load_lds_dwordx4 v[144:145], off
	s_add_i32 m0, s46, 0x2000
	s_add_u32 s46, s20, 0x40000
	v_lshl_add_u64 v[214:215], s[20:21], 0, v[130:131]
	s_addc_u32 s47, s21, 0
	s_add_i32 s80, s67, s48
	global_load_lds_dwordx4 v[214:215], off
	v_lshl_add_u64 v[216:217], s[46:47], 0, v[128:129]
	s_mov_b32 m0, s80
	v_lshl_add_u64 v[218:219], s[22:23], 0, v[132:133]
	global_load_lds_dwordx4 v[216:217], off
	v_lshl_add_u64 v[216:217], s[46:47], 0, v[130:131]
	s_add_i32 m0, s80, 0x2000
	s_nop 0
	global_load_lds_dwordx4 v[216:217], off
	v_lshl_add_u64 v[216:217], s[22:23], 0, v[134:135]
	s_mov_b32 m0, s49
	s_nop 0
	global_load_lds_dwordx4 v[216:217], off
	s_mov_b32 m0, s50
	s_nop 0
	global_load_lds_dwordx4 v[218:219], off
	s_waitcnt vmcnt(8)
	s_waitcnt lgkmcnt(0)
	s_barrier
; #define PG8_STAGE_A(bufoff, gbase, h, nx) do { _Pragma("unroll") for (int _i = 0; _i < 2; ++_i) { \
;         const unsigned vo_ = GA ? ((nx) ? vgn[h][_i] : vgc[h][_i]) : voffA[_i]; \
;         __builtin_amdgcn_global_load_lds((const unsigned*)((const char*)(gbase) + vo_), (PG8_LAS unsigned*)(lds + (bufoff) + ldsw + _i * 8192), 16, 0, 0); } } while (0)
; #define PG8_LDA(dst, b, h) do { _Pragma("unroll") for (int m = 0; m < 4; ++m) _Pragma("unroll") for (int k = 0; k < 2; ++k) dst[m][k] = *(const PG8_LAS bf16x8*)(lds + PG8_SA(b, h) + aoff + m * 2048 + k * 1024); } while (0)
; #define PG8_LDB(dst, b, h) do { _Pragma("unroll") for (int n = 0; n < 2; ++n) _Pragma("unroll") for (int k = 0; k < 2; ++k) dst[n][k] = *(const PG8_LAS bf16x8*)(lds + PG8_SB(b, h) + boff + n * 2048 + k * 1024); } while (0)
; #define PG8_MMA(ai, bj, At, Bt) do { __builtin_amdgcn_s_setprio(1); _Pragma("unroll") for (int m = 0; m < 4; ++m) _Pragma("unroll") for (int n = 0; n < 2; ++n) _Pragma("unroll") for (int k = 0; k < 2; ++k) \
;         acc[ai][bj][m][n] = __builtin_amdgcn_mfma_f32_16x16x32_bf16(Bt[n][k], At[m][k], acc[ai][bj][m][n], 0, 0, 0); __builtin_amdgcn_s_setprio(0); } while (0)
; #define PG8_WAIT_V(n) asm volatile("s_waitcnt vmcnt(" #n ")" ::: "memory")
; #define PG8_WAIT_L(n) asm volatile("s_waitcnt lgkmcnt(" #n ")" ::: "memory")
; #define PG8_BAR __builtin_amdgcn_s_barrier()
; #define PG8_SCHED __builtin_amdgcn_sched_barrier(0)
; template <class Epi, class Sched>
; __device__ __forceinline__ void gemm_phase(const int WID_, PG8_LAS unsigned char* lds, const Sched& S, const Epi& E) {
;     ...
;             PG8_WAIT_V(8); PG8_WAIT_L(0); PG8_BAR; PG8_MMA(1, 0, At, B0); PG8_MMA(1, 1, At, B1); PG8_BAR; PG8_SCHED;
;             PG8_LDB(B0, 1, 0); PG8_LDB(B1, 1, 1); PG8_SCHED; PG8_LDA(At, 1, 0); PG8_STAGE_A(PG8_SA(0, 1), a2 + hstepA, 1, last);
;             PG8_WAIT_V(8); PG8_WAIT_L(0); PG8_BAR; PG8_MMA(0, 0, At, B0); PG8_MMA(0, 1, At, B1); PG8_BAR; PG8_SCHED;
	s_waitcnt lgkmcnt(0)
	v_mfma_f32_16x16x32_bf16 v[60:63], v[140:143], v[178:181], v[60:63]
	v_mfma_f32_16x16x32_bf16 v[56:59], v[154:157], v[178:181], v[56:59]
	v_mfma_f32_16x16x32_bf16 v[44:47], v[140:143], v[186:189], v[44:47]
	v_mfma_f32_16x16x32_bf16 v[40:43], v[154:157], v[186:189], v[40:43]
	v_mfma_f32_16x16x32_bf16 v[28:31], v[140:143], v[198:201], v[28:31]
	v_mfma_f32_16x16x32_bf16 v[24:27], v[154:157], v[198:201], v[24:27]
	v_mfma_f32_16x16x32_bf16 v[12:15], v[140:143], v[206:209], v[12:15]
	v_mfma_f32_16x16x32_bf16 v[8:11], v[154:157], v[206:209], v[8:11]
	v_mfma_f32_16x16x32_bf16 v[60:63], v[150:153], v[182:185], v[60:63]
	v_mfma_f32_16x16x32_bf16 v[56:59], v[158:161], v[182:185], v[56:59]
	v_mfma_f32_16x16x32_bf16 v[44:47], v[150:153], v[190:193], v[44:47]
	v_mfma_f32_16x16x32_bf16 v[40:43], v[158:161], v[190:193], v[40:43]
	v_mfma_f32_16x16x32_bf16 v[28:31], v[150:153], v[202:205], v[28:31]
	v_mfma_f32_16x16x32_bf16 v[24:27], v[158:161], v[202:205], v[24:27]
	v_mfma_f32_16x16x32_bf16 v[12:15], v[150:153], v[210:213], v[12:15]
	v_mfma_f32_16x16x32_bf16 v[8:11], v[158:161], v[210:213], v[8:11]
	v_mfma_f32_16x16x32_bf16 v[52:55], v[162:165], v[178:181], v[52:55]
	v_mfma_f32_16x16x32_bf16 v[48:51], v[170:173], v[178:181], v[48:51]
	v_mfma_f32_16x16x32_bf16 v[36:39], v[162:165], v[186:189], v[36:39]
	v_mfma_f32_16x16x32_bf16 v[32:35], v[170:173], v[186:189], v[32:35]
	v_mfma_f32_16x16x32_bf16 v[20:23], v[162:165], v[198:201], v[20:23]
	v_mfma_f32_16x16x32_bf16 v[16:19], v[170:173], v[198:201], v[16:19]
	v_mfma_f32_16x16x32_bf16 v[4:7], v[162:165], v[206:209], v[4:7]
	v_mfma_f32_16x16x32_bf16 v[0:3], v[170:173], v[206:209], v[0:3]
	v_mfma_f32_16x16x32_bf16 v[52:55], v[166:169], v[182:185], v[52:55]
	v_mfma_f32_16x16x32_bf16 v[48:51], v[174:177], v[182:185], v[48:51]
	v_mfma_f32_16x16x32_bf16 v[36:39], v[166:169], v[190:193], v[36:39]
	v_mfma_f32_16x16x32_bf16 v[32:35], v[174:177], v[190:193], v[32:35]
	v_mfma_f32_16x16x32_bf16 v[20:23], v[166:169], v[202:205], v[20:23]
	v_mfma_f32_16x16x32_bf16 v[16:19], v[174:177], v[202:205], v[16:19]
	v_mfma_f32_16x16x32_bf16 v[4:7], v[166:169], v[210:213], v[4:7]
	v_mfma_f32_16x16x32_bf16 v[0:3], v[174:177], v[210:213], v[0:3]
	s_barrier
	v_add_u32_e32 v158, s82, v147
	v_add_u32_e32 v174, s83, v147
	ds_read_b128 v[140:143], v158
	ds_read_b128 v[150:153], v158 offset:1024
	ds_read_b128 v[154:157], v158 offset:2048
	ds_read_b128 v[158:161], v158 offset:3072
	ds_read_b128 v[162:165], v174
	ds_read_b128 v[166:169], v174 offset:1024
	ds_read_b128 v[170:173], v174 offset:2048
	ds_read_b128 v[174:177], v174 offset:3072
	s_add_u32 s22, s22, 0x40000
	s_addc_u32 s23, s23, 0
	s_mov_b32 m0, s51
	v_lshl_add_u64 v[220:221], s[22:23], 0, v[134:135]
	ds_read_b128 v[178:181], v149 offset:32768
	ds_read_b128 v[182:185], v149 offset:33792
	ds_read_b128 v[186:189], v149 offset:34816
	ds_read_b128 v[190:193], v149 offset:35840
	ds_read_b128 v[198:201], v149 offset:36864
	ds_read_b128 v[202:205], v149 offset:37888
	ds_read_b128 v[206:209], v149 offset:38912
	ds_read_b128 v[210:213], v149 offset:39936
	global_load_lds_dwordx4 v[220:221], off
	v_lshl_add_u64 v[220:221], s[22:23], 0, v[132:133]
	s_mov_b32 m0, s60
	s_nop 0
	global_load_lds_dwordx4 v[220:221], off
	s_waitcnt vmcnt(8)
	s_waitcnt lgkmcnt(0)
	s_barrier
	s_waitcnt lgkmcnt(0)
	v_mfma_f32_16x16x32_bf16 v[124:127], v[140:143], v[178:181], v[124:127]
	v_mfma_f32_16x16x32_bf16 v[120:123], v[154:157], v[178:181], v[120:123]
	v_mfma_f32_16x16x32_bf16 v[108:111], v[140:143], v[186:189], v[108:111]
	v_mfma_f32_16x16x32_bf16 v[104:107], v[154:157], v[186:189], v[104:107]
	v_mfma_f32_16x16x32_bf16 v[92:95], v[140:143], v[198:201], v[92:95]
	v_mfma_f32_16x16x32_bf16 v[88:91], v[154:157], v[198:201], v[88:91]
	v_mfma_f32_16x16x32_bf16 v[76:79], v[140:143], v[206:209], v[76:79]
	v_mfma_f32_16x16x32_bf16 v[72:75], v[154:157], v[206:209], v[72:75]
	v_mfma_f32_16x16x32_bf16 v[124:127], v[150:153], v[182:185], v[124:127]
	v_mfma_f32_16x16x32_bf16 v[120:123], v[158:161], v[182:185], v[120:123]
	v_mfma_f32_16x16x32_bf16 v[108:111], v[150:153], v[190:193], v[108:111]
	v_mfma_f32_16x16x32_bf16 v[104:107], v[158:161], v[190:193], v[104:107]
	v_mfma_f32_16x16x32_bf16 v[92:95], v[150:153], v[202:205], v[92:95]
	v_mfma_f32_16x16x32_bf16 v[88:91], v[158:161], v[202:205], v[88:91]
	v_mfma_f32_16x16x32_bf16 v[76:79], v[150:153], v[210:213], v[76:79]
	v_mfma_f32_16x16x32_bf16 v[72:75], v[158:161], v[210:213], v[72:75]
	v_mfma_f32_16x16x32_bf16 v[116:119], v[162:165], v[178:181], v[116:119]
	v_mfma_f32_16x16x32_bf16 v[112:115], v[170:173], v[178:181], v[112:115]
	v_mfma_f32_16x16x32_bf16 v[100:103], v[162:165], v[186:189], v[100:103]
	v_mfma_f32_16x16x32_bf16 v[96:99], v[170:173], v[186:189], v[96:99]
	v_mfma_f32_16x16x32_bf16 v[84:87], v[162:165], v[198:201], v[84:87]
	v_mfma_f32_16x16x32_bf16 v[80:83], v[170:173], v[198:201], v[80:83]
	v_mfma_f32_16x16x32_bf16 v[68:71], v[162:165], v[206:209], v[68:71]
	v_mfma_f32_16x16x32_bf16 v[64:67], v[170:173], v[206:209], v[64:67]
	v_mfma_f32_16x16x32_bf16 v[116:119], v[166:169], v[182:185], v[116:119]
	v_mfma_f32_16x16x32_bf16 v[112:115], v[174:177], v[182:185], v[112:115]
	v_mfma_f32_16x16x32_bf16 v[100:103], v[166:169], v[190:193], v[100:103]
	v_mfma_f32_16x16x32_bf16 v[96:99], v[174:177], v[190:193], v[96:99]
	v_mfma_f32_16x16x32_bf16 v[84:87], v[166:169], v[202:205], v[84:87]
	v_mfma_f32_16x16x32_bf16 v[80:83], v[174:177], v[202:205], v[80:83]
	v_mfma_f32_16x16x32_bf16 v[68:71], v[166:169], v[210:213], v[68:71]
	v_mfma_f32_16x16x32_bf16 v[64:67], v[174:177], v[210:213], v[64:67]
	s_barrier
; #define PG8_STAGE(bufoff, gbase, voff) do { _Pragma("unroll") for (int _i = 0; _i < 2; ++_i) \
;         __builtin_amdgcn_global_load_lds((const unsigned*)((const char*)(gbase) + (voff)[_i]), (PG8_LAS unsigned*)(lds + (bufoff) + ldsw + _i * 8192), 16, 0, 0); } while (0)
; #define PG8_STAGE_A(bufoff, gbase, h, nx) do { _Pragma("unroll") for (int _i = 0; _i < 2; ++_i) { \
;         const unsigned vo_ = GA ? ((nx) ? vgn[h][_i] : vgc[h][_i]) : voffA[_i]; \
;         __builtin_amdgcn_global_load_lds((const unsigned*)((const char*)(gbase) + vo_), (PG8_LAS unsigned*)(lds + (bufoff) + ldsw + _i * 8192), 16, 0, 0); } } while (0)
; #define PG8_LDA(dst, b, h) do { _Pragma("unroll") for (int m = 0; m < 4; ++m) _Pragma("unroll") for (int k = 0; k < 2; ++k) dst[m][k] = *(const PG8_LAS bf16x8*)(lds + PG8_SA(b, h) + aoff + m * 2048 + k * 1024); } while (0)
; #define PG8_MMA(ai, bj, At, Bt) do { __builtin_amdgcn_s_setprio(1); _Pragma("unroll") for (int m = 0; m < 4; ++m) _Pragma("unroll") for (int n = 0; n < 2; ++n) _Pragma("unroll") for (int k = 0; k < 2; ++k) \
;         acc[ai][bj][m][n] = __builtin_amdgcn_mfma_f32_16x16x32_bf16(Bt[n][k], At[m][k], acc[ai][bj][m][n], 0, 0, 0); __builtin_amdgcn_s_setprio(0); } while (0)
; #define PG8_WAIT_V(n) asm volatile("s_waitcnt vmcnt(" #n ")" ::: "memory")
; #define PG8_WAIT_L(n) asm volatile("s_waitcnt lgkmcnt(" #n ")" ::: "memory")
; #define PG8_BAR __builtin_amdgcn_s_barrier()
; #define PG8_SCHED __builtin_amdgcn_sched_barrier(0)
; template <class Epi, class Sched>
; __device__ __forceinline__ void gemm_phase(const int WID_, PG8_LAS unsigned char* lds, const Sched& S, const Epi& E) {
;     ...
;             PG8_LDA(At, 1, 1); PG8_STAGE(PG8_SB(1, 0), b3, voffB); PG8_STAGE(PG8_SB(1, 1), b3 + hstepB, voffB); PG8_STAGE_A(PG8_SA(1, 0), a3, 0, last);
;             PG8_WAIT_V(8); PG8_WAIT_L(0); PG8_BAR; PG8_MMA(1, 0, At, B0); PG8_MMA(1, 1, At, B1); PG8_BAR; PG8_SCHED;
;         }
;         if (wr == 0) PG8_BAR;
	s_add_i32 s22, s82, s48
	v_lshl_add_u64 v[144:145], v[144:145], 0, s[68:69]
	s_mov_b32 m0, s22
	ds_read_b128 v[178:181], v149 offset:49152
	ds_read_b128 v[182:185], v149 offset:50176
	ds_read_b128 v[186:189], v149 offset:51200
	ds_read_b128 v[190:193], v149 offset:52224
	ds_read_b128 v[198:201], v149 offset:53248
	ds_read_b128 v[202:205], v149 offset:54272
	ds_read_b128 v[206:209], v149 offset:55296
	ds_read_b128 v[210:213], v149 offset:56320
	global_load_lds_dwordx4 v[144:145], off
	s_add_i32 m0, s22, 0x2000
	s_add_u32 s20, s20, 0x40080
	v_lshl_add_u64 v[144:145], v[214:215], 0, s[68:69]
	s_addc_u32 s21, s21, 0
	s_add_i32 s22, s83, s48
	global_load_lds_dwordx4 v[144:145], off
	v_lshl_add_u64 v[144:145], s[20:21], 0, v[128:129]
	s_mov_b32 m0, s22
	s_nop 0
	global_load_lds_dwordx4 v[144:145], off
	v_lshl_add_u64 v[144:145], s[20:21], 0, v[130:131]
	s_add_i32 m0, s22, 0x2000
	s_nop 0
	global_load_lds_dwordx4 v[144:145], off
	v_lshl_add_u64 v[144:145], v[216:217], 0, s[68:69]
	s_mov_b32 m0, s61
	s_nop 0
	global_load_lds_dwordx4 v[144:145], off
	v_lshl_add_u64 v[144:145], v[218:219], 0, s[68:69]
	s_mov_b32 m0, s62
	s_nop 0
	global_load_lds_dwordx4 v[144:145], off
	s_waitcnt vmcnt(8)
	s_waitcnt lgkmcnt(0)
	s_barrier
	s_waitcnt lgkmcnt(0)
	v_mfma_f32_16x16x32_bf16 v[60:63], v[140:143], v[178:181], v[60:63]
	v_mfma_f32_16x16x32_bf16 v[56:59], v[154:157], v[178:181], v[56:59]
	v_mfma_f32_16x16x32_bf16 v[44:47], v[140:143], v[186:189], v[44:47]
	v_mfma_f32_16x16x32_bf16 v[40:43], v[154:157], v[186:189], v[40:43]
	v_mfma_f32_16x16x32_bf16 v[28:31], v[140:143], v[198:201], v[28:31]
	v_mfma_f32_16x16x32_bf16 v[24:27], v[154:157], v[198:201], v[24:27]
	v_mfma_f32_16x16x32_bf16 v[12:15], v[140:143], v[206:209], v[12:15]
	v_mfma_f32_16x16x32_bf16 v[8:11], v[154:157], v[206:209], v[8:11]
	v_mfma_f32_16x16x32_bf16 v[60:63], v[150:153], v[182:185], v[60:63]
	v_mfma_f32_16x16x32_bf16 v[56:59], v[158:161], v[182:185], v[56:59]
	v_mfma_f32_16x16x32_bf16 v[44:47], v[150:153], v[190:193], v[44:47]
	v_mfma_f32_16x16x32_bf16 v[40:43], v[158:161], v[190:193], v[40:43]
	v_mfma_f32_16x16x32_bf16 v[28:31], v[150:153], v[202:205], v[28:31]
	v_mfma_f32_16x16x32_bf16 v[24:27], v[158:161], v[202:205], v[24:27]
	v_mfma_f32_16x16x32_bf16 v[12:15], v[150:153], v[210:213], v[12:15]
	v_mfma_f32_16x16x32_bf16 v[8:11], v[158:161], v[210:213], v[8:11]
	v_mfma_f32_16x16x32_bf16 v[52:55], v[162:165], v[178:181], v[52:55]
	v_mfma_f32_16x16x32_bf16 v[48:51], v[170:173], v[178:181], v[48:51]
	v_mfma_f32_16x16x32_bf16 v[36:39], v[162:165], v[186:189], v[36:39]
	v_mfma_f32_16x16x32_bf16 v[32:35], v[170:173], v[186:189], v[32:35]
	v_mfma_f32_16x16x32_bf16 v[20:23], v[162:165], v[198:201], v[20:23]
	v_mfma_f32_16x16x32_bf16 v[16:19], v[170:173], v[198:201], v[16:19]
	v_mfma_f32_16x16x32_bf16 v[4:7], v[162:165], v[206:209], v[4:7]
	v_mfma_f32_16x16x32_bf16 v[0:3], v[170:173], v[206:209], v[0:3]
	v_mfma_f32_16x16x32_bf16 v[52:55], v[166:169], v[182:185], v[52:55]
	v_mfma_f32_16x16x32_bf16 v[48:51], v[174:177], v[182:185], v[48:51]
	v_mfma_f32_16x16x32_bf16 v[36:39], v[166:169], v[190:193], v[36:39]
	v_mfma_f32_16x16x32_bf16 v[32:35], v[174:177], v[190:193], v[32:35]
	v_mfma_f32_16x16x32_bf16 v[20:23], v[166:169], v[202:205], v[20:23]
	v_mfma_f32_16x16x32_bf16 v[16:19], v[174:177], v[202:205], v[16:19]
	v_mfma_f32_16x16x32_bf16 v[4:7], v[166:169], v[210:213], v[4:7]
	v_mfma_f32_16x16x32_bf16 v[0:3], v[174:177], v[210:213], v[0:3]
	s_barrier
	s_add_i32 s79, s79, 2
	s_add_u32 s18, s18, 0x100
	s_addc_u32 s19, s19, 0
	s_add_u32 s9, s9, 0x100
	s_addc_u32 s11, s11, 0
	s_cmp_gt_u32 s79, 13
	s_cbranch_scc0 .LBB0_2120
	s_and_b64 vcc, exec, s[6:7]
	s_cbranch_vccz .LBB0_2123
	s_barrier

;     __device__ __forceinline__ const char* aptr(const Unit& u) const { return (const char*)(A + (size_t)u.pm * BM * lda); }
;     __device__ __forceinline__ const char* bptr(const Unit& u) const { return (const char*)(Bt + (size_t)u.pn * BM * ldb); }
;     __device__ __forceinline__ const char* aptr(const Unit& u) const { return (const char*)(A + (size_t)u.pm * BM * lda + koff(u)); }
;     __device__ __forceinline__ const char* bptr(const Unit& u) const { return (const char*)(Bt + (size_t)u.pn * BM * ldb + koff(u)); }
;     __device__ bool next(int i, Unit& u) const { if (i >= 6) return false; int pm_ = pm; asm volatile("" : "+s"(pm_)); u.pm = pm_; u.pn = (i + (GB >> 3)) % 6; return true; }
;     __device__ __forceinline__ const char* aptr(const Unit& u) const { return (const char*)(A + (size_t)u.pm * BM * lda + koff(u)); }
;     __device__ __forceinline__ const char* bptr(const Unit& u) const { return (const char*)(Bt + (size_t)u.pn * BM * ldb + koff(u)); }
; #define PG8_WAIT_V(n) asm volatile("s_waitcnt vmcnt(" #n ")" ::: "memory")
; #define PG8_BAR __builtin_amdgcn_s_barrier()
; template <class Epi, class Sched>
; __device__ __forceinline__ void gemm_phase(const int WID_, PG8_LAS unsigned char* lds, const Sched& S, const Epi& E) {
;     ...
;         const bool has_next = S.next(ui + 1, nxt);
;         const char* nA = has_next ? S.aptr(nxt) : cA; const char* nB = has_next ? S.bptr(nxt) : cB;
;         if (has_next) PG8_GOFF(vgn, nxt); else { if constexpr (GA) { _Pragma("unroll") for (int h_ = 0; h_ < 2; ++h_) _Pragma("unroll") for (int i_ = 0; i_ < 2; ++i_) vgn[h_][i_] = vgc[h_][i_]; } }
;         for (int t = 0; t < nt; t += 2) {
;             const bool last = (t == nt - 2);
;             const char* a1 = cA + (size_t)(t + 1) * kstep;
;             const char* a2 = last ? nA : cA + (size_t)(t + 2) * kstep; const char* b2 = last ? nB : cB + (size_t)(t + 2) * kstep;
;             const char* a3 = a2 + kstep; const char* b3 = b2 + kstep;
;             PG8_LDB(B0, 0, 0); PG8_LDB(B1, 0, 1); PG8_SCHED; PG8_LDA(At, 0, 0); PG8_STAGE_A(PG8_SA(1, 1), a1 + hstepA, 1, false);
;             PG8_WAIT_V(8); PG8_WAIT_L(0); PG8_BAR; PG8_MMA(0, 0, At, B0); PG8_MMA(0, 1, At, B1); PG8_BAR; PG8_SCHED;
;             PG8_LDA(At, 0, 1); PG8_STAGE(PG8_SB(0, 0), b2, voffB); PG8_STAGE(PG8_SB(0, 1), b2 + hstepB, voffB); PG8_STAGE_A(PG8_SA(0, 0), a2, 0, last);
.Lg1_nofix:
	ds_read_b128 v[162:165], v151
	ds_read_b128 v[166:169], v151 offset:1024
	ds_read_b128 v[170:173], v151 offset:2048
	ds_read_b128 v[174:177], v151 offset:3072
	ds_read_b128 v[178:181], v152
	ds_read_b128 v[182:185], v152 offset:1024
	ds_read_b128 v[186:189], v152 offset:2048
	ds_read_b128 v[190:193], v152 offset:3072
	s_add_u32 s8, s2, s4
	s_addc_u32 s9, s3, s5
	s_cmpk_eq_i32 s4, 0x800
	s_cselect_b64 vcc, -1, 0
	s_and_b64 s[6:7], vcc, exec
	s_cselect_b32 s66, 0, s4
	s_cselect_b32 s45, 0, s5
	s_cselect_b32 s6, s42, s8
	s_cselect_b32 s7, s43, s9
	s_add_u32 s8, s92, s66
	s_addc_u32 s9, s93, s45
	v_lshl_add_u64 v[226:227], v[142:143], 0, s[4:5]
	s_mov_b32 m0, s51
	v_lshl_add_u64 v[226:227], v[226:227], 0, s[40:41]
	ds_read_b128 v[194:197], v153
	ds_read_b128 v[198:201], v153 offset:1024
	ds_read_b128 v[202:205], v153 offset:2048
	ds_read_b128 v[206:209], v153 offset:3072
	ds_read_b128 v[210:213], v153 offset:4096
	ds_read_b128 v[214:217], v153 offset:5120
	ds_read_b128 v[218:221], v153 offset:6144
	ds_read_b128 v[222:225], v153 offset:7168
	global_load_lds_dwordx4 v[226:227], off
	v_lshl_add_u64 v[226:227], v[144:145], 0, s[4:5]
	v_lshl_add_u64 v[226:227], v[226:227], 0, s[40:41]
	s_mov_b32 m0, s52
	s_nop 0
	global_load_lds_dwordx4 v[226:227], off
	s_waitcnt vmcnt(8)
	s_waitcnt lgkmcnt(0)
	s_barrier
	s_waitcnt lgkmcnt(0)
	v_mfma_f32_16x16x32_bf16 v[124:127], v[162:165], v[194:197], v[124:127]
	v_mfma_f32_16x16x32_bf16 v[116:119], v[170:173], v[194:197], v[116:119]
	v_mfma_f32_16x16x32_bf16 v[108:111], v[162:165], v[202:205], v[108:111]
	v_mfma_f32_16x16x32_bf16 v[100:103], v[170:173], v[202:205], v[100:103]
	v_mfma_f32_16x16x32_bf16 v[92:95], v[162:165], v[210:213], v[92:95]
	v_mfma_f32_16x16x32_bf16 v[84:87], v[170:173], v[210:213], v[84:87]
	v_mfma_f32_16x16x32_bf16 v[76:79], v[162:165], v[218:221], v[76:79]
	v_mfma_f32_16x16x32_bf16 v[68:71], v[170:173], v[218:221], v[68:71]
	v_mfma_f32_16x16x32_bf16 v[124:127], v[166:169], v[198:201], v[124:127]
	v_mfma_f32_16x16x32_bf16 v[116:119], v[174:177], v[198:201], v[116:119]
	v_mfma_f32_16x16x32_bf16 v[108:111], v[166:169], v[206:209], v[108:111]
	v_mfma_f32_16x16x32_bf16 v[100:103], v[174:177], v[206:209], v[100:103]
	v_mfma_f32_16x16x32_bf16 v[92:95], v[166:169], v[214:217], v[92:95]
	v_mfma_f32_16x16x32_bf16 v[84:87], v[174:177], v[214:217], v[84:87]
	v_mfma_f32_16x16x32_bf16 v[76:79], v[166:169], v[222:225], v[76:79]
	v_mfma_f32_16x16x32_bf16 v[68:71], v[174:177], v[222:225], v[68:71]
	v_mfma_f32_16x16x32_bf16 v[120:123], v[178:181], v[194:197], v[120:123]
	v_mfma_f32_16x16x32_bf16 v[112:115], v[186:189], v[194:197], v[112:115]
	v_mfma_f32_16x16x32_bf16 v[104:107], v[178:181], v[202:205], v[104:107]
	v_mfma_f32_16x16x32_bf16 v[96:99], v[186:189], v[202:205], v[96:99]
	v_mfma_f32_16x16x32_bf16 v[88:91], v[178:181], v[210:213], v[88:91]
	v_mfma_f32_16x16x32_bf16 v[80:83], v[186:189], v[210:213], v[80:83]
	v_mfma_f32_16x16x32_bf16 v[72:75], v[178:181], v[218:221], v[72:75]
	v_mfma_f32_16x16x32_bf16 v[64:67], v[186:189], v[218:221], v[64:67]
	v_mfma_f32_16x16x32_bf16 v[120:123], v[182:185], v[198:201], v[120:123]
	v_mfma_f32_16x16x32_bf16 v[112:115], v[190:193], v[198:201], v[112:115]
	v_mfma_f32_16x16x32_bf16 v[104:107], v[182:185], v[206:209], v[104:107]
	v_mfma_f32_16x16x32_bf16 v[96:99], v[190:193], v[206:209], v[96:99]
	v_mfma_f32_16x16x32_bf16 v[88:91], v[182:185], v[214:217], v[88:91]
	v_mfma_f32_16x16x32_bf16 v[80:83], v[190:193], v[214:217], v[80:83]
	v_mfma_f32_16x16x32_bf16 v[72:75], v[182:185], v[222:225], v[72:75]
	v_mfma_f32_16x16x32_bf16 v[64:67], v[190:193], v[222:225], v[64:67]
	s_barrier
	s_mov_b32 m0, s53
	v_lshl_add_u64 v[226:227], s[6:7], 0, v[128:129]
	s_add_u32 s66, s6, 0x40000
	ds_read_b128 v[194:197], v153 offset:16384
	ds_read_b128 v[198:201], v153 offset:17408
	ds_read_b128 v[202:205], v153 offset:18432
	ds_read_b128 v[206:209], v153 offset:19456
	ds_read_b128 v[210:213], v153 offset:20480
	ds_read_b128 v[214:217], v153 offset:21504
	ds_read_b128 v[218:221], v153 offset:22528
	ds_read_b128 v[222:225], v153 offset:23552
	global_load_lds_dwordx4 v[226:227], off
	v_lshl_add_u64 v[228:229], s[6:7], 0, v[130:131]
	s_mov_b32 m0, s54
	s_addc_u32 s67, s7, 0
	global_load_lds_dwordx4 v[228:229], off
	v_lshl_add_u64 v[230:231], s[66:67], 0, v[128:129]
	s_mov_b32 m0, s55
	v_cndmask_b32_e32 v132, v134, v157, vcc
	global_load_lds_dwordx4 v[230:231], off
	v_lshl_add_u64 v[230:231], s[66:67], 0, v[130:131]
	s_mov_b32 m0, s56
	s_nop 0
	global_load_lds_dwordx4 v[230:231], off
	s_mov_b32 m0, s21
	v_lshl_add_u64 v[230:231], s[8:9], 0, v[132:133]
	global_load_lds_dwordx4 v132, s[8:9]
	v_cndmask_b32_e32 v132, v136, v158, vcc
	s_mov_b32 m0, s33
	v_lshl_add_u64 v[232:233], s[8:9], 0, v[132:133]
	global_load_lds_dwordx4 v132, s[8:9]
	s_waitcnt vmcnt(8)
	s_waitcnt lgkmcnt(0)
	s_barrier
; #define PG8_STAGE_A(bufoff, gbase, h, nx) do { _Pragma("unroll") for (int _i = 0; _i < 2; ++_i) { \
;         const unsigned vo_ = GA ? ((nx) ? vgn[h][_i] : vgc[h][_i]) : voffA[_i]; \
;         __builtin_amdgcn_global_load_lds((const unsigned*)((const char*)(gbase) + vo_), (PG8_LAS unsigned*)(lds + (bufoff) + ldsw + _i * 8192), 16, 0, 0); } } while (0)
; #define PG8_LDA(dst, b, h) do { _Pragma("unroll") for (int m = 0; m < 4; ++m) _Pragma("unroll") for (int k = 0; k < 2; ++k) dst[m][k] = *(const PG8_LAS bf16x8*)(lds + PG8_SA(b, h) + aoff + m * 2048 + k * 1024); } while (0)
; #define PG8_LDB(dst, b, h) do { _Pragma("unroll") for (int n = 0; n < 2; ++n) _Pragma("unroll") for (int k = 0; k < 2; ++k) dst[n][k] = *(const PG8_LAS bf16x8*)(lds + PG8_SB(b, h) + boff + n * 2048 + k * 1024); } while (0)
; #define PG8_MMA(ai, bj, At, Bt) do { __builtin_amdgcn_s_setprio(1); _Pragma("unroll") for (int m = 0; m < 4; ++m) _Pragma("unroll") for (int n = 0; n < 2; ++n) _Pragma("unroll") for (int k = 0; k < 2; ++k) \
;         acc[ai][bj][m][n] = __builtin_amdgcn_mfma_f32_16x16x32_bf16(Bt[n][k], At[m][k], acc[ai][bj][m][n], 0, 0, 0); __builtin_amdgcn_s_setprio(0); } while (0)
; #define PG8_WAIT_V(n) asm volatile("s_waitcnt vmcnt(" #n ")" ::: "memory")
; #define PG8_WAIT_L(n) asm volatile("s_waitcnt lgkmcnt(" #n ")" ::: "memory")
; #define PG8_BAR __builtin_amdgcn_s_barrier()
; #define PG8_SCHED __builtin_amdgcn_sched_barrier(0)
; template <class Epi, class Sched>
; __device__ __forceinline__ void gemm_phase(const int WID_, PG8_LAS unsigned char* lds, const Sched& S, const Epi& E) {
;     ...
;             PG8_WAIT_V(8); PG8_WAIT_L(0); PG8_BAR; PG8_MMA(1, 0, At, B0); PG8_MMA(1, 1, At, B1); PG8_BAR; PG8_SCHED;
;             PG8_LDB(B0, 1, 0); PG8_LDB(B1, 1, 1); PG8_SCHED; PG8_LDA(At, 1, 0); PG8_STAGE_A(PG8_SA(0, 1), a2 + hstepA, 1, last);
;             PG8_WAIT_V(8); PG8_WAIT_L(0); PG8_BAR; PG8_MMA(0, 0, At, B0); PG8_MMA(0, 1, At, B1); PG8_BAR; PG8_SCHED;
	s_waitcnt lgkmcnt(0)
	v_mfma_f32_16x16x32_bf16 v[60:63], v[162:165], v[194:197], v[60:63]
	v_mfma_f32_16x16x32_bf16 v[52:55], v[170:173], v[194:197], v[52:55]
	v_mfma_f32_16x16x32_bf16 v[44:47], v[162:165], v[202:205], v[44:47]
	v_mfma_f32_16x16x32_bf16 v[36:39], v[170:173], v[202:205], v[36:39]
	v_mfma_f32_16x16x32_bf16 v[28:31], v[162:165], v[210:213], v[28:31]
	v_mfma_f32_16x16x32_bf16 v[20:23], v[170:173], v[210:213], v[20:23]
	v_mfma_f32_16x16x32_bf16 v[12:15], v[162:165], v[218:221], v[12:15]
	v_mfma_f32_16x16x32_bf16 v[4:7], v[170:173], v[218:221], v[4:7]
	v_mfma_f32_16x16x32_bf16 v[60:63], v[166:169], v[198:201], v[60:63]
	v_mfma_f32_16x16x32_bf16 v[52:55], v[174:177], v[198:201], v[52:55]
	v_mfma_f32_16x16x32_bf16 v[44:47], v[166:169], v[206:209], v[44:47]
	v_mfma_f32_16x16x32_bf16 v[36:39], v[174:177], v[206:209], v[36:39]
	v_mfma_f32_16x16x32_bf16 v[28:31], v[166:169], v[214:217], v[28:31]
	v_mfma_f32_16x16x32_bf16 v[20:23], v[174:177], v[214:217], v[20:23]
	v_mfma_f32_16x16x32_bf16 v[12:15], v[166:169], v[222:225], v[12:15]
	v_mfma_f32_16x16x32_bf16 v[4:7], v[174:177], v[222:225], v[4:7]
	v_mfma_f32_16x16x32_bf16 v[56:59], v[178:181], v[194:197], v[56:59]
	v_mfma_f32_16x16x32_bf16 v[48:51], v[186:189], v[194:197], v[48:51]
	v_mfma_f32_16x16x32_bf16 v[40:43], v[178:181], v[202:205], v[40:43]
	v_mfma_f32_16x16x32_bf16 v[32:35], v[186:189], v[202:205], v[32:35]
	v_mfma_f32_16x16x32_bf16 v[24:27], v[178:181], v[210:213], v[24:27]
	v_mfma_f32_16x16x32_bf16 v[16:19], v[186:189], v[210:213], v[16:19]
	v_mfma_f32_16x16x32_bf16 v[8:11], v[178:181], v[218:221], v[8:11]
	v_mfma_f32_16x16x32_bf16 v[0:3], v[186:189], v[218:221], v[0:3]
	v_mfma_f32_16x16x32_bf16 v[56:59], v[182:185], v[198:201], v[56:59]
	v_mfma_f32_16x16x32_bf16 v[48:51], v[190:193], v[198:201], v[48:51]
	v_mfma_f32_16x16x32_bf16 v[40:43], v[182:185], v[206:209], v[40:43]
	v_mfma_f32_16x16x32_bf16 v[32:35], v[190:193], v[206:209], v[32:35]
	v_mfma_f32_16x16x32_bf16 v[24:27], v[182:185], v[214:217], v[24:27]
	v_mfma_f32_16x16x32_bf16 v[16:19], v[190:193], v[214:217], v[16:19]
	v_mfma_f32_16x16x32_bf16 v[8:11], v[182:185], v[222:225], v[8:11]
	v_mfma_f32_16x16x32_bf16 v[0:3], v[190:193], v[222:225], v[0:3]
	s_barrier
	ds_read_b128 v[162:165], v154
	ds_read_b128 v[166:169], v154 offset:1024
	ds_read_b128 v[170:173], v154 offset:2048
	ds_read_b128 v[174:177], v154 offset:3072
	ds_read_b128 v[178:181], v155
	ds_read_b128 v[182:185], v155 offset:1024
	ds_read_b128 v[186:189], v155 offset:2048
	ds_read_b128 v[190:193], v155 offset:3072
	s_mov_b32 m0, s46
	v_cndmask_b32_e32 v132, v138, v159, vcc
	ds_read_b128 v[194:197], v153 offset:32768
	ds_read_b128 v[198:201], v153 offset:33792
	ds_read_b128 v[202:205], v153 offset:34816
	ds_read_b128 v[206:209], v153 offset:35840
	ds_read_b128 v[210:213], v153 offset:36864
	ds_read_b128 v[214:217], v153 offset:37888
	ds_read_b128 v[218:221], v153 offset:38912
	ds_read_b128 v[222:225], v153 offset:39936
	global_load_lds_dwordx4 v132, s[8:9]
	v_cndmask_b32_e32 v132, v140, v160, vcc
	s_mov_b32 m0, s47
	s_nop 0
	global_load_lds_dwordx4 v132, s[8:9]
	s_waitcnt vmcnt(8)
	s_waitcnt lgkmcnt(0)
	s_barrier
	s_waitcnt lgkmcnt(0)
	v_mfma_f32_16x16x32_bf16 v[124:127], v[162:165], v[194:197], v[124:127]
	v_mfma_f32_16x16x32_bf16 v[116:119], v[170:173], v[194:197], v[116:119]
	v_mfma_f32_16x16x32_bf16 v[108:111], v[162:165], v[202:205], v[108:111]
	v_mfma_f32_16x16x32_bf16 v[100:103], v[170:173], v[202:205], v[100:103]
	v_mfma_f32_16x16x32_bf16 v[92:95], v[162:165], v[210:213], v[92:95]
	v_mfma_f32_16x16x32_bf16 v[84:87], v[170:173], v[210:213], v[84:87]
	v_mfma_f32_16x16x32_bf16 v[76:79], v[162:165], v[218:221], v[76:79]
	v_mfma_f32_16x16x32_bf16 v[68:71], v[170:173], v[218:221], v[68:71]
	v_mfma_f32_16x16x32_bf16 v[124:127], v[166:169], v[198:201], v[124:127]
	v_mfma_f32_16x16x32_bf16 v[116:119], v[174:177], v[198:201], v[116:119]
	v_mfma_f32_16x16x32_bf16 v[108:111], v[166:169], v[206:209], v[108:111]
	v_mfma_f32_16x16x32_bf16 v[100:103], v[174:177], v[206:209], v[100:103]
	v_mfma_f32_16x16x32_bf16 v[92:95], v[166:169], v[214:217], v[92:95]
	v_mfma_f32_16x16x32_bf16 v[84:87], v[174:177], v[214:217], v[84:87]
	v_mfma_f32_16x16x32_bf16 v[76:79], v[166:169], v[222:225], v[76:79]
	v_mfma_f32_16x16x32_bf16 v[68:71], v[174:177], v[222:225], v[68:71]
	v_mfma_f32_16x16x32_bf16 v[120:123], v[178:181], v[194:197], v[120:123]
	v_mfma_f32_16x16x32_bf16 v[112:115], v[186:189], v[194:197], v[112:115]
	v_mfma_f32_16x16x32_bf16 v[104:107], v[178:181], v[202:205], v[104:107]
	v_mfma_f32_16x16x32_bf16 v[96:99], v[186:189], v[202:205], v[96:99]
	v_mfma_f32_16x16x32_bf16 v[88:91], v[178:181], v[210:213], v[88:91]
	v_mfma_f32_16x16x32_bf16 v[80:83], v[186:189], v[210:213], v[80:83]
	v_mfma_f32_16x16x32_bf16 v[72:75], v[178:181], v[218:221], v[72:75]
	v_mfma_f32_16x16x32_bf16 v[64:67], v[186:189], v[218:221], v[64:67]
	v_mfma_f32_16x16x32_bf16 v[120:123], v[182:185], v[198:201], v[120:123]
	v_mfma_f32_16x16x32_bf16 v[112:115], v[190:193], v[198:201], v[112:115]
	v_mfma_f32_16x16x32_bf16 v[104:107], v[182:185], v[206:209], v[104:107]
	v_mfma_f32_16x16x32_bf16 v[96:99], v[190:193], v[206:209], v[96:99]
	v_mfma_f32_16x16x32_bf16 v[88:91], v[182:185], v[214:217], v[88:91]
	v_mfma_f32_16x16x32_bf16 v[80:83], v[190:193], v[214:217], v[80:83]
	v_mfma_f32_16x16x32_bf16 v[72:75], v[182:185], v[222:225], v[72:75]
	v_mfma_f32_16x16x32_bf16 v[64:67], v[190:193], v[222:225], v[64:67]
	s_barrier
; #define PG8_STAGE(bufoff, gbase, voff) do { _Pragma("unroll") for (int _i = 0; _i < 2; ++_i) \
;         __builtin_amdgcn_global_load_lds((const unsigned*)((const char*)(gbase) + (voff)[_i]), (PG8_LAS unsigned*)(lds + (bufoff) + ldsw + _i * 8192), 16, 0, 0); } while (0)
; #define PG8_STAGE_A(bufoff, gbase, h, nx) do { _Pragma("unroll") for (int _i = 0; _i < 2; ++_i) { \
;         const unsigned vo_ = GA ? ((nx) ? vgn[h][_i] : vgc[h][_i]) : voffA[_i]; \
;         __builtin_amdgcn_global_load_lds((const unsigned*)((const char*)(gbase) + vo_), (PG8_LAS unsigned*)(lds + (bufoff) + ldsw + _i * 8192), 16, 0, 0); } } while (0)
; #define PG8_LDA(dst, b, h) do { _Pragma("unroll") for (int m = 0; m < 4; ++m) _Pragma("unroll") for (int k = 0; k < 2; ++k) dst[m][k] = *(const PG8_LAS bf16x8*)(lds + PG8_SA(b, h) + aoff + m * 2048 + k * 1024); } while (0)
; #define PG8_MMA(ai, bj, At, Bt) do { __builtin_amdgcn_s_setprio(1); _Pragma("unroll") for (int m = 0; m < 4; ++m) _Pragma("unroll") for (int n = 0; n < 2; ++n) _Pragma("unroll") for (int k = 0; k < 2; ++k) \
;         acc[ai][bj][m][n] = __builtin_amdgcn_mfma_f32_16x16x32_bf16(Bt[n][k], At[m][k], acc[ai][bj][m][n], 0, 0, 0); __builtin_amdgcn_s_setprio(0); } while (0)
; #define PG8_WAIT_V(n) asm volatile("s_waitcnt vmcnt(" #n ")" ::: "memory")
; #define PG8_WAIT_L(n) asm volatile("s_waitcnt lgkmcnt(" #n ")" ::: "memory")
; #define PG8_BAR __builtin_amdgcn_s_barrier()
; #define PG8_SCHED __builtin_amdgcn_sched_barrier(0)
; template <class Epi, class Sched>
; __device__ __forceinline__ void gemm_phase(const int WID_, PG8_LAS unsigned char* lds, const Sched& S, const Epi& E) {
;     ...
;             PG8_LDA(At, 1, 1); PG8_STAGE(PG8_SB(1, 0), b3, voffB); PG8_STAGE(PG8_SB(1, 1), b3 + hstepB, voffB); PG8_STAGE_A(PG8_SA(1, 0), a3, 0, last);
;             PG8_WAIT_V(8); PG8_WAIT_L(0); PG8_BAR; PG8_MMA(1, 0, At, B0); PG8_MMA(1, 1, At, B1); PG8_BAR; PG8_SCHED;
;         }
;         if (wr == 0) PG8_BAR;
	s_mov_b32 m0, s60
	v_lshl_add_u64 v[226:227], v[226:227], 0, s[36:37]
	s_add_u32 s6, s6, 0x40080
	ds_read_b128 v[194:197], v153 offset:49152
	ds_read_b128 v[198:201], v153 offset:50176
	ds_read_b128 v[202:205], v153 offset:51200
	ds_read_b128 v[206:209], v153 offset:52224
	ds_read_b128 v[210:213], v153 offset:53248
	ds_read_b128 v[214:217], v153 offset:54272
	ds_read_b128 v[218:221], v153 offset:55296
	ds_read_b128 v[222:225], v153 offset:56320
	global_load_lds_dwordx4 v[226:227], off
	v_lshl_add_u64 v[226:227], v[228:229], 0, s[36:37]
	s_mov_b32 m0, s61
	s_addc_u32 s7, s7, 0
	global_load_lds_dwordx4 v[226:227], off
	v_lshl_add_u64 v[226:227], s[6:7], 0, v[128:129]
	s_mov_b32 m0, s62
	s_nop 0
	global_load_lds_dwordx4 v[226:227], off
	v_lshl_add_u64 v[226:227], s[6:7], 0, v[130:131]
	s_mov_b32 m0, s63
	s_nop 0
	global_load_lds_dwordx4 v[226:227], off
	v_lshl_add_u64 v[226:227], v[230:231], 0, s[36:37]
	s_mov_b32 m0, s49
	s_nop 0
	global_load_lds_dwordx4 v[226:227], off
	v_lshl_add_u64 v[226:227], v[232:233], 0, s[36:37]
	s_mov_b32 m0, s50
	s_nop 0
	global_load_lds_dwordx4 v[226:227], off
	s_waitcnt vmcnt(8)
	s_waitcnt lgkmcnt(0)
	s_barrier
	s_waitcnt lgkmcnt(0)
	v_mfma_f32_16x16x32_bf16 v[60:63], v[162:165], v[194:197], v[60:63]
	v_mfma_f32_16x16x32_bf16 v[52:55], v[170:173], v[194:197], v[52:55]
	v_mfma_f32_16x16x32_bf16 v[44:47], v[162:165], v[202:205], v[44:47]
	v_mfma_f32_16x16x32_bf16 v[36:39], v[170:173], v[202:205], v[36:39]
	v_mfma_f32_16x16x32_bf16 v[28:31], v[162:165], v[210:213], v[28:31]
	v_mfma_f32_16x16x32_bf16 v[20:23], v[170:173], v[210:213], v[20:23]
	v_mfma_f32_16x16x32_bf16 v[12:15], v[162:165], v[218:221], v[12:15]
	v_mfma_f32_16x16x32_bf16 v[4:7], v[170:173], v[218:221], v[4:7]
	v_mfma_f32_16x16x32_bf16 v[60:63], v[166:169], v[198:201], v[60:63]
	v_mfma_f32_16x16x32_bf16 v[52:55], v[174:177], v[198:201], v[52:55]
	v_mfma_f32_16x16x32_bf16 v[44:47], v[166:169], v[206:209], v[44:47]
	v_mfma_f32_16x16x32_bf16 v[36:39], v[174:177], v[206:209], v[36:39]
	v_mfma_f32_16x16x32_bf16 v[28:31], v[166:169], v[214:217], v[28:31]
	v_mfma_f32_16x16x32_bf16 v[20:23], v[174:177], v[214:217], v[20:23]
	v_mfma_f32_16x16x32_bf16 v[12:15], v[166:169], v[222:225], v[12:15]
	v_mfma_f32_16x16x32_bf16 v[4:7], v[174:177], v[222:225], v[4:7]
	v_mfma_f32_16x16x32_bf16 v[56:59], v[178:181], v[194:197], v[56:59]
	v_mfma_f32_16x16x32_bf16 v[48:51], v[186:189], v[194:197], v[48:51]
	v_mfma_f32_16x16x32_bf16 v[40:43], v[178:181], v[202:205], v[40:43]
	v_mfma_f32_16x16x32_bf16 v[32:35], v[186:189], v[202:205], v[32:35]
	v_mfma_f32_16x16x32_bf16 v[24:27], v[178:181], v[210:213], v[24:27]
	v_mfma_f32_16x16x32_bf16 v[16:19], v[186:189], v[210:213], v[16:19]
	v_mfma_f32_16x16x32_bf16 v[8:11], v[178:181], v[218:221], v[8:11]
	v_mfma_f32_16x16x32_bf16 v[0:3], v[186:189], v[218:221], v[0:3]
	v_mfma_f32_16x16x32_bf16 v[56:59], v[182:185], v[198:201], v[56:59]
	v_mfma_f32_16x16x32_bf16 v[48:51], v[190:193], v[198:201], v[48:51]
	v_mfma_f32_16x16x32_bf16 v[40:43], v[182:185], v[206:209], v[40:43]
	v_mfma_f32_16x16x32_bf16 v[32:35], v[190:193], v[206:209], v[32:35]
	v_mfma_f32_16x16x32_bf16 v[24:27], v[182:185], v[214:217], v[24:27]
	v_mfma_f32_16x16x32_bf16 v[16:19], v[190:193], v[214:217], v[16:19]
	v_mfma_f32_16x16x32_bf16 v[8:11], v[182:185], v[222:225], v[8:11]
	v_mfma_f32_16x16x32_bf16 v[0:3], v[190:193], v[222:225], v[0:3]
	s_barrier
	s_add_i32 s11, s11, 2
	s_add_u32 s4, s4, 0x100
	s_addc_u32 s5, s5, 0
	s_cmp_gt_u32 s11, 13
	s_cbranch_scc0 .LBB0_2294
	s_and_b64 vcc, exec, s[38:39]
	s_cbranch_vccz .LBB0_2297
	s_barrier

;     __device__ __forceinline__ const char* aptr(const Unit& u) const { return (const char*)(A + (size_t)u.pm * BM * lda); }
;     __device__ __forceinline__ const char* bptr(const Unit& u) const { return (const char*)(Bt + (size_t)u.pn * BM * ldb); }
;     __device__ __forceinline__ const char* aptr(const Unit& u) const { return (const char*)(A + (size_t)u.pm * BM * lda + koff(u)); }
;     __device__ __forceinline__ const char* bptr(const Unit& u) const { return (const char*)(Bt + (size_t)u.pn * BM * ldb + koff(u)); }
;     __device__ bool next(int i, Unit& u) const { if (i >= 6) return false; int pm_ = pm; asm volatile("" : "+s"(pm_)); u.pm = pm_; u.pn = (i + (GB >> 3)) % 6; return true; }
;     __device__ __forceinline__ const char* aptr(const Unit& u) const { return (const char*)(A + (size_t)u.pm * BM * lda + koff(u)); }
;     __device__ __forceinline__ const char* bptr(const Unit& u) const { return (const char*)(Bt + (size_t)u.pn * BM * ldb + koff(u)); }
; #define PG8_WAIT_V(n) asm volatile("s_waitcnt vmcnt(" #n ")" ::: "memory")
; #define PG8_BAR __builtin_amdgcn_s_barrier()
; template <class Epi, class Sched>
; __device__ __forceinline__ void gemm_phase(const int WID_, PG8_LAS unsigned char* lds, const Sched& S, const Epi& E) {
;     ...
;         const bool has_next = S.next(ui + 1, nxt);
;         const char* nA = has_next ? S.aptr(nxt) : cA; const char* nB = has_next ? S.bptr(nxt) : cB;
;         if (has_next) PG8_GOFF(vgn, nxt); else { if constexpr (GA) { _Pragma("unroll") for (int h_ = 0; h_ < 2; ++h_) _Pragma("unroll") for (int i_ = 0; i_ < 2; ++i_) vgn[h_][i_] = vgc[h_][i_]; } }
;         for (int t = 0; t < nt; t += 2) {
;             const bool last = (t == nt - 2);
;             const char* a1 = cA + (size_t)(t + 1) * kstep;
;             const char* a2 = last ? nA : cA + (size_t)(t + 2) * kstep; const char* b2 = last ? nB : cB + (size_t)(t + 2) * kstep;
;             const char* a3 = a2 + kstep; const char* b3 = b2 + kstep;
;             PG8_LDB(B0, 0, 0); PG8_LDB(B1, 0, 1); PG8_SCHED; PG8_LDA(At, 0, 0); PG8_STAGE_A(PG8_SA(1, 1), a1 + hstepA, 1, false);
;             PG8_WAIT_V(8); PG8_WAIT_L(0); PG8_BAR; PG8_MMA(0, 0, At, B0); PG8_MMA(0, 1, At, B1); PG8_BAR; PG8_SCHED;
;             PG8_LDA(At, 0, 1); PG8_STAGE(PG8_SB(0, 0), b2, voffB); PG8_STAGE(PG8_SB(0, 1), b2 + hstepB, voffB); PG8_STAGE_A(PG8_SA(0, 0), a2, 0, last);
.Lg2_nofix:
	ds_read_b128 v[142:145], v148
	ds_read_b128 v[152:155], v148 offset:1024
	ds_read_b128 v[156:159], v148 offset:2048
	ds_read_b128 v[160:163], v148 offset:3072
	ds_read_b128 v[164:167], v149
	ds_read_b128 v[168:171], v149 offset:1024
	ds_read_b128 v[172:175], v149 offset:2048
	ds_read_b128 v[176:179], v149 offset:3072
	s_add_u32 s40, s38, 0xfffe0080
	s_addc_u32 s41, s39, -1
	s_cmp_eq_u32 s62, 4
	s_cselect_b32 s43, s31, s41
	s_cselect_b32 s42, s59, s40
	s_cselect_b32 s41, s29, s61
	s_cselect_b32 s40, s28, s60
	s_mov_b32 m0, s55
	v_lshl_add_u64 v[212:213], s[38:39], 0, v[138:139]
	ds_read_b128 v[180:183], v150
	ds_read_b128 v[184:187], v150 offset:1024
	ds_read_b128 v[188:191], v150 offset:2048
	ds_read_b128 v[192:195], v150 offset:3072
	ds_read_b128 v[196:199], v150 offset:4096
	ds_read_b128 v[200:203], v150 offset:5120
	ds_read_b128 v[204:207], v150 offset:6144
	ds_read_b128 v[208:211], v150 offset:7168
	global_load_lds_dwordx4 v[212:213], off
	v_lshl_add_u64 v[212:213], s[38:39], 0, v[140:141]
	s_mov_b32 m0, s56
	s_nop 0
	global_load_lds_dwordx4 v[212:213], off
	s_waitcnt vmcnt(8)
	s_waitcnt lgkmcnt(0)
	s_barrier
	s_waitcnt lgkmcnt(0)
	v_mfma_f32_16x16x32_bf16 v[124:127], v[142:145], v[180:183], v[124:127]
	v_mfma_f32_16x16x32_bf16 v[120:123], v[156:159], v[180:183], v[120:123]
	v_mfma_f32_16x16x32_bf16 v[108:111], v[142:145], v[188:191], v[108:111]
	v_mfma_f32_16x16x32_bf16 v[104:107], v[156:159], v[188:191], v[104:107]
	v_mfma_f32_16x16x32_bf16 v[92:95], v[142:145], v[196:199], v[92:95]
	v_mfma_f32_16x16x32_bf16 v[88:91], v[156:159], v[196:199], v[88:91]
	v_mfma_f32_16x16x32_bf16 v[76:79], v[142:145], v[204:207], v[76:79]
	v_mfma_f32_16x16x32_bf16 v[72:75], v[156:159], v[204:207], v[72:75]
	v_mfma_f32_16x16x32_bf16 v[124:127], v[152:155], v[184:187], v[124:127]
	v_mfma_f32_16x16x32_bf16 v[120:123], v[160:163], v[184:187], v[120:123]
	v_mfma_f32_16x16x32_bf16 v[108:111], v[152:155], v[192:195], v[108:111]
	v_mfma_f32_16x16x32_bf16 v[104:107], v[160:163], v[192:195], v[104:107]
	v_mfma_f32_16x16x32_bf16 v[92:95], v[152:155], v[200:203], v[92:95]
	v_mfma_f32_16x16x32_bf16 v[88:91], v[160:163], v[200:203], v[88:91]
	v_mfma_f32_16x16x32_bf16 v[76:79], v[152:155], v[208:211], v[76:79]
	v_mfma_f32_16x16x32_bf16 v[72:75], v[160:163], v[208:211], v[72:75]
	v_mfma_f32_16x16x32_bf16 v[116:119], v[164:167], v[180:183], v[116:119]
	v_mfma_f32_16x16x32_bf16 v[112:115], v[172:175], v[180:183], v[112:115]
	v_mfma_f32_16x16x32_bf16 v[100:103], v[164:167], v[188:191], v[100:103]
	v_mfma_f32_16x16x32_bf16 v[96:99], v[172:175], v[188:191], v[96:99]
	v_mfma_f32_16x16x32_bf16 v[84:87], v[164:167], v[196:199], v[84:87]
	v_mfma_f32_16x16x32_bf16 v[80:83], v[172:175], v[196:199], v[80:83]
	v_mfma_f32_16x16x32_bf16 v[68:71], v[164:167], v[204:207], v[68:71]
	v_mfma_f32_16x16x32_bf16 v[64:67], v[172:175], v[204:207], v[64:67]
	v_mfma_f32_16x16x32_bf16 v[116:119], v[168:171], v[184:187], v[116:119]
	v_mfma_f32_16x16x32_bf16 v[112:115], v[176:179], v[184:187], v[112:115]
	v_mfma_f32_16x16x32_bf16 v[100:103], v[168:171], v[192:195], v[100:103]
	v_mfma_f32_16x16x32_bf16 v[96:99], v[176:179], v[192:195], v[96:99]
	v_mfma_f32_16x16x32_bf16 v[84:87], v[168:171], v[200:203], v[84:87]
	v_mfma_f32_16x16x32_bf16 v[80:83], v[176:179], v[200:203], v[80:83]
	v_mfma_f32_16x16x32_bf16 v[68:71], v[168:171], v[208:211], v[68:71]
	v_mfma_f32_16x16x32_bf16 v[64:67], v[176:179], v[208:211], v[64:67]
	s_barrier
	s_mov_b32 m0, s57
	v_lshl_add_u64 v[212:213], s[40:41], 0, v[130:131]
	ds_read_b128 v[180:183], v150 offset:16384
	ds_read_b128 v[184:187], v150 offset:17408
	ds_read_b128 v[188:191], v150 offset:18432
	ds_read_b128 v[192:195], v150 offset:19456
	ds_read_b128 v[196:199], v150 offset:20480
	ds_read_b128 v[200:203], v150 offset:21504
	ds_read_b128 v[204:207], v150 offset:22528
	ds_read_b128 v[208:211], v150 offset:23552
	global_load_lds_dwordx4 v[212:213], off
	s_add_i32 m0, s57, 0x2000
	s_add_u32 s64, s40, 0x20000
	v_lshl_add_u64 v[214:215], s[40:41], 0, v[134:135]
	s_addc_u32 s65, s41, 0
	s_add_i32 s63, s50, s33
	global_load_lds_dwordx4 v[214:215], off
	v_lshl_add_u64 v[216:217], s[64:65], 0, v[130:131]
	s_mov_b32 m0, s63
	v_lshl_add_u64 v[218:219], s[42:43], 0, v[136:137]
	global_load_lds_dwordx4 v[216:217], off
	v_lshl_add_u64 v[216:217], s[64:65], 0, v[134:135]
	s_add_i32 m0, s63, 0x2000
	s_nop 0
	global_load_lds_dwordx4 v[216:217], off
	v_lshl_add_u64 v[216:217], s[42:43], 0, v[132:133]
	s_mov_b32 m0, s44
	s_nop 0
	global_load_lds_dwordx4 v[216:217], off
	s_mov_b32 m0, s21
	s_nop 0
	global_load_lds_dwordx4 v[218:219], off
	s_waitcnt vmcnt(8)
	s_waitcnt lgkmcnt(0)
	s_barrier
; #define PG8_STAGE_A(bufoff, gbase, h, nx) do { _Pragma("unroll") for (int _i = 0; _i < 2; ++_i) { \
;         const unsigned vo_ = GA ? ((nx) ? vgn[h][_i] : vgc[h][_i]) : voffA[_i]; \
;         __builtin_amdgcn_global_load_lds((const unsigned*)((const char*)(gbase) + vo_), (PG8_LAS unsigned*)(lds + (bufoff) + ldsw + _i * 8192), 16, 0, 0); } } while (0)
; #define PG8_LDA(dst, b, h) do { _Pragma("unroll") for (int m = 0; m < 4; ++m) _Pragma("unroll") for (int k = 0; k < 2; ++k) dst[m][k] = *(const PG8_LAS bf16x8*)(lds + PG8_SA(b, h) + aoff + m * 2048 + k * 1024); } while (0)
; #define PG8_LDB(dst, b, h) do { _Pragma("unroll") for (int n = 0; n < 2; ++n) _Pragma("unroll") for (int k = 0; k < 2; ++k) dst[n][k] = *(const PG8_LAS bf16x8*)(lds + PG8_SB(b, h) + boff + n * 2048 + k * 1024); } while (0)
; #define PG8_MMA(ai, bj, At, Bt) do { __builtin_amdgcn_s_setprio(1); _Pragma("unroll") for (int m = 0; m < 4; ++m) _Pragma("unroll") for (int n = 0; n < 2; ++n) _Pragma("unroll") for (int k = 0; k < 2; ++k) \
;         acc[ai][bj][m][n] = __builtin_amdgcn_mfma_f32_16x16x32_bf16(Bt[n][k], At[m][k], acc[ai][bj][m][n], 0, 0, 0); __builtin_amdgcn_s_setprio(0); } while (0)
; #define PG8_WAIT_V(n) asm volatile("s_waitcnt vmcnt(" #n ")" ::: "memory")
; #define PG8_WAIT_L(n) asm volatile("s_waitcnt lgkmcnt(" #n ")" ::: "memory")
; #define PG8_BAR __builtin_amdgcn_s_barrier()
; #define PG8_SCHED __builtin_amdgcn_sched_barrier(0)
; template <class Epi, class Sched>
; __device__ __forceinline__ void gemm_phase(const int WID_, PG8_LAS unsigned char* lds, const Sched& S, const Epi& E) {
;     ...
;             PG8_WAIT_V(8); PG8_WAIT_L(0); PG8_BAR; PG8_MMA(1, 0, At, B0); PG8_MMA(1, 1, At, B1); PG8_BAR; PG8_SCHED;
;             PG8_LDB(B0, 1, 0); PG8_LDB(B1, 1, 1); PG8_SCHED; PG8_LDA(At, 1, 0); PG8_STAGE_A(PG8_SA(0, 1), a2 + hstepA, 1, last);
;             PG8_WAIT_V(8); PG8_WAIT_L(0); PG8_BAR; PG8_MMA(0, 0, At, B0); PG8_MMA(0, 1, At, B1); PG8_BAR; PG8_SCHED;
	s_waitcnt lgkmcnt(0)
	v_mfma_f32_16x16x32_bf16 v[60:63], v[142:145], v[180:183], v[60:63]
	v_mfma_f32_16x16x32_bf16 v[56:59], v[156:159], v[180:183], v[56:59]
	v_mfma_f32_16x16x32_bf16 v[44:47], v[142:145], v[188:191], v[44:47]
	v_mfma_f32_16x16x32_bf16 v[40:43], v[156:159], v[188:191], v[40:43]
	v_mfma_f32_16x16x32_bf16 v[28:31], v[142:145], v[196:199], v[28:31]
	v_mfma_f32_16x16x32_bf16 v[24:27], v[156:159], v[196:199], v[24:27]
	v_mfma_f32_16x16x32_bf16 v[12:15], v[142:145], v[204:207], v[12:15]
	v_mfma_f32_16x16x32_bf16 v[8:11], v[156:159], v[204:207], v[8:11]
	v_mfma_f32_16x16x32_bf16 v[60:63], v[152:155], v[184:187], v[60:63]
	v_mfma_f32_16x16x32_bf16 v[56:59], v[160:163], v[184:187], v[56:59]
	v_mfma_f32_16x16x32_bf16 v[44:47], v[152:155], v[192:195], v[44:47]
	v_mfma_f32_16x16x32_bf16 v[40:43], v[160:163], v[192:195], v[40:43]
	v_mfma_f32_16x16x32_bf16 v[28:31], v[152:155], v[200:203], v[28:31]
	v_mfma_f32_16x16x32_bf16 v[24:27], v[160:163], v[200:203], v[24:27]
	v_mfma_f32_16x16x32_bf16 v[12:15], v[152:155], v[208:211], v[12:15]
	v_mfma_f32_16x16x32_bf16 v[8:11], v[160:163], v[208:211], v[8:11]
	v_mfma_f32_16x16x32_bf16 v[52:55], v[164:167], v[180:183], v[52:55]
	v_mfma_f32_16x16x32_bf16 v[48:51], v[172:175], v[180:183], v[48:51]
	v_mfma_f32_16x16x32_bf16 v[36:39], v[164:167], v[188:191], v[36:39]
	v_mfma_f32_16x16x32_bf16 v[32:35], v[172:175], v[188:191], v[32:35]
	v_mfma_f32_16x16x32_bf16 v[20:23], v[164:167], v[196:199], v[20:23]
	v_mfma_f32_16x16x32_bf16 v[16:19], v[172:175], v[196:199], v[16:19]
	v_mfma_f32_16x16x32_bf16 v[4:7], v[164:167], v[204:207], v[4:7]
	v_mfma_f32_16x16x32_bf16 v[0:3], v[172:175], v[204:207], v[0:3]
	v_mfma_f32_16x16x32_bf16 v[52:55], v[168:171], v[184:187], v[52:55]
	v_mfma_f32_16x16x32_bf16 v[48:51], v[176:179], v[184:187], v[48:51]
	v_mfma_f32_16x16x32_bf16 v[36:39], v[168:171], v[192:195], v[36:39]
	v_mfma_f32_16x16x32_bf16 v[32:35], v[176:179], v[192:195], v[32:35]
	v_mfma_f32_16x16x32_bf16 v[20:23], v[168:171], v[200:203], v[20:23]
	v_mfma_f32_16x16x32_bf16 v[16:19], v[176:179], v[200:203], v[16:19]
	v_mfma_f32_16x16x32_bf16 v[4:7], v[168:171], v[208:211], v[4:7]
	v_mfma_f32_16x16x32_bf16 v[0:3], v[176:179], v[208:211], v[0:3]
	s_barrier
	s_add_i32 s63, 0, 0x18000
	v_add_u32_e32 v128, s63, v147
	s_add_i32 s64, 0, 0x1c000
	ds_read_b128 v[142:145], v128
	ds_read_b128 v[152:155], v128 offset:1024
	ds_read_b128 v[156:159], v128 offset:2048
	ds_read_b128 v[160:163], v128 offset:3072
	v_add_u32_e32 v128, s64, v147
	ds_read_b128 v[164:167], v128
	ds_read_b128 v[168:171], v128 offset:1024
	ds_read_b128 v[172:175], v128 offset:2048
	ds_read_b128 v[176:179], v128 offset:3072
	s_add_u32 s42, s42, 0x20000
	s_addc_u32 s43, s43, 0
	s_mov_b32 m0, s45
	v_lshl_add_u64 v[220:221], s[42:43], 0, v[132:133]
	ds_read_b128 v[180:183], v150 offset:32768
	ds_read_b128 v[184:187], v150 offset:33792
	ds_read_b128 v[188:191], v150 offset:34816
	ds_read_b128 v[192:195], v150 offset:35840
	ds_read_b128 v[196:199], v150 offset:36864
	ds_read_b128 v[200:203], v150 offset:37888
	ds_read_b128 v[204:207], v150 offset:38912
	ds_read_b128 v[208:211], v150 offset:39936
	global_load_lds_dwordx4 v[220:221], off
	v_lshl_add_u64 v[220:221], s[42:43], 0, v[136:137]
	s_mov_b32 m0, s46
	s_nop 0
	global_load_lds_dwordx4 v[220:221], off
	s_waitcnt vmcnt(8)
	s_waitcnt lgkmcnt(0)
	s_barrier
	s_waitcnt lgkmcnt(0)
	v_mfma_f32_16x16x32_bf16 v[124:127], v[142:145], v[180:183], v[124:127]
	v_mfma_f32_16x16x32_bf16 v[120:123], v[156:159], v[180:183], v[120:123]
	v_mfma_f32_16x16x32_bf16 v[108:111], v[142:145], v[188:191], v[108:111]
	v_mfma_f32_16x16x32_bf16 v[104:107], v[156:159], v[188:191], v[104:107]
	v_mfma_f32_16x16x32_bf16 v[92:95], v[142:145], v[196:199], v[92:95]
	v_mfma_f32_16x16x32_bf16 v[88:91], v[156:159], v[196:199], v[88:91]
	v_mfma_f32_16x16x32_bf16 v[76:79], v[142:145], v[204:207], v[76:79]
	v_mfma_f32_16x16x32_bf16 v[72:75], v[156:159], v[204:207], v[72:75]
	v_mfma_f32_16x16x32_bf16 v[124:127], v[152:155], v[184:187], v[124:127]
	v_mfma_f32_16x16x32_bf16 v[120:123], v[160:163], v[184:187], v[120:123]
	v_mfma_f32_16x16x32_bf16 v[108:111], v[152:155], v[192:195], v[108:111]
	v_mfma_f32_16x16x32_bf16 v[104:107], v[160:163], v[192:195], v[104:107]
	v_mfma_f32_16x16x32_bf16 v[92:95], v[152:155], v[200:203], v[92:95]
	v_mfma_f32_16x16x32_bf16 v[88:91], v[160:163], v[200:203], v[88:91]
	v_mfma_f32_16x16x32_bf16 v[76:79], v[152:155], v[208:211], v[76:79]
	v_mfma_f32_16x16x32_bf16 v[72:75], v[160:163], v[208:211], v[72:75]
	v_mfma_f32_16x16x32_bf16 v[116:119], v[164:167], v[180:183], v[116:119]
	v_mfma_f32_16x16x32_bf16 v[112:115], v[172:175], v[180:183], v[112:115]
	v_mfma_f32_16x16x32_bf16 v[100:103], v[164:167], v[188:191], v[100:103]
	v_mfma_f32_16x16x32_bf16 v[96:99], v[172:175], v[188:191], v[96:99]
	v_mfma_f32_16x16x32_bf16 v[84:87], v[164:167], v[196:199], v[84:87]
	v_mfma_f32_16x16x32_bf16 v[80:83], v[172:175], v[196:199], v[80:83]
	v_mfma_f32_16x16x32_bf16 v[68:71], v[164:167], v[204:207], v[68:71]
	v_mfma_f32_16x16x32_bf16 v[64:67], v[172:175], v[204:207], v[64:67]
	v_mfma_f32_16x16x32_bf16 v[116:119], v[168:171], v[184:187], v[116:119]
	v_mfma_f32_16x16x32_bf16 v[112:115], v[176:179], v[184:187], v[112:115]
	v_mfma_f32_16x16x32_bf16 v[100:103], v[168:171], v[192:195], v[100:103]
	v_mfma_f32_16x16x32_bf16 v[96:99], v[176:179], v[192:195], v[96:99]
	v_mfma_f32_16x16x32_bf16 v[84:87], v[168:171], v[200:203], v[84:87]
	v_mfma_f32_16x16x32_bf16 v[80:83], v[176:179], v[200:203], v[80:83]
	v_mfma_f32_16x16x32_bf16 v[68:71], v[168:171], v[208:211], v[68:71]
	v_mfma_f32_16x16x32_bf16 v[64:67], v[176:179], v[208:211], v[64:67]
	s_barrier
; #define PG8_STAGE(bufoff, gbase, voff) do { _Pragma("unroll") for (int _i = 0; _i < 2; ++_i) \
;         __builtin_amdgcn_global_load_lds((const unsigned*)((const char*)(gbase) + (voff)[_i]), (PG8_LAS unsigned*)(lds + (bufoff) + ldsw + _i * 8192), 16, 0, 0); } while (0)
; #define PG8_STAGE_A(bufoff, gbase, h, nx) do { _Pragma("unroll") for (int _i = 0; _i < 2; ++_i) { \
;         const unsigned vo_ = GA ? ((nx) ? vgn[h][_i] : vgc[h][_i]) : voffA[_i]; \
;         __builtin_amdgcn_global_load_lds((const unsigned*)((const char*)(gbase) + vo_), (PG8_LAS unsigned*)(lds + (bufoff) + ldsw + _i * 8192), 16, 0, 0); } } while (0)
; #define PG8_LDA(dst, b, h) do { _Pragma("unroll") for (int m = 0; m < 4; ++m) _Pragma("unroll") for (int k = 0; k < 2; ++k) dst[m][k] = *(const PG8_LAS bf16x8*)(lds + PG8_SA(b, h) + aoff + m * 2048 + k * 1024); } while (0)
; #define PG8_MMA(ai, bj, At, Bt) do { __builtin_amdgcn_s_setprio(1); _Pragma("unroll") for (int m = 0; m < 4; ++m) _Pragma("unroll") for (int n = 0; n < 2; ++n) _Pragma("unroll") for (int k = 0; k < 2; ++k) \
;         acc[ai][bj][m][n] = __builtin_amdgcn_mfma_f32_16x16x32_bf16(Bt[n][k], At[m][k], acc[ai][bj][m][n], 0, 0, 0); __builtin_amdgcn_s_setprio(0); } while (0)
; #define PG8_WAIT_V(n) asm volatile("s_waitcnt vmcnt(" #n ")" ::: "memory")
; #define PG8_WAIT_L(n) asm volatile("s_waitcnt lgkmcnt(" #n ")" ::: "memory")
; #define PG8_BAR __builtin_amdgcn_s_barrier()
; #define PG8_SCHED __builtin_amdgcn_sched_barrier(0)
; template <class Epi, class Sched>
; __device__ __forceinline__ void gemm_phase(const int WID_, PG8_LAS unsigned char* lds, const Sched& S, const Epi& E) {
;     ...
;             PG8_LDA(At, 1, 1); PG8_STAGE(PG8_SB(1, 0), b3, voffB); PG8_STAGE(PG8_SB(1, 1), b3 + hstepB, voffB); PG8_STAGE_A(PG8_SA(1, 0), a3, 0, last);
;             PG8_WAIT_V(8); PG8_WAIT_L(0); PG8_BAR; PG8_MMA(1, 0, At, B0); PG8_MMA(1, 1, At, B1); PG8_BAR; PG8_SCHED;
;         }
;         if (wr == 0) PG8_BAR;
	s_add_i32 s42, s63, s33
	v_lshl_add_u64 v[212:213], v[212:213], 0, s[6:7]
	s_mov_b32 m0, s42
	ds_read_b128 v[180:183], v150 offset:49152
	ds_read_b128 v[184:187], v150 offset:50176
	ds_read_b128 v[188:191], v150 offset:51200
	ds_read_b128 v[192:195], v150 offset:52224
	ds_read_b128 v[196:199], v150 offset:53248
	ds_read_b128 v[200:203], v150 offset:54272
	ds_read_b128 v[204:207], v150 offset:55296
	ds_read_b128 v[208:211], v150 offset:56320
	global_load_lds_dwordx4 v[212:213], off
	s_add_i32 m0, s42, 0x2000
	s_add_u32 s40, s40, 0x20080
	v_lshl_add_u64 v[212:213], v[214:215], 0, s[6:7]
	s_addc_u32 s41, s41, 0
	s_add_i32 s42, s64, s33
	global_load_lds_dwordx4 v[212:213], off
	v_lshl_add_u64 v[212:213], s[40:41], 0, v[130:131]
	s_mov_b32 m0, s42
	s_nop 0
	global_load_lds_dwordx4 v[212:213], off
	v_lshl_add_u64 v[212:213], s[40:41], 0, v[134:135]
	s_add_i32 m0, s42, 0x2000
	s_nop 0
	global_load_lds_dwordx4 v[212:213], off
	v_lshl_add_u64 v[212:213], v[216:217], 0, s[6:7]
	s_mov_b32 m0, s48
	s_nop 0
	global_load_lds_dwordx4 v[212:213], off
	v_lshl_add_u64 v[212:213], v[218:219], 0, s[6:7]
	s_mov_b32 m0, s49
	s_nop 0
	global_load_lds_dwordx4 v[212:213], off
	s_waitcnt vmcnt(8)
	s_waitcnt lgkmcnt(0)
	s_barrier
	s_waitcnt lgkmcnt(0)
	v_mfma_f32_16x16x32_bf16 v[60:63], v[142:145], v[180:183], v[60:63]
	v_mfma_f32_16x16x32_bf16 v[56:59], v[156:159], v[180:183], v[56:59]
	v_mfma_f32_16x16x32_bf16 v[44:47], v[142:145], v[188:191], v[44:47]
	v_mfma_f32_16x16x32_bf16 v[40:43], v[156:159], v[188:191], v[40:43]
	v_mfma_f32_16x16x32_bf16 v[28:31], v[142:145], v[196:199], v[28:31]
	v_mfma_f32_16x16x32_bf16 v[24:27], v[156:159], v[196:199], v[24:27]
	v_mfma_f32_16x16x32_bf16 v[12:15], v[142:145], v[204:207], v[12:15]
	v_mfma_f32_16x16x32_bf16 v[8:11], v[156:159], v[204:207], v[8:11]
	v_mfma_f32_16x16x32_bf16 v[60:63], v[152:155], v[184:187], v[60:63]
	v_mfma_f32_16x16x32_bf16 v[56:59], v[160:163], v[184:187], v[56:59]
	v_mfma_f32_16x16x32_bf16 v[44:47], v[152:155], v[192:195], v[44:47]
	v_mfma_f32_16x16x32_bf16 v[40:43], v[160:163], v[192:195], v[40:43]
	v_mfma_f32_16x16x32_bf16 v[28:31], v[152:155], v[200:203], v[28:31]
	v_mfma_f32_16x16x32_bf16 v[24:27], v[160:163], v[200:203], v[24:27]
	v_mfma_f32_16x16x32_bf16 v[12:15], v[152:155], v[208:211], v[12:15]
	v_mfma_f32_16x16x32_bf16 v[8:11], v[160:163], v[208:211], v[8:11]
	v_mfma_f32_16x16x32_bf16 v[52:55], v[164:167], v[180:183], v[52:55]
	v_mfma_f32_16x16x32_bf16 v[48:51], v[172:175], v[180:183], v[48:51]
	v_mfma_f32_16x16x32_bf16 v[36:39], v[164:167], v[188:191], v[36:39]
	v_mfma_f32_16x16x32_bf16 v[32:35], v[172:175], v[188:191], v[32:35]
	v_mfma_f32_16x16x32_bf16 v[20:23], v[164:167], v[196:199], v[20:23]
	v_mfma_f32_16x16x32_bf16 v[16:19], v[172:175], v[196:199], v[16:19]
	v_mfma_f32_16x16x32_bf16 v[4:7], v[164:167], v[204:207], v[4:7]
	v_mfma_f32_16x16x32_bf16 v[0:3], v[172:175], v[204:207], v[0:3]
	v_mfma_f32_16x16x32_bf16 v[52:55], v[168:171], v[184:187], v[52:55]
	v_mfma_f32_16x16x32_bf16 v[48:51], v[176:179], v[184:187], v[48:51]
	v_mfma_f32_16x16x32_bf16 v[36:39], v[168:171], v[192:195], v[36:39]
	v_mfma_f32_16x16x32_bf16 v[32:35], v[176:179], v[192:195], v[32:35]
	v_mfma_f32_16x16x32_bf16 v[20:23], v[168:171], v[200:203], v[20:23]
	v_mfma_f32_16x16x32_bf16 v[16:19], v[176:179], v[200:203], v[16:19]
	v_mfma_f32_16x16x32_bf16 v[4:7], v[168:171], v[208:211], v[4:7]
	v_mfma_f32_16x16x32_bf16 v[0:3], v[176:179], v[208:211], v[0:3]
	s_barrier
	s_add_i32 s62, s62, 2
	s_add_u32 s38, s38, 0x100
	s_addc_u32 s39, s39, 0
	s_add_u32 s60, s60, 0x100
	s_addc_u32 s61, s61, 0
	s_cmp_gt_u32 s62, 5
	s_cbranch_scc0 .LBB0_2362
	s_and_b64 vcc, exec, s[8:9]
	s_cbranch_vccz .LBB0_2365
	s_barrier
